# k24: k15 + dead fp8-cvt register inits removed (all phases), P5 gelu epilogue argument chain 5->3 instrs, P6 GLU epilogue log2e folded into fmamk + pk_mul copies removed
# speedup vs baseline: 1.0037x; 1.0037x over previous
; #define LAS __attribute__((address_space(3)))
; #define EPI_ALD16(dst_, ptr_) asm volatile("global_load_dwordx4 %0, %1, off" : "=v"(dst_) : "v"(ptr_))
; __global__ void __launch_bounds__(NWAVES * 64, 2) fwd_kernel(Args args) {
;     ...
;             const int RPW = (T + NGW - 1) / NGW; int cb = -1; f32x4 Av[8], Bv[8];
;             const unsigned nvo = 16u * lane;
;     ...
;             if (RPW == 8 && (vcu * NWAVES + NWAVES - 1) * 8 + 7 < T) {
;                 f32x4 va[8], wa[8], vb[8], wb[8];
;                 const int r0 = gw * 8;
;                 {
;                     constexpr size_t QS = (size_t)4 * 8 * D; LAS float* NA = (LAS float*)(lds + RING_OFF); LAS float* NB = NA + D;
;                     const int bW = (vcu * NWAVES * 8) >> 12; const int k = 4 * tid; const float* mp = MODP + (size_t)bW * (8 * D) + k; f32x4 g, bs, bc, ps[4], pc[4];
;                     EPI_ALD16(g, norm1_g + k); EPI_ALD16(bs, ada_b + k); EPI_ALD16(bc, ada_b + D + k);
; #pragma unroll
;                     for (int q = 0; q < 4; ++q) { EPI_ALD16(ps[q], mp + q * QS); EPI_ALD16(pc[q], mp + q * QS + D); }
;                     asm volatile("s_waitcnt vmcnt(0)" : "+v"(g), "+v"(bs), "+v"(bc), "+v"(ps[0]), "+v"(ps[1]), "+v"(ps[2]), "+v"(ps[3]), "+v"(pc[0]), "+v"(pc[1]), "+v"(pc[2]), "+v"(pc[3]));
;                     const f32x4 sh = bs + ps[0] + ps[1] + ps[2] + ps[3], sc = bc + pc[0] + pc[1] + pc[2] + pc[3];
;                     *(LAS f32x4*)(NA + k) = g * (sc + 1.0f); *(LAS f32x4*)(NB + k) = sh;
.LBB0_166:
	s_add_u32 s3, s56, 0x34400000
	s_addc_u32 s33, s57, 0
	s_add_u32 s10, s36, 0x2000
	v_readlane_b32 s1, v254, 9
	s_addc_u32 s11, s37, 0
	s_add_i32 s8, s1, 0x3fff
	s_lshl_b32 s6, s51, 6
	s_cmpk_gt_i32 s6, 0x3fc0
	s_cselect_b64 s[6:7], -1, 0
	s_abs_i32 s9, s1
	v_cvt_f32_u32_e32 v2, s9
	s_sub_i32 s15, 0, s9
	s_xor_b32 s14, s8, s1
	s_abs_i32 s8, s8
	v_rcp_iflag_f32_e32 v2, v2
	s_ashr_i32 s14, s14, 31
	v_lshlrev_b32_e32 v196, 2, v194
	v_mov_b32_e32 v197, 0
	v_mul_f32_e32 v2, 0x4f7ffffe, v2
	v_cvt_u32_f32_e32 v2, v2
	s_nop 0
	v_readfirstlane_b32 s48, v2
	s_mul_i32 s15, s15, s48
	s_mul_hi_u32 s15, s48, s15
	s_add_i32 s48, s48, s15
	s_mul_hi_u32 s15, s8, s48
	s_mul_i32 s48, s15, s9
	s_sub_i32 s8, s8, s48
	s_add_i32 s48, s15, 1
	s_sub_i32 s49, s8, s9
	s_cmp_ge_u32 s8, s9
	s_cselect_b32 s15, s48, s15
	s_cselect_b32 s8, s49, s8
	s_add_i32 s48, s15, 1
	s_cmp_ge_u32 s8, s9
	s_cselect_b32 s8, s48, s15
	s_xor_b32 s8, s8, s14
	s_sub_i32 s48, s8, s14
	s_cmp_lg_u32 s48, 8
	s_cselect_b64 s[8:9], -1, 0
	s_or_b64 s[8:9], s[8:9], s[6:7]
	s_mov_b64 s[6:7], -1
	s_and_b64 vcc, exec, s[8:9]
	s_cbranch_vccnz .LBB0_168
	v_readlane_b32 s1, v254, 8
	s_ashr_i32 s6, s51, 6
	s_lshl_b32 s8, s1, 3
	s_ashr_i32 s7, s6, 31
	s_lshl_b64 s[14:15], s[6:7], 16
	s_or_b32 s6, s8, 6
	s_ashr_i32 s7, s6, 31
	s_or_b32 s58, s8, 1
	s_or_b32 s84, s8, 2
	s_or_b32 s86, s8, 3
	s_mov_b64 s[72:73], s[88:89]
	s_or_b32 s88, s8, 4
	s_or_b32 s92, s8, 5
	s_lshl_b64 s[60:61], s[6:7], 11
	s_or_b32 s82, s8, 7
	s_ashr_i32 s9, s8, 31
	s_ashr_i32 s59, s58, 31
	s_ashr_i32 s85, s84, 31
	s_ashr_i32 s87, s86, 31
	s_ashr_i32 s89, s88, 31
	s_ashr_i32 s93, s92, 31
	v_writelane_b32 v254, s60, 18
	s_ashr_i32 s83, s82, 31
	s_lshl_b64 s[52:53], s[8:9], 11
	s_lshl_b64 s[80:81], s[58:59], 11
	s_lshl_b64 s[78:79], s[84:85], 11
	s_lshl_b64 vcc, s[86:87], 11
	s_lshl_b64 s[74:75], s[88:89], 11
	s_lshl_b64 s[76:77], s[92:93], 11
	v_writelane_b32 v254, s61, 19
	s_lshl_b64 s[60:61], s[82:83], 11
	s_add_u32 s14, s66, s14
	s_addc_u32 s15, s67, s15
	s_lshl_b64 s[8:9], s[8:9], 13
	s_add_u32 s64, s68, s8
	v_writelane_b32 v254, s60, 20
	s_addc_u32 s65, s69, s9
	v_lshlrev_b32_e32 v2, 4, v0
	v_writelane_b32 v254, s61, 21
	s_add_u32 s60, s64, 0x1000
	s_addc_u32 s61, s65, 0
	s_lshl_b64 s[8:9], s[58:59], 13
	s_add_u32 s62, s68, s8
	v_mov_b32_e32 v3, v197
	s_addc_u32 s63, s69, s9
	v_lshl_add_u64 v[44:45], s[14:15], 0, v[2:3]
	s_add_u32 s14, s62, 0x1000
	s_addc_u32 s15, s63, 0
	s_lshl_b64 s[8:9], s[84:85], 13
	s_add_u32 s58, s68, s8
	s_addc_u32 s59, s69, s9
	s_add_u32 s84, s58, 0x1000
	s_addc_u32 s85, s59, 0
	s_lshl_b64 s[8:9], s[86:87], 13
	s_add_u32 s86, s68, s8
	s_addc_u32 s87, s69, s9
	s_add_u32 s8, s86, 0x1000
	s_addc_u32 s9, s87, 0
	s_add_u32 s52, s3, s52
	s_addc_u32 s53, s33, s53
	s_mov_b32 s34, s0
	s_mov_b64 s[0:1], s[96:97]
	s_add_u32 s96, s3, s80
	s_addc_u32 s97, s33, s81
	s_lshl_b64 s[80:81], s[88:89], 13
	s_mov_b64 s[70:71], s[94:95]
	s_add_u32 s94, s68, s80
	s_addc_u32 s95, s69, s81
	s_add_u32 s90, s94, 0x1000
	s_addc_u32 s91, s95, 0
	s_lshl_b64 s[80:81], s[92:93], 13
	s_add_u32 s92, s68, s80
	s_addc_u32 s93, s69, s81
	s_add_u32 s88, s92, 0x1000
	s_addc_u32 s89, s93, 0
	s_add_u32 s80, s3, s78
	s_addc_u32 s81, s33, s79
	s_add_u32 s78, s3, vcc_lo
	s_addc_u32 s79, s33, vcc_hi
	s_mov_b64 vcc, 0x2000
	v_lshl_add_u64 v[18:19], v[44:45], 0, vcc
	s_mov_b64 vcc, 0x40000
	v_lshl_add_u64 v[22:23], v[44:45], 0, vcc
	s_mov_b64 vcc, 0x42000
	v_lshl_add_u64 v[28:29], v[44:45], 0, vcc
	s_mov_b64 vcc, 0x80000
	v_lshl_add_u64 v[32:33], v[44:45], 0, vcc
	s_mov_b64 vcc, 0x82000
	v_lshl_add_u64 v[36:37], v[44:45], 0, vcc
	s_mov_b64 vcc, 0xc0000
	v_lshl_add_u64 v[4:5], s[38:39], 0, v[2:3]
	v_lshl_add_u64 v[6:7], s[36:37], 0, v[2:3]
	v_lshl_add_u64 v[10:11], s[10:11], 0, v[2:3]
	v_lshl_add_u64 v[40:41], v[44:45], 0, vcc
	s_mov_b64 vcc, 0xc2000
	global_load_dwordx4 v[2:5], v[4:5], off
	global_load_dwordx4 v[6:9], v[6:7], off
	global_load_dwordx4 v[10:13], v[10:11], off
	global_load_dwordx4 v[14:17], v[44:45], off
	v_lshl_add_u64 v[44:45], v[44:45], 0, vcc
	global_load_dwordx4 v[18:21], v[18:19], off
	global_load_dwordx4 v[22:25], v[22:23], off
	global_load_dwordx4 v[28:31], v[28:29], off
	global_load_dwordx4 v[32:35], v[32:33], off
	global_load_dwordx4 v[36:39], v[36:37], off
	global_load_dwordx4 v[40:43], v[40:41], off
	global_load_dwordx4 v[44:47], v[44:45], off
	v_lshlrev_b32_e32 v216, 4, v194
	s_waitcnt vmcnt(0)
	s_mov_b32 s49, 0xc3e00000
	v_pk_add_f32 v[12:13], v[12:13], v[20:21]
	v_pk_add_f32 v[10:11], v[10:11], v[18:19]
	v_pk_add_f32 v[12:13], v[30:31], v[12:13]
	v_pk_add_f32 v[10:11], v[28:29], v[10:11]
	v_pk_add_f32 v[6:7], v[6:7], v[14:15]
	v_pk_add_f32 v[12:13], v[38:39], v[12:13]
	v_pk_add_f32 v[10:11], v[36:37], v[10:11]
	v_pk_add_f32 v[8:9], v[8:9], v[16:17]
	v_pk_add_f32 v[6:7], v[22:23], v[6:7]
	v_pk_add_f32 v[12:13], v[46:47], v[12:13]
	v_pk_add_f32 v[10:11], v[44:45], v[10:11]
	v_pk_add_f32 v[8:9], v[24:25], v[8:9]
	v_pk_add_f32 v[6:7], v[32:33], v[6:7]
	v_pk_add_f32 v[12:13], v[12:13], 1.0 op_sel_hi:[1,0]
	v_pk_add_f32 v[10:11], v[10:11], 1.0 op_sel_hi:[1,0]
	v_pk_add_f32 v[8:9], v[34:35], v[8:9]
	v_pk_add_f32 v[6:7], v[40:41], v[6:7]
	v_pk_mul_f32 v[4:5], v[4:5], v[12:13]
	v_pk_mul_f32 v[2:3], v[2:3], v[10:11]
	v_add_u32_e32 v10, v1, v26
	v_pk_add_f32 v[8:9], v[42:43], v[8:9]
	ds_write_b128 v10, v[2:5]
	ds_write_b128 v10, v[6:9] offset:8192
	v_lshl_add_u32 v6, v196, 2, 0
	s_waitcnt lgkmcnt(0)
	s_barrier
; #define LAS __attribute__((address_space(3)))
; #define N1_TIE(V_, W_, cnt_) do { asm volatile("s_waitcnt vmcnt(" #cnt_ ")" : "+v"(V_[0]), "+v"(V_[1]), "+v"(V_[2]), "+v"(V_[3]), "+v"(V_[4]), "+v"(V_[5]), "+v"(V_[6]), "+v"(V_[7])); \
;                 asm volatile("" : "+v"(W_[0]), "+v"(W_[1]), "+v"(W_[2]), "+v"(W_[3]), "+v"(W_[4]), "+v"(W_[5]), "+v"(W_[6]), "+v"(W_[7])); } while (0)
; __global__ void __launch_bounds__(NWAVES * 64, 2) fwd_kernel(Args args) {
;     ...
;                     __syncthreads();
; #pragma unroll
;                     for (int j = 0; j < 8; ++j) { const int kk = 4 * lane + 256 * j; Av[j] = *(const LAS f32x4*)(NA + kk); Bv[j] = *(const LAS f32x4*)(NB + kk); }
;                     __syncthreads(); cb = bW; }
;                 N1_LOAD(va, wa, r0, r0 + 1); N1_LOAD(vb, wb, r0 + 2, r0 + 3);
;                 N1_TIE(va, wa, 16); N1_BODY(va, wa, r0, r0 + 1);
	ds_read_b128 v[58:61], v6
	ds_read_b128 v[50:53], v6 offset:1024
	ds_read_b128 v[62:65], v6 offset:8192
	ds_read_b128 v[54:57], v6 offset:9216
	ds_read_b128 v[42:45], v6 offset:2048
	ds_read_b128 v[34:37], v6 offset:3072
	ds_read_b128 v[46:49], v6 offset:10240
	ds_read_b128 v[38:41], v6 offset:11264
	ds_read_b128 v[26:29], v6 offset:4096
	ds_read_b128 v[18:21], v6 offset:5120
	ds_read_b128 v[30:33], v6 offset:12288
	ds_read_b128 v[22:25], v6 offset:13312
	ds_read_b128 v[10:13], v6 offset:6144
	ds_read_b128 v[2:5], v6 offset:7168
	ds_read_b128 v[14:17], v6 offset:14336
	ds_read_b128 v[6:9], v6 offset:15360
	s_waitcnt lgkmcnt(0)
	s_barrier
	global_load_dwordx4 v[190:193], v216, s[64:65] offset:0
	global_load_dwordx4 v[178:181], v216, s[64:65] offset:1024
	global_load_dwordx4 v[162:165], v216, s[64:65] offset:2048
	global_load_dwordx4 v[150:153], v216, s[64:65] offset:3072
	global_load_dwordx4 v[138:141], v216, s[60:61] offset:0
	global_load_dwordx4 v[122:125], v216, s[60:61] offset:1024
	global_load_dwordx4 v[106:109], v216, s[60:61] offset:2048
	global_load_dwordx4 v[90:93], v216, s[60:61] offset:3072
	global_load_dwordx4 v[186:189], v216, s[62:63] offset:0
	global_load_dwordx4 v[182:185], v216, s[62:63] offset:1024
	global_load_dwordx4 v[174:177], v216, s[62:63] offset:2048
	global_load_dwordx4 v[158:161], v216, s[62:63] offset:3072
	global_load_dwordx4 v[142:145], v216, s[14:15] offset:0
	global_load_dwordx4 v[126:129], v216, s[14:15] offset:1024
	global_load_dwordx4 v[110:113], v216, s[14:15] offset:2048
	global_load_dwordx4 v[94:97], v216, s[14:15] offset:3072
	global_load_dwordx4 v[166:169], v216, s[58:59] offset:0
	global_load_dwordx4 v[146:149], v216, s[58:59] offset:1024
	global_load_dwordx4 v[130:133], v216, s[58:59] offset:2048
	global_load_dwordx4 v[114:117], v216, s[58:59] offset:3072
	global_load_dwordx4 v[98:101], v216, s[84:85] offset:0
	global_load_dwordx4 v[82:85], v216, s[84:85] offset:1024
	global_load_dwordx4 v[74:77], v216, s[84:85] offset:2048
	global_load_dwordx4 v[66:69], v216, s[84:85] offset:3072
	global_load_dwordx4 v[170:173], v216, s[86:87] offset:0
	global_load_dwordx4 v[154:157], v216, s[86:87] offset:1024
	global_load_dwordx4 v[134:137], v216, s[86:87] offset:2048
	global_load_dwordx4 v[118:121], v216, s[86:87] offset:3072
	global_load_dwordx4 v[102:105], v216, s[8:9] offset:0
	global_load_dwordx4 v[86:89], v216, s[8:9] offset:1024
	global_load_dwordx4 v[78:81], v216, s[8:9] offset:2048
	global_load_dwordx4 v[70:73], v216, s[8:9] offset:3072
	s_nop 0
	s_waitcnt vmcnt(16)
	s_mov_b32 s58, 0xf800000
	v_mul_f32_e32 v198, v191, v191
	v_mul_f32_e32 v200, v179, v179
	v_fmac_f32_e32 v198, v190, v190
	v_fmac_f32_e32 v200, v178, v178
	v_fmac_f32_e32 v198, v192, v192
	v_fmac_f32_e32 v200, v180, v180
	v_fmac_f32_e32 v198, v193, v193
	v_fmac_f32_e32 v200, v181, v181
	v_mul_f32_e32 v199, v187, v187
	v_add_f32_e32 v198, v198, v200
	v_mul_f32_e32 v200, v183, v183
	v_fmac_f32_e32 v199, v186, v186
	v_fmac_f32_e32 v200, v182, v182
	v_fmac_f32_e32 v199, v188, v188
	v_fmac_f32_e32 v200, v184, v184
	v_fmac_f32_e32 v199, v189, v189
	v_fmac_f32_e32 v200, v185, v185
	v_add_f32_e32 v199, v199, v200
	v_mul_f32_e32 v200, v163, v163
	v_fmac_f32_e32 v200, v162, v162
	v_fmac_f32_e32 v200, v164, v164
	v_fmac_f32_e32 v200, v165, v165
	v_add_f32_e32 v198, v198, v200
	v_mul_f32_e32 v200, v175, v175
	v_fmac_f32_e32 v200, v174, v174
	v_fmac_f32_e32 v200, v176, v176
	v_fmac_f32_e32 v200, v177, v177
	v_add_f32_e32 v199, v199, v200
	v_mul_f32_e32 v200, v151, v151
	v_fmac_f32_e32 v200, v150, v150
	v_fmac_f32_e32 v200, v152, v152
	v_fmac_f32_e32 v200, v153, v153
	v_add_f32_e32 v198, v198, v200
	v_mul_f32_e32 v200, v159, v159
	v_fmac_f32_e32 v200, v158, v158
	v_fmac_f32_e32 v200, v160, v160
	v_fmac_f32_e32 v200, v161, v161
	v_add_f32_e32 v200, v199, v200
	v_mul_f32_e32 v199, v139, v139
	v_fmac_f32_e32 v199, v138, v138
	v_fmac_f32_e32 v199, v140, v140
	v_fmac_f32_e32 v199, v141, v141
	v_add_f32_e32 v198, v198, v199
	v_mul_f32_e32 v199, v123, v123
	v_fmac_f32_e32 v199, v122, v122
	v_fmac_f32_e32 v199, v124, v124
	v_fmac_f32_e32 v199, v125, v125
	v_mov_b32_e32 v208, v107
	v_mov_b32_e32 v209, v91
	v_add_f32_e32 v210, v198, v199
	v_mov_b32_e32 v198, v106
	v_mov_b32_e32 v199, v90
	v_pk_mul_f32 v[208:209], v[208:209], v[208:209]
	v_mul_f32_e32 v211, v127, v127
	v_pk_fma_f32 v[198:199], v[198:199], v[198:199], v[208:209]
	v_mov_b32_e32 v208, v108
	v_mov_b32_e32 v209, v92
	v_pk_fma_f32 v[198:199], v[208:209], v[208:209], v[198:199]
	v_mov_b32_e32 v208, v109
	v_mov_b32_e32 v209, v93
	v_pk_fma_f32 v[198:199], v[208:209], v[208:209], v[198:199]
	v_fmac_f32_e32 v211, v126, v126
	v_add_f32_e32 v198, v210, v198
	v_add_f32_e32 v198, v198, v199
	v_mbcnt_lo_u32_b32 v199, -1, 0
	v_mbcnt_hi_u32_b32 v217, -1, v199
	v_and_b32_e32 v199, 64, v217
	v_add_u32_e32 v219, 64, v199
	v_xor_b32_e32 v199, 1, v217
	v_cmp_lt_i32_e32 vcc, v199, v219
	v_mul_f32_e32 v210, v143, v143
	v_fmac_f32_e32 v210, v142, v142
	v_cndmask_b32_e32 v199, v217, v199, vcc
	v_lshlrev_b32_e32 v208, 2, v199
	ds_bpermute_b32 v199, v208, v198
	v_fmac_f32_e32 v210, v144, v144
	v_fmac_f32_e32 v210, v145, v145
	v_add_f32_e32 v200, v200, v210
	v_fmac_f32_e32 v211, v128, v128
	s_waitcnt lgkmcnt(0)
	v_add_f32_e32 v198, v198, v199
	v_xor_b32_e32 v199, 2, v217
	v_cmp_lt_i32_e32 vcc, v199, v219
	v_fmac_f32_e32 v211, v129, v129
	v_add_f32_e32 v200, v200, v211
	v_cndmask_b32_e32 v199, v217, v199, vcc
	v_lshlrev_b32_e32 v209, 2, v199
	ds_bpermute_b32 v199, v209, v198
	v_xor_b32_e32 v211, 8, v217
	v_mov_b32_e32 v218, v113
	s_lshl_b64 s[8:9], s[6:7], 13
	s_add_u32 s84, s68, s8
	s_waitcnt lgkmcnt(0)
	v_add_f32_e32 v212, v198, v199
	v_xor_b32_e32 v198, 4, v217
	v_cmp_lt_i32_e32 vcc, v198, v219
	v_mov_b32_e32 v199, v94
	s_addc_u32 s85, s69, s9
	v_cndmask_b32_e32 v198, v217, v198, vcc
	v_lshlrev_b32_e32 v210, 2, v198
	ds_bpermute_b32 v213, v210, v212
	v_cmp_lt_i32_e32 vcc, v211, v219
	v_mov_b32_e32 v198, v110
	s_add_u32 s86, s84, 0x1000
	v_cndmask_b32_e32 v211, v217, v211, vcc
	s_waitcnt lgkmcnt(0)
	v_add_f32_e32 v214, v212, v213
	v_lshlrev_b32_e32 v211, 2, v211
	ds_bpermute_b32 v215, v211, v214
	v_mov_b32_e32 v212, v111
	v_mov_b32_e32 v213, v95
	v_pk_mul_f32 v[212:213], v[212:213], v[212:213]
	s_addc_u32 s87, s85, 0
	v_pk_fma_f32 v[198:199], v[198:199], v[198:199], v[212:213]
	v_xor_b32_e32 v213, 16, v217
	v_cmp_lt_i32_e32 vcc, v213, v219
	s_waitcnt lgkmcnt(0)
	v_add_f32_e32 v212, v214, v215
	v_mov_b32_e32 v214, v112
	v_cndmask_b32_e32 v213, v217, v213, vcc
	v_lshlrev_b32_e32 v213, 2, v213
	ds_bpermute_b32 v220, v213, v212
	v_mov_b32_e32 v215, v96
	v_pk_fma_f32 v[198:199], v[214:215], v[214:215], v[198:199]
	v_xor_b32_e32 v214, 32, v217
	v_cmp_lt_i32_e32 vcc, v214, v219
	s_waitcnt lgkmcnt(0)
	v_add_f32_e32 v212, v212, v220
	v_mov_b32_e32 v219, v97
	v_cndmask_b32_e32 v214, v217, v214, vcc
	v_lshlrev_b32_e32 v214, 2, v214
	ds_bpermute_b32 v215, v214, v212
	v_pk_fma_f32 v[198:199], v[218:219], v[218:219], v[198:199]
	s_nop 0
	v_add_f32_e32 v198, v200, v198
	v_add_f32_e32 v198, v198, v199
	s_waitcnt lgkmcnt(0)
	v_add_f32_e32 v199, v212, v215
	ds_bpermute_b32 v215, v208, v198
	v_mov_b32_e32 v212, 0x358637bd
	v_fmamk_f32 v199, v199, 0x3a000000, v212
	v_mul_f32_e32 v200, 0x4f800000, v199
	v_cmp_gt_f32_e32 vcc, s58, v199
	s_waitcnt lgkmcnt(0)
	v_add_f32_e32 v198, v198, v215
	ds_bpermute_b32 v215, v209, v198
	v_cndmask_b32_e32 v199, v199, v200, vcc
	v_sqrt_f32_e32 v200, v199
	s_waitcnt lgkmcnt(0)
	v_add_f32_e32 v198, v198, v215
	ds_bpermute_b32 v219, v210, v198
	v_add_u32_e32 v217, -1, v200
	v_fma_f32 v218, -v217, v200, v199
	v_cmp_ge_f32_e64 s[6:7], 0, v218
	v_add_u32_e32 v218, 1, v200
	s_waitcnt lgkmcnt(0)
	v_add_f32_e32 v198, v198, v219
	v_cndmask_b32_e64 v217, v200, v217, s[6:7]
	v_fma_f32 v200, -v218, v200, v199
	v_cmp_lt_f32_e64 s[6:7], 0, v200
	s_nop 1
	v_cndmask_b32_e64 v200, v217, v218, s[6:7]
	ds_bpermute_b32 v217, v211, v198
	v_mul_f32_e32 v215, 0x37800000, v200
	v_cndmask_b32_e32 v200, v200, v215, vcc
	v_mov_b32_e32 v215, 0x260
	v_cmp_class_f32_e32 vcc, v199, v215
	s_waitcnt lgkmcnt(0)
	v_add_f32_e32 v198, v198, v217
	ds_bpermute_b32 v217, v213, v198
	v_cndmask_b32_e32 v199, v200, v199, vcc
	v_div_scale_f32 v200, s[6:7], v199, v199, 1.0
	v_rcp_f32_e32 v218, v200
	s_waitcnt lgkmcnt(0)
	v_add_f32_e32 v198, v198, v217
	ds_bpermute_b32 v217, v214, v198
	v_fma_f32 v219, -v200, v218, 1.0
	v_fmac_f32_e32 v218, v219, v218
	v_div_scale_f32 v219, vcc, 1.0, v199, 1.0
	s_waitcnt lgkmcnt(0)
	v_add_f32_e32 v198, v198, v217
	v_fmamk_f32 v198, v198, 0x3a000000, v212
	v_mul_f32_e32 v217, 0x4f800000, v198
	v_cmp_gt_f32_e64 s[6:7], s58, v198
	v_mul_f32_e32 v220, v219, v218
	v_fma_f32 v221, -v200, v220, v219
	v_cndmask_b32_e64 v198, v198, v217, s[6:7]
	v_sqrt_f32_e32 v217, v198
	v_fmac_f32_e32 v220, v221, v218
	v_fma_f32 v200, -v200, v220, v219
	v_add_u32_e32 v219, -1, v217
	v_fma_f32 v221, -v219, v217, v198
	v_cmp_ge_f32_e64 s[8:9], 0, v221
	v_add_u32_e32 v221, 1, v217
	s_nop 0
	v_cndmask_b32_e64 v219, v217, v219, s[8:9]
	v_fma_f32 v217, -v221, v217, v198
	v_cmp_lt_f32_e64 s[8:9], 0, v217
	s_nop 1
	v_cndmask_b32_e64 v217, v219, v221, s[8:9]
	v_mul_f32_e32 v219, 0x37800000, v217
	v_cndmask_b32_e64 v217, v217, v219, s[6:7]
	v_cmp_class_f32_e64 s[6:7], v198, v215
	s_lshl_b64 s[8:9], s[82:83], 13
	s_nop 0
	v_cndmask_b32_e64 v217, v217, v198, s[6:7]
	v_div_scale_f32 v219, s[6:7], v217, v217, 1.0
	v_rcp_f32_e32 v221, v219
	v_div_fmas_f32 v198, v200, v218, v220
	v_div_fixup_f32 v198, v198, v199, 1.0
	v_fma_f32 v199, -v219, v221, 1.0
	v_fmac_f32_e32 v221, v199, v221
	v_div_scale_f32 v199, vcc, 1.0, v217, 1.0
	v_mul_f32_e32 v200, v199, v221
	v_fma_f32 v218, -v219, v200, v199
	v_fmac_f32_e32 v200, v218, v221
	v_fma_f32 v199, -v219, v200, v199
	v_div_fmas_f32 v199, v199, v221, v200
	v_pk_mul_f32 v[190:191], v[198:199], v[190:191] op_sel_hi:[0,1]
	v_div_fixup_f32 v200, v199, v217, 1.0
	v_pk_mul_f32 v[192:193], v[198:199], v[192:193] op_sel_hi:[0,1]
	v_pk_fma_f32 v[190:191], v[190:191], v[58:59], v[62:63]
	v_mov_b32_e32 v199, 0x43e00000
	v_pk_mul_f32 v[186:187], v[200:201], v[186:187] op_sel_hi:[0,1]
	v_med3_f32 v190, v190, s49, v199
	v_med3_f32 v191, v191, s49, v199
	v_pk_fma_f32 v[192:193], v[192:193], v[60:61], v[64:65]
	v_cvt_pk_fp8_f32 v217, v190, v191
	v_pk_fma_f32 v[190:191], v[58:59], v[186:187], v[62:63]
	v_med3_f32 v186, v192, s49, v199
	v_med3_f32 v190, v190, s49, v199
	v_med3_f32 v191, v191, s49, v199
	v_cvt_pk_fp8_f32 v192, v190, v191
	v_pk_mul_f32 v[188:189], v[200:201], v[188:189] op_sel_hi:[0,1]
	v_pk_fma_f32 v[188:189], v[60:61], v[188:189], v[64:65]
	v_pk_mul_f32 v[178:179], v[198:199], v[178:179] op_sel_hi:[0,1]
	v_med3_f32 v188, v188, s49, v199
	v_med3_f32 v189, v189, s49, v199
	v_pk_fma_f32 v[178:179], v[178:179], v[50:51], v[54:55]
	v_cvt_pk_fp8_f32 v192, v188, v189 op_sel:[0,0,1]
	v_med3_f32 v178, v178, s49, v199
	v_med3_f32 v179, v179, s49, v199
	v_cvt_pk_fp8_f32 v188, v178, v179
	v_pk_mul_f32 v[180:181], v[198:199], v[180:181] op_sel_hi:[0,1]
	v_pk_fma_f32 v[180:181], v[180:181], v[52:53], v[56:57]
	v_pk_mul_f32 v[162:163], v[198:199], v[162:163] op_sel_hi:[0,1]
	v_med3_f32 v180, v180, s49, v199
	v_med3_f32 v181, v181, s49, v199
	v_pk_fma_f32 v[162:163], v[162:163], v[42:43], v[46:47]
	v_pk_mul_f32 v[174:175], v[200:201], v[174:175] op_sel_hi:[0,1]
	v_cvt_pk_fp8_f32 v188, v180, v181 op_sel:[0,0,1]
	v_pk_fma_f32 v[174:175], v[42:43], v[174:175], v[46:47]
	v_med3_f32 v162, v162, s49, v199
	v_med3_f32 v163, v163, s49, v199
	v_cvt_pk_fp8_f32 v180, v162, v163
	v_med3_f32 v162, v174, s49, v199
	v_med3_f32 v163, v175, s49, v199
	v_cvt_pk_fp8_f32 v174, v162, v163
	v_pk_mul_f32 v[176:177], v[200:201], v[176:177] op_sel_hi:[0,1]
	v_pk_fma_f32 v[176:177], v[44:45], v[176:177], v[48:49]
	v_pk_mul_f32 v[150:151], v[198:199], v[150:151] op_sel_hi:[0,1]
	v_med3_f32 v162, v176, s49, v199
	v_med3_f32 v163, v177, s49, v199
	v_pk_fma_f32 v[150:151], v[150:151], v[34:35], v[38:39]
	v_pk_mul_f32 v[158:159], v[200:201], v[158:159] op_sel_hi:[0,1]
	v_cvt_pk_fp8_f32 v174, v162, v163 op_sel:[0,0,1]
	v_pk_fma_f32 v[158:159], v[34:35], v[158:159], v[38:39]
	v_med3_f32 v150, v150, s49, v199
	v_med3_f32 v151, v151, s49, v199
	v_cvt_pk_fp8_f32 v162, v150, v151
	v_med3_f32 v150, v158, s49, v199
	v_med3_f32 v151, v159, s49, v199
	v_cvt_pk_fp8_f32 v158, v150, v151
	v_pk_mul_f32 v[160:161], v[200:201], v[160:161] op_sel_hi:[0,1]
	v_pk_fma_f32 v[160:161], v[36:37], v[160:161], v[40:41]
	v_pk_mul_f32 v[138:139], v[198:199], v[138:139] op_sel_hi:[0,1]
	v_med3_f32 v150, v160, s49, v199
	v_med3_f32 v151, v161, s49, v199
	v_pk_fma_f32 v[138:139], v[138:139], v[26:27], v[30:31]
	v_pk_mul_f32 v[142:143], v[200:201], v[142:143] op_sel_hi:[0,1]
	v_cvt_pk_fp8_f32 v158, v150, v151 op_sel:[0,0,1]
	v_pk_fma_f32 v[142:143], v[26:27], v[142:143], v[30:31]
	v_med3_f32 v138, v138, s49, v199
	v_med3_f32 v139, v139, s49, v199
	v_cvt_pk_fp8_f32 v150, v138, v139
	v_med3_f32 v138, v142, s49, v199
	v_med3_f32 v139, v143, s49, v199
	v_cvt_pk_fp8_f32 v142, v138, v139
	v_pk_mul_f32 v[144:145], v[200:201], v[144:145] op_sel_hi:[0,1]
	v_pk_fma_f32 v[144:145], v[28:29], v[144:145], v[32:33]
	v_pk_mul_f32 v[122:123], v[198:199], v[122:123] op_sel_hi:[0,1]
	v_med3_f32 v138, v144, s49, v199
	v_med3_f32 v139, v145, s49, v199
	v_pk_fma_f32 v[122:123], v[122:123], v[18:19], v[22:23]
	v_pk_mul_f32 v[126:127], v[200:201], v[126:127] op_sel_hi:[0,1]
	v_cvt_pk_fp8_f32 v142, v138, v139 op_sel:[0,0,1]
	v_pk_fma_f32 v[126:127], v[18:19], v[126:127], v[22:23]
	v_med3_f32 v122, v122, s49, v199
	v_med3_f32 v123, v123, s49, v199
	v_cvt_pk_fp8_f32 v138, v122, v123
	v_med3_f32 v122, v126, s49, v199
	v_med3_f32 v123, v127, s49, v199
	v_cvt_pk_fp8_f32 v126, v122, v123
	v_pk_mul_f32 v[128:129], v[200:201], v[128:129] op_sel_hi:[0,1]
	v_pk_fma_f32 v[128:129], v[20:21], v[128:129], v[24:25]
	v_pk_mul_f32 v[106:107], v[198:199], v[106:107] op_sel_hi:[0,1]
	v_med3_f32 v122, v128, s49, v199
	v_med3_f32 v123, v129, s49, v199
	v_pk_fma_f32 v[106:107], v[106:107], v[10:11], v[14:15]
	v_pk_mul_f32 v[110:111], v[200:201], v[110:111] op_sel_hi:[0,1]
	v_cvt_pk_fp8_f32 v126, v122, v123 op_sel:[0,0,1]
	v_pk_fma_f32 v[110:111], v[10:11], v[110:111], v[14:15]
	v_med3_f32 v106, v106, s49, v199
	v_med3_f32 v107, v107, s49, v199
	v_cvt_pk_fp8_f32 v122, v106, v107
	v_med3_f32 v106, v110, s49, v199
	v_med3_f32 v107, v111, s49, v199
	v_cvt_pk_fp8_f32 v110, v106, v107
	v_pk_mul_f32 v[112:113], v[200:201], v[112:113] op_sel_hi:[0,1]
	v_pk_mul_f32 v[182:183], v[200:201], v[182:183] op_sel_hi:[0,1]
	v_pk_fma_f32 v[112:113], v[12:13], v[112:113], v[16:17]
	v_pk_mul_f32 v[90:91], v[198:199], v[90:91] op_sel_hi:[0,1]
	v_pk_fma_f32 v[182:183], v[50:51], v[182:183], v[54:55]
	v_med3_f32 v106, v112, s49, v199
	v_med3_f32 v107, v113, s49, v199
	v_pk_fma_f32 v[90:91], v[90:91], v[2:3], v[6:7]
	v_pk_mul_f32 v[94:95], v[200:201], v[94:95] op_sel_hi:[0,1]
	v_med3_f32 v178, v182, s49, v199
	v_med3_f32 v179, v183, s49, v199
	v_pk_mul_f32 v[164:165], v[198:199], v[164:165] op_sel_hi:[0,1]
	v_pk_mul_f32 v[140:141], v[198:199], v[140:141] op_sel_hi:[0,1]
	v_pk_mul_f32 v[108:109], v[198:199], v[108:109] op_sel_hi:[0,1]
	v_cvt_pk_fp8_f32 v110, v106, v107 op_sel:[0,0,1]
	v_pk_fma_f32 v[94:95], v[2:3], v[94:95], v[6:7]
	v_med3_f32 v90, v90, s49, v199
	v_med3_f32 v91, v91, s49, v199
	v_cvt_pk_fp8_f32 v182, v178, v179
	v_pk_fma_f32 v[164:165], v[164:165], v[44:45], v[48:49]
	v_pk_fma_f32 v[140:141], v[140:141], v[28:29], v[32:33]
	v_pk_fma_f32 v[108:109], v[108:109], v[12:13], v[16:17]
	v_cvt_pk_fp8_f32 v106, v90, v91
	v_med3_f32 v90, v94, s49, v199
	v_med3_f32 v91, v95, s49, v199
	v_med3_f32 v187, v193, s49, v199
	v_pk_mul_f32 v[184:185], v[200:201], v[184:185] op_sel_hi:[0,1]
	v_med3_f32 v164, v164, s49, v199
	v_med3_f32 v165, v165, s49, v199
	v_pk_mul_f32 v[152:153], v[198:199], v[152:153] op_sel_hi:[0,1]
	v_med3_f32 v140, v140, s49, v199
	v_med3_f32 v141, v141, s49, v199
	v_pk_mul_f32 v[124:125], v[198:199], v[124:125] op_sel_hi:[0,1]
	v_med3_f32 v108, v108, s49, v199
	v_med3_f32 v109, v109, s49, v199
	v_pk_mul_f32 v[92:93], v[198:199], v[92:93] op_sel_hi:[0,1]
	v_cvt_pk_fp8_f32 v94, v90, v91
	v_cvt_pk_fp8_f32 v217, v186, v187 op_sel:[0,0,1]
	v_pk_fma_f32 v[184:185], v[52:53], v[184:185], v[56:57]
	v_cvt_pk_fp8_f32 v180, v164, v165 op_sel:[0,0,1]
	v_pk_fma_f32 v[152:153], v[152:153], v[36:37], v[40:41]
	v_cvt_pk_fp8_f32 v150, v140, v141 op_sel:[0,0,1]
	v_pk_fma_f32 v[124:125], v[124:125], v[20:21], v[24:25]
	v_cvt_pk_fp8_f32 v122, v108, v109 op_sel:[0,0,1]
	v_pk_fma_f32 v[92:93], v[92:93], v[4:5], v[8:9]
	v_pk_mul_f32 v[96:97], v[200:201], v[96:97] op_sel_hi:[0,1]
	v_med3_f32 v178, v184, s49, v199
	v_med3_f32 v179, v185, s49, v199
	v_med3_f32 v152, v152, s49, v199
	v_med3_f32 v153, v153, s49, v199
	v_med3_f32 v124, v124, s49, v199
	v_med3_f32 v125, v125, s49, v199
	v_pk_fma_f32 v[96:97], v[4:5], v[96:97], v[8:9]
	v_med3_f32 v92, v92, s49, v199
	v_med3_f32 v93, v93, s49, v199
	v_cvt_pk_fp8_f32 v182, v178, v179 op_sel:[0,0,1]
; #define N1_TIE(V_, W_, cnt_) do { asm volatile("s_waitcnt vmcnt(" #cnt_ ")" : "+v"(V_[0]), "+v"(V_[1]), "+v"(V_[2]), "+v"(V_[3]), "+v"(V_[4]), "+v"(V_[5]), "+v"(V_[6]), "+v"(V_[7])); \
;                 asm volatile("" : "+v"(W_[0]), "+v"(W_[1]), "+v"(W_[2]), "+v"(W_[3]), "+v"(W_[4]), "+v"(W_[5]), "+v"(W_[6]), "+v"(W_[7])); } while (0)
; __global__ void __launch_bounds__(NWAVES * 64, 2) fwd_kernel(Args args) {
;     ...
;                 N1_LOAD(va, wa, r0 + 4, r0 + 5);
;                 N1_TIE(vb, wb, 16); N1_BODY(vb, wb, r0 + 2, r0 + 3);
;                 N1_LOAD(vb, wb, r0 + 6, r0 + 7);
;                 N1_TIE(va, wa, 16); N1_BODY(va, wa, r0 + 4, r0 + 5);
	v_cvt_pk_fp8_f32 v162, v152, v153 op_sel:[0,0,1]
	v_cvt_pk_fp8_f32 v138, v124, v125 op_sel:[0,0,1]
	v_cvt_pk_fp8_f32 v106, v92, v93 op_sel:[0,0,1]
	v_med3_f32 v90, v96, s49, v199
	v_med3_f32 v91, v97, s49, v199
	v_lshl_add_u64 v[186:187], s[52:53], 0, v[196:197]
	v_lshl_add_u64 v[178:179], s[96:97], 0, v[196:197]
	v_cvt_pk_fp8_f32 v94, v90, v91 op_sel:[0,0,1]
	global_store_dword v[186:187], v217, off
	global_store_dword v[178:179], v192, off
	global_store_dword v[186:187], v188, off offset:256
	global_store_dword v[178:179], v182, off offset:256
	global_store_dword v[186:187], v180, off offset:512
	global_store_dword v[178:179], v174, off offset:512
	global_store_dword v[186:187], v162, off offset:768
	global_store_dword v[178:179], v158, off offset:768
	global_store_dword v[186:187], v150, off offset:1024
	global_store_dword v[178:179], v142, off offset:1024
	global_store_dword v[186:187], v138, off offset:1280
	global_store_dword v[178:179], v126, off offset:1280
	global_store_dword v[186:187], v122, off offset:1536
	global_store_dword v[178:179], v110, off offset:1536
	global_store_dword v[186:187], v106, off offset:1792
	global_store_dword v[178:179], v94, off offset:1792
	global_load_dwordx4 v[186:189], v216, s[94:95] offset:0
	global_load_dwordx4 v[178:181], v216, s[94:95] offset:1024
	global_load_dwordx4 v[162:165], v216, s[94:95] offset:2048
	global_load_dwordx4 v[150:153], v216, s[94:95] offset:3072
	global_load_dwordx4 v[138:141], v216, s[90:91] offset:0
	global_load_dwordx4 v[122:125], v216, s[90:91] offset:1024
	global_load_dwordx4 v[106:109], v216, s[90:91] offset:2048
	global_load_dwordx4 v[90:93], v216, s[90:91] offset:3072
	global_load_dwordx4 v[190:193], v216, s[92:93] offset:0
	global_load_dwordx4 v[182:185], v216, s[92:93] offset:1024
	global_load_dwordx4 v[174:177], v216, s[92:93] offset:2048
	global_load_dwordx4 v[158:161], v216, s[92:93] offset:3072
	global_load_dwordx4 v[142:145], v216, s[88:89] offset:0
	global_load_dwordx4 v[126:129], v216, s[88:89] offset:1024
	global_load_dwordx4 v[110:113], v216, s[88:89] offset:2048
	global_load_dwordx4 v[94:97], v216, s[88:89] offset:3072
	s_waitcnt vmcnt(16)
	s_add_u32 s52, s68, s8
	v_mul_f32_e32 v198, v167, v167
	v_mul_f32_e32 v217, v147, v147
	v_fmac_f32_e32 v198, v166, v166
	v_fmac_f32_e32 v217, v146, v146
	v_fmac_f32_e32 v198, v168, v168
	v_fmac_f32_e32 v217, v148, v148
	v_fmac_f32_e32 v198, v169, v169
	v_fmac_f32_e32 v217, v149, v149
	v_mul_f32_e32 v200, v171, v171
	v_add_f32_e32 v198, v198, v217
	v_mul_f32_e32 v217, v155, v155
	v_fmac_f32_e32 v200, v170, v170
	v_fmac_f32_e32 v217, v154, v154
	v_fmac_f32_e32 v200, v172, v172
	v_fmac_f32_e32 v217, v156, v156
	v_fmac_f32_e32 v200, v173, v173
	v_fmac_f32_e32 v217, v157, v157
	v_add_f32_e32 v200, v200, v217
	v_mul_f32_e32 v217, v131, v131
	v_fmac_f32_e32 v217, v130, v130
	v_fmac_f32_e32 v217, v132, v132
	v_fmac_f32_e32 v217, v133, v133
	v_add_f32_e32 v198, v198, v217
	v_mul_f32_e32 v217, v135, v135
	v_fmac_f32_e32 v217, v134, v134
	v_fmac_f32_e32 v217, v136, v136
	v_fmac_f32_e32 v217, v137, v137
	v_add_f32_e32 v200, v200, v217
	v_mul_f32_e32 v217, v115, v115
	v_fmac_f32_e32 v217, v114, v114
	v_fmac_f32_e32 v217, v116, v116
	v_fmac_f32_e32 v217, v117, v117
	v_add_f32_e32 v198, v198, v217
	v_mul_f32_e32 v217, v119, v119
	v_fmac_f32_e32 v217, v118, v118
	v_fmac_f32_e32 v217, v120, v120
	v_fmac_f32_e32 v217, v121, v121
	v_add_f32_e32 v200, v200, v217
	v_mul_f32_e32 v217, v99, v99
	v_fmac_f32_e32 v217, v98, v98
	v_fmac_f32_e32 v217, v100, v100
	v_fmac_f32_e32 v217, v101, v101
	v_add_f32_e32 v198, v198, v217
	v_mul_f32_e32 v217, v83, v83
	v_mov_b32_e32 v220, v75
	v_mov_b32_e32 v221, v67
	v_fmac_f32_e32 v217, v82, v82
	v_mov_b32_e32 v218, v74
	v_mov_b32_e32 v219, v66
	v_pk_mul_f32 v[220:221], v[220:221], v[220:221]
	v_fmac_f32_e32 v217, v84, v84
	v_pk_fma_f32 v[218:219], v[218:219], v[218:219], v[220:221]
	v_mov_b32_e32 v220, v76
	v_mov_b32_e32 v221, v68
	v_fmac_f32_e32 v217, v85, v85
	v_pk_fma_f32 v[218:219], v[220:221], v[220:221], v[218:219]
	v_mov_b32_e32 v220, v77
	v_mov_b32_e32 v221, v69
	v_add_f32_e32 v198, v198, v217
	v_pk_fma_f32 v[218:219], v[220:221], v[220:221], v[218:219]
	v_mov_b32_e32 v220, v79
	v_add_f32_e32 v198, v198, v218
	v_add_f32_e32 v198, v198, v219
	ds_bpermute_b32 v217, v208, v198
	v_mul_f32_e32 v218, v103, v103
	v_fmac_f32_e32 v218, v102, v102
	v_fmac_f32_e32 v218, v104, v104
	v_fmac_f32_e32 v218, v105, v105
	s_waitcnt lgkmcnt(0)
	v_add_f32_e32 v198, v198, v217
	ds_bpermute_b32 v217, v209, v198
	v_add_f32_e32 v200, v200, v218
	v_mul_f32_e32 v218, v87, v87
	v_fmac_f32_e32 v218, v86, v86
	v_fmac_f32_e32 v218, v88, v88
	s_waitcnt lgkmcnt(0)
	v_add_f32_e32 v198, v198, v217
	ds_bpermute_b32 v217, v210, v198
	v_fmac_f32_e32 v218, v89, v89
	v_mov_b32_e32 v221, v71
	v_add_f32_e32 v200, v200, v218
	v_mov_b32_e32 v218, v78
	v_mov_b32_e32 v219, v70
	v_pk_mul_f32 v[220:221], v[220:221], v[220:221]
	s_waitcnt lgkmcnt(0)
	v_add_f32_e32 v198, v198, v217
	v_pk_fma_f32 v[218:219], v[218:219], v[218:219], v[220:221]
	v_mov_b32_e32 v220, v80
	v_mov_b32_e32 v221, v72
	v_pk_fma_f32 v[218:219], v[220:221], v[220:221], v[218:219]
	v_mov_b32_e32 v220, v81
	v_mov_b32_e32 v221, v73
	v_pk_fma_f32 v[218:219], v[220:221], v[220:221], v[218:219]
	ds_bpermute_b32 v217, v211, v198
	v_add_f32_e32 v200, v200, v218
	v_add_f32_e32 v200, v200, v219
	ds_bpermute_b32 v218, v208, v200
	s_addc_u32 s53, s69, s9
	s_waitcnt lgkmcnt(1)
	v_add_f32_e32 v198, v198, v217
	ds_bpermute_b32 v217, v213, v198
	s_add_u32 s82, s52, 0x1000
	s_waitcnt lgkmcnt(1)
	v_add_f32_e32 v200, v200, v218
	ds_bpermute_b32 v218, v209, v200
	s_addc_u32 s83, s53, 0
	s_waitcnt lgkmcnt(1)
	v_add_f32_e32 v198, v198, v217
	ds_bpermute_b32 v217, v214, v198
	s_mov_b64 s[96:97], s[0:1]
	s_waitcnt lgkmcnt(1)
	v_add_f32_e32 v200, v200, v218
	ds_bpermute_b32 v218, v210, v200
	s_mov_b32 s0, s34
	s_waitcnt lgkmcnt(1)
	v_add_f32_e32 v198, v198, v217
	v_fmamk_f32 v198, v198, 0x3a000000, v212
	v_mul_f32_e32 v217, 0x4f800000, v198
	s_waitcnt lgkmcnt(0)
	v_add_f32_e32 v200, v200, v218
	v_cmp_gt_f32_e32 vcc, s58, v198
	ds_bpermute_b32 v218, v211, v200
	s_mov_b64 s[94:95], s[70:71]
	v_cndmask_b32_e32 v198, v198, v217, vcc
	v_sqrt_f32_e32 v217, v198
	s_mov_b64 s[88:89], s[72:73]
	s_waitcnt lgkmcnt(0)
	v_add_f32_e32 v200, v200, v218
	ds_bpermute_b32 v218, v213, v200
	v_add_u32_e32 v219, -1, v217
	v_fma_f32 v220, -v219, v217, v198
	v_cmp_ge_f32_e64 s[6:7], 0, v220
	v_add_u32_e32 v220, 1, v217
	s_waitcnt lgkmcnt(0)
	v_add_f32_e32 v200, v200, v218
	v_cndmask_b32_e64 v219, v217, v219, s[6:7]
	v_fma_f32 v217, -v220, v217, v198
	v_cmp_lt_f32_e64 s[6:7], 0, v217
	ds_bpermute_b32 v218, v214, v200
	s_waitcnt lgkmcnt(0)
	v_add_f32_e32 v200, v200, v218
	v_cndmask_b32_e64 v217, v219, v220, s[6:7]
	v_mul_f32_e32 v219, 0x37800000, v217
	v_cndmask_b32_e32 v217, v217, v219, vcc
	v_cmp_class_f32_e32 vcc, v198, v215
	v_fmamk_f32 v200, v200, 0x3a000000, v212
	v_mul_f32_e32 v218, 0x4f800000, v200
	v_cndmask_b32_e32 v198, v217, v198, vcc
	v_div_scale_f32 v217, s[6:7], v198, v198, 1.0
	v_rcp_f32_e32 v219, v217
	v_cmp_gt_f32_e64 s[6:7], s58, v200
	v_fma_f32 v220, -v217, v219, 1.0
	s_nop 0
	v_cndmask_b32_e64 v200, v200, v218, s[6:7]
	v_fmac_f32_e32 v219, v220, v219
	v_div_scale_f32 v220, vcc, 1.0, v198, 1.0
	v_sqrt_f32_e32 v218, v200
	v_mul_f32_e32 v221, v220, v219
	v_fma_f32 v222, -v217, v221, v220
	v_fmac_f32_e32 v221, v222, v219
	v_fma_f32 v217, -v217, v221, v220
	v_add_u32_e32 v220, -1, v218
	v_fma_f32 v222, -v220, v218, v200
	v_cmp_ge_f32_e64 s[8:9], 0, v222
	v_add_u32_e32 v222, 1, v218
	v_div_fmas_f32 v217, v217, v219, v221
	v_cndmask_b32_e64 v220, v218, v220, s[8:9]
	v_fma_f32 v218, -v222, v218, v200
	v_cmp_lt_f32_e64 s[8:9], 0, v218
	v_div_fixup_f32 v198, v217, v198, 1.0
	v_pk_mul_f32 v[166:167], v[198:199], v[166:167] op_sel_hi:[0,1]
	v_cndmask_b32_e64 v218, v220, v222, s[8:9]
	v_mul_f32_e32 v220, 0x37800000, v218
	v_cndmask_b32_e64 v218, v218, v220, s[6:7]
	v_cmp_class_f32_e64 s[6:7], v200, v215
	v_pk_fma_f32 v[166:167], v[166:167], v[58:59], v[62:63]
	v_pk_mul_f32 v[146:147], v[198:199], v[146:147] op_sel_hi:[0,1]
	v_cndmask_b32_e64 v200, v218, v200, s[6:7]
	v_div_scale_f32 v218, s[6:7], v200, v200, 1.0
	v_rcp_f32_e32 v220, v218
	v_med3_f32 v166, v166, s49, v199
	v_med3_f32 v167, v167, s49, v199
	v_pk_fma_f32 v[146:147], v[146:147], v[50:51], v[54:55]
	v_fma_f32 v217, -v218, v220, 1.0
	v_fmac_f32_e32 v220, v217, v220
	v_div_scale_f32 v217, vcc, 1.0, v200, 1.0
	v_mul_f32_e32 v219, v217, v220
	v_fma_f32 v221, -v218, v219, v217
	v_fmac_f32_e32 v219, v221, v220
	v_fma_f32 v217, -v218, v219, v217
	v_div_fmas_f32 v217, v217, v220, v219
	v_div_fixup_f32 v200, v217, v200, 1.0
	v_pk_mul_f32 v[170:171], v[200:201], v[170:171] op_sel_hi:[0,1]
	v_cvt_pk_fp8_f32 v217, v166, v167
	v_pk_fma_f32 v[166:167], v[58:59], v[170:171], v[62:63]
	v_med3_f32 v166, v166, s49, v199
	v_med3_f32 v167, v167, s49, v199
	v_cvt_pk_fp8_f32 v170, v166, v167
	v_pk_mul_f32 v[172:173], v[200:201], v[172:173] op_sel_hi:[0,1]
	v_pk_fma_f32 v[172:173], v[60:61], v[172:173], v[64:65]
	v_med3_f32 v146, v146, s49, v199
	v_med3_f32 v166, v172, s49, v199
	v_med3_f32 v167, v173, s49, v199
	v_cvt_pk_fp8_f32 v170, v166, v167 op_sel:[0,0,1]
	v_med3_f32 v147, v147, s49, v199
	v_cvt_pk_fp8_f32 v166, v146, v147
	v_pk_mul_f32 v[148:149], v[198:199], v[148:149] op_sel_hi:[0,1]
	v_pk_fma_f32 v[148:149], v[148:149], v[52:53], v[56:57]
	v_pk_mul_f32 v[130:131], v[198:199], v[130:131] op_sel_hi:[0,1]
	v_med3_f32 v148, v148, s49, v199
	v_med3_f32 v149, v149, s49, v199
	v_pk_fma_f32 v[130:131], v[130:131], v[42:43], v[46:47]
	v_pk_mul_f32 v[134:135], v[200:201], v[134:135] op_sel_hi:[0,1]
	v_cvt_pk_fp8_f32 v166, v148, v149 op_sel:[0,0,1]
	v_pk_fma_f32 v[134:135], v[42:43], v[134:135], v[46:47]
	v_med3_f32 v130, v130, s49, v199
	v_med3_f32 v131, v131, s49, v199
	v_cvt_pk_fp8_f32 v148, v130, v131
	v_med3_f32 v130, v134, s49, v199
	v_med3_f32 v131, v135, s49, v199
	v_cvt_pk_fp8_f32 v134, v130, v131
	v_pk_mul_f32 v[136:137], v[200:201], v[136:137] op_sel_hi:[0,1]
	v_pk_fma_f32 v[136:137], v[44:45], v[136:137], v[48:49]
	v_pk_mul_f32 v[114:115], v[198:199], v[114:115] op_sel_hi:[0,1]
	v_med3_f32 v130, v136, s49, v199
	v_med3_f32 v131, v137, s49, v199
	v_pk_fma_f32 v[114:115], v[114:115], v[34:35], v[38:39]
	v_pk_mul_f32 v[118:119], v[200:201], v[118:119] op_sel_hi:[0,1]
	v_cvt_pk_fp8_f32 v134, v130, v131 op_sel:[0,0,1]
	v_pk_fma_f32 v[118:119], v[34:35], v[118:119], v[38:39]
	v_med3_f32 v114, v114, s49, v199
	v_med3_f32 v115, v115, s49, v199
	v_cvt_pk_fp8_f32 v130, v114, v115
	v_med3_f32 v114, v118, s49, v199
	v_med3_f32 v115, v119, s49, v199
	v_cvt_pk_fp8_f32 v118, v114, v115
	v_pk_mul_f32 v[120:121], v[200:201], v[120:121] op_sel_hi:[0,1]
	v_pk_fma_f32 v[120:121], v[36:37], v[120:121], v[40:41]
	v_pk_mul_f32 v[98:99], v[198:199], v[98:99] op_sel_hi:[0,1]
	v_med3_f32 v114, v120, s49, v199
	v_med3_f32 v115, v121, s49, v199
	v_pk_fma_f32 v[98:99], v[98:99], v[26:27], v[30:31]
	v_pk_mul_f32 v[102:103], v[200:201], v[102:103] op_sel_hi:[0,1]
	v_cvt_pk_fp8_f32 v118, v114, v115 op_sel:[0,0,1]
	v_pk_fma_f32 v[102:103], v[26:27], v[102:103], v[30:31]
	v_med3_f32 v98, v98, s49, v199
	v_med3_f32 v99, v99, s49, v199
	v_cvt_pk_fp8_f32 v114, v98, v99
	v_med3_f32 v98, v102, s49, v199
	v_med3_f32 v99, v103, s49, v199
; __global__ void __launch_bounds__(NWAVES * 64, 2) fwd_kernel(Args args) {
;     ...
;                 N1_LOAD(vb, wb, r0 + 6, r0 + 7);
	v_cvt_pk_fp8_f32 v102, v98, v99
	v_pk_mul_f32 v[104:105], v[200:201], v[104:105] op_sel_hi:[0,1]
	v_pk_fma_f32 v[104:105], v[28:29], v[104:105], v[32:33]
	v_pk_mul_f32 v[82:83], v[198:199], v[82:83] op_sel_hi:[0,1]
	v_med3_f32 v98, v104, s49, v199
	v_med3_f32 v99, v105, s49, v199
	v_pk_fma_f32 v[82:83], v[82:83], v[18:19], v[22:23]
	v_pk_mul_f32 v[86:87], v[200:201], v[86:87] op_sel_hi:[0,1]
	v_cvt_pk_fp8_f32 v102, v98, v99 op_sel:[0,0,1]
	v_pk_fma_f32 v[86:87], v[18:19], v[86:87], v[22:23]
	v_med3_f32 v82, v82, s49, v199
	v_med3_f32 v83, v83, s49, v199
	v_cvt_pk_fp8_f32 v98, v82, v83
	v_med3_f32 v82, v86, s49, v199
	v_med3_f32 v83, v87, s49, v199
	v_cvt_pk_fp8_f32 v86, v82, v83
	v_pk_mul_f32 v[88:89], v[200:201], v[88:89] op_sel_hi:[0,1]
	v_pk_fma_f32 v[88:89], v[20:21], v[88:89], v[24:25]
	v_pk_mul_f32 v[74:75], v[198:199], v[74:75] op_sel_hi:[0,1]
	v_med3_f32 v82, v88, s49, v199
	v_med3_f32 v83, v89, s49, v199
	v_pk_fma_f32 v[74:75], v[74:75], v[10:11], v[14:15]
	v_pk_mul_f32 v[78:79], v[200:201], v[78:79] op_sel_hi:[0,1]
	v_cvt_pk_fp8_f32 v86, v82, v83 op_sel:[0,0,1]
	v_pk_fma_f32 v[78:79], v[10:11], v[78:79], v[14:15]
	v_med3_f32 v74, v74, s49, v199
	v_med3_f32 v75, v75, s49, v199
	v_cvt_pk_fp8_f32 v82, v74, v75
	v_med3_f32 v74, v78, s49, v199
	v_med3_f32 v75, v79, s49, v199
	v_cvt_pk_fp8_f32 v78, v74, v75
	v_pk_mul_f32 v[80:81], v[200:201], v[80:81] op_sel_hi:[0,1]
	v_pk_mul_f32 v[154:155], v[200:201], v[154:155] op_sel_hi:[0,1]
	v_pk_fma_f32 v[80:81], v[12:13], v[80:81], v[16:17]
	v_pk_mul_f32 v[66:67], v[198:199], v[66:67] op_sel_hi:[0,1]
	v_pk_fma_f32 v[154:155], v[50:51], v[154:155], v[54:55]
	v_med3_f32 v74, v80, s49, v199
	v_med3_f32 v75, v81, s49, v199
	v_pk_fma_f32 v[66:67], v[66:67], v[2:3], v[6:7]
	v_pk_mul_f32 v[70:71], v[200:201], v[70:71] op_sel_hi:[0,1]
	v_pk_mul_f32 v[168:169], v[198:199], v[168:169] op_sel_hi:[0,1]
	v_med3_f32 v146, v154, s49, v199
	v_med3_f32 v147, v155, s49, v199
	v_pk_mul_f32 v[132:133], v[198:199], v[132:133] op_sel_hi:[0,1]
	v_pk_mul_f32 v[100:101], v[198:199], v[100:101] op_sel_hi:[0,1]
	v_pk_mul_f32 v[76:77], v[198:199], v[76:77] op_sel_hi:[0,1]
	v_cvt_pk_fp8_f32 v78, v74, v75 op_sel:[0,0,1]
	v_pk_fma_f32 v[70:71], v[2:3], v[70:71], v[6:7]
	v_med3_f32 v66, v66, s49, v199
	v_med3_f32 v67, v67, s49, v199
	v_pk_fma_f32 v[168:169], v[168:169], v[60:61], v[64:65]
	v_cvt_pk_fp8_f32 v154, v146, v147
	v_pk_fma_f32 v[132:133], v[132:133], v[44:45], v[48:49]
	v_pk_fma_f32 v[100:101], v[100:101], v[28:29], v[32:33]
	v_pk_fma_f32 v[76:77], v[76:77], v[12:13], v[16:17]
	v_cvt_pk_fp8_f32 v74, v66, v67
	v_med3_f32 v66, v70, s49, v199
	v_med3_f32 v67, v71, s49, v199
	v_med3_f32 v168, v168, s49, v199
	v_med3_f32 v169, v169, s49, v199
	v_pk_mul_f32 v[156:157], v[200:201], v[156:157] op_sel_hi:[0,1]
	v_med3_f32 v132, v132, s49, v199
	v_med3_f32 v133, v133, s49, v199
	v_pk_mul_f32 v[116:117], v[198:199], v[116:117] op_sel_hi:[0,1]
	v_med3_f32 v100, v100, s49, v199
	v_med3_f32 v101, v101, s49, v199
	v_pk_mul_f32 v[84:85], v[198:199], v[84:85] op_sel_hi:[0,1]
	v_med3_f32 v76, v76, s49, v199
	v_med3_f32 v77, v77, s49, v199
	v_pk_mul_f32 v[68:69], v[198:199], v[68:69] op_sel_hi:[0,1]
	v_cvt_pk_fp8_f32 v70, v66, v67
	v_cvt_pk_fp8_f32 v217, v168, v169 op_sel:[0,0,1]
	v_pk_fma_f32 v[156:157], v[52:53], v[156:157], v[56:57]
	v_cvt_pk_fp8_f32 v148, v132, v133 op_sel:[0,0,1]
	v_pk_fma_f32 v[116:117], v[116:117], v[36:37], v[40:41]
	v_cvt_pk_fp8_f32 v114, v100, v101 op_sel:[0,0,1]
	v_pk_fma_f32 v[84:85], v[84:85], v[20:21], v[24:25]
	v_cvt_pk_fp8_f32 v82, v76, v77 op_sel:[0,0,1]
	v_pk_fma_f32 v[68:69], v[68:69], v[4:5], v[8:9]
	v_pk_mul_f32 v[72:73], v[200:201], v[72:73] op_sel_hi:[0,1]
	v_med3_f32 v146, v156, s49, v199
	v_med3_f32 v147, v157, s49, v199
	v_med3_f32 v116, v116, s49, v199
	v_med3_f32 v117, v117, s49, v199
	v_med3_f32 v84, v84, s49, v199
	v_med3_f32 v85, v85, s49, v199
	v_pk_fma_f32 v[72:73], v[4:5], v[72:73], v[8:9]
	v_med3_f32 v68, v68, s49, v199
	v_med3_f32 v69, v69, s49, v199
	v_cvt_pk_fp8_f32 v154, v146, v147 op_sel:[0,0,1]
	v_cvt_pk_fp8_f32 v130, v116, v117 op_sel:[0,0,1]
	v_cvt_pk_fp8_f32 v98, v84, v85 op_sel:[0,0,1]
	v_cvt_pk_fp8_f32 v74, v68, v69 op_sel:[0,0,1]
	v_med3_f32 v66, v72, s49, v199
	v_med3_f32 v67, v73, s49, v199
	v_lshl_add_u64 v[168:169], s[80:81], 0, v[196:197]
	v_lshl_add_u64 v[146:147], s[78:79], 0, v[196:197]
	v_cvt_pk_fp8_f32 v70, v66, v67 op_sel:[0,0,1]
	global_store_dword v[168:169], v217, off
	global_store_dword v[146:147], v170, off
	global_store_dword v[168:169], v166, off offset:256
	global_store_dword v[146:147], v154, off offset:256
	global_store_dword v[168:169], v148, off offset:512
	global_store_dword v[146:147], v134, off offset:512
	global_store_dword v[168:169], v130, off offset:768
	global_store_dword v[146:147], v118, off offset:768
	global_store_dword v[168:169], v114, off offset:1024
	global_store_dword v[146:147], v102, off offset:1024
	global_store_dword v[168:169], v98, off offset:1280
	global_store_dword v[146:147], v86, off offset:1280
	global_store_dword v[168:169], v82, off offset:1536
	global_store_dword v[146:147], v78, off offset:1536
	global_store_dword v[168:169], v74, off offset:1792
	global_store_dword v[146:147], v70, off offset:1792
	global_load_dwordx4 v[166:169], v216, s[84:85] offset:0
	global_load_dwordx4 v[146:149], v216, s[84:85] offset:1024
	global_load_dwordx4 v[130:133], v216, s[84:85] offset:2048
	global_load_dwordx4 v[114:117], v216, s[84:85] offset:3072
	global_load_dwordx4 v[98:101], v216, s[86:87] offset:0
	global_load_dwordx4 v[82:85], v216, s[86:87] offset:1024
	global_load_dwordx4 v[74:77], v216, s[86:87] offset:2048
	global_load_dwordx4 v[66:69], v216, s[86:87] offset:3072
	global_load_dwordx4 v[170:173], v216, s[52:53] offset:0
	global_load_dwordx4 v[154:157], v216, s[52:53] offset:1024
	global_load_dwordx4 v[134:137], v216, s[52:53] offset:2048
	global_load_dwordx4 v[118:121], v216, s[52:53] offset:3072
	global_load_dwordx4 v[102:105], v216, s[82:83] offset:0
	global_load_dwordx4 v[86:89], v216, s[82:83] offset:1024
	global_load_dwordx4 v[78:81], v216, s[82:83] offset:2048
	global_load_dwordx4 v[70:73], v216, s[82:83] offset:3072
	s_waitcnt vmcnt(16)
	s_add_u32 s52, s3, s74
	v_mul_f32_e32 v198, v187, v187
	v_mul_f32_e32 v216, v179, v179
	v_fmac_f32_e32 v198, v186, v186
	v_fmac_f32_e32 v216, v178, v178
	v_fmac_f32_e32 v198, v188, v188
	v_fmac_f32_e32 v216, v180, v180
	v_fmac_f32_e32 v198, v189, v189
	v_fmac_f32_e32 v216, v181, v181
	v_mul_f32_e32 v200, v191, v191
	v_add_f32_e32 v198, v198, v216
	v_mul_f32_e32 v216, v183, v183
	v_fmac_f32_e32 v200, v190, v190
	v_fmac_f32_e32 v216, v182, v182
	v_fmac_f32_e32 v200, v192, v192
	v_fmac_f32_e32 v216, v184, v184
	v_fmac_f32_e32 v200, v193, v193
	v_fmac_f32_e32 v216, v185, v185
	v_add_f32_e32 v200, v200, v216
	v_mul_f32_e32 v216, v163, v163
	v_fmac_f32_e32 v216, v162, v162
	v_fmac_f32_e32 v216, v164, v164
	v_fmac_f32_e32 v216, v165, v165
	v_add_f32_e32 v198, v198, v216
	v_mul_f32_e32 v216, v175, v175
	v_fmac_f32_e32 v216, v174, v174
	v_fmac_f32_e32 v216, v176, v176
	v_fmac_f32_e32 v216, v177, v177
	v_add_f32_e32 v200, v200, v216
	v_mul_f32_e32 v216, v151, v151
	v_fmac_f32_e32 v216, v150, v150
	v_fmac_f32_e32 v216, v152, v152
	v_fmac_f32_e32 v216, v153, v153
	v_add_f32_e32 v198, v198, v216
	v_mul_f32_e32 v216, v159, v159
	v_fmac_f32_e32 v216, v158, v158
	v_fmac_f32_e32 v216, v160, v160
	v_fmac_f32_e32 v216, v161, v161
	v_add_f32_e32 v200, v200, v216
	v_mul_f32_e32 v216, v139, v139
	v_fmac_f32_e32 v216, v138, v138
	v_fmac_f32_e32 v216, v140, v140
	v_fmac_f32_e32 v216, v141, v141
	v_add_f32_e32 v198, v198, v216
	v_mul_f32_e32 v216, v123, v123
	v_fmac_f32_e32 v216, v122, v122
	v_fmac_f32_e32 v216, v124, v124
	v_fmac_f32_e32 v216, v125, v125
	v_mov_b32_e32 v218, v107
	v_mov_b32_e32 v219, v91
	v_add_f32_e32 v198, v198, v216
	v_mov_b32_e32 v216, v106
	v_mov_b32_e32 v217, v90
	v_pk_mul_f32 v[218:219], v[218:219], v[218:219]
	s_addc_u32 s53, s33, s75
	v_pk_fma_f32 v[216:217], v[216:217], v[216:217], v[218:219]
	v_mov_b32_e32 v218, v108
	v_mov_b32_e32 v219, v92
	v_pk_fma_f32 v[216:217], v[218:219], v[218:219], v[216:217]
	v_mov_b32_e32 v218, v109
	v_mov_b32_e32 v219, v93
	v_pk_fma_f32 v[216:217], v[218:219], v[218:219], v[216:217]
	v_mov_b32_e32 v219, v95
	v_add_f32_e32 v198, v198, v216
	v_add_f32_e32 v198, v198, v217
	ds_bpermute_b32 v216, v208, v198
	v_mul_f32_e32 v217, v143, v143
	v_fmac_f32_e32 v217, v142, v142
	v_fmac_f32_e32 v217, v144, v144
	v_fmac_f32_e32 v217, v145, v145
	s_waitcnt lgkmcnt(0)
	v_add_f32_e32 v198, v198, v216
	ds_bpermute_b32 v216, v209, v198
	v_add_f32_e32 v200, v200, v217
	v_mul_f32_e32 v217, v127, v127
	v_fmac_f32_e32 v217, v126, v126
	v_fmac_f32_e32 v217, v128, v128
	s_waitcnt lgkmcnt(0)
	v_add_f32_e32 v198, v198, v216
	ds_bpermute_b32 v218, v210, v198
	v_fmac_f32_e32 v217, v129, v129
	v_add_f32_e32 v200, v200, v217
	v_mov_b32_e32 v216, v110
	v_mov_b32_e32 v217, v94
	s_waitcnt lgkmcnt(0)
	v_add_f32_e32 v198, v198, v218
	v_mov_b32_e32 v218, v111
	v_pk_mul_f32 v[218:219], v[218:219], v[218:219]
	ds_bpermute_b32 v220, v211, v198
	v_pk_fma_f32 v[216:217], v[216:217], v[216:217], v[218:219]
	v_mov_b32_e32 v218, v112
	v_mov_b32_e32 v219, v96
	v_pk_fma_f32 v[216:217], v[218:219], v[218:219], v[216:217]
	v_mov_b32_e32 v218, v113
	v_mov_b32_e32 v219, v97
	v_pk_fma_f32 v[216:217], v[218:219], v[218:219], v[216:217]
	s_waitcnt lgkmcnt(0)
	v_add_f32_e32 v198, v198, v220
	v_add_f32_e32 v200, v200, v216
	v_add_f32_e32 v200, v200, v217
	ds_bpermute_b32 v217, v208, v200
	ds_bpermute_b32 v220, v213, v198
	s_add_u32 s14, s3, s76
	s_addc_u32 s15, s33, s77
	s_waitcnt lgkmcnt(1)
	v_add_f32_e32 v200, v200, v217
	ds_bpermute_b32 v217, v209, v200
	s_waitcnt lgkmcnt(1)
	v_add_f32_e32 v198, v198, v220
	ds_bpermute_b32 v220, v214, v198
	s_waitcnt lgkmcnt(1)
	v_add_f32_e32 v200, v200, v217
	ds_bpermute_b32 v217, v210, v200
	s_waitcnt lgkmcnt(1)
	v_add_f32_e32 v198, v198, v220
	v_fmamk_f32 v198, v198, 0x3a000000, v212
	v_mul_f32_e32 v216, 0x4f800000, v198
	v_cmp_gt_f32_e32 vcc, s58, v198
	s_waitcnt lgkmcnt(0)
	v_add_f32_e32 v200, v200, v217
	ds_bpermute_b32 v217, v211, v200
	v_cndmask_b32_e32 v198, v198, v216, vcc
	v_sqrt_f32_e32 v216, v198
	s_waitcnt lgkmcnt(0)
	v_add_f32_e32 v200, v200, v217
	v_add_u32_e32 v218, -1, v216
	ds_bpermute_b32 v217, v213, v200
	v_fma_f32 v219, -v218, v216, v198
	v_cmp_ge_f32_e64 s[6:7], 0, v219
	v_add_u32_e32 v219, 1, v216
	s_waitcnt lgkmcnt(0)
	v_add_f32_e32 v200, v200, v217
	v_cndmask_b32_e64 v218, v216, v218, s[6:7]
	v_fma_f32 v216, -v219, v216, v198
	v_cmp_lt_f32_e64 s[6:7], 0, v216
	ds_bpermute_b32 v217, v214, v200
	s_waitcnt lgkmcnt(0)
	v_add_f32_e32 v200, v200, v217
	v_cndmask_b32_e64 v216, v218, v219, s[6:7]
	v_mul_f32_e32 v218, 0x37800000, v216
	v_cndmask_b32_e32 v216, v216, v218, vcc
	v_cmp_class_f32_e32 vcc, v198, v215
	v_fmamk_f32 v200, v200, 0x3a000000, v212
	v_mul_f32_e32 v217, 0x4f800000, v200
	v_cndmask_b32_e32 v198, v216, v198, vcc
	v_div_scale_f32 v216, s[6:7], v198, v198, 1.0
	v_rcp_f32_e32 v218, v216
	v_cmp_gt_f32_e64 s[6:7], s58, v200
	v_fma_f32 v219, -v216, v218, 1.0
	s_nop 0
	v_cndmask_b32_e64 v200, v200, v217, s[6:7]
	v_fmac_f32_e32 v218, v219, v218
	v_div_scale_f32 v219, vcc, 1.0, v198, 1.0
	v_sqrt_f32_e32 v217, v200
	v_mul_f32_e32 v220, v219, v218
	v_fma_f32 v221, -v216, v220, v219
	v_fmac_f32_e32 v220, v221, v218
	v_fma_f32 v216, -v216, v220, v219
	v_add_u32_e32 v219, -1, v217
	v_fma_f32 v221, -v219, v217, v200
	v_cmp_ge_f32_e64 s[8:9], 0, v221
	v_add_u32_e32 v221, 1, v217
	v_div_fmas_f32 v216, v216, v218, v220
	v_cndmask_b32_e64 v219, v217, v219, s[8:9]
	v_fma_f32 v217, -v221, v217, v200
	v_cmp_lt_f32_e64 s[8:9], 0, v217
	v_div_fixup_f32 v198, v216, v198, 1.0
	v_pk_mul_f32 v[186:187], v[198:199], v[186:187] op_sel_hi:[0,1]
	v_cndmask_b32_e64 v217, v219, v221, s[8:9]
	v_mul_f32_e32 v219, 0x37800000, v217
	v_cndmask_b32_e64 v217, v217, v219, s[6:7]
	v_cmp_class_f32_e64 s[6:7], v200, v215
	v_pk_fma_f32 v[186:187], v[186:187], v[58:59], v[62:63]
	v_pk_mul_f32 v[178:179], v[198:199], v[178:179] op_sel_hi:[0,1]
	v_cndmask_b32_e64 v200, v217, v200, s[6:7]
	v_div_scale_f32 v217, s[6:7], v200, v200, 1.0
	v_rcp_f32_e32 v219, v217
	v_med3_f32 v186, v186, s49, v199
	v_med3_f32 v187, v187, s49, v199
	v_pk_fma_f32 v[178:179], v[178:179], v[50:51], v[54:55]
	v_fma_f32 v216, -v217, v219, 1.0
	v_fmac_f32_e32 v219, v216, v219
	v_div_scale_f32 v216, vcc, 1.0, v200, 1.0
	v_mul_f32_e32 v218, v216, v219
	v_fma_f32 v220, -v217, v218, v216
	v_fmac_f32_e32 v218, v220, v219
	v_fma_f32 v216, -v217, v218, v216
	v_div_fmas_f32 v216, v216, v219, v218
	v_div_fixup_f32 v200, v216, v200, 1.0
	v_pk_mul_f32 v[190:191], v[200:201], v[190:191] op_sel_hi:[0,1]
	v_cvt_pk_fp8_f32 v216, v186, v187
	v_pk_fma_f32 v[186:187], v[58:59], v[190:191], v[62:63]
	v_med3_f32 v186, v186, s49, v199
	v_med3_f32 v187, v187, s49, v199
	v_cvt_pk_fp8_f32 v190, v186, v187
	v_pk_mul_f32 v[192:193], v[200:201], v[192:193] op_sel_hi:[0,1]
	v_pk_fma_f32 v[192:193], v[60:61], v[192:193], v[64:65]
	v_med3_f32 v178, v178, s49, v199
	v_med3_f32 v186, v192, s49, v199
	v_med3_f32 v187, v193, s49, v199
	v_cvt_pk_fp8_f32 v190, v186, v187 op_sel:[0,0,1]
	v_med3_f32 v179, v179, s49, v199
	v_cvt_pk_fp8_f32 v186, v178, v179
	v_pk_mul_f32 v[180:181], v[198:199], v[180:181] op_sel_hi:[0,1]
	v_pk_fma_f32 v[180:181], v[180:181], v[52:53], v[56:57]
	v_pk_mul_f32 v[162:163], v[198:199], v[162:163] op_sel_hi:[0,1]
	v_med3_f32 v180, v180, s49, v199
	v_med3_f32 v181, v181, s49, v199
	v_pk_fma_f32 v[162:163], v[162:163], v[42:43], v[46:47]
	v_pk_mul_f32 v[174:175], v[200:201], v[174:175] op_sel_hi:[0,1]
	v_cvt_pk_fp8_f32 v186, v180, v181 op_sel:[0,0,1]
	v_pk_fma_f32 v[174:175], v[42:43], v[174:175], v[46:47]
	v_med3_f32 v162, v162, s49, v199
	v_med3_f32 v163, v163, s49, v199
	v_cvt_pk_fp8_f32 v180, v162, v163
	v_med3_f32 v162, v174, s49, v199
	v_med3_f32 v163, v175, s49, v199
	v_cvt_pk_fp8_f32 v174, v162, v163
	v_pk_mul_f32 v[176:177], v[200:201], v[176:177] op_sel_hi:[0,1]
	v_pk_fma_f32 v[176:177], v[44:45], v[176:177], v[48:49]
	v_pk_mul_f32 v[150:151], v[198:199], v[150:151] op_sel_hi:[0,1]
	v_med3_f32 v162, v176, s49, v199
	v_med3_f32 v163, v177, s49, v199
	v_pk_fma_f32 v[150:151], v[150:151], v[34:35], v[38:39]
	v_pk_mul_f32 v[158:159], v[200:201], v[158:159] op_sel_hi:[0,1]
	v_cvt_pk_fp8_f32 v174, v162, v163 op_sel:[0,0,1]
	v_pk_fma_f32 v[158:159], v[34:35], v[158:159], v[38:39]
	v_med3_f32 v150, v150, s49, v199
	v_med3_f32 v151, v151, s49, v199
	v_cvt_pk_fp8_f32 v162, v150, v151
	v_med3_f32 v150, v158, s49, v199
	v_med3_f32 v151, v159, s49, v199
	v_cvt_pk_fp8_f32 v158, v150, v151
	v_pk_mul_f32 v[160:161], v[200:201], v[160:161] op_sel_hi:[0,1]
	v_pk_fma_f32 v[160:161], v[36:37], v[160:161], v[40:41]
	v_pk_mul_f32 v[138:139], v[198:199], v[138:139] op_sel_hi:[0,1]
	v_med3_f32 v150, v160, s49, v199
	v_med3_f32 v151, v161, s49, v199
	v_pk_fma_f32 v[138:139], v[138:139], v[26:27], v[30:31]
	v_pk_mul_f32 v[142:143], v[200:201], v[142:143] op_sel_hi:[0,1]
	v_cvt_pk_fp8_f32 v158, v150, v151 op_sel:[0,0,1]
	v_pk_fma_f32 v[142:143], v[26:27], v[142:143], v[30:31]
	v_med3_f32 v138, v138, s49, v199
	v_med3_f32 v139, v139, s49, v199
	v_cvt_pk_fp8_f32 v150, v138, v139
	v_med3_f32 v138, v142, s49, v199
	v_med3_f32 v139, v143, s49, v199
	v_cvt_pk_fp8_f32 v142, v138, v139
	v_pk_mul_f32 v[144:145], v[200:201], v[144:145] op_sel_hi:[0,1]
	v_pk_fma_f32 v[144:145], v[28:29], v[144:145], v[32:33]
	v_pk_mul_f32 v[122:123], v[198:199], v[122:123] op_sel_hi:[0,1]
	v_med3_f32 v138, v144, s49, v199
	v_med3_f32 v139, v145, s49, v199
	v_pk_fma_f32 v[122:123], v[122:123], v[18:19], v[22:23]
	v_pk_mul_f32 v[126:127], v[200:201], v[126:127] op_sel_hi:[0,1]
	v_cvt_pk_fp8_f32 v142, v138, v139 op_sel:[0,0,1]
	v_pk_fma_f32 v[126:127], v[18:19], v[126:127], v[22:23]
	v_med3_f32 v122, v122, s49, v199
	v_med3_f32 v123, v123, s49, v199
	v_cvt_pk_fp8_f32 v138, v122, v123
	v_med3_f32 v122, v126, s49, v199
	v_med3_f32 v123, v127, s49, v199
	v_cvt_pk_fp8_f32 v126, v122, v123
	v_pk_mul_f32 v[128:129], v[200:201], v[128:129] op_sel_hi:[0,1]
	v_pk_fma_f32 v[128:129], v[20:21], v[128:129], v[24:25]
	v_pk_mul_f32 v[106:107], v[198:199], v[106:107] op_sel_hi:[0,1]
	v_med3_f32 v122, v128, s49, v199
	v_med3_f32 v123, v129, s49, v199
	v_pk_fma_f32 v[106:107], v[106:107], v[10:11], v[14:15]
; #define N1_TIE(V_, W_, cnt_) do { asm volatile("s_waitcnt vmcnt(" #cnt_ ")" : "+v"(V_[0]), "+v"(V_[1]), "+v"(V_[2]), "+v"(V_[3]), "+v"(V_[4]), "+v"(V_[5]), "+v"(V_[6]), "+v"(V_[7])); \
;                 asm volatile("" : "+v"(W_[0]), "+v"(W_[1]), "+v"(W_[2]), "+v"(W_[3]), "+v"(W_[4]), "+v"(W_[5]), "+v"(W_[6]), "+v"(W_[7])); } while (0)
; __global__ void __launch_bounds__(NWAVES * 64, 2) fwd_kernel(Args args) {
;     ...
;                 N1_TIE(vb, wb, 0); N1_BODY(vb, wb, r0 + 6, r0 + 7);
	v_pk_mul_f32 v[110:111], v[200:201], v[110:111] op_sel_hi:[0,1]
	v_cvt_pk_fp8_f32 v126, v122, v123 op_sel:[0,0,1]
	v_pk_fma_f32 v[110:111], v[10:11], v[110:111], v[14:15]
	v_med3_f32 v106, v106, s49, v199
	v_med3_f32 v107, v107, s49, v199
	v_cvt_pk_fp8_f32 v122, v106, v107
	v_med3_f32 v106, v110, s49, v199
	v_med3_f32 v107, v111, s49, v199
	v_cvt_pk_fp8_f32 v110, v106, v107
	v_pk_mul_f32 v[112:113], v[200:201], v[112:113] op_sel_hi:[0,1]
	v_pk_mul_f32 v[182:183], v[200:201], v[182:183] op_sel_hi:[0,1]
	v_pk_fma_f32 v[112:113], v[12:13], v[112:113], v[16:17]
	v_pk_mul_f32 v[90:91], v[198:199], v[90:91] op_sel_hi:[0,1]
	v_pk_fma_f32 v[182:183], v[50:51], v[182:183], v[54:55]
	v_med3_f32 v106, v112, s49, v199
	v_med3_f32 v107, v113, s49, v199
	v_pk_fma_f32 v[90:91], v[90:91], v[2:3], v[6:7]
	v_pk_mul_f32 v[94:95], v[200:201], v[94:95] op_sel_hi:[0,1]
	v_pk_mul_f32 v[188:189], v[198:199], v[188:189] op_sel_hi:[0,1]
	v_med3_f32 v178, v182, s49, v199
	v_med3_f32 v179, v183, s49, v199
	v_pk_mul_f32 v[164:165], v[198:199], v[164:165] op_sel_hi:[0,1]
	v_pk_mul_f32 v[140:141], v[198:199], v[140:141] op_sel_hi:[0,1]
	v_pk_mul_f32 v[108:109], v[198:199], v[108:109] op_sel_hi:[0,1]
	v_cvt_pk_fp8_f32 v110, v106, v107 op_sel:[0,0,1]
	v_pk_fma_f32 v[94:95], v[2:3], v[94:95], v[6:7]
	v_med3_f32 v90, v90, s49, v199
	v_med3_f32 v91, v91, s49, v199
	v_pk_fma_f32 v[188:189], v[188:189], v[60:61], v[64:65]
	v_cvt_pk_fp8_f32 v182, v178, v179
	v_pk_fma_f32 v[164:165], v[164:165], v[44:45], v[48:49]
	v_pk_fma_f32 v[140:141], v[140:141], v[28:29], v[32:33]
	v_pk_fma_f32 v[108:109], v[108:109], v[12:13], v[16:17]
	v_cvt_pk_fp8_f32 v106, v90, v91
	v_med3_f32 v90, v94, s49, v199
	v_med3_f32 v91, v95, s49, v199
	v_med3_f32 v188, v188, s49, v199
	v_med3_f32 v189, v189, s49, v199
	v_pk_mul_f32 v[184:185], v[200:201], v[184:185] op_sel_hi:[0,1]
	v_med3_f32 v164, v164, s49, v199
	v_med3_f32 v165, v165, s49, v199
	v_pk_mul_f32 v[152:153], v[198:199], v[152:153] op_sel_hi:[0,1]
	v_med3_f32 v140, v140, s49, v199
	v_med3_f32 v141, v141, s49, v199
	v_pk_mul_f32 v[124:125], v[198:199], v[124:125] op_sel_hi:[0,1]
	v_med3_f32 v108, v108, s49, v199
	v_med3_f32 v109, v109, s49, v199
	v_pk_mul_f32 v[92:93], v[198:199], v[92:93] op_sel_hi:[0,1]
	v_cvt_pk_fp8_f32 v94, v90, v91
	v_cvt_pk_fp8_f32 v216, v188, v189 op_sel:[0,0,1]
	v_pk_fma_f32 v[184:185], v[52:53], v[184:185], v[56:57]
	v_cvt_pk_fp8_f32 v180, v164, v165 op_sel:[0,0,1]
	v_pk_fma_f32 v[152:153], v[152:153], v[36:37], v[40:41]
	v_cvt_pk_fp8_f32 v150, v140, v141 op_sel:[0,0,1]
	v_pk_fma_f32 v[124:125], v[124:125], v[20:21], v[24:25]
	v_cvt_pk_fp8_f32 v122, v108, v109 op_sel:[0,0,1]
	v_pk_fma_f32 v[92:93], v[92:93], v[4:5], v[8:9]
	v_pk_mul_f32 v[96:97], v[200:201], v[96:97] op_sel_hi:[0,1]
	v_med3_f32 v178, v184, s49, v199
	v_med3_f32 v179, v185, s49, v199
	v_med3_f32 v152, v152, s49, v199
	v_med3_f32 v153, v153, s49, v199
	v_med3_f32 v124, v124, s49, v199
	v_med3_f32 v125, v125, s49, v199
	v_pk_fma_f32 v[96:97], v[4:5], v[96:97], v[8:9]
	v_med3_f32 v92, v92, s49, v199
	v_med3_f32 v93, v93, s49, v199
	v_cvt_pk_fp8_f32 v182, v178, v179 op_sel:[0,0,1]
	v_cvt_pk_fp8_f32 v162, v152, v153 op_sel:[0,0,1]
	v_cvt_pk_fp8_f32 v138, v124, v125 op_sel:[0,0,1]
	v_cvt_pk_fp8_f32 v106, v92, v93 op_sel:[0,0,1]
	v_med3_f32 v90, v96, s49, v199
	v_med3_f32 v91, v97, s49, v199
	v_lshl_add_u64 v[188:189], s[52:53], 0, v[196:197]
	v_lshl_add_u64 v[178:179], s[14:15], 0, v[196:197]
	v_cvt_pk_fp8_f32 v94, v90, v91 op_sel:[0,0,1]
	global_store_dword v[188:189], v216, off
	global_store_dword v[178:179], v190, off
	global_store_dword v[188:189], v186, off offset:256
	global_store_dword v[178:179], v182, off offset:256
	global_store_dword v[188:189], v180, off offset:512
	global_store_dword v[178:179], v174, off offset:512
	global_store_dword v[188:189], v162, off offset:768
	global_store_dword v[178:179], v158, off offset:768
	global_store_dword v[188:189], v150, off offset:1024
	global_store_dword v[178:179], v142, off offset:1024
	global_store_dword v[188:189], v138, off offset:1280
	global_store_dword v[178:179], v126, off offset:1280
	global_store_dword v[188:189], v122, off offset:1536
	global_store_dword v[178:179], v110, off offset:1536
	global_store_dword v[188:189], v106, off offset:1792
	global_store_dword v[178:179], v94, off offset:1792
	s_waitcnt vmcnt(0)
	v_readlane_b32 s8, v254, 18
	v_mul_f32_e32 v90, v167, v167
	v_mul_f32_e32 v92, v147, v147
	v_fmac_f32_e32 v90, v166, v166
	v_fmac_f32_e32 v92, v146, v146
	v_fmac_f32_e32 v90, v168, v168
	v_fmac_f32_e32 v92, v148, v148
	v_fmac_f32_e32 v90, v169, v169
	v_fmac_f32_e32 v92, v149, v149
	v_mul_f32_e32 v91, v171, v171
	v_add_f32_e32 v90, v90, v92
	v_mul_f32_e32 v92, v155, v155
	v_fmac_f32_e32 v91, v170, v170
	v_fmac_f32_e32 v92, v154, v154
	v_fmac_f32_e32 v91, v172, v172
	v_fmac_f32_e32 v92, v156, v156
	v_fmac_f32_e32 v91, v173, v173
	v_fmac_f32_e32 v92, v157, v157
	v_add_f32_e32 v91, v91, v92
	v_mul_f32_e32 v92, v131, v131
	v_fmac_f32_e32 v92, v130, v130
	v_fmac_f32_e32 v92, v132, v132
	v_fmac_f32_e32 v92, v133, v133
	v_add_f32_e32 v90, v90, v92
	v_mul_f32_e32 v92, v135, v135
	v_fmac_f32_e32 v92, v134, v134
	v_fmac_f32_e32 v92, v136, v136
	v_fmac_f32_e32 v92, v137, v137
	v_add_f32_e32 v91, v91, v92
	v_mul_f32_e32 v92, v115, v115
	v_fmac_f32_e32 v92, v114, v114
	v_fmac_f32_e32 v92, v116, v116
	v_fmac_f32_e32 v92, v117, v117
	v_add_f32_e32 v90, v90, v92
	v_mul_f32_e32 v92, v119, v119
	v_fmac_f32_e32 v92, v118, v118
	v_fmac_f32_e32 v92, v120, v120
	v_fmac_f32_e32 v92, v121, v121
	v_add_f32_e32 v94, v91, v92
	v_mul_f32_e32 v91, v99, v99
	v_fmac_f32_e32 v91, v98, v98
	v_fmac_f32_e32 v91, v100, v100
	v_fmac_f32_e32 v91, v101, v101
	v_add_f32_e32 v90, v90, v91
	v_mul_f32_e32 v91, v83, v83
	v_fmac_f32_e32 v91, v82, v82
	v_fmac_f32_e32 v91, v84, v84
	v_fmac_f32_e32 v91, v85, v85
	v_mov_b32_e32 v92, v75
	v_mov_b32_e32 v93, v67
	v_add_f32_e32 v95, v90, v91
	v_mov_b32_e32 v90, v74
	v_mov_b32_e32 v91, v66
	v_pk_mul_f32 v[92:93], v[92:93], v[92:93]
	v_readlane_b32 s9, v254, 19
	v_pk_fma_f32 v[90:91], v[90:91], v[90:91], v[92:93]
	v_mov_b32_e32 v92, v76
	v_mov_b32_e32 v93, v68
	v_pk_fma_f32 v[90:91], v[92:93], v[92:93], v[90:91]
	v_mov_b32_e32 v92, v77
	v_mov_b32_e32 v93, v69
	v_pk_fma_f32 v[90:91], v[92:93], v[92:93], v[90:91]
	v_mul_f32_e32 v92, v103, v103
	v_add_f32_e32 v90, v95, v90
	v_add_f32_e32 v90, v90, v91
	ds_bpermute_b32 v91, v208, v90
	v_fmac_f32_e32 v92, v102, v102
	v_mul_f32_e32 v93, v87, v87
	v_fmac_f32_e32 v92, v104, v104
	v_fmac_f32_e32 v93, v86, v86
	s_waitcnt lgkmcnt(0)
	v_add_f32_e32 v90, v90, v91
	ds_bpermute_b32 v91, v209, v90
	v_fmac_f32_e32 v92, v105, v105
	v_fmac_f32_e32 v93, v88, v88
	v_add_f32_e32 v92, v94, v92
	v_fmac_f32_e32 v93, v89, v89
	s_waitcnt lgkmcnt(0)
	v_add_f32_e32 v94, v90, v91
	ds_bpermute_b32 v95, v210, v94
	v_add_f32_e32 v96, v92, v93
	v_mov_b32_e32 v92, v79
	v_mov_b32_e32 v93, v71
	v_mov_b32_e32 v90, v78
	v_mov_b32_e32 v91, v70
	v_pk_mul_f32 v[92:93], v[92:93], v[92:93]
	s_waitcnt lgkmcnt(0)
	v_add_f32_e32 v94, v94, v95
	v_pk_fma_f32 v[90:91], v[90:91], v[90:91], v[92:93]
	v_mov_b32_e32 v92, v80
	v_mov_b32_e32 v93, v72
	v_pk_fma_f32 v[90:91], v[92:93], v[92:93], v[90:91]
	v_mov_b32_e32 v92, v81
	v_mov_b32_e32 v93, v73
	v_pk_fma_f32 v[90:91], v[92:93], v[92:93], v[90:91]
	ds_bpermute_b32 v95, v211, v94
	v_add_f32_e32 v90, v96, v90
	v_add_f32_e32 v90, v90, v91
	ds_bpermute_b32 v93, v208, v90
	s_add_u32 s52, s3, s8
	s_waitcnt lgkmcnt(1)
	v_add_f32_e32 v94, v94, v95
	ds_bpermute_b32 v95, v213, v94
	s_addc_u32 s53, s33, s9
	s_waitcnt lgkmcnt(1)
	v_add_f32_e32 v90, v90, v93
	ds_bpermute_b32 v93, v209, v90
	s_waitcnt lgkmcnt(1)
	v_add_f32_e32 v94, v94, v95
	ds_bpermute_b32 v95, v214, v94
	s_waitcnt lgkmcnt(1)
	v_add_f32_e32 v90, v90, v93
	ds_bpermute_b32 v93, v210, v90
	s_waitcnt lgkmcnt(1)
	v_add_f32_e32 v91, v94, v95
	v_fmamk_f32 v91, v91, 0x3a000000, v212
	v_mul_f32_e32 v92, 0x4f800000, v91
	s_waitcnt lgkmcnt(0)
	v_add_f32_e32 v90, v90, v93
	v_cmp_gt_f32_e32 vcc, s58, v91
	ds_bpermute_b32 v93, v211, v90
	s_waitcnt lgkmcnt(0)
	v_add_f32_e32 v90, v90, v93
	v_cndmask_b32_e32 v91, v91, v92, vcc
	v_sqrt_f32_e32 v92, v91
	ds_bpermute_b32 v93, v213, v90
	v_add_u32_e32 v94, -1, v92
	v_fma_f32 v95, -v94, v92, v91
	v_cmp_ge_f32_e64 s[6:7], 0, v95
	v_add_u32_e32 v95, 1, v92
	s_waitcnt lgkmcnt(0)
	v_add_f32_e32 v90, v90, v93
	v_cndmask_b32_e64 v94, v92, v94, s[6:7]
	v_fma_f32 v92, -v95, v92, v91
	v_cmp_lt_f32_e64 s[6:7], 0, v92
	ds_bpermute_b32 v93, v214, v90
	s_waitcnt lgkmcnt(0)
	v_add_f32_e32 v90, v90, v93
	v_cndmask_b32_e64 v92, v94, v95, s[6:7]
	v_mul_f32_e32 v94, 0x37800000, v92
	v_cndmask_b32_e32 v92, v92, v94, vcc
	v_cmp_class_f32_e32 vcc, v91, v215
	v_fmac_f32_e32 v212, 0x3a000000, v90
	v_mul_f32_e32 v90, 0x4f800000, v212
	v_cndmask_b32_e32 v91, v92, v91, vcc
	v_div_scale_f32 v92, s[6:7], v91, v91, 1.0
	v_rcp_f32_e32 v94, v92
	v_readlane_b32 s6, v254, 20
	v_readlane_b32 s7, v254, 21
	s_add_u32 s14, s3, s6
	s_addc_u32 s15, s33, s7
	v_cmp_gt_f32_e64 s[6:7], s58, v212
	v_fma_f32 v95, -v92, v94, 1.0
	v_fmac_f32_e32 v94, v95, v94
	v_cndmask_b32_e64 v90, v212, v90, s[6:7]
	v_div_scale_f32 v95, vcc, 1.0, v91, 1.0
	v_sqrt_f32_e32 v93, v90
	v_mul_f32_e32 v96, v95, v94
	v_fma_f32 v97, -v92, v96, v95
	v_fmac_f32_e32 v96, v97, v94
	v_fma_f32 v92, -v92, v96, v95
	v_add_u32_e32 v95, -1, v93
	v_fma_f32 v97, -v95, v93, v90
	v_cmp_ge_f32_e64 s[8:9], 0, v97
	v_add_u32_e32 v97, 1, v93
	s_nop 0
	v_cndmask_b32_e64 v95, v93, v95, s[8:9]
	v_fma_f32 v93, -v97, v93, v90
	v_cmp_lt_f32_e64 s[8:9], 0, v93
	s_nop 1
	v_cndmask_b32_e64 v93, v95, v97, s[8:9]
	v_mul_f32_e32 v95, 0x37800000, v93
	v_cndmask_b32_e64 v93, v93, v95, s[6:7]
	v_cmp_class_f32_e64 s[6:7], v90, v215
	s_nop 1
	v_cndmask_b32_e64 v93, v93, v90, s[6:7]
	v_div_scale_f32 v95, s[6:7], v93, v93, 1.0
	v_rcp_f32_e32 v97, v95
	v_div_fmas_f32 v90, v92, v94, v96
	v_div_fixup_f32 v90, v90, v91, 1.0
	s_mov_b64 s[6:7], 0
	v_fma_f32 v91, -v95, v97, 1.0
	v_fmac_f32_e32 v97, v91, v97
	v_div_scale_f32 v91, vcc, 1.0, v93, 1.0
	v_mul_f32_e32 v92, v91, v97
	v_fma_f32 v94, -v95, v92, v91
	v_fmac_f32_e32 v92, v94, v97
	v_fma_f32 v91, -v95, v92, v91
	v_div_fmas_f32 v91, v91, v97, v92
	v_div_fixup_f32 v92, v91, v93, 1.0
	v_pk_mul_f32 v[94:95], v[90:91], v[166:167] op_sel_hi:[0,1]
	v_pk_mul_f32 v[96:97], v[90:91], v[168:169] op_sel_hi:[0,1]
	v_pk_fma_f32 v[94:95], v[94:95], v[58:59], v[62:63]
	v_pk_mul_f32 v[106:107], v[92:93], v[170:171] op_sel_hi:[0,1]
	v_pk_mul_f32 v[108:109], v[92:93], v[172:173] op_sel_hi:[0,1]
	v_pk_fma_f32 v[96:97], v[96:97], v[60:61], v[64:65]
	v_pk_fma_f32 v[60:61], v[60:61], v[108:109], v[64:65]
	v_med3_f32 v64, v94, s49, v199
	v_med3_f32 v65, v95, s49, v199
	v_pk_fma_f32 v[58:59], v[58:59], v[106:107], v[62:63]
	v_cvt_pk_fp8_f32 v91, v64, v65
	v_med3_f32 v58, v58, s49, v199
	v_med3_f32 v59, v59, s49, v199
	v_cvt_pk_fp8_f32 v93, v58, v59
	v_med3_f32 v62, v96, s49, v199
	v_med3_f32 v63, v97, s49, v199
	v_cvt_pk_fp8_f32 v91, v62, v63 op_sel:[0,0,1]
	v_med3_f32 v58, v60, s49, v199
	v_med3_f32 v59, v61, s49, v199
	v_cvt_pk_fp8_f32 v93, v58, v59 op_sel:[0,0,1]
	v_pk_mul_f32 v[58:59], v[90:91], v[146:147] op_sel_hi:[0,1]
	v_pk_fma_f32 v[58:59], v[58:59], v[50:51], v[54:55]
	v_pk_mul_f32 v[60:61], v[90:91], v[148:149] op_sel_hi:[0,1]
	v_pk_mul_f32 v[64:65], v[92:93], v[154:155] op_sel_hi:[0,1]
	v_pk_fma_f32 v[50:51], v[50:51], v[64:65], v[54:55]
	v_med3_f32 v54, v58, s49, v199
	v_med3_f32 v55, v59, s49, v199
	v_cvt_pk_fp8_f32 v58, v54, v55
	v_med3_f32 v50, v50, s49, v199
	v_med3_f32 v51, v51, s49, v199
	v_pk_fma_f32 v[60:61], v[60:61], v[52:53], v[56:57]
	v_pk_mul_f32 v[94:95], v[92:93], v[156:157] op_sel_hi:[0,1]
	v_cvt_pk_fp8_f32 v54, v50, v51
	v_pk_fma_f32 v[52:53], v[52:53], v[94:95], v[56:57]
	v_med3_f32 v56, v60, s49, v199
	v_med3_f32 v57, v61, s49, v199
	v_cvt_pk_fp8_f32 v58, v56, v57 op_sel:[0,0,1]
	v_med3_f32 v50, v52, s49, v199
	v_med3_f32 v51, v53, s49, v199
	v_pk_mul_f32 v[52:53], v[90:91], v[130:131] op_sel_hi:[0,1]
	v_pk_mul_f32 v[56:57], v[92:93], v[134:135] op_sel_hi:[0,1]
	v_pk_fma_f32 v[52:53], v[52:53], v[42:43], v[46:47]
	v_pk_fma_f32 v[42:43], v[42:43], v[56:57], v[46:47]
	v_cvt_pk_fp8_f32 v54, v50, v51 op_sel:[0,0,1]
	v_med3_f32 v47, v53, s49, v199
	v_med3_f32 v42, v42, s49, v199
	v_med3_f32 v43, v43, s49, v199
	v_lshl_add_u64 v[62:63], s[52:53], 0, v[196:197]
	v_lshl_add_u64 v[50:51], s[14:15], 0, v[196:197]
	v_cvt_pk_fp8_f32 v53, v42, v43
	global_store_dword v[62:63], v91, off
	global_store_dword v[50:51], v93, off
	global_store_dword v[62:63], v58, off offset:256
	global_store_dword v[50:51], v54, off offset:256
	v_pk_mul_f32 v[54:55], v[90:91], v[132:133] op_sel_hi:[0,1]
	v_pk_mul_f32 v[58:59], v[92:93], v[136:137] op_sel_hi:[0,1]
	v_pk_fma_f32 v[54:55], v[54:55], v[44:45], v[48:49]
	v_pk_fma_f32 v[44:45], v[44:45], v[58:59], v[48:49]
	v_med3_f32 v46, v52, s49, v199
	v_med3_f32 v42, v44, s49, v199
	v_med3_f32 v43, v45, s49, v199
	v_cvt_pk_fp8_f32 v53, v42, v43 op_sel:[0,0,1]
	v_pk_mul_f32 v[42:43], v[90:91], v[114:115] op_sel_hi:[0,1]
	v_cvt_pk_fp8_f32 v52, v46, v47
	v_pk_fma_f32 v[42:43], v[42:43], v[34:35], v[38:39]
	v_pk_mul_f32 v[46:47], v[92:93], v[118:119] op_sel_hi:[0,1]
	v_pk_fma_f32 v[34:35], v[34:35], v[46:47], v[38:39]
	v_med3_f32 v38, v42, s49, v199
	v_med3_f32 v39, v43, s49, v199
	v_cvt_pk_fp8_f32 v42, v38, v39
	v_med3_f32 v34, v34, s49, v199
	v_med3_f32 v35, v35, s49, v199
	v_med3_f32 v48, v54, s49, v199
	v_med3_f32 v49, v55, s49, v199
	v_pk_mul_f32 v[44:45], v[90:91], v[116:117] op_sel_hi:[0,1]
	v_cvt_pk_fp8_f32 v38, v34, v35
	v_cvt_pk_fp8_f32 v52, v48, v49 op_sel:[0,0,1]
	v_pk_fma_f32 v[44:45], v[44:45], v[36:37], v[40:41]
	v_pk_mul_f32 v[48:49], v[92:93], v[120:121] op_sel_hi:[0,1]
	v_pk_fma_f32 v[36:37], v[36:37], v[48:49], v[40:41]
	v_med3_f32 v40, v44, s49, v199
	v_med3_f32 v41, v45, s49, v199
	v_cvt_pk_fp8_f32 v42, v40, v41 op_sel:[0,0,1]
	v_med3_f32 v34, v36, s49, v199
	v_med3_f32 v35, v37, s49, v199
	v_cvt_pk_fp8_f32 v38, v34, v35 op_sel:[0,0,1]
	global_store_dword v[62:63], v52, off offset:512
	global_store_dword v[50:51], v53, off offset:512
	global_store_dword v[62:63], v42, off offset:768
	global_store_dword v[50:51], v38, off offset:768
	v_pk_mul_f32 v[34:35], v[90:91], v[98:99] op_sel_hi:[0,1]
	v_pk_mul_f32 v[38:39], v[92:93], v[102:103] op_sel_hi:[0,1]
	v_pk_fma_f32 v[34:35], v[34:35], v[26:27], v[30:31]
	v_pk_fma_f32 v[26:27], v[26:27], v[38:39], v[30:31]
	v_med3_f32 v31, v35, s49, v199
	v_med3_f32 v26, v26, s49, v199
	v_med3_f32 v27, v27, s49, v199
	v_cvt_pk_fp8_f32 v35, v26, v27
	v_pk_mul_f32 v[36:37], v[90:91], v[100:101] op_sel_hi:[0,1]
	v_pk_mul_f32 v[40:41], v[92:93], v[104:105] op_sel_hi:[0,1]
	v_pk_fma_f32 v[36:37], v[36:37], v[28:29], v[32:33]
	v_pk_fma_f32 v[28:29], v[28:29], v[40:41], v[32:33]
	v_med3_f32 v30, v34, s49, v199
	v_med3_f32 v26, v28, s49, v199
	v_med3_f32 v27, v29, s49, v199
	v_cvt_pk_fp8_f32 v35, v26, v27 op_sel:[0,0,1]
	v_pk_mul_f32 v[26:27], v[90:91], v[82:83] op_sel_hi:[0,1]
	v_cvt_pk_fp8_f32 v34, v30, v31
	v_pk_fma_f32 v[26:27], v[26:27], v[18:19], v[22:23]
	v_pk_mul_f32 v[30:31], v[92:93], v[86:87] op_sel_hi:[0,1]
	v_pk_fma_f32 v[18:19], v[18:19], v[30:31], v[22:23]
	v_med3_f32 v22, v26, s49, v199
	v_med3_f32 v23, v27, s49, v199
	v_cvt_pk_fp8_f32 v26, v22, v23
	v_med3_f32 v18, v18, s49, v199
	v_med3_f32 v19, v19, s49, v199
	v_med3_f32 v32, v36, s49, v199
	v_med3_f32 v33, v37, s49, v199
	v_pk_mul_f32 v[28:29], v[90:91], v[84:85] op_sel_hi:[0,1]
	v_cvt_pk_fp8_f32 v22, v18, v19
	v_cvt_pk_fp8_f32 v34, v32, v33 op_sel:[0,0,1]
	v_pk_fma_f32 v[28:29], v[28:29], v[20:21], v[24:25]
	v_pk_mul_f32 v[32:33], v[92:93], v[88:89] op_sel_hi:[0,1]
	v_pk_fma_f32 v[20:21], v[20:21], v[32:33], v[24:25]
	v_med3_f32 v24, v28, s49, v199
	v_med3_f32 v25, v29, s49, v199
	v_cvt_pk_fp8_f32 v26, v24, v25 op_sel:[0,0,1]
	v_med3_f32 v18, v20, s49, v199
	v_med3_f32 v19, v21, s49, v199
	v_cvt_pk_fp8_f32 v22, v18, v19 op_sel:[0,0,1]
	global_store_dword v[62:63], v34, off offset:1024
	global_store_dword v[50:51], v35, off offset:1024
	global_store_dword v[62:63], v26, off offset:1280
	global_store_dword v[50:51], v22, off offset:1280
	v_pk_mul_f32 v[18:19], v[90:91], v[74:75] op_sel_hi:[0,1]
	v_pk_mul_f32 v[22:23], v[92:93], v[78:79] op_sel_hi:[0,1]
	v_pk_fma_f32 v[18:19], v[18:19], v[10:11], v[14:15]
	v_pk_fma_f32 v[10:11], v[10:11], v[22:23], v[14:15]
	v_med3_f32 v15, v19, s49, v199
	v_med3_f32 v10, v10, s49, v199
	v_med3_f32 v11, v11, s49, v199
	v_cvt_pk_fp8_f32 v19, v10, v11
	v_pk_mul_f32 v[20:21], v[90:91], v[76:77] op_sel_hi:[0,1]
	v_pk_mul_f32 v[24:25], v[92:93], v[80:81] op_sel_hi:[0,1]
	v_pk_fma_f32 v[20:21], v[20:21], v[12:13], v[16:17]
	v_pk_fma_f32 v[12:13], v[12:13], v[24:25], v[16:17]
	v_med3_f32 v14, v18, s49, v199
	v_med3_f32 v10, v12, s49, v199
	v_med3_f32 v11, v13, s49, v199
	v_cvt_pk_fp8_f32 v19, v10, v11 op_sel:[0,0,1]
	v_pk_mul_f32 v[10:11], v[90:91], v[66:67] op_sel_hi:[0,1]
	v_cvt_pk_fp8_f32 v18, v14, v15
	v_pk_fma_f32 v[10:11], v[10:11], v[2:3], v[6:7]
	v_pk_mul_f32 v[14:15], v[92:93], v[70:71] op_sel_hi:[0,1]
	v_pk_fma_f32 v[2:3], v[2:3], v[14:15], v[6:7]
	v_med3_f32 v6, v10, s49, v199
	v_med3_f32 v7, v11, s49, v199
	v_cvt_pk_fp8_f32 v10, v6, v7
	v_med3_f32 v2, v2, s49, v199
	v_med3_f32 v3, v3, s49, v199
	v_med3_f32 v16, v20, s49, v199
	v_med3_f32 v17, v21, s49, v199
	v_pk_mul_f32 v[12:13], v[90:91], v[68:69] op_sel_hi:[0,1]
	v_cvt_pk_fp8_f32 v6, v2, v3
	v_cvt_pk_fp8_f32 v18, v16, v17 op_sel:[0,0,1]
	v_pk_fma_f32 v[12:13], v[12:13], v[4:5], v[8:9]
	v_pk_mul_f32 v[16:17], v[92:93], v[72:73] op_sel_hi:[0,1]
	v_pk_fma_f32 v[4:5], v[4:5], v[16:17], v[8:9]
	v_med3_f32 v8, v12, s49, v199
	v_med3_f32 v9, v13, s49, v199
	v_cvt_pk_fp8_f32 v10, v8, v9 op_sel:[0,0,1]
	v_med3_f32 v2, v4, s49, v199
	v_med3_f32 v3, v5, s49, v199
	v_cvt_pk_fp8_f32 v6, v2, v3 op_sel:[0,0,1]
	global_store_dword v[62:63], v18, off offset:1536
	global_store_dword v[50:51], v19, off offset:1536
	global_store_dword v[62:63], v10, off offset:1792
	global_store_dword v[50:51], v6, off offset:1792

; __global__ void __launch_bounds__(NWAVES * 64, 2) fwd_kernel(Args args) {
;     ...
;                 for (int i = 0; i < RPW; i += 2) {
;                     N1_ROWS(i, row, row2); if (row >= T) break;
;                     f32x4 v[8], w[8];
;                     const float* xr = x + (size_t)row * D + 4 * lane; const float* xr2 = x + (size_t)row2 * D + 4 * lane;
; #pragma unroll
;                     for (int j = 0; j < 8; ++j) { v[j] = *(const f32x4*)(xr + 256 * j); w[j] = *(const f32x4*)(xr2 + 256 * j); }
;                     N1_VECS(row); N1_BODY(v, w, row, row2);
.LBB0_171:
	s_waitcnt vmcnt(15)
	v_mul_f32_e32 v130, v83, v83
	s_waitcnt vmcnt(14)
	v_mul_f32_e32 v132, v75, v75
	v_fmac_f32_e32 v130, v82, v82
	v_fmac_f32_e32 v132, v74, v74
	v_fmac_f32_e32 v130, v84, v84
	v_fmac_f32_e32 v132, v76, v76
	v_fmac_f32_e32 v130, v85, v85
	v_fmac_f32_e32 v132, v77, v77
	s_waitcnt vmcnt(13)
	v_mul_f32_e32 v131, v79, v79
	v_add_f32_e32 v130, v130, v132
	s_waitcnt vmcnt(12)
	v_mul_f32_e32 v132, v67, v67
	v_fmac_f32_e32 v131, v78, v78
	v_fmac_f32_e32 v132, v66, v66
	v_fmac_f32_e32 v131, v80, v80
	v_fmac_f32_e32 v132, v68, v68
	v_fmac_f32_e32 v131, v81, v81
	v_fmac_f32_e32 v132, v69, v69
	v_add_f32_e32 v131, v131, v132
	s_waitcnt vmcnt(11)
	v_mul_f32_e32 v132, v63, v63
	v_fmac_f32_e32 v132, v62, v62
	v_fmac_f32_e32 v132, v64, v64
	v_fmac_f32_e32 v132, v65, v65
	v_add_f32_e32 v130, v130, v132
	s_waitcnt vmcnt(10)
	v_mul_f32_e32 v132, v59, v59
	v_fmac_f32_e32 v132, v58, v58
	v_fmac_f32_e32 v132, v60, v60
	v_fmac_f32_e32 v132, v61, v61
	v_add_f32_e32 v131, v131, v132
	s_waitcnt vmcnt(8)
	v_mul_f32_e32 v132, v55, v55
	v_fmac_f32_e32 v132, v54, v54
	v_fmac_f32_e32 v132, v56, v56
	v_fmac_f32_e32 v132, v57, v57
	v_add_f32_e32 v130, v130, v132
	v_mul_f32_e32 v132, v47, v47
	v_fmac_f32_e32 v132, v46, v46
	v_fmac_f32_e32 v132, v48, v48
	v_fmac_f32_e32 v132, v49, v49
	v_add_f32_e32 v192, v131, v132
	s_waitcnt vmcnt(7)
	v_mul_f32_e32 v131, v43, v43
	v_fmac_f32_e32 v131, v42, v42
	v_fmac_f32_e32 v131, v44, v44
	v_fmac_f32_e32 v131, v45, v45
	v_add_f32_e32 v130, v130, v131
	s_waitcnt vmcnt(4)
	v_mul_f32_e32 v131, v35, v35
	v_fmac_f32_e32 v131, v34, v34
	v_fmac_f32_e32 v131, v36, v36
	v_fmac_f32_e32 v131, v37, v37
	s_waitcnt vmcnt(3)
	v_mov_b32_e32 v132, v23
	s_waitcnt vmcnt(2)
	v_mov_b32_e32 v133, v15
	v_add_f32_e32 v193, v130, v131
	v_mov_b32_e32 v130, v22
	v_mov_b32_e32 v131, v14
	v_pk_mul_f32 v[132:133], v[132:133], v[132:133]
	s_lshl_b64 s[58:59], s[8:9], 11
	v_pk_fma_f32 v[130:131], v[130:131], v[130:131], v[132:133]
	v_mov_b32_e32 v132, v24
	v_mov_b32_e32 v133, v16
	v_pk_fma_f32 v[130:131], v[132:133], v[132:133], v[130:131]
	v_mov_b32_e32 v132, v25
	v_mov_b32_e32 v133, v17
	v_pk_fma_f32 v[130:131], v[132:133], v[132:133], v[130:131]
	v_mul_f32_e32 v132, v39, v39
	v_add_f32_e32 v130, v193, v130
	v_add_f32_e32 v130, v130, v131
	v_and_b32_e32 v131, 64, v208
	v_add_u32_e32 v193, 64, v131
	v_xor_b32_e32 v131, 1, v208
	v_cmp_lt_i32_e32 vcc, v131, v193
	v_fmac_f32_e32 v132, v38, v38
	v_fmac_f32_e32 v132, v40, v40
	v_cndmask_b32_e32 v131, v208, v131, vcc
	v_lshlrev_b32_e32 v198, 2, v131
	ds_bpermute_b32 v131, v198, v130
	v_fmac_f32_e32 v132, v41, v41
	v_add_f32_e32 v132, v192, v132
	v_mul_f32_e32 v133, v31, v31
	v_fmac_f32_e32 v133, v30, v30
	s_waitcnt lgkmcnt(0)
	v_add_f32_e32 v130, v130, v131
	v_xor_b32_e32 v131, 2, v208
	v_cmp_lt_i32_e32 vcc, v131, v193
	v_fmac_f32_e32 v133, v32, v32
	v_fmac_f32_e32 v133, v33, v33
	v_cndmask_b32_e32 v131, v208, v131, vcc
	v_lshlrev_b32_e32 v199, 2, v131
	ds_bpermute_b32 v131, v199, v130
	v_add_f32_e32 v212, v132, v133
	v_xor_b32_e32 v132, 8, v208
	s_waitcnt vmcnt(0)
	v_mov_b32_e32 v133, v11
	s_waitcnt lgkmcnt(0)
	v_add_f32_e32 v192, v130, v131
	v_xor_b32_e32 v130, 4, v208
	v_cmp_lt_i32_e32 vcc, v130, v193
	v_mov_b32_e32 v131, v10
	s_nop 0
	v_cndmask_b32_e32 v130, v208, v130, vcc
	v_lshlrev_b32_e32 v210, 2, v130
	ds_bpermute_b32 v211, v210, v192
	v_cmp_lt_i32_e32 vcc, v132, v193
	v_mov_b32_e32 v130, v18
	s_waitcnt lgkmcnt(0)
	v_add_f32_e32 v192, v192, v211
	v_cndmask_b32_e32 v132, v208, v132, vcc
	v_lshlrev_b32_e32 v211, 2, v132
	ds_bpermute_b32 v213, v211, v192
	v_mov_b32_e32 v132, v19
	v_pk_mul_f32 v[132:133], v[132:133], v[132:133]
	s_waitcnt lgkmcnt(0)
	v_add_f32_e32 v192, v192, v213
	v_pk_fma_f32 v[130:131], v[130:131], v[130:131], v[132:133]
	v_xor_b32_e32 v132, 16, v208
	v_cmp_lt_i32_e32 vcc, v132, v193
	v_mov_b32_e32 v133, v12
	s_nop 0
	v_cndmask_b32_e32 v132, v208, v132, vcc
	v_lshlrev_b32_e32 v213, 2, v132
	v_mov_b32_e32 v132, v20
	v_pk_fma_f32 v[130:131], v[132:133], v[132:133], v[130:131]
	v_xor_b32_e32 v133, 32, v208
	v_cmp_lt_i32_e32 vcc, v133, v193
	v_mov_b32_e32 v132, v21
	ds_bpermute_b32 v214, v213, v192
	v_cndmask_b32_e32 v133, v208, v133, vcc
	v_lshlrev_b32_e32 v193, 2, v133
	v_mov_b32_e32 v133, v13
	v_pk_fma_f32 v[130:131], v[132:133], v[132:133], v[130:131]
	s_waitcnt lgkmcnt(0)
	v_add_f32_e32 v192, v192, v214
	v_add_f32_e32 v130, v212, v130
	v_add_f32_e32 v130, v130, v131
	ds_bpermute_b32 v133, v198, v130
	ds_bpermute_b32 v214, v193, v192
	s_waitcnt lgkmcnt(1)
	v_add_f32_e32 v130, v130, v133
	ds_bpermute_b32 v133, v199, v130
	s_waitcnt lgkmcnt(1)
	v_add_f32_e32 v131, v192, v214
	v_fmamk_f32 v131, v131, 0x3a000000, v135
	v_mul_f32_e32 v132, 0x4f800000, v131
	v_cmp_gt_f32_e32 vcc, s49, v131
	s_waitcnt lgkmcnt(0)
	v_add_f32_e32 v130, v130, v133
	ds_bpermute_b32 v133, v210, v130
	v_cndmask_b32_e32 v131, v131, v132, vcc
	v_sqrt_f32_e32 v132, v131
	s_waitcnt lgkmcnt(0)
	v_add_f32_e32 v130, v130, v133
	ds_bpermute_b32 v133, v211, v130
	v_add_u32_e32 v192, -1, v132
	v_fma_f32 v198, -v192, v132, v131
	v_cmp_ge_f32_e64 s[6:7], 0, v198
	v_add_u32_e32 v198, 1, v132
	s_waitcnt lgkmcnt(0)
	v_add_f32_e32 v130, v130, v133
	ds_bpermute_b32 v133, v213, v130
	v_cndmask_b32_e64 v192, v132, v192, s[6:7]
	v_fma_f32 v132, -v198, v132, v131
	v_cmp_lt_f32_e64 s[6:7], 0, v132
	s_waitcnt lgkmcnt(0)
	v_add_f32_e32 v130, v130, v133
	v_cndmask_b32_e64 v132, v192, v198, s[6:7]
	v_mul_f32_e32 v192, 0x37800000, v132
	ds_bpermute_b32 v133, v193, v130
	v_cndmask_b32_e32 v132, v132, v192, vcc
	v_cmp_class_f32_e32 vcc, v131, v200
	s_waitcnt lgkmcnt(0)
	v_add_f32_e32 v130, v130, v133
	v_cndmask_b32_e32 v131, v132, v131, vcc
	v_div_scale_f32 v132, s[6:7], v131, v131, 1.0
	v_rcp_f32_e32 v192, v132
	v_fmamk_f32 v130, v130, 0x3a000000, v135
	v_mul_f32_e32 v133, 0x4f800000, v130
	v_cmp_gt_f32_e64 s[6:7], s49, v130
	v_fma_f32 v198, -v132, v192, 1.0
	v_fmac_f32_e32 v192, v198, v192
	v_cndmask_b32_e64 v130, v130, v133, s[6:7]
	v_div_scale_f32 v193, vcc, 1.0, v131, 1.0
	v_sqrt_f32_e32 v133, v130
	v_mul_f32_e32 v198, v193, v192
	v_fma_f32 v199, -v132, v198, v193
	v_fmac_f32_e32 v198, v199, v192
	v_fma_f32 v132, -v132, v198, v193
	v_add_u32_e32 v193, -1, v133
	v_fma_f32 v199, -v193, v133, v130
	v_cmp_ge_f32_e64 s[8:9], 0, v199
	v_add_u32_e32 v199, 1, v133
	s_nop 0
	v_cndmask_b32_e64 v193, v133, v193, s[8:9]
	v_fma_f32 v133, -v199, v133, v130
	v_cmp_lt_f32_e64 s[8:9], 0, v133
	s_nop 1
	v_cndmask_b32_e64 v133, v193, v199, s[8:9]
	v_mul_f32_e32 v193, 0x37800000, v133
	v_cndmask_b32_e64 v133, v133, v193, s[6:7]
	v_cmp_class_f32_e64 s[6:7], v130, v200
	s_nop 1
	v_cndmask_b32_e64 v133, v133, v130, s[6:7]
	v_div_scale_f32 v193, s[6:7], v133, v133, 1.0
	v_rcp_f32_e32 v199, v193
	v_div_fmas_f32 v130, v132, v192, v198
	v_div_fixup_f32 v130, v130, v131, 1.0
	s_add_u32 s6, s3, s58
	v_fma_f32 v131, -v193, v199, 1.0
	v_fmac_f32_e32 v199, v131, v199
	v_div_scale_f32 v131, vcc, 1.0, v133, 1.0
	v_mul_f32_e32 v132, v131, v199
	v_fma_f32 v192, -v193, v132, v131
	v_fmac_f32_e32 v132, v192, v199
	v_fma_f32 v131, -v193, v132, v131
	v_div_fmas_f32 v131, v131, v199, v132
	v_pk_mul_f32 v[82:83], v[130:131], v[82:83] op_sel_hi:[0,1]
	v_pk_fma_f32 v[82:83], v[82:83], v[6:7], v[2:3]
	v_div_fixup_f32 v132, v131, v133, 1.0
	v_pk_mul_f32 v[84:85], v[130:131], v[84:85] op_sel_hi:[0,1]
	v_med3_f32 v82, v82, s52, v209
	v_med3_f32 v83, v83, s52, v209
	v_cvt_pk_fp8_f32 v131, v82, v83
	v_pk_fma_f32 v[84:85], v[84:85], v[8:9], v[4:5]
	v_pk_mul_f32 v[78:79], v[132:133], v[78:79] op_sel_hi:[0,1]
	v_med3_f32 v82, v84, s52, v209
	v_med3_f32 v83, v85, s52, v209
	v_cvt_pk_fp8_f32 v131, v82, v83 op_sel:[0,0,1]
	v_pk_mul_f32 v[80:81], v[132:133], v[80:81] op_sel_hi:[0,1]
	v_pk_fma_f32 v[78:79], v[6:7], v[78:79], v[2:3]
	v_pk_fma_f32 v[80:81], v[8:9], v[80:81], v[4:5]
	v_pk_mul_f32 v[74:75], v[130:131], v[74:75] op_sel_hi:[0,1]
	v_med3_f32 v78, v78, s52, v209
	v_med3_f32 v79, v79, s52, v209
	v_pk_fma_f32 v[74:75], v[74:75], v[50:51], v[26:27]
	v_pk_mul_f32 v[66:67], v[132:133], v[66:67] op_sel_hi:[0,1]
	v_cvt_pk_fp8_f32 v82, v78, v79
	v_med3_f32 v78, v80, s52, v209
	v_pk_fma_f32 v[66:67], v[50:51], v[66:67], v[26:27]
	v_med3_f32 v74, v74, s52, v209
	v_med3_f32 v75, v75, s52, v209
	v_cvt_pk_fp8_f32 v80, v74, v75
	v_med3_f32 v66, v66, s52, v209
	v_med3_f32 v67, v67, s52, v209
	v_cvt_pk_fp8_f32 v74, v66, v67
	v_pk_mul_f32 v[68:69], v[132:133], v[68:69] op_sel_hi:[0,1]
	v_pk_mul_f32 v[76:77], v[130:131], v[76:77] op_sel_hi:[0,1]
	v_pk_fma_f32 v[68:69], v[52:53], v[68:69], v[28:29]
	v_med3_f32 v79, v81, s52, v209
	v_pk_fma_f32 v[76:77], v[76:77], v[52:53], v[28:29]
	v_med3_f32 v66, v68, s52, v209
	v_med3_f32 v67, v69, s52, v209
	v_cvt_pk_fp8_f32 v82, v78, v79 op_sel:[0,0,1]
	v_med3_f32 v76, v76, s52, v209
	v_med3_f32 v77, v77, s52, v209
	v_cvt_pk_fp8_f32 v74, v66, v67 op_sel:[0,0,1]
	v_cvt_pk_fp8_f32 v80, v76, v77 op_sel:[0,0,1]
	s_addc_u32 s7, s33, s59
	v_pk_mul_f32 v[62:63], v[130:131], v[62:63] op_sel_hi:[0,1]
	v_lshl_add_u64 v[78:79], s[6:7], 0, v[196:197]
	v_lshl_add_u64 v[66:67], s[6:7], 0, v[144:145]
	v_pk_fma_f32 v[62:63], v[62:63], v[86:87], v[70:71]
	global_store_dword v[190:191], v131, off offset:-1792
	global_store_dword v[78:79], v82, off
	global_store_dword v[190:191], v80, off offset:-1536
	global_store_dword v[66:67], v74, off
	v_med3_f32 v62, v62, s52, v209
	v_med3_f32 v63, v63, s52, v209
	v_cvt_pk_fp8_f32 v66, v62, v63
	v_pk_mul_f32 v[64:65], v[130:131], v[64:65] op_sel_hi:[0,1]
	v_pk_fma_f32 v[64:65], v[64:65], v[88:89], v[72:73]
	v_pk_mul_f32 v[58:59], v[132:133], v[58:59] op_sel_hi:[0,1]
	v_pk_mul_f32 v[60:61], v[132:133], v[60:61] op_sel_hi:[0,1]
	v_pk_fma_f32 v[58:59], v[86:87], v[58:59], v[70:71]
	v_med3_f32 v62, v64, s52, v209
	v_med3_f32 v63, v65, s52, v209
	v_pk_mul_f32 v[54:55], v[130:131], v[54:55] op_sel_hi:[0,1]
	v_pk_fma_f32 v[60:61], v[88:89], v[60:61], v[72:73]
	v_cvt_pk_fp8_f32 v66, v62, v63 op_sel:[0,0,1]
	v_med3_f32 v58, v58, s52, v209
	v_med3_f32 v59, v59, s52, v209
	v_pk_fma_f32 v[54:55], v[54:55], v[94:95], v[90:91]
	v_pk_mul_f32 v[46:47], v[132:133], v[46:47] op_sel_hi:[0,1]
	v_cvt_pk_fp8_f32 v62, v58, v59
	v_med3_f32 v58, v60, s52, v209
	v_pk_fma_f32 v[46:47], v[94:95], v[46:47], v[90:91]
	v_med3_f32 v54, v54, s52, v209
	v_med3_f32 v55, v55, s52, v209
	v_cvt_pk_fp8_f32 v60, v54, v55
	v_med3_f32 v46, v46, s52, v209
	v_med3_f32 v47, v47, s52, v209
	v_cvt_pk_fp8_f32 v54, v46, v47
	v_pk_mul_f32 v[48:49], v[132:133], v[48:49] op_sel_hi:[0,1]
	v_pk_mul_f32 v[56:57], v[130:131], v[56:57] op_sel_hi:[0,1]
	v_pk_fma_f32 v[48:49], v[96:97], v[48:49], v[92:93]
	v_med3_f32 v59, v61, s52, v209
	v_pk_fma_f32 v[56:57], v[56:57], v[96:97], v[92:93]
	v_med3_f32 v46, v48, s52, v209
	v_med3_f32 v47, v49, s52, v209
	v_cvt_pk_fp8_f32 v62, v58, v59 op_sel:[0,0,1]
	v_med3_f32 v56, v56, s52, v209
	v_med3_f32 v57, v57, s52, v209
	v_cvt_pk_fp8_f32 v54, v46, v47 op_sel:[0,0,1]
	v_cvt_pk_fp8_f32 v60, v56, v57 op_sel:[0,0,1]
	v_pk_mul_f32 v[42:43], v[130:131], v[42:43] op_sel_hi:[0,1]
	v_lshl_add_u64 v[58:59], s[6:7], 0, v[148:149]
	v_lshl_add_u64 v[46:47], s[6:7], 0, v[152:153]
	v_pk_fma_f32 v[42:43], v[42:43], v[102:103], v[98:99]
	global_store_dword v[190:191], v66, off offset:-1280
	global_store_dword v[58:59], v62, off
	global_store_dword v[190:191], v60, off offset:-1024
	global_store_dword v[46:47], v54, off
	v_med3_f32 v42, v42, s52, v209
	v_med3_f32 v43, v43, s52, v209
	v_cvt_pk_fp8_f32 v46, v42, v43
	v_pk_mul_f32 v[44:45], v[130:131], v[44:45] op_sel_hi:[0,1]
	v_pk_fma_f32 v[44:45], v[44:45], v[104:105], v[100:101]
	v_pk_mul_f32 v[38:39], v[132:133], v[38:39] op_sel_hi:[0,1]
	v_pk_mul_f32 v[40:41], v[132:133], v[40:41] op_sel_hi:[0,1]
	v_pk_fma_f32 v[38:39], v[102:103], v[38:39], v[98:99]
	v_med3_f32 v42, v44, s52, v209
	v_med3_f32 v43, v45, s52, v209
	v_pk_mul_f32 v[34:35], v[130:131], v[34:35] op_sel_hi:[0,1]
	v_pk_fma_f32 v[40:41], v[104:105], v[40:41], v[100:101]
	v_cvt_pk_fp8_f32 v46, v42, v43 op_sel:[0,0,1]
	v_med3_f32 v38, v38, s52, v209
	v_med3_f32 v39, v39, s52, v209
	v_pk_fma_f32 v[34:35], v[34:35], v[110:111], v[106:107]
	v_pk_mul_f32 v[30:31], v[132:133], v[30:31] op_sel_hi:[0,1]
	v_cvt_pk_fp8_f32 v42, v38, v39
	v_med3_f32 v38, v40, s52, v209
	v_pk_fma_f32 v[30:31], v[110:111], v[30:31], v[106:107]
	v_med3_f32 v34, v34, s52, v209
	v_med3_f32 v35, v35, s52, v209
	v_cvt_pk_fp8_f32 v40, v34, v35
	v_med3_f32 v30, v30, s52, v209
	v_med3_f32 v31, v31, s52, v209
	v_cvt_pk_fp8_f32 v34, v30, v31
	v_pk_mul_f32 v[32:33], v[132:133], v[32:33] op_sel_hi:[0,1]
	v_pk_mul_f32 v[36:37], v[130:131], v[36:37] op_sel_hi:[0,1]
	v_pk_fma_f32 v[32:33], v[112:113], v[32:33], v[108:109]
	v_med3_f32 v39, v41, s52, v209
	v_pk_fma_f32 v[36:37], v[36:37], v[112:113], v[108:109]
	v_med3_f32 v30, v32, s52, v209
	v_med3_f32 v31, v33, s52, v209
	v_cvt_pk_fp8_f32 v42, v38, v39 op_sel:[0,0,1]
	v_med3_f32 v36, v36, s52, v209
	v_med3_f32 v37, v37, s52, v209
	v_cvt_pk_fp8_f32 v34, v30, v31 op_sel:[0,0,1]
	v_cvt_pk_fp8_f32 v40, v36, v37 op_sel:[0,0,1]
	v_pk_mul_f32 v[22:23], v[130:131], v[22:23] op_sel_hi:[0,1]
	v_lshl_add_u64 v[38:39], s[6:7], 0, v[156:157]
	v_lshl_add_u64 v[30:31], s[6:7], 0, v[164:165]
	v_pk_fma_f32 v[22:23], v[22:23], v[118:119], v[114:115]
	global_store_dword v[190:191], v46, off offset:-768
	global_store_dword v[38:39], v42, off
	global_store_dword v[190:191], v40, off offset:-512
	global_store_dword v[30:31], v34, off
	v_med3_f32 v22, v22, s52, v209
	v_med3_f32 v23, v23, s52, v209
	v_cvt_pk_fp8_f32 v30, v22, v23
	v_pk_mul_f32 v[24:25], v[130:131], v[24:25] op_sel_hi:[0,1]
	v_pk_fma_f32 v[24:25], v[24:25], v[120:121], v[116:117]
	v_pk_mul_f32 v[18:19], v[132:133], v[18:19] op_sel_hi:[0,1]
	v_pk_mul_f32 v[20:21], v[132:133], v[20:21] op_sel_hi:[0,1]
	v_pk_fma_f32 v[18:19], v[118:119], v[18:19], v[114:115]
	v_med3_f32 v22, v24, s52, v209
	v_med3_f32 v23, v25, s52, v209
	v_pk_mul_f32 v[14:15], v[130:131], v[14:15] op_sel_hi:[0,1]
	v_pk_fma_f32 v[20:21], v[120:121], v[20:21], v[116:117]
	v_cvt_pk_fp8_f32 v30, v22, v23 op_sel:[0,0,1]
	v_med3_f32 v18, v18, s52, v209
	v_med3_f32 v19, v19, s52, v209
	v_pk_fma_f32 v[14:15], v[14:15], v[126:127], v[122:123]
	v_pk_mul_f32 v[10:11], v[132:133], v[10:11] op_sel_hi:[0,1]
	v_cvt_pk_fp8_f32 v22, v18, v19
	v_med3_f32 v18, v20, s52, v209
	v_pk_fma_f32 v[10:11], v[126:127], v[10:11], v[122:123]
	v_med3_f32 v14, v14, s52, v209
	v_med3_f32 v15, v15, s52, v209
	v_cvt_pk_fp8_f32 v20, v14, v15
	v_med3_f32 v10, v10, s52, v209
	v_med3_f32 v11, v11, s52, v209
	v_cvt_pk_fp8_f32 v14, v10, v11
	v_pk_mul_f32 v[12:13], v[132:133], v[12:13] op_sel_hi:[0,1]
	v_pk_mul_f32 v[16:17], v[130:131], v[16:17] op_sel_hi:[0,1]
	v_pk_fma_f32 v[12:13], v[128:129], v[12:13], v[124:125]
	v_med3_f32 v19, v21, s52, v209
	v_pk_fma_f32 v[16:17], v[16:17], v[128:129], v[124:125]
	v_med3_f32 v10, v12, s52, v209
	v_med3_f32 v11, v13, s52, v209
	v_cvt_pk_fp8_f32 v22, v18, v19 op_sel:[0,0,1]
	v_med3_f32 v16, v16, s52, v209
	v_med3_f32 v17, v17, s52, v209
	v_cvt_pk_fp8_f32 v14, v10, v11 op_sel:[0,0,1]
	v_cvt_pk_fp8_f32 v20, v16, v17 op_sel:[0,0,1]
	v_lshl_add_u64 v[18:19], s[6:7], 0, v[172:173]
	v_lshl_add_u64 v[10:11], s[6:7], 0, v[180:181]
	global_store_dword v[190:191], v30, off offset:-256
	global_store_dword v[18:19], v22, off
	global_store_dword v[190:191], v20, off
	global_store_dword v[10:11], v14, off

.LBB0_232:
	s_waitcnt vmcnt(1)
	v_mul_f32_e32 v131, 0x42000000, v62
	v_mul_f32_e32 v132, 0x42000000, v2
	v_med3_f32 v131, v131, s69, v148
	v_med3_f32 v134, v132, s69, v148
	v_cvt_pk_fp8_f32 v132, v131, v134
	v_mul_f32_e32 v133, 0x42000000, v6
	v_mul_f32_e32 v131, 0x42000000, v10
	v_med3_f32 v133, v133, s69, v148
	v_med3_f32 v131, v131, s69, v148
	v_cvt_pk_fp8_f32 v132, v133, v131 op_sel:[0,0,1]
	v_mul_f32_e32 v131, 0x42000000, v14
	v_mul_f32_e32 v133, 0x42000000, v18
	v_med3_f32 v131, v131, s69, v148
	v_med3_f32 v135, v133, s69, v148
	v_cvt_pk_fp8_f32 v133, v131, v135
	v_mul_f32_e32 v134, 0x42000000, v22
	s_waitcnt vmcnt(0)
	v_mul_f32_e32 v131, 0x42000000, v26
	v_med3_f32 v134, v134, s69, v148
	v_med3_f32 v131, v131, s69, v148
	v_cvt_pk_fp8_f32 v133, v134, v131 op_sel:[0,0,1]
	v_mul_f32_e32 v131, 0x42000000, v30
	v_mul_f32_e32 v134, 0x42000000, v34
	v_med3_f32 v131, v131, s69, v148
	v_med3_f32 v136, v134, s69, v148
	v_cvt_pk_fp8_f32 v134, v131, v136
	v_mul_f32_e32 v135, 0x42000000, v38
	v_mul_f32_e32 v131, 0x42000000, v42
	v_med3_f32 v135, v135, s69, v148
	v_med3_f32 v131, v131, s69, v148
	v_cvt_pk_fp8_f32 v134, v135, v131 op_sel:[0,0,1]
	v_mul_f32_e32 v131, 0x42000000, v46
	v_mul_f32_e32 v135, 0x42000000, v50
	v_med3_f32 v131, v131, s69, v148
	v_med3_f32 v137, v135, s69, v148
	v_cvt_pk_fp8_f32 v135, v131, v137
	v_mul_f32_e32 v136, 0x42000000, v54
	v_mul_f32_e32 v131, 0x42000000, v58
	v_med3_f32 v136, v136, s69, v148
	v_med3_f32 v131, v131, s69, v148
	v_cvt_pk_fp8_f32 v135, v136, v131 op_sel:[0,0,1]
	v_mul_f32_e32 v131, 0x42000000, v63
	v_mul_f32_e32 v136, 0x42000000, v3
	v_med3_f32 v131, v131, s69, v148
	v_med3_f32 v136, v136, s69, v148
	v_cvt_pk_fp8_f32 v154, v131, v136
	v_mul_f32_e32 v137, 0x42000000, v7
	v_mul_f32_e32 v131, 0x42000000, v11
	v_med3_f32 v136, v137, s69, v148
	v_med3_f32 v131, v131, s69, v148
	v_cvt_pk_fp8_f32 v154, v136, v131 op_sel:[0,0,1]
	v_mul_f32_e32 v131, 0x42000000, v15
	v_mul_f32_e32 v136, 0x42000000, v19
	v_med3_f32 v131, v131, s69, v148
	v_med3_f32 v136, v136, s69, v148
	v_cvt_pk_fp8_f32 v155, v131, v136
	v_mul_f32_e32 v137, 0x42000000, v23
	v_mul_f32_e32 v131, 0x42000000, v27
	v_med3_f32 v136, v137, s69, v148
	v_med3_f32 v131, v131, s69, v148
	v_cvt_pk_fp8_f32 v155, v136, v131 op_sel:[0,0,1]
	v_mul_f32_e32 v131, 0x42000000, v31
	v_mul_f32_e32 v136, 0x42000000, v35
	v_med3_f32 v131, v131, s69, v148
	v_med3_f32 v136, v136, s69, v148
	v_cvt_pk_fp8_f32 v156, v131, v136
	v_mul_f32_e32 v137, 0x42000000, v39
	v_mul_f32_e32 v131, 0x42000000, v43
	v_med3_f32 v136, v137, s69, v148
	v_med3_f32 v131, v131, s69, v148
	v_cvt_pk_fp8_f32 v156, v136, v131 op_sel:[0,0,1]
	v_mul_f32_e32 v131, 0x42000000, v47
	v_mul_f32_e32 v136, 0x42000000, v51
	v_med3_f32 v131, v131, s69, v148
	v_med3_f32 v136, v136, s69, v148
	v_cvt_pk_fp8_f32 v157, v131, v136
	v_mul_f32_e32 v137, 0x42000000, v55
	v_mul_f32_e32 v131, 0x42000000, v59
	v_med3_f32 v136, v137, s69, v148
	v_med3_f32 v131, v131, s69, v148
	v_cvt_pk_fp8_f32 v157, v136, v131 op_sel:[0,0,1]
	v_mul_f32_e32 v131, 0x42000000, v64
	v_mul_f32_e32 v136, 0x42000000, v4
	v_med3_f32 v131, v131, s69, v148
	v_med3_f32 v136, v136, s69, v148
	v_cvt_pk_fp8_f32 v158, v131, v136
	v_mul_f32_e32 v137, 0x42000000, v8
	v_mul_f32_e32 v131, 0x42000000, v12
	v_med3_f32 v136, v137, s69, v148
	v_med3_f32 v131, v131, s69, v148
	v_cvt_pk_fp8_f32 v158, v136, v131 op_sel:[0,0,1]
	v_mul_f32_e32 v131, 0x42000000, v16
	v_mul_f32_e32 v136, 0x42000000, v20
	v_med3_f32 v131, v131, s69, v148
	v_med3_f32 v136, v136, s69, v148
	v_cvt_pk_fp8_f32 v159, v131, v136
	v_mul_f32_e32 v137, 0x42000000, v24
	v_mul_f32_e32 v131, 0x42000000, v28
	v_med3_f32 v136, v137, s69, v148
	v_med3_f32 v131, v131, s69, v148
	v_cvt_pk_fp8_f32 v159, v136, v131 op_sel:[0,0,1]
	v_mul_f32_e32 v131, 0x42000000, v32
	v_mul_f32_e32 v136, 0x42000000, v36
	v_med3_f32 v131, v131, s69, v148
	v_med3_f32 v136, v136, s69, v148
	v_cvt_pk_fp8_f32 v160, v131, v136
	v_mul_f32_e32 v137, 0x42000000, v40
	v_mul_f32_e32 v131, 0x42000000, v44
	v_med3_f32 v136, v137, s69, v148
	v_med3_f32 v131, v131, s69, v148
	v_cvt_pk_fp8_f32 v160, v136, v131 op_sel:[0,0,1]
	v_mul_f32_e32 v131, 0x42000000, v48
	v_mul_f32_e32 v136, 0x42000000, v52
	v_med3_f32 v131, v131, s69, v148
	v_med3_f32 v136, v136, s69, v148
	v_cvt_pk_fp8_f32 v161, v131, v136
	v_mul_f32_e32 v137, 0x42000000, v56
	v_mul_f32_e32 v131, 0x42000000, v60
	v_med3_f32 v136, v137, s69, v148
	v_med3_f32 v131, v131, s69, v148
	v_cvt_pk_fp8_f32 v161, v136, v131 op_sel:[0,0,1]
	v_mul_f32_e32 v131, 0x42000000, v65
	v_mul_f32_e32 v136, 0x42000000, v5
	v_med3_f32 v131, v131, s69, v148
	v_med3_f32 v136, v136, s69, v148
	v_cvt_pk_fp8_f32 v162, v131, v136
	v_mul_f32_e32 v137, 0x42000000, v9
	v_mul_f32_e32 v131, 0x42000000, v13
	v_med3_f32 v136, v137, s69, v148
	v_med3_f32 v131, v131, s69, v148
	v_cvt_pk_fp8_f32 v162, v136, v131 op_sel:[0,0,1]
	v_mul_f32_e32 v131, 0x42000000, v17
	v_mul_f32_e32 v136, 0x42000000, v21
	v_med3_f32 v131, v131, s69, v148
	v_med3_f32 v136, v136, s69, v148
	v_cvt_pk_fp8_f32 v163, v131, v136
	v_mul_f32_e32 v137, 0x42000000, v25
	v_mul_f32_e32 v131, 0x42000000, v29
	v_med3_f32 v136, v137, s69, v148
	v_med3_f32 v131, v131, s69, v148
	v_cvt_pk_fp8_f32 v163, v136, v131 op_sel:[0,0,1]
	v_mul_f32_e32 v131, 0x42000000, v33
	v_mul_f32_e32 v136, 0x42000000, v37
	v_med3_f32 v131, v131, s69, v148
	v_med3_f32 v136, v136, s69, v148
	v_cvt_pk_fp8_f32 v164, v131, v136
	v_mul_f32_e32 v137, 0x42000000, v41
	v_mul_f32_e32 v131, 0x42000000, v45
	v_med3_f32 v136, v137, s69, v148
	v_med3_f32 v131, v131, s69, v148
	v_cvt_pk_fp8_f32 v164, v136, v131 op_sel:[0,0,1]
	v_mul_f32_e32 v131, 0x42000000, v49
	v_mul_f32_e32 v136, 0x42000000, v53
	v_med3_f32 v131, v131, s69, v148
	v_med3_f32 v136, v136, s69, v148
	v_cvt_pk_fp8_f32 v165, v131, v136
	s_add_i32 s84, s53, s48
	v_mul_f32_e32 v137, 0x42000000, v57
	v_mul_f32_e32 v131, 0x42000000, v61
	s_cmp_ge_i32 s84, s62
	v_med3_f32 v136, v137, s69, v148
	v_med3_f32 v131, v131, s69, v148
	s_cselect_b64 s[74:75], -1, 0
	v_cvt_pk_fp8_f32 v165, v136, v131 op_sel:[0,0,1]
	s_and_b64 vcc, exec, s[74:75]
	s_mov_b32 s70, s81
	s_mov_b32 s78, s76
	ds_write_b128 v149, v[132:135]
	ds_write_b128 v149, v[154:157] offset:144
	ds_write_b128 v149, v[158:161] offset:288
	ds_write_b128 v149, v[162:165] offset:432
	s_cbranch_vccnz .LBB0_251
	s_cmpk_lt_i32 s84, 0x180
	s_cbranch_scc1 .LBB0_241
	s_cmpk_gt_u32 s84, 0x1ff
	s_cbranch_scc0 .LBB0_242
	s_cmpk_gt_u32 s84, 0x23f
	s_cbranch_scc0 .LBB0_243
	s_cmpk_gt_u32 s84, 0x2bf
	s_cbranch_scc0 .LBB0_244
	s_cmpk_gt_u32 s84, 0x22bf
	s_mov_b64 s[14:15], -1
	s_cbranch_scc0 .LBB0_239
	s_add_i32 s8, s84, 0xffffdd40
	s_lshr_b32 s70, s8, 7
	s_and_b32 s77, s8, 0x7f
	s_lshl_b64 s[14:15], s[70:71], 22
	s_lshl_b64 s[8:9], s[70:71], 24
	s_mov_b32 s1, s35
	v_readlane_b32 s34, v254, 14
	v_readlane_b32 s35, v254, 15
	s_add_u32 s8, s34, s8
	s_addc_u32 s9, s35, s9
	s_add_u32 s72, s60, s14
	s_mov_b32 s35, s1
	s_addc_u32 s73, s61, s15
	s_mov_b64 s[14:15], 0

.LBB0_259:
	v_ashrrev_i32_e32 v137, 31, v134
	v_mad_u64_u32 v[134:135], s[6:7], v134, s63, v[142:143]
	v_mov_b32_e32 v136, v135
	s_add_i32 s8, s50, s53
	v_mad_u64_u32 v[136:137], s[6:7], v137, s63, v[136:137]
	v_mov_b32_e32 v135, v136
	s_cmp_lt_i32 s8, s62
	s_waitcnt lgkmcnt(0)
	global_store_dwordx4 v[134:135], v[130:133], off nt
	s_cbranch_scc0 .LBB0_230
	s_nop 0
	v_mul_f32_e32 v130, 0x42000000, v86
	v_mul_f32_e32 v131, 0x42000000, v66
	v_med3_f32 v133, v130, s69, v148
	v_med3_f32 v131, v131, s69, v148
	v_cvt_pk_fp8_f32 v130, v133, v131
	v_mul_f32_e32 v132, 0x42000000, v70
	v_mul_f32_e32 v131, 0x42000000, v74
	v_med3_f32 v132, v132, s69, v148
	v_med3_f32 v131, v131, s69, v148
	v_cvt_pk_fp8_f32 v130, v132, v131 op_sel:[0,0,1]
	v_mul_f32_e32 v131, 0x42000000, v78
	v_mul_f32_e32 v132, 0x42000000, v82
	v_med3_f32 v134, v131, s69, v148
	v_med3_f32 v132, v132, s69, v148
	v_cvt_pk_fp8_f32 v131, v134, v132
	v_mul_f32_e32 v133, 0x42000000, v90
	v_mul_f32_e32 v132, 0x42000000, v94
	v_med3_f32 v133, v133, s69, v148
	v_med3_f32 v132, v132, s69, v148
	v_cvt_pk_fp8_f32 v131, v133, v132 op_sel:[0,0,1]
	v_mul_f32_e32 v132, 0x42000000, v98
	v_mul_f32_e32 v133, 0x42000000, v106
	v_med3_f32 v135, v132, s69, v148
	v_med3_f32 v133, v133, s69, v148
	v_cvt_pk_fp8_f32 v132, v135, v133
	v_mul_f32_e32 v134, 0x42000000, v102
	v_mul_f32_e32 v133, 0x42000000, v110
	v_med3_f32 v134, v134, s69, v148
	v_med3_f32 v133, v133, s69, v148
	v_cvt_pk_fp8_f32 v132, v134, v133 op_sel:[0,0,1]
	v_mul_f32_e32 v133, 0x42000000, v114
	v_mul_f32_e32 v134, 0x42000000, v118
	v_med3_f32 v136, v133, s69, v148
	v_med3_f32 v134, v134, s69, v148
	v_cvt_pk_fp8_f32 v133, v136, v134
	v_mul_f32_e32 v135, 0x42000000, v122
	v_mul_f32_e32 v134, 0x42000000, v126
	v_med3_f32 v135, v135, s69, v148
	v_med3_f32 v134, v134, s69, v148
	v_cvt_pk_fp8_f32 v133, v135, v134 op_sel:[0,0,1]
	v_mul_f32_e32 v134, 0x42000000, v87
	v_mul_f32_e32 v135, 0x42000000, v67
	v_med3_f32 v137, v134, s69, v148
	v_med3_f32 v135, v135, s69, v148
	v_cvt_pk_fp8_f32 v134, v137, v135
	v_mul_f32_e32 v136, 0x42000000, v71
	v_mul_f32_e32 v135, 0x42000000, v75
	v_med3_f32 v136, v136, s69, v148
	v_med3_f32 v135, v135, s69, v148
	v_cvt_pk_fp8_f32 v134, v136, v135 op_sel:[0,0,1]
	v_mul_f32_e32 v135, 0x42000000, v79
	v_mul_f32_e32 v136, 0x42000000, v83
	v_med3_f32 v140, v135, s69, v148
	v_med3_f32 v136, v136, s69, v148
	v_cvt_pk_fp8_f32 v135, v140, v136
	v_mul_f32_e32 v137, 0x42000000, v91
	v_mul_f32_e32 v136, 0x42000000, v95
	v_med3_f32 v137, v137, s69, v148
	v_med3_f32 v136, v136, s69, v148
	v_cvt_pk_fp8_f32 v135, v137, v136 op_sel:[0,0,1]
	v_mul_f32_e32 v136, 0x42000000, v99
	v_mul_f32_e32 v137, 0x42000000, v107
	v_med3_f32 v142, v136, s69, v148
	v_med3_f32 v137, v137, s69, v148
	v_cvt_pk_fp8_f32 v136, v142, v137
	v_mul_f32_e32 v140, 0x42000000, v103
	v_mul_f32_e32 v137, 0x42000000, v111
	v_med3_f32 v140, v140, s69, v148
	v_med3_f32 v137, v137, s69, v148
	v_cvt_pk_fp8_f32 v136, v140, v137 op_sel:[0,0,1]
	v_mul_f32_e32 v137, 0x42000000, v115
	v_mul_f32_e32 v140, 0x42000000, v119
	v_med3_f32 v143, v137, s69, v148
	v_med3_f32 v140, v140, s69, v148
	v_cvt_pk_fp8_f32 v137, v143, v140
	v_mul_f32_e32 v142, 0x42000000, v123
	v_mul_f32_e32 v140, 0x42000000, v127
	v_med3_f32 v142, v142, s69, v148
	v_med3_f32 v140, v140, s69, v148
	v_cvt_pk_fp8_f32 v137, v142, v140 op_sel:[0,0,1]
	v_mul_f32_e32 v140, 0x42000000, v88
	v_mul_f32_e32 v142, 0x42000000, v68
	v_med3_f32 v140, v140, s69, v148
	v_med3_f32 v142, v142, s69, v148
	v_cvt_pk_fp8_f32 v154, v140, v142
	v_mul_f32_e32 v143, 0x42000000, v72
	v_mul_f32_e32 v140, 0x42000000, v76
	v_med3_f32 v142, v143, s69, v148
	v_med3_f32 v140, v140, s69, v148
	v_cvt_pk_fp8_f32 v154, v142, v140 op_sel:[0,0,1]
	v_mul_f32_e32 v140, 0x42000000, v80
	v_mul_f32_e32 v142, 0x42000000, v84
	v_med3_f32 v140, v140, s69, v148
	v_med3_f32 v142, v142, s69, v148
	v_cvt_pk_fp8_f32 v155, v140, v142
	v_mul_f32_e32 v143, 0x42000000, v92
	v_mul_f32_e32 v140, 0x42000000, v96
	v_med3_f32 v142, v143, s69, v148
	v_med3_f32 v140, v140, s69, v148
	v_cvt_pk_fp8_f32 v155, v142, v140 op_sel:[0,0,1]
	v_mul_f32_e32 v140, 0x42000000, v100
	v_mul_f32_e32 v142, 0x42000000, v108
	v_med3_f32 v140, v140, s69, v148
	v_med3_f32 v142, v142, s69, v148
	v_cvt_pk_fp8_f32 v156, v140, v142
	v_mul_f32_e32 v143, 0x42000000, v104
	v_mul_f32_e32 v140, 0x42000000, v112
	v_med3_f32 v142, v143, s69, v148
	v_med3_f32 v140, v140, s69, v148
	v_cvt_pk_fp8_f32 v156, v142, v140 op_sel:[0,0,1]
	v_mul_f32_e32 v140, 0x42000000, v116
	v_mul_f32_e32 v142, 0x42000000, v120
	v_med3_f32 v140, v140, s69, v148
	v_med3_f32 v142, v142, s69, v148
	v_cvt_pk_fp8_f32 v157, v140, v142
	v_mul_f32_e32 v143, 0x42000000, v124
	v_mul_f32_e32 v140, 0x42000000, v128
	v_med3_f32 v142, v143, s69, v148
	v_med3_f32 v140, v140, s69, v148
	v_cvt_pk_fp8_f32 v157, v142, v140 op_sel:[0,0,1]
	v_mul_f32_e32 v140, 0x42000000, v89
	v_mul_f32_e32 v142, 0x42000000, v69
	v_med3_f32 v140, v140, s69, v148
	v_med3_f32 v142, v142, s69, v148
	v_cvt_pk_fp8_f32 v158, v140, v142
	v_mul_f32_e32 v143, 0x42000000, v73
	v_mul_f32_e32 v140, 0x42000000, v77
	v_med3_f32 v142, v143, s69, v148
	v_med3_f32 v140, v140, s69, v148
	v_cvt_pk_fp8_f32 v158, v142, v140 op_sel:[0,0,1]
	v_mul_f32_e32 v140, 0x42000000, v81
	v_mul_f32_e32 v142, 0x42000000, v85
	v_med3_f32 v140, v140, s69, v148
	v_med3_f32 v142, v142, s69, v148
	v_cvt_pk_fp8_f32 v159, v140, v142
	v_mul_f32_e32 v143, 0x42000000, v93
	v_mul_f32_e32 v140, 0x42000000, v97
	v_med3_f32 v142, v143, s69, v148
	v_med3_f32 v140, v140, s69, v148
	v_cvt_pk_fp8_f32 v159, v142, v140 op_sel:[0,0,1]
	v_mul_f32_e32 v140, 0x42000000, v101
	v_mul_f32_e32 v142, 0x42000000, v109
	v_med3_f32 v140, v140, s69, v148
	v_med3_f32 v142, v142, s69, v148
	v_cvt_pk_fp8_f32 v160, v140, v142
	v_mul_f32_e32 v143, 0x42000000, v105
	v_mul_f32_e32 v140, 0x42000000, v113
	v_med3_f32 v142, v143, s69, v148
	v_med3_f32 v140, v140, s69, v148
	v_cvt_pk_fp8_f32 v160, v142, v140 op_sel:[0,0,1]
	v_mul_f32_e32 v140, 0x42000000, v117
	v_mul_f32_e32 v142, 0x42000000, v121
	v_med3_f32 v140, v140, s69, v148
	v_med3_f32 v142, v142, s69, v148
	v_cvt_pk_fp8_f32 v161, v140, v142
	v_mul_f32_e32 v143, 0x42000000, v125
	v_mul_f32_e32 v140, 0x42000000, v129
	v_med3_f32 v142, v143, s69, v148
	v_med3_f32 v140, v140, s69, v148
	s_add_i32 s3, s3, s48
	s_add_i32 s53, s49, s53
	v_cvt_pk_fp8_f32 v161, v142, v140 op_sel:[0,0,1]
	s_cmp_lt_i32 s53, s62
	s_mov_b64 s[76:77], s[66:67]
	s_mov_b32 s15, s64
	s_mov_b32 s80, s65
	v_mov_b32_e32 v140, v145
	s_mov_b32 s79, s82
	s_mov_b32 s52, s68
	ds_write_b128 v149, v[130:133] offset:36864
	ds_write_b128 v149, v[134:137] offset:37008
	ds_write_b128 v149, v[154:157] offset:37152
	ds_write_b128 v149, v[158:161] offset:37296
	s_cbranch_scc0 .LBB0_280
	s_cmpk_lt_i32 s53, 0x180
	s_cbranch_scc1 .LBB0_269
	s_cmpk_gt_u32 s53, 0x1ff
	s_cbranch_scc0 .LBB0_270
	s_cmpk_gt_u32 s53, 0x23f
	s_cbranch_scc0 .LBB0_271
	s_cmpk_gt_u32 s53, 0x2bf
	s_cbranch_scc0 .LBB0_273
	s_cmpk_gt_u32 s53, 0x22bf
	s_mov_b64 s[8:9], -1
	s_cbranch_scc0 .LBB0_267
	s_add_i32 s7, s53, 0xffffdd40
	s_lshr_b32 s6, s7, 7
	s_and_b32 s52, s7, 0x7f
	s_mov_b32 s7, s71
	s_lshl_b64 s[8:9], s[6:7], 22
	s_lshl_b64 s[6:7], s[6:7], 24
	s_mov_b32 s1, s35
	v_readlane_b32 s34, v254, 14
	v_readlane_b32 s35, v254, 15
	s_add_u32 s6, s34, s6
	s_addc_u32 s7, s35, s7
	s_add_u32 s76, s60, s8
	s_mov_b32 s35, s1
	s_addc_u32 s77, s61, s9
	s_mov_b64 s[8:9], 0

.LBB0_441:
	s_waitcnt vmcnt(1)
	v_mul_f32_e32 v131, 0x42000000, v62
	v_mul_f32_e32 v132, 0x42000000, v2
	v_med3_f32 v131, v131, s28, v149
	v_med3_f32 v134, v132, s28, v149
	v_cvt_pk_fp8_f32 v132, v131, v134
	v_mul_f32_e32 v133, 0x42000000, v6
	v_mul_f32_e32 v131, 0x42000000, v10
	v_med3_f32 v133, v133, s28, v149
	v_med3_f32 v131, v131, s28, v149
	v_cvt_pk_fp8_f32 v132, v133, v131 op_sel:[0,0,1]
	v_mul_f32_e32 v131, 0x42000000, v14
	v_mul_f32_e32 v133, 0x42000000, v18
	v_med3_f32 v131, v131, s28, v149
	v_med3_f32 v135, v133, s28, v149
	v_cvt_pk_fp8_f32 v133, v131, v135
	v_mul_f32_e32 v134, 0x42000000, v22
	s_waitcnt vmcnt(0)
	v_mul_f32_e32 v131, 0x42000000, v26
	v_med3_f32 v134, v134, s28, v149
	v_med3_f32 v131, v131, s28, v149
	v_cvt_pk_fp8_f32 v133, v134, v131 op_sel:[0,0,1]
	v_mul_f32_e32 v131, 0x42000000, v30
	v_mul_f32_e32 v134, 0x42000000, v34
	v_med3_f32 v131, v131, s28, v149
	v_med3_f32 v136, v134, s28, v149
	v_cvt_pk_fp8_f32 v134, v131, v136
	v_mul_f32_e32 v135, 0x42000000, v38
	v_mul_f32_e32 v131, 0x42000000, v42
	v_med3_f32 v135, v135, s28, v149
	v_med3_f32 v131, v131, s28, v149
	v_cvt_pk_fp8_f32 v134, v135, v131 op_sel:[0,0,1]
	v_mul_f32_e32 v131, 0x42000000, v46
	v_mul_f32_e32 v135, 0x42000000, v50
	v_med3_f32 v131, v131, s28, v149
	v_med3_f32 v137, v135, s28, v149
	v_cvt_pk_fp8_f32 v135, v131, v137
	v_mul_f32_e32 v136, 0x42000000, v54
	v_mul_f32_e32 v131, 0x42000000, v58
	v_med3_f32 v136, v136, s28, v149
	v_med3_f32 v131, v131, s28, v149
	v_cvt_pk_fp8_f32 v135, v136, v131 op_sel:[0,0,1]
	v_mul_f32_e32 v131, 0x42000000, v63
	v_med3_f32 v131, v131, s28, v149
	ds_write_b128 v150, v[132:135]
	v_mul_f32_e32 v132, 0x42000000, v3
	v_med3_f32 v134, v132, s28, v149
	v_cvt_pk_fp8_f32 v132, v131, v134
	v_mul_f32_e32 v133, 0x42000000, v7
	v_mul_f32_e32 v131, 0x42000000, v11
	v_med3_f32 v133, v133, s28, v149
	v_med3_f32 v131, v131, s28, v149
	v_cvt_pk_fp8_f32 v132, v133, v131 op_sel:[0,0,1]
	v_mul_f32_e32 v131, 0x42000000, v15
	v_mul_f32_e32 v133, 0x42000000, v19
	v_med3_f32 v131, v131, s28, v149
	v_med3_f32 v135, v133, s28, v149
	v_cvt_pk_fp8_f32 v133, v131, v135
	v_mul_f32_e32 v134, 0x42000000, v23
	v_mul_f32_e32 v131, 0x42000000, v27
	v_med3_f32 v134, v134, s28, v149
	v_med3_f32 v131, v131, s28, v149
	v_cvt_pk_fp8_f32 v133, v134, v131 op_sel:[0,0,1]
	v_mul_f32_e32 v131, 0x42000000, v31
	v_mul_f32_e32 v134, 0x42000000, v35
	v_med3_f32 v131, v131, s28, v149
	v_med3_f32 v136, v134, s28, v149
	v_cvt_pk_fp8_f32 v134, v131, v136
	v_mul_f32_e32 v135, 0x42000000, v39
	v_mul_f32_e32 v131, 0x42000000, v43
	v_med3_f32 v135, v135, s28, v149
	v_med3_f32 v131, v131, s28, v149
	v_cvt_pk_fp8_f32 v134, v135, v131 op_sel:[0,0,1]
	v_mul_f32_e32 v131, 0x42000000, v47
	v_mul_f32_e32 v135, 0x42000000, v51
	v_med3_f32 v131, v131, s28, v149
	v_med3_f32 v137, v135, s28, v149
	v_cvt_pk_fp8_f32 v135, v131, v137
	v_mul_f32_e32 v136, 0x42000000, v55
	v_mul_f32_e32 v131, 0x42000000, v59
	v_med3_f32 v136, v136, s28, v149
	v_med3_f32 v131, v131, s28, v149
	v_cvt_pk_fp8_f32 v135, v136, v131 op_sel:[0,0,1]
	v_mul_f32_e32 v131, 0x42000000, v64
	v_mul_f32_e32 v136, 0x42000000, v4
	v_med3_f32 v131, v131, s28, v149
	v_med3_f32 v136, v136, s28, v149
	v_cvt_pk_fp8_f32 v154, v131, v136
	v_mul_f32_e32 v137, 0x42000000, v8
	v_mul_f32_e32 v131, 0x42000000, v12
	v_med3_f32 v136, v137, s28, v149
	v_med3_f32 v131, v131, s28, v149
	v_cvt_pk_fp8_f32 v154, v136, v131 op_sel:[0,0,1]
	v_mul_f32_e32 v131, 0x42000000, v16
	v_mul_f32_e32 v136, 0x42000000, v20
	v_med3_f32 v131, v131, s28, v149
	v_med3_f32 v136, v136, s28, v149
	v_cvt_pk_fp8_f32 v155, v131, v136
	v_mul_f32_e32 v137, 0x42000000, v24
	v_mul_f32_e32 v131, 0x42000000, v28
	v_med3_f32 v136, v137, s28, v149
	v_med3_f32 v131, v131, s28, v149
	v_cvt_pk_fp8_f32 v155, v136, v131 op_sel:[0,0,1]
	v_mul_f32_e32 v131, 0x42000000, v32
	v_mul_f32_e32 v136, 0x42000000, v36
	v_med3_f32 v131, v131, s28, v149
	v_med3_f32 v136, v136, s28, v149
	v_cvt_pk_fp8_f32 v156, v131, v136
	v_mul_f32_e32 v137, 0x42000000, v40
	v_mul_f32_e32 v131, 0x42000000, v44
	v_med3_f32 v136, v137, s28, v149
	v_med3_f32 v131, v131, s28, v149
	v_cvt_pk_fp8_f32 v156, v136, v131 op_sel:[0,0,1]
	v_mul_f32_e32 v131, 0x42000000, v48
	v_mul_f32_e32 v136, 0x42000000, v52
	v_med3_f32 v131, v131, s28, v149
	v_med3_f32 v136, v136, s28, v149
	v_cvt_pk_fp8_f32 v157, v131, v136
	v_mul_f32_e32 v137, 0x42000000, v56
	v_mul_f32_e32 v131, 0x42000000, v60
	v_med3_f32 v136, v137, s28, v149
	v_med3_f32 v131, v131, s28, v149
	v_cvt_pk_fp8_f32 v157, v136, v131 op_sel:[0,0,1]
	v_mul_f32_e32 v131, 0x42000000, v65
	v_mul_f32_e32 v136, 0x42000000, v5
	v_med3_f32 v131, v131, s28, v149
	v_med3_f32 v136, v136, s28, v149
	v_cvt_pk_fp8_f32 v158, v131, v136
	v_mul_f32_e32 v137, 0x42000000, v9
	v_mul_f32_e32 v131, 0x42000000, v13
	v_med3_f32 v136, v137, s28, v149
	v_med3_f32 v131, v131, s28, v149
	v_cvt_pk_fp8_f32 v158, v136, v131 op_sel:[0,0,1]
	v_mul_f32_e32 v131, 0x42000000, v17
	v_mul_f32_e32 v136, 0x42000000, v21
	v_med3_f32 v131, v131, s28, v149
	v_med3_f32 v136, v136, s28, v149
	v_cvt_pk_fp8_f32 v159, v131, v136
	v_mul_f32_e32 v137, 0x42000000, v25
	v_mul_f32_e32 v131, 0x42000000, v29
	v_med3_f32 v136, v137, s28, v149
	v_med3_f32 v131, v131, s28, v149
	v_cvt_pk_fp8_f32 v159, v136, v131 op_sel:[0,0,1]
	v_mul_f32_e32 v131, 0x42000000, v33
	v_mul_f32_e32 v136, 0x42000000, v37
	v_med3_f32 v131, v131, s28, v149
	v_med3_f32 v136, v136, s28, v149
	v_cvt_pk_fp8_f32 v160, v131, v136
	v_mul_f32_e32 v137, 0x42000000, v41
	v_mul_f32_e32 v131, 0x42000000, v45
	v_med3_f32 v136, v137, s28, v149
	v_med3_f32 v131, v131, s28, v149
	v_cvt_pk_fp8_f32 v160, v136, v131 op_sel:[0,0,1]
	v_mul_f32_e32 v131, 0x42000000, v49
	v_mul_f32_e32 v136, 0x42000000, v53
	v_med3_f32 v131, v131, s28, v149
	v_med3_f32 v136, v136, s28, v149
	v_cvt_pk_fp8_f32 v161, v131, v136
	v_mul_f32_e32 v137, 0x42000000, v57
	v_mul_f32_e32 v131, 0x42000000, v61
	v_med3_f32 v136, v137, s28, v149
	v_med3_f32 v131, v131, s28, v149
	v_cvt_pk_fp8_f32 v161, v136, v131 op_sel:[0,0,1]
	s_add_i32 s58, s27, 0xffffff80
	s_cmp_ge_i32 s58, s100
	ds_write_b128 v150, v[132:135] offset:144
	ds_write_b128 v150, v[154:157] offset:288
	ds_write_b128 v150, v[158:161] offset:432
	s_cbranch_scc1 .LBB0_443
	s_cmpk_lt_i32 s58, 0x21c0
	s_cselect_b64 s[6:7], -1, 0
	v_cndmask_b32_e64 v153, 0, 1, s[6:7]
	s_and_b64 s[6:7], s[6:7], exec
	s_cselect_b32 s7, s29, 0xffffde40
	s_movk_i32 s55, 0x800
	s_cselect_b32 s15, 8, 7
	s_cselect_b32 s22, s37, 0x7f
	s_waitcnt lgkmcnt(0)
	s_cselect_b32 s25, s11, s17
	s_cselect_b32 s63, s10, s16
	s_cselect_b32 s65, s30, s33
	s_cselect_b32 s67, s3, s31
	s_cselect_b32 s54, 0x1000, s55
	s_cselect_b32 s23, 23, 22
	s_cselect_b32 s69, 4, 3
	s_cselect_b32 s71, 12, 11
	s_cselect_b32 s64, s38, 0x6000
	s_cselect_b32 s66, s39, 0xa000
	s_cselect_b32 s68, s40, 0xc000
	s_cselect_b32 s70, s41, 0xe000
	s_cselect_b32 s72, s42, 0x12000
	s_cselect_b32 s74, s43, 0x14000
	s_cselect_b32 s76, s44, 0x16000
	s_cselect_b32 s78, s45, 0x18000
	s_cselect_b32 s24, s46, 0x1a000
	s_cselect_b32 s14, s47, 0x1c000
	s_cselect_b32 s6, s48, 0x1e000
	s_add_i32 s7, s7, s27
	s_addk_i32 s7, 0xff80
	s_lshr_b32 s20, s7, s15
	s_and_b32 s7, s7, s22
	s_lshl_b64 s[22:23], s[20:21], s23
	s_lshl_b64 s[56:57], s[22:23], 2
	s_add_u32 s15, s63, s56
	s_addc_u32 s25, s25, s57
	s_add_u32 s22, s67, s22
	s_addc_u32 s23, s65, s23
	s_lshr_b32 s20, s54, 8
	s_lshr_b32 s56, s7, s69
	s_lshl_b32 s56, s56, 7
	s_add_i32 s20, s20, -1
	s_and_b32 s7, s20, s7
	s_add_i32 s20, s56, s26
	s_lshl_b64 s[80:81], s[20:21], s71
	s_lshl_b32 s57, s7, 8
	s_lshl_b64 s[80:81], s[80:81], 2
	s_add_u32 s15, s15, s80
	s_addc_u32 s20, s25, s81
	s_lshl_b32 s7, s7, 10
	s_add_u32 s80, s15, s7
	s_addc_u32 s81, s20, 0
	v_lshlrev_b32_e32 v140, 2, v138
	v_lshl_add_u64 v[58:59], s[80:81], 0, v[140:141]
	s_lshl_b32 s20, s54, 2
	v_lshl_add_u64 v[2:3], v[58:59], 0, s[20:21]
	s_lshl_b32 s20, s54, 3
	v_lshl_add_u64 v[6:7], v[58:59], 0, s[20:21]
	s_lshl_b32 s20, s54, 4
	s_mov_b32 s65, s21
	v_lshl_add_u64 v[14:15], v[58:59], 0, s[20:21]
	s_mov_b32 s67, s21
	s_mov_b32 s69, s21
	s_mov_b32 s71, s21
	s_lshl_b32 s20, s54, 5
	s_mov_b32 s73, s21
	s_mov_b32 s75, s21
	s_mov_b32 s77, s21
	s_mov_b32 s79, s21
	s_mov_b32 s25, s21
	s_mov_b32 s15, s21
	s_mov_b32 s7, s21
	v_lshl_add_u64 v[10:11], v[58:59], 0, s[64:65]
	v_lshl_add_u64 v[18:19], v[58:59], 0, s[66:67]
	v_lshl_add_u64 v[22:23], v[58:59], 0, s[68:69]
	v_lshl_add_u64 v[26:27], v[58:59], 0, s[70:71]
	v_lshl_add_u64 v[30:31], v[58:59], 0, s[20:21]
	v_lshl_add_u64 v[34:35], v[58:59], 0, s[72:73]
	v_lshl_add_u64 v[38:39], v[58:59], 0, s[74:75]
	v_lshl_add_u64 v[42:43], v[58:59], 0, s[76:77]
	v_lshl_add_u64 v[46:47], v[58:59], 0, s[78:79]
	v_lshl_add_u64 v[50:51], v[58:59], 0, s[24:25]
	v_lshl_add_u64 v[54:55], v[58:59], 0, s[14:15]
	v_lshl_add_u64 v[58:59], v[58:59], 0, s[6:7]
	global_load_dwordx4 v[2:5], v[2:3], off nt
	s_nop 0
	global_load_dwordx4 v[6:9], v[6:7], off nt
	s_nop 0
	global_load_dwordx4 v[10:13], v[10:11], off nt
	s_nop 0
	global_load_dwordx4 v[14:17], v[14:15], off nt
	s_nop 0
	global_load_dwordx4 v[18:21], v[18:19], off nt
	s_nop 0
	global_load_dwordx4 v[22:25], v[22:23], off nt
	s_nop 0
	global_load_dwordx4 v[26:29], v[26:27], off nt
	s_nop 0
	global_load_dwordx4 v[30:33], v[30:31], off nt
	s_nop 0
	global_load_dwordx4 v[34:37], v[34:35], off nt
	s_nop 0
	global_load_dwordx4 v[38:41], v[38:39], off nt
	s_nop 0
	global_load_dwordx4 v[42:45], v[42:43], off nt
	s_nop 0
	global_load_dwordx4 v[46:49], v[46:47], off nt
	s_nop 0
	global_load_dwordx4 v[50:53], v[50:51], off nt
	s_nop 0
	global_load_dwordx4 v[54:57], v[54:55], off nt
	s_nop 0
	global_load_dwordx4 v[62:65], v140, s[80:81] nt
	s_nop 0
	global_load_dwordx4 v[58:61], v[58:59], off nt

.LBB0_451:
	v_ashrrev_i32_e32 v137, 31, v134
	v_mad_u64_u32 v[134:135], s[4:5], v134, s61, v[144:145]
	v_mov_b32_e32 v136, v135
	v_mad_u64_u32 v[136:137], s[4:5], v137, s61, v[136:137]
	v_mov_b32_e32 v135, v136
	s_cmp_lt_i32 s27, s98
	s_waitcnt lgkmcnt(0)
	global_store_dwordx4 v[134:135], v[130:133], off nt
	s_cbranch_scc0 .LBB0_439
	s_nop 0
	v_mul_f32_e32 v130, 0x42000000, v122
	v_mul_f32_e32 v131, 0x42000000, v66
	v_med3_f32 v133, v130, s28, v149
	v_med3_f32 v131, v131, s28, v149
	v_cvt_pk_fp8_f32 v130, v133, v131
	v_mul_f32_e32 v132, 0x42000000, v70
	v_mul_f32_e32 v131, 0x42000000, v74
	v_med3_f32 v132, v132, s28, v149
	v_med3_f32 v131, v131, s28, v149
	v_cvt_pk_fp8_f32 v130, v132, v131 op_sel:[0,0,1]
	v_mul_f32_e32 v131, 0x42000000, v78
	v_mul_f32_e32 v132, 0x42000000, v82
	v_med3_f32 v134, v131, s28, v149
	v_med3_f32 v132, v132, s28, v149
	v_cvt_pk_fp8_f32 v131, v134, v132
	v_mul_f32_e32 v133, 0x42000000, v86
	v_mul_f32_e32 v132, 0x42000000, v90
	v_med3_f32 v133, v133, s28, v149
	v_med3_f32 v132, v132, s28, v149
	v_cvt_pk_fp8_f32 v131, v133, v132 op_sel:[0,0,1]
	v_mul_f32_e32 v132, 0x42000000, v94
	v_mul_f32_e32 v133, 0x42000000, v98
	v_med3_f32 v135, v132, s28, v149
	v_med3_f32 v133, v133, s28, v149
	v_cvt_pk_fp8_f32 v132, v135, v133
	v_mul_f32_e32 v134, 0x42000000, v102
	v_mul_f32_e32 v133, 0x42000000, v106
	v_med3_f32 v134, v134, s28, v149
	v_med3_f32 v133, v133, s28, v149
	v_cvt_pk_fp8_f32 v132, v134, v133 op_sel:[0,0,1]
	v_mul_f32_e32 v133, 0x42000000, v110
	v_mul_f32_e32 v134, 0x42000000, v114
	v_med3_f32 v136, v133, s28, v149
	v_med3_f32 v134, v134, s28, v149
	v_cvt_pk_fp8_f32 v133, v136, v134
	v_mul_f32_e32 v135, 0x42000000, v118
	v_mul_f32_e32 v134, 0x42000000, v126
	v_med3_f32 v135, v135, s28, v149
	v_med3_f32 v134, v134, s28, v149
	v_cvt_pk_fp8_f32 v133, v135, v134 op_sel:[0,0,1]
	v_mul_f32_e32 v134, 0x42000000, v123
	v_mul_f32_e32 v135, 0x42000000, v67
	v_med3_f32 v137, v134, s28, v149
	v_med3_f32 v135, v135, s28, v149
	v_cvt_pk_fp8_f32 v134, v137, v135
	v_mul_f32_e32 v136, 0x42000000, v71
	v_mul_f32_e32 v135, 0x42000000, v75
	v_med3_f32 v136, v136, s28, v149
	v_med3_f32 v135, v135, s28, v149
	v_cvt_pk_fp8_f32 v134, v136, v135 op_sel:[0,0,1]
	v_mul_f32_e32 v135, 0x42000000, v79
	v_mul_f32_e32 v136, 0x42000000, v83
	v_med3_f32 v140, v135, s28, v149
	v_med3_f32 v136, v136, s28, v149
	v_cvt_pk_fp8_f32 v135, v140, v136
	v_mul_f32_e32 v137, 0x42000000, v87
	v_mul_f32_e32 v136, 0x42000000, v91
	v_med3_f32 v137, v137, s28, v149
	v_med3_f32 v136, v136, s28, v149
	v_cvt_pk_fp8_f32 v135, v137, v136 op_sel:[0,0,1]
	v_mul_f32_e32 v136, 0x42000000, v95
	v_mul_f32_e32 v137, 0x42000000, v99
	v_med3_f32 v144, v136, s28, v149
	v_med3_f32 v137, v137, s28, v149
	v_cvt_pk_fp8_f32 v136, v144, v137
	v_mul_f32_e32 v140, 0x42000000, v103
	v_mul_f32_e32 v137, 0x42000000, v107
	v_med3_f32 v140, v140, s28, v149
	v_med3_f32 v137, v137, s28, v149
	v_cvt_pk_fp8_f32 v136, v140, v137 op_sel:[0,0,1]
	v_mul_f32_e32 v137, 0x42000000, v111
	v_mul_f32_e32 v140, 0x42000000, v115
	v_med3_f32 v145, v137, s28, v149
	v_med3_f32 v140, v140, s28, v149
	v_cvt_pk_fp8_f32 v137, v145, v140
	v_mul_f32_e32 v144, 0x42000000, v119
	v_mul_f32_e32 v140, 0x42000000, v127
	v_med3_f32 v144, v144, s28, v149
	v_med3_f32 v140, v140, s28, v149
	v_cvt_pk_fp8_f32 v137, v144, v140 op_sel:[0,0,1]
	v_mul_f32_e32 v140, 0x42000000, v124
	v_mul_f32_e32 v144, 0x42000000, v68
	v_med3_f32 v140, v140, s28, v149
	v_med3_f32 v144, v144, s28, v149
	v_cvt_pk_fp8_f32 v154, v140, v144
	v_mul_f32_e32 v145, 0x42000000, v72
	v_mul_f32_e32 v140, 0x42000000, v76
	v_med3_f32 v144, v145, s28, v149
	v_med3_f32 v140, v140, s28, v149
	v_cvt_pk_fp8_f32 v154, v144, v140 op_sel:[0,0,1]
	v_mul_f32_e32 v140, 0x42000000, v80
	v_mul_f32_e32 v144, 0x42000000, v84
	v_med3_f32 v140, v140, s28, v149
	v_med3_f32 v144, v144, s28, v149
	v_cvt_pk_fp8_f32 v155, v140, v144
	v_mul_f32_e32 v145, 0x42000000, v88
	v_mul_f32_e32 v140, 0x42000000, v92
	v_med3_f32 v144, v145, s28, v149
	v_med3_f32 v140, v140, s28, v149
	v_cvt_pk_fp8_f32 v155, v144, v140 op_sel:[0,0,1]
	v_mul_f32_e32 v140, 0x42000000, v96
	v_mul_f32_e32 v144, 0x42000000, v100
	v_med3_f32 v140, v140, s28, v149
	v_med3_f32 v144, v144, s28, v149
	v_cvt_pk_fp8_f32 v156, v140, v144
	v_mul_f32_e32 v145, 0x42000000, v104
	v_mul_f32_e32 v140, 0x42000000, v108
	v_med3_f32 v144, v145, s28, v149
	v_med3_f32 v140, v140, s28, v149
	v_cvt_pk_fp8_f32 v156, v144, v140 op_sel:[0,0,1]
	v_mul_f32_e32 v140, 0x42000000, v112
	v_mul_f32_e32 v144, 0x42000000, v116
	v_med3_f32 v140, v140, s28, v149
	v_med3_f32 v144, v144, s28, v149
	v_cvt_pk_fp8_f32 v157, v140, v144
	v_mul_f32_e32 v145, 0x42000000, v120
	v_mul_f32_e32 v140, 0x42000000, v128
	v_med3_f32 v144, v145, s28, v149
	v_med3_f32 v140, v140, s28, v149
	v_cvt_pk_fp8_f32 v157, v144, v140 op_sel:[0,0,1]
	v_mul_f32_e32 v140, 0x42000000, v125
	v_mul_f32_e32 v144, 0x42000000, v69
	v_med3_f32 v140, v140, s28, v149
	v_med3_f32 v144, v144, s28, v149
	v_cvt_pk_fp8_f32 v158, v140, v144
	v_mul_f32_e32 v145, 0x42000000, v73
	v_mul_f32_e32 v140, 0x42000000, v77
	v_med3_f32 v144, v145, s28, v149
	v_med3_f32 v140, v140, s28, v149
	v_cvt_pk_fp8_f32 v158, v144, v140 op_sel:[0,0,1]
	v_mul_f32_e32 v140, 0x42000000, v81
	v_mul_f32_e32 v144, 0x42000000, v85
	v_med3_f32 v140, v140, s28, v149
	v_med3_f32 v144, v144, s28, v149
	v_cvt_pk_fp8_f32 v159, v140, v144
	v_mul_f32_e32 v145, 0x42000000, v89
	v_mul_f32_e32 v140, 0x42000000, v93
	v_med3_f32 v144, v145, s28, v149
	v_med3_f32 v140, v140, s28, v149
	v_cvt_pk_fp8_f32 v159, v144, v140 op_sel:[0,0,1]
	v_mul_f32_e32 v140, 0x42000000, v97
	v_mul_f32_e32 v144, 0x42000000, v101
	v_med3_f32 v140, v140, s28, v149
	v_med3_f32 v144, v144, s28, v149
	v_cvt_pk_fp8_f32 v160, v140, v144
	v_mul_f32_e32 v145, 0x42000000, v105
	v_mul_f32_e32 v140, 0x42000000, v109
	v_med3_f32 v144, v145, s28, v149
	v_med3_f32 v140, v140, s28, v149
	v_cvt_pk_fp8_f32 v160, v144, v140 op_sel:[0,0,1]
	v_mul_f32_e32 v140, 0x42000000, v113
	v_mul_f32_e32 v144, 0x42000000, v117
	v_med3_f32 v140, v140, s28, v149
	v_med3_f32 v144, v144, s28, v149
	v_cvt_pk_fp8_f32 v161, v140, v144
	v_mul_f32_e32 v145, 0x42000000, v121
	v_mul_f32_e32 v140, 0x42000000, v129
	v_med3_f32 v144, v145, s28, v149
	v_med3_f32 v140, v140, s28, v149
	v_cvt_pk_fp8_f32 v161, v144, v140 op_sel:[0,0,1]
	ds_write_b128 v150, v[130:133] offset:36864
	ds_write_b128 v150, v[134:137] offset:37008
	ds_write_b128 v150, v[154:157] offset:37152
	ds_write_b128 v150, v[158:161] offset:37296
	s_cmp_lt_i32 s27, s100
	s_mov_b32 s65, s36
	s_mov_b32 s66, s53
	v_mov_b32_e32 v154, v1
	s_mov_b32 s63, s49
	s_mov_b32 s64, s52
	s_mov_b64 s[24:25], s[18:19]
	s_cbranch_scc0 .LBB0_454
	s_cmpk_lt_i32 s27, 0x21c0
	s_cselect_b64 s[4:5], -1, 0
	v_cndmask_b32_e64 v154, 0, 1, s[4:5]
	s_and_b64 s[4:5], s[4:5], exec
	s_cselect_b32 s5, s29, 0xffffde40
	s_movk_i32 s64, 0x800
	s_cselect_b32 s7, 8, 7
	s_cselect_b32 s15, s37, 0x7f
	s_cselect_b32 s59, s11, s17
	s_cselect_b32 s61, s10, s16
	s_cselect_b32 s62, s30, s33
	s_cselect_b32 s65, s3, s31
	s_cselect_b32 s63, 0x1000, s64
	s_cselect_b32 s24, 23, 22
	s_cselect_b32 s69, 4, 3
	s_cselect_b32 s71, 12, 11
	s_cselect_b32 s60, s38, 0x6000
	s_cselect_b32 s68, s39, 0xa000
	s_cselect_b32 s70, s40, 0xc000
	s_cselect_b32 s72, s41, 0xe000
	s_cselect_b32 s74, s42, 0x12000
	s_cselect_b32 s76, s43, 0x14000
	s_cselect_b32 s78, s44, 0x16000
	s_cselect_b32 s80, s45, 0x18000
	s_cselect_b32 s14, s46, 0x1a000
	s_cselect_b32 s6, s47, 0x1c000
	s_cselect_b32 s4, s48, 0x1e000
	s_add_i32 s5, s5, s27
	s_lshr_b32 s20, s5, s7
	s_lshl_b64 s[24:25], s[20:21], s24
	s_and_b32 s5, s5, s15
	s_lshl_b64 s[66:67], s[24:25], 2
	s_add_u32 s7, s61, s66
	s_addc_u32 s15, s59, s67
	s_add_u32 s24, s65, s24
	s_addc_u32 s25, s62, s25
	s_lshr_b32 s20, s63, 8
	s_lshr_b32 s59, s5, s69
	s_lshl_b32 s66, s59, 7
	s_add_i32 s20, s20, -1
	s_and_b32 s5, s20, s5
	s_add_i32 s20, s66, s26
	s_lshl_b64 s[82:83], s[20:21], s71
	s_lshl_b32 s65, s5, 8
	s_lshl_b64 s[82:83], s[82:83], 2
	s_add_u32 s7, s7, s82
	s_addc_u32 s15, s15, s83
	s_lshl_b32 s5, s5, 10
	s_add_u32 s82, s7, s5
	s_addc_u32 s83, s15, 0
	v_lshlrev_b32_e32 v140, 2, v138
	v_lshl_add_u64 v[122:123], s[82:83], 0, v[140:141]
	s_lshl_b32 s20, s63, 2
	v_lshl_add_u64 v[66:67], v[122:123], 0, s[20:21]
	s_lshl_b32 s20, s63, 3
	v_lshl_add_u64 v[70:71], v[122:123], 0, s[20:21]
	s_lshl_b32 s20, s63, 4
	s_mov_b32 s61, s21
	v_lshl_add_u64 v[78:79], v[122:123], 0, s[20:21]
	s_mov_b32 s69, s21
	s_mov_b32 s71, s21
	s_mov_b32 s73, s21
	s_lshl_b32 s20, s63, 5
	s_mov_b32 s75, s21
	s_mov_b32 s77, s21
	s_mov_b32 s79, s21
	s_mov_b32 s81, s21
	s_mov_b32 s15, s21
	s_mov_b32 s7, s21
	s_mov_b32 s5, s21
	v_lshl_add_u64 v[74:75], v[122:123], 0, s[60:61]
	v_lshl_add_u64 v[82:83], v[122:123], 0, s[68:69]
	v_lshl_add_u64 v[86:87], v[122:123], 0, s[70:71]
	v_lshl_add_u64 v[90:91], v[122:123], 0, s[72:73]
	v_lshl_add_u64 v[94:95], v[122:123], 0, s[20:21]
	v_lshl_add_u64 v[98:99], v[122:123], 0, s[74:75]
	v_lshl_add_u64 v[102:103], v[122:123], 0, s[76:77]
	v_lshl_add_u64 v[106:107], v[122:123], 0, s[78:79]
	v_lshl_add_u64 v[110:111], v[122:123], 0, s[80:81]
	v_lshl_add_u64 v[114:115], v[122:123], 0, s[14:15]
	v_lshl_add_u64 v[118:119], v[122:123], 0, s[6:7]
	v_lshl_add_u64 v[126:127], v[122:123], 0, s[4:5]
	global_load_dwordx4 v[66:69], v[66:67], off nt
	s_nop 0
	global_load_dwordx4 v[70:73], v[70:71], off nt
	s_nop 0
	global_load_dwordx4 v[74:77], v[74:75], off nt
	s_nop 0
	global_load_dwordx4 v[78:81], v[78:79], off nt
	s_nop 0
	global_load_dwordx4 v[82:85], v[82:83], off nt
	s_nop 0
	global_load_dwordx4 v[86:89], v[86:87], off nt
	s_nop 0
	global_load_dwordx4 v[90:93], v[90:91], off nt
	s_nop 0
	global_load_dwordx4 v[94:97], v[94:95], off nt
	s_nop 0
	global_load_dwordx4 v[98:101], v[98:99], off nt
	s_nop 0
	global_load_dwordx4 v[102:105], v[102:103], off nt
	s_nop 0
	global_load_dwordx4 v[106:109], v[106:107], off nt
	s_nop 0
	global_load_dwordx4 v[110:113], v[110:111], off nt
	s_nop 0
	global_load_dwordx4 v[114:117], v[114:115], off nt
	s_nop 0
	global_load_dwordx4 v[118:121], v[118:119], off nt
	s_nop 0
	global_load_dwordx4 v[122:125], v140, s[82:83] nt
	s_nop 0
	global_load_dwordx4 v[126:129], v[126:127], off nt

; __device__ __forceinline__ unsigned cvt_pk_bf16(float lo, float hi) { unsigned r; asm volatile("v_cvt_pk_bf16_f32 %0, %1, %2" : "=v"(r) : "v"(lo), "v"(hi)); return r; }
; __device__ __forceinline__ unsigned pk4_fp8(float a, float b, float c, float d) {
;     a = __builtin_amdgcn_fmed3f(a, -448.f, 448.f); b = __builtin_amdgcn_fmed3f(b, -448.f, 448.f); c = __builtin_amdgcn_fmed3f(c, -448.f, 448.f); d = __builtin_amdgcn_fmed3f(d, -448.f, 448.f);
;     int w = 0; w = __builtin_amdgcn_cvt_pk_fp8_f32(a, b, w, false); w = __builtin_amdgcn_cvt_pk_fp8_f32(c, d, w, true); return (unsigned)w; }
;     __device__ __forceinline__ void operator()(EPI_ARGS) const {
;     ...
;         for (int bj = 0; bj < 2; ++bj) { const int col = u.e * 256 + bj * 128 + wc * 32 + 8 * fq; const f32x4 s0 = *(const f32x4*)(scale + col), s1 = *(const f32x4*)(scale + col + 4);
; #pragma unroll
;             for (int ai = 0; ai < 2; ++ai)
; #pragma unroll
;                 for (int m = 0; m < 4; ++m) { const int row = u.pm * 256 + ai * 128 + wr * 64 + m * 16 + fr; const f32x4 v0 = acc[ai][bj][m][0] * s0, v1 = acc[ai][bj][m][1] * s1;
;                     if (PO_FP8) { v2u w; w.x = pk4_fp8(v0[0], v0[1], v0[2], v0[3]); w.y = pk4_fp8(v1[0], v1[1], v1[2], v1[3]); *(v2u*)((unsigned char*)PM + (size_t)row * PW + col) = w; }
;                     else { u32x4 w; w.x = cvt_pk_bf16(v0[0], v0[1]); w.y = cvt_pk_bf16(v0[2], v0[3]); w.z = cvt_pk_bf16(v1[0], v1[1]); w.w = cvt_pk_bf16(v1[2], v1[3]);
;                     *(u32x4*)(PM + (size_t)row * PW + col) = w; } } }
.LBB0_659:
	v_lshl_or_b32 v138, s30, 8, v1
	v_ashrrev_i32_e32 v139, 31, v138
	v_lshl_add_u64 v[140:141], v[138:139], 2, s[10:11]
	global_load_dwordx4 v[134:137], v[140:141], off
	global_load_dwordx4 v[130:133], v[140:141], off offset:16
	v_lshl_add_u32 v148, s28, 8, v209
	v_or_b32_e32 v158, 48, v148
	v_ashrrev_i32_e32 v149, 31, v148
	v_or_b32_e32 v142, 16, v148
	v_or_b32_e32 v144, 32, v148
	v_ashrrev_i32_e32 v159, 31, v158
	v_lshlrev_b64 v[146:147], 10, v[148:149]
	v_ashrrev_i32_e32 v143, 31, v142
	v_ashrrev_i32_e32 v145, 31, v144
	v_lshl_add_u64 v[146:147], s[16:17], 0, v[146:147]
	v_lshlrev_b64 v[160:161], 10, v[142:143]
	v_lshlrev_b64 v[144:145], 10, v[144:145]
	v_lshl_add_u64 v[142:143], v[146:147], 0, v[138:139]
	v_lshl_add_u64 v[146:147], s[16:17], 0, v[160:161]
	v_lshl_add_u64 v[160:161], s[16:17], 0, v[144:145]
	v_lshl_add_u64 v[144:145], v[146:147], 0, v[138:139]
	v_lshl_add_u64 v[146:147], v[160:161], 0, v[138:139]
	s_and_b64 vcc, exec, s[6:7]
	s_mov_b64 s[6:7], -1
	s_waitcnt vmcnt(0)
	v_pk_mul_f32 v[94:95], v[94:95], v[134:135]
	v_pk_mul_f32 v[98:99], v[98:99], v[130:131]
	v_pk_mul_f32 v[100:101], v[100:101], v[132:133]
	v_med3_f32 v98, v98, s70, v214
	v_med3_f32 v99, v99, s70, v214
	v_cvt_pk_fp8_f32 v157, v98, v99
	v_med3_f32 v98, v101, s70, v214
	v_pk_mul_f32 v[90:91], v[90:91], v[130:131]
	v_med3_f32 v101, v94, s70, v214
	v_med3_f32 v95, v95, s70, v214
	v_pk_mul_f32 v[92:93], v[92:93], v[132:133]
	v_cvt_pk_fp8_f32 v94, v101, v95
	v_med3_f32 v90, v90, s70, v214
	v_med3_f32 v91, v91, s70, v214
	v_pk_mul_f32 v[86:87], v[86:87], v[134:135]
	v_cvt_pk_fp8_f32 v95, v90, v91
	v_med3_f32 v91, v93, s70, v214
	v_pk_mul_f32 v[78:79], v[78:79], v[130:131]
	v_med3_f32 v93, v86, s70, v214
	v_med3_f32 v87, v87, s70, v214
	v_pk_mul_f32 v[80:81], v[80:81], v[132:133]
	v_cvt_pk_fp8_f32 v86, v93, v87
	v_med3_f32 v78, v78, s70, v214
	v_med3_f32 v79, v79, s70, v214
	v_pk_mul_f32 v[66:67], v[66:67], v[134:135]
	v_cvt_pk_fp8_f32 v87, v78, v79
	v_med3_f32 v79, v81, s70, v214
	v_pk_mul_f32 v[58:59], v[58:59], v[130:131]
	v_med3_f32 v81, v66, s70, v214
	v_med3_f32 v67, v67, s70, v214
	v_pk_mul_f32 v[60:61], v[60:61], v[132:133]
	v_cvt_pk_fp8_f32 v66, v81, v67
	v_med3_f32 v58, v58, s70, v214
	v_med3_f32 v59, v59, s70, v214
	v_pk_mul_f32 v[46:47], v[46:47], v[134:135]
	v_pk_mul_f32 v[126:127], v[126:127], v[134:135]
	v_pk_mul_f32 v[122:123], v[122:123], v[130:131]
	v_pk_mul_f32 v[102:103], v[102:103], v[134:135]
	v_cvt_pk_fp8_f32 v67, v58, v59
	v_med3_f32 v59, v61, s70, v214
	v_pk_mul_f32 v[42:43], v[42:43], v[130:131]
	v_med3_f32 v61, v46, s70, v214
	v_med3_f32 v47, v47, s70, v214
	v_pk_mul_f32 v[118:119], v[118:119], v[134:135]
	v_pk_mul_f32 v[114:115], v[114:115], v[130:131]
	v_med3_f32 v126, v126, s70, v214
	v_med3_f32 v127, v127, s70, v214
	v_med3_f32 v122, v122, s70, v214
	v_med3_f32 v123, v123, s70, v214
	v_med3_f32 v102, v102, s70, v214
	v_med3_f32 v103, v103, s70, v214
	v_cvt_pk_fp8_f32 v46, v61, v47
	v_med3_f32 v42, v42, s70, v214
	v_med3_f32 v43, v43, s70, v214
	v_pk_mul_f32 v[110:111], v[110:111], v[134:135]
	v_pk_mul_f32 v[106:107], v[106:107], v[130:131]
	v_med3_f32 v118, v118, s70, v214
	v_med3_f32 v119, v119, s70, v214
	v_med3_f32 v114, v114, s70, v214
	v_med3_f32 v115, v115, s70, v214
	v_cvt_pk_fp8_f32 v150, v126, v127
	v_cvt_pk_fp8_f32 v151, v122, v123
	v_cvt_pk_fp8_f32 v156, v102, v103
	v_cvt_pk_fp8_f32 v47, v42, v43
	v_med3_f32 v110, v110, s70, v214
	v_med3_f32 v111, v111, s70, v214
	v_med3_f32 v106, v106, s70, v214
	v_med3_f32 v107, v107, s70, v214
	v_cvt_pk_fp8_f32 v152, v118, v119
	v_cvt_pk_fp8_f32 v153, v114, v115
	v_pk_mul_f32 v[128:129], v[128:129], v[136:137]
	v_pk_mul_f32 v[124:125], v[124:125], v[132:133]
	v_pk_mul_f32 v[104:105], v[104:105], v[136:137]
	v_med3_f32 v100, v100, s70, v214
	v_cvt_pk_fp8_f32 v154, v110, v111
	v_cvt_pk_fp8_f32 v155, v106, v107
	v_pk_mul_f32 v[96:97], v[96:97], v[136:137]
	v_pk_mul_f32 v[88:89], v[88:89], v[136:137]
	v_pk_mul_f32 v[68:69], v[68:69], v[136:137]
	v_pk_mul_f32 v[48:49], v[48:49], v[136:137]
	v_pk_mul_f32 v[44:45], v[44:45], v[132:133]
	v_pk_mul_f32 v[120:121], v[120:121], v[136:137]
	v_pk_mul_f32 v[116:117], v[116:117], v[132:133]
	v_med3_f32 v128, v128, s70, v214
	v_med3_f32 v129, v129, s70, v214
	v_med3_f32 v124, v124, s70, v214
	v_med3_f32 v125, v125, s70, v214
	v_med3_f32 v104, v104, s70, v214
	v_med3_f32 v105, v105, s70, v214
	v_cvt_pk_fp8_f32 v157, v100, v98 op_sel:[0,0,1]
	v_add_u32_e32 v100, 0x80, v148
	v_med3_f32 v96, v96, s70, v214
	v_med3_f32 v97, v97, s70, v214
	v_med3_f32 v90, v92, s70, v214
	v_add_u32_e32 v92, 0x90, v148
	v_med3_f32 v88, v88, s70, v214
	v_med3_f32 v89, v89, s70, v214
	v_med3_f32 v78, v80, s70, v214
	v_add_u32_e32 v80, 0xa0, v148
	v_med3_f32 v68, v68, s70, v214
	v_med3_f32 v69, v69, s70, v214
	v_med3_f32 v58, v60, s70, v214
	v_add_u32_e32 v60, 0xb0, v148
	v_med3_f32 v48, v48, s70, v214
	v_med3_f32 v49, v49, s70, v214
	v_med3_f32 v42, v44, s70, v214
	v_med3_f32 v43, v45, s70, v214
	v_pk_mul_f32 v[112:113], v[112:113], v[136:137]
	v_pk_mul_f32 v[108:109], v[108:109], v[132:133]
	v_med3_f32 v120, v120, s70, v214
	v_med3_f32 v121, v121, s70, v214
	v_med3_f32 v116, v116, s70, v214
	v_med3_f32 v117, v117, s70, v214
	v_cvt_pk_fp8_f32 v150, v128, v129 op_sel:[0,0,1]
	v_cvt_pk_fp8_f32 v151, v124, v125 op_sel:[0,0,1]
	v_cvt_pk_fp8_f32 v156, v104, v105 op_sel:[0,0,1]
	v_cvt_pk_fp8_f32 v94, v96, v97 op_sel:[0,0,1]
	v_cvt_pk_fp8_f32 v95, v90, v91 op_sel:[0,0,1]
	v_ashrrev_i32_e32 v101, 31, v100
	v_cvt_pk_fp8_f32 v86, v88, v89 op_sel:[0,0,1]
	v_cvt_pk_fp8_f32 v87, v78, v79 op_sel:[0,0,1]
	v_ashrrev_i32_e32 v93, 31, v92
	v_cvt_pk_fp8_f32 v66, v68, v69 op_sel:[0,0,1]
; __device__ __forceinline__ unsigned cvt_pk_bf16(float lo, float hi) { unsigned r; asm volatile("v_cvt_pk_bf16_f32 %0, %1, %2" : "=v"(r) : "v"(lo), "v"(hi)); return r; }
;     __device__ __forceinline__ void operator()(EPI_ARGS) const {
;     ...
;         for (int bj = 0; bj < 2; ++bj) { const int col = u.e * 256 + bj * 128 + wc * 32 + 8 * fq; const f32x4 s0 = *(const f32x4*)(scale + col), s1 = *(const f32x4*)(scale + col + 4);
; #pragma unroll
;             for (int ai = 0; ai < 2; ++ai)
; #pragma unroll
;                 for (int m = 0; m < 4; ++m) { const int row = u.pm * 256 + ai * 128 + wr * 64 + m * 16 + fr; const f32x4 v0 = acc[ai][bj][m][0] * s0, v1 = acc[ai][bj][m][1] * s1;
;                     if (PO_FP8) { v2u w; w.x = pk4_fp8(v0[0], v0[1], v0[2], v0[3]); w.y = pk4_fp8(v1[0], v1[1], v1[2], v1[3]); *(v2u*)((unsigned char*)PM + (size_t)row * PW + col) = w; }
;                     else { u32x4 w; w.x = cvt_pk_bf16(v0[0], v0[1]); w.y = cvt_pk_bf16(v0[2], v0[3]); w.z = cvt_pk_bf16(v1[0], v1[1]); w.w = cvt_pk_bf16(v1[2], v1[3]);
;                     *(u32x4*)(PM + (size_t)row * PW + col) = w; } } }
	v_cvt_pk_fp8_f32 v67, v58, v59 op_sel:[0,0,1]
	v_ashrrev_i32_e32 v81, 31, v80
	v_cvt_pk_fp8_f32 v46, v48, v49 op_sel:[0,0,1]
	v_cvt_pk_fp8_f32 v47, v42, v43 op_sel:[0,0,1]
	v_ashrrev_i32_e32 v61, 31, v60
	v_med3_f32 v112, v112, s70, v214
	v_med3_f32 v113, v113, s70, v214
	v_med3_f32 v108, v108, s70, v214
	v_med3_f32 v109, v109, s70, v214
	v_cvt_pk_fp8_f32 v152, v120, v121 op_sel:[0,0,1]
	v_cvt_pk_fp8_f32 v153, v116, v117 op_sel:[0,0,1]
	v_lshlrev_b64 v[98:99], 10, v[158:159]
	v_lshlrev_b64 v[90:91], 10, v[100:101]
	v_lshlrev_b64 v[78:79], 10, v[92:93]
	v_lshlrev_b64 v[58:59], 10, v[80:81]
	v_lshlrev_b64 v[42:43], 10, v[60:61]
	v_cvt_pk_fp8_f32 v154, v112, v113 op_sel:[0,0,1]
	v_cvt_pk_fp8_f32 v155, v108, v109 op_sel:[0,0,1]
	v_lshl_add_u64 v[98:99], s[16:17], 0, v[98:99]
	v_lshl_add_u64 v[90:91], s[16:17], 0, v[90:91]
	v_lshl_add_u64 v[78:79], s[16:17], 0, v[78:79]
	v_lshl_add_u64 v[58:59], s[16:17], 0, v[58:59]
	v_lshl_add_u64 v[42:43], s[16:17], 0, v[42:43]
	v_lshl_add_u64 v[98:99], v[98:99], 0, v[138:139]
	v_lshl_add_u64 v[90:91], v[90:91], 0, v[138:139]
	v_lshl_add_u64 v[78:79], v[78:79], 0, v[138:139]
	v_lshl_add_u64 v[58:59], v[58:59], 0, v[138:139]
	v_lshl_add_u64 v[60:61], v[42:43], 0, v[138:139]
	global_store_dwordx2 v[142:143], v[150:151], off
	global_store_dwordx2 v[144:145], v[152:153], off
	global_store_dwordx2 v[146:147], v[154:155], off
	global_store_dwordx2 v[98:99], v[156:157], off
	global_store_dwordx2 v[90:91], v[94:95], off
	global_store_dwordx2 v[78:79], v[86:87], off
	global_store_dwordx2 v[58:59], v[66:67], off
	global_store_dwordx2 v[60:61], v[46:47], off
	global_load_dwordx4 v[42:45], v[140:141], off offset:512
	s_nop 0
	global_load_dwordx4 v[46:49], v[140:141], off offset:528
	s_waitcnt vmcnt(1)
	v_pk_mul_f32 v[66:67], v[84:85], v[44:45]
	v_pk_mul_f32 v[68:69], v[82:83], v[42:43]
	s_waitcnt vmcnt(0)
	v_pk_mul_f32 v[74:75], v[74:75], v[46:47]
	v_med3_f32 v68, v68, s70, v214
	v_med3_f32 v69, v69, s70, v214
	v_med3_f32 v80, v66, s70, v214
	v_med3_f32 v81, v67, s70, v214
	v_cvt_pk_fp8_f32 v66, v68, v69
	v_med3_f32 v68, v74, s70, v214
	v_med3_f32 v69, v75, s70, v214
	v_cvt_pk_fp8_f32 v67, v68, v69
	v_pk_mul_f32 v[76:77], v[76:77], v[48:49]
	v_pk_mul_f32 v[62:63], v[62:63], v[46:47]
	v_med3_f32 v68, v76, s70, v214
	v_med3_f32 v69, v77, s70, v214
	v_cvt_pk_fp8_f32 v67, v68, v69 op_sel:[0,0,1]
	v_pk_mul_f32 v[68:69], v[72:73], v[44:45]
	v_med3_f32 v62, v62, s70, v214
	v_med3_f32 v73, v69, s70, v214
	v_med3_f32 v63, v63, s70, v214
	v_cvt_pk_fp8_f32 v69, v62, v63
	v_pk_mul_f32 v[64:65], v[64:65], v[48:49]
	v_pk_mul_f32 v[54:55], v[54:55], v[42:43]
	v_med3_f32 v62, v64, s70, v214
	v_med3_f32 v63, v65, s70, v214
	v_cvt_pk_fp8_f32 v69, v62, v63 op_sel:[0,0,1]
	v_pk_mul_f32 v[50:51], v[50:51], v[46:47]
	v_med3_f32 v62, v54, s70, v214
	v_med3_f32 v55, v55, s70, v214
	v_cvt_pk_fp8_f32 v54, v62, v55
	v_med3_f32 v50, v50, s70, v214
	v_med3_f32 v51, v51, s70, v214
	v_cvt_pk_fp8_f32 v55, v50, v51
	v_pk_mul_f32 v[52:53], v[52:53], v[48:49]
	v_pk_mul_f32 v[38:39], v[38:39], v[42:43]
	v_med3_f32 v50, v52, s70, v214
	v_med3_f32 v51, v53, s70, v214
	v_cvt_pk_fp8_f32 v55, v50, v51 op_sel:[0,0,1]
	v_pk_mul_f32 v[34:35], v[34:35], v[46:47]
	v_med3_f32 v50, v38, s70, v214
	v_med3_f32 v39, v39, s70, v214
	v_cvt_pk_fp8_f32 v38, v50, v39
	v_med3_f32 v34, v34, s70, v214
	v_med3_f32 v35, v35, s70, v214
	v_cvt_pk_fp8_f32 v39, v34, v35
	v_pk_mul_f32 v[36:37], v[36:37], v[48:49]
	v_pk_mul_f32 v[26:27], v[26:27], v[42:43]
	v_med3_f32 v34, v36, s70, v214
	v_med3_f32 v35, v37, s70, v214
	v_cvt_pk_fp8_f32 v39, v34, v35 op_sel:[0,0,1]
	v_pk_mul_f32 v[30:31], v[30:31], v[46:47]
	v_med3_f32 v34, v26, s70, v214
	v_med3_f32 v27, v27, s70, v214
	v_cvt_pk_fp8_f32 v26, v34, v27
	v_med3_f32 v30, v30, s70, v214
	v_med3_f32 v31, v31, s70, v214
	v_cvt_pk_fp8_f32 v27, v30, v31
	v_pk_mul_f32 v[28:29], v[28:29], v[44:45]
	v_pk_mul_f32 v[32:33], v[32:33], v[48:49]
	v_med3_f32 v28, v28, s70, v214
	v_med3_f32 v29, v29, s70, v214
	v_cvt_pk_fp8_f32 v26, v28, v29 op_sel:[0,0,1]
	v_med3_f32 v28, v32, s70, v214
	v_med3_f32 v29, v33, s70, v214
	v_pk_mul_f32 v[18:19], v[18:19], v[42:43]
	v_cvt_pk_fp8_f32 v27, v28, v29 op_sel:[0,0,1]
	v_pk_mul_f32 v[22:23], v[22:23], v[46:47]
	v_med3_f32 v28, v18, s70, v214
	v_med3_f32 v19, v19, s70, v214
	v_cvt_pk_fp8_f32 v18, v28, v19
	v_med3_f32 v22, v22, s70, v214
	v_med3_f32 v23, v23, s70, v214
	v_cvt_pk_fp8_f32 v19, v22, v23
	v_pk_mul_f32 v[20:21], v[20:21], v[44:45]
	v_pk_mul_f32 v[24:25], v[24:25], v[48:49]
	v_med3_f32 v20, v20, s70, v214
	v_med3_f32 v21, v21, s70, v214
	v_cvt_pk_fp8_f32 v18, v20, v21 op_sel:[0,0,1]
	v_med3_f32 v20, v24, s70, v214
	v_med3_f32 v21, v25, s70, v214
	v_pk_mul_f32 v[10:11], v[10:11], v[42:43]
	v_cvt_pk_fp8_f32 v19, v20, v21 op_sel:[0,0,1]
	v_pk_mul_f32 v[14:15], v[14:15], v[46:47]
	v_med3_f32 v20, v10, s70, v214
	v_med3_f32 v11, v11, s70, v214
	v_cvt_pk_fp8_f32 v10, v20, v11
	v_med3_f32 v14, v14, s70, v214
	v_med3_f32 v15, v15, s70, v214
	v_cvt_pk_fp8_f32 v11, v14, v15
	v_pk_mul_f32 v[12:13], v[12:13], v[44:45]
	v_pk_mul_f32 v[70:71], v[70:71], v[42:43]
	v_pk_mul_f32 v[16:17], v[16:17], v[48:49]
	v_med3_f32 v12, v12, s70, v214
	v_med3_f32 v13, v13, s70, v214
	v_med3_f32 v70, v70, s70, v214
	v_med3_f32 v71, v71, s70, v214
	v_med3_f32 v72, v68, s70, v214
	v_cvt_pk_fp8_f32 v10, v12, v13 op_sel:[0,0,1]
	v_med3_f32 v12, v16, s70, v214
	v_med3_f32 v13, v17, s70, v214
	v_pk_mul_f32 v[2:3], v[2:3], v[42:43]
	v_cvt_pk_fp8_f32 v68, v70, v71
	v_cvt_pk_fp8_f32 v11, v12, v13 op_sel:[0,0,1]
	v_pk_mul_f32 v[6:7], v[6:7], v[46:47]
	v_med3_f32 v12, v2, s70, v214
	v_med3_f32 v3, v3, s70, v214
	v_cvt_pk_fp8_f32 v2, v12, v3
	v_med3_f32 v6, v6, s70, v214
	v_med3_f32 v7, v7, s70, v214
	v_cvt_pk_fp8_f32 v3, v6, v7
	v_cvt_pk_fp8_f32 v66, v80, v81 op_sel:[0,0,1]
	v_pk_mul_f32 v[56:57], v[56:57], v[44:45]
	v_pk_mul_f32 v[4:5], v[4:5], v[44:45]
	v_cvt_pk_fp8_f32 v68, v72, v73 op_sel:[0,0,1]
	v_med3_f32 v56, v56, s70, v214
	v_med3_f32 v57, v57, s70, v214
	v_pk_mul_f32 v[40:41], v[40:41], v[44:45]
	v_pk_mul_f32 v[8:9], v[8:9], v[48:49]
	v_med3_f32 v4, v4, s70, v214
	v_med3_f32 v5, v5, s70, v214
	v_cvt_pk_fp8_f32 v54, v56, v57 op_sel:[0,0,1]
	v_med3_f32 v40, v40, s70, v214
	v_med3_f32 v41, v41, s70, v214
	v_cvt_pk_fp8_f32 v2, v4, v5 op_sel:[0,0,1]
	v_med3_f32 v4, v8, s70, v214
	v_med3_f32 v5, v9, s70, v214
	v_cvt_pk_fp8_f32 v38, v40, v41 op_sel:[0,0,1]
	v_cvt_pk_fp8_f32 v3, v4, v5 op_sel:[0,0,1]
	global_store_dwordx2 v[142:143], v[66:67], off offset:128
	global_store_dwordx2 v[144:145], v[68:69], off offset:128
	global_store_dwordx2 v[146:147], v[54:55], off offset:128
	global_store_dwordx2 v[98:99], v[38:39], off offset:128
	global_store_dwordx2 v[90:91], v[26:27], off offset:128
	global_store_dwordx2 v[78:79], v[18:19], off offset:128
	global_store_dwordx2 v[58:59], v[10:11], off offset:128
	global_store_dwordx2 v[60:61], v[2:3], off offset:128
	s_cbranch_vccnz .LBB0_640
	s_andn2_b64 vcc, exec, s[12:13]
	s_cbranch_vccnz .LBB0_639
	s_barrier
	s_branch .LBB0_639

; __device__ __forceinline__ unsigned cvt_pk_bf16(float lo, float hi) { unsigned r; asm volatile("v_cvt_pk_bf16_f32 %0, %1, %2" : "=v"(r) : "v"(lo), "v"(hi)); return r; }
; __device__ __forceinline__ float gelu_tanh_(float x) { const float u = 0.7978845608f * (x + 0.044715f * x * x * x); return x * __builtin_amdgcn_rcpf(1.0f + __builtin_amdgcn_exp2f(-2.88539008178f * u)); }
;     __device__ __forceinline__ void operator()(EPI_ARGS) const {
;     ...
;             for (int bj = 0; bj < 2; ++bj) { const int lc = bj * 128 + wc * 32 + 8 * fq, t = lc >> 4, h0 = lc & 15;
; #pragma unroll
;                 for (int mp = 0; mp < 2; ++mp) { unsigned px[2], py[2];
; #pragma unroll
;                     for (int h = 0; h < 2; ++h) { const int m = 2 * mp + h; f32x4 v0 = acc[ai][bj][m][0], v1 = acc[ai][bj][m][1];
; #pragma unroll
;                         for (int j = 0; j < 4; ++j) { v0[j] = gelu_tanh_(v0[j]); v1[j] = gelu_tanh_(v1[j]); }
;                         if (GLU_FP8) { px[h] = pk4_fp8(v0[0], v0[1], v0[2], v0[3]); py[h] = pk4_fp8(v1[0], v1[1], v1[2], v1[3]); }
;                         else { const int r = u.pm * 256 + ai * 128 + wr * 64 + m * 16 + fr, b = r >> 8, c = r & 255; u32x4 w; w.x = cvt_pk_bf16(v0[0], v0[1]); w.y = cvt_pk_bf16(v0[2], v0[3]); w.z = cvt_pk_bf16(v1[0], v1[1]); w.w = cvt_pk_bf16(v1[2], v1[3]);
;                             *(u32x4*)(YS + (size_t)(b * SEQ + c * CL + t) * SW + u.e * 16 + h0) = w; } }
;                     if (GLU_FP8) { const u32x4 q = pair16(px[0], py[0], px[1], py[1]);
;                         const int r = u.pm * 256 + ai * 128 + wr * 64 + (2 * mp + (fq & 1)) * 16 + fr, b = r >> 8, c = r & 255;
;                         *(u32x4*)((unsigned char*)YS + (size_t)(b * SEQ + c * CL + t) * SW + u.e * 16) = q; } } }
.LBB0_783:
	s_mov_b32 s90, 0xbdd2d3e7
	v_mov_b32_e32 v231, 0xc0135761
	v_mul_f32_e32 v130, v126, v126
	v_fma_f32 v130, v130, s90, v231
	v_mul_f32_e32 v130, v126, v130
	v_exp_f32_e32 v130, v130
	v_mul_f32_e32 v131, v122, v122
	v_fma_f32 v131, v131, s90, v231
	v_mul_f32_e32 v131, v122, v131
	v_add_f32_e32 v130, 1.0, v130
	v_rcp_f32_e32 v130, v130
	v_exp_f32_e32 v131, v131
	v_mul_f32_e32 v132, v123, v123
	v_fma_f32 v132, v132, s90, v231
	v_mul_f32_e32 v126, v126, v130
	v_add_f32_e32 v130, 1.0, v131
	v_mul_f32_e32 v131, v127, v127
	v_fma_f32 v131, v131, s90, v231
	v_mul_f32_e32 v131, v127, v131
	v_exp_f32_e32 v131, v131
	v_mul_f32_e32 v132, v123, v132
	v_exp_f32_e32 v132, v132
	v_add_f32_e32 v131, 1.0, v131
	v_rcp_f32_e32 v130, v130
	v_rcp_f32_e32 v131, v131
	v_add_f32_e32 v132, 1.0, v132
	v_rcp_f32_e32 v132, v132
	v_mul_f32_e32 v130, v122, v130
	v_mul_f32_e32 v122, v127, v131
	v_mul_f32_e32 v131, v124, v124
	v_fma_f32 v131, v131, s90, v231
	v_mul_f32_e32 v131, v124, v131
	v_mul_f32_e32 v133, v128, v128
	v_mul_f32_e32 v123, v123, v132
	v_mul_f32_e32 v132, v129, v129
	v_fma_f32 v133, v133, s90, v231
	v_fma_f32 v132, v132, s90, v231
	v_mul_f32_e32 v133, v128, v133
	v_exp_f32_e32 v131, v131
	v_mul_f32_e32 v132, v129, v132
	v_exp_f32_e32 v133, v133
	v_exp_f32_e32 v132, v132
	v_add_f32_e32 v131, 1.0, v131
	v_rcp_f32_e32 v131, v131
	v_add_f32_e32 v127, 1.0, v133
	v_add_f32_e32 v132, 1.0, v132
	v_rcp_f32_e32 v127, v127
	v_rcp_f32_e32 v132, v132
	v_mul_f32_e32 v133, v125, v125
	v_fma_f32 v133, v133, s90, v231
	v_mul_f32_e32 v124, v124, v131
	v_med3_f32 v126, v126, s61, v230
	v_med3_f32 v131, v122, s61, v230
	v_mul_f32_e32 v133, v125, v133
	v_cvt_pk_fp8_f32 v122, v126, v131
	v_mul_f32_e32 v127, v128, v127
	v_mul_f32_e32 v128, v129, v132
	v_exp_f32_e32 v133, v133
	v_med3_f32 v126, v127, s61, v230
	v_med3_f32 v127, v128, s61, v230
	v_cvt_pk_fp8_f32 v122, v126, v127 op_sel:[0,0,1]
	v_med3_f32 v126, v130, s61, v230
	v_med3_f32 v127, v123, s61, v230
	v_cvt_pk_fp8_f32 v123, v126, v127
	v_mul_f32_e32 v126, v118, v118
	v_fma_f32 v126, v126, s90, v231
	v_add_f32_e32 v129, 1.0, v133
	v_mul_f32_e32 v126, v118, v126
	v_rcp_f32_e32 v129, v129
	v_exp_f32_e32 v126, v126
	v_mul_f32_e32 v125, v125, v129
	v_med3_f32 v124, v124, s61, v230
	v_med3_f32 v125, v125, s61, v230
	v_cvt_pk_fp8_f32 v123, v124, v125 op_sel:[0,0,1]
	v_add_f32_e32 v124, 1.0, v126
	v_mul_f32_e32 v125, v114, v114
	v_mul_f32_e32 v126, v119, v119
	v_fma_f32 v125, v125, s90, v231
	v_fma_f32 v126, v126, s90, v231
	v_mul_f32_e32 v125, v114, v125
	v_mul_f32_e32 v126, v119, v126
	v_exp_f32_e32 v125, v125
	v_exp_f32_e32 v126, v126
	v_mul_f32_e32 v127, v115, v115
	v_fma_f32 v127, v127, s90, v231
	v_add_f32_e32 v125, 1.0, v125
	v_add_f32_e32 v126, 1.0, v126
	v_rcp_f32_e32 v125, v125
	v_rcp_f32_e32 v126, v126
	v_mul_f32_e32 v127, v115, v127
	v_rcp_f32_e32 v124, v124
	v_exp_f32_e32 v127, v127
	v_mul_f32_e32 v114, v114, v125
	v_mul_f32_e32 v119, v119, v126
	v_mul_f32_e32 v125, v120, v120
	v_mul_f32_e32 v126, v116, v116
	v_fma_f32 v125, v125, s90, v231
	v_fma_f32 v126, v126, s90, v231
	v_mul_f32_e32 v125, v120, v125
	v_mul_f32_e32 v126, v116, v126
	v_mul_f32_e32 v118, v118, v124
	v_add_f32_e32 v124, 1.0, v127
	v_rcp_f32_e32 v124, v124
	v_exp_f32_e32 v125, v125
	v_exp_f32_e32 v126, v126
	v_mul_f32_e32 v127, v117, v117
	v_mul_f32_e32 v115, v115, v124
	v_add_f32_e32 v124, 1.0, v125
	v_add_f32_e32 v125, 1.0, v126
	v_mul_f32_e32 v126, v121, v121
	v_fma_f32 v127, v127, s90, v231
	v_fma_f32 v126, v126, s90, v231
	v_mul_f32_e32 v127, v117, v127
	v_mul_f32_e32 v126, v121, v126
	v_exp_f32_e32 v127, v127
	v_exp_f32_e32 v126, v126
	v_rcp_f32_e32 v125, v125
	v_rcp_f32_e32 v124, v124
	v_add_f32_e32 v127, 1.0, v127
	v_add_f32_e32 v126, 1.0, v126
	v_rcp_f32_e32 v127, v127
	v_rcp_f32_e32 v126, v126
	v_mul_f32_e32 v116, v116, v125
	v_med3_f32 v114, v114, s61, v230
	v_med3_f32 v115, v115, s61, v230
	v_mul_f32_e32 v120, v120, v124
	v_med3_f32 v118, v118, s61, v230
	v_med3_f32 v119, v119, s61, v230
	v_cvt_pk_fp8_f32 v125, v114, v115
	v_cvt_pk_fp8_f32 v124, v118, v119
	v_mul_f32_e32 v117, v117, v127
	v_mul_f32_e32 v121, v121, v126
	v_med3_f32 v114, v116, s61, v230
	v_med3_f32 v115, v117, s61, v230
	v_med3_f32 v120, v120, s61, v230
	v_med3_f32 v121, v121, s61, v230
	v_cvt_pk_fp8_f32 v125, v114, v115 op_sel:[0,0,1]
	v_lshl_add_u32 v114, s64, 12, v225
	v_cvt_pk_fp8_f32 v124, v120, v121 op_sel:[0,0,1]
	v_or_b32_e32 v116, v114, v223
	v_mul_f32_e32 v115, v110, v110
	v_fma_f32 v115, v115, s90, v231
	v_ashrrev_i32_e32 v117, 31, v116
	s_lshl_b32 s22, s65, 4
	v_mul_f32_e32 v115, v110, v115
	v_lshlrev_b64 v[116:117], 10, v[116:117]
	s_ashr_i32 s23, s22, 31
	v_lshl_add_u64 v[116:117], s[10:11], 0, v[116:117]
	v_permlane16_swap_b32_e32 v122, v124
	v_permlane16_swap_b32_e32 v123, v125
	v_lshl_add_u64 v[116:117], v[116:117], 0, s[22:23]
	v_exp_f32_e32 v115, v115
	v_mul_f32_e32 v118, v106, v106
	global_store_dwordx4 v[116:117], v[122:125], off
	v_mul_f32_e32 v116, v111, v111
	v_fma_f32 v118, v118, s90, v231
	v_fma_f32 v116, v116, s90, v231
	v_mul_f32_e32 v118, v106, v118
	v_mul_f32_e32 v116, v111, v116
	v_mul_f32_e32 v117, v107, v107
	v_add_f32_e32 v115, 1.0, v115
	v_fma_f32 v117, v117, s90, v231
	v_rcp_f32_e32 v115, v115
	v_exp_f32_e32 v118, v118
	v_exp_f32_e32 v116, v116
	v_mul_f32_e32 v117, v107, v117
	v_exp_f32_e32 v117, v117
	v_mul_f32_e32 v110, v110, v115
	v_add_f32_e32 v115, 1.0, v118
	v_add_f32_e32 v116, 1.0, v116
	v_rcp_f32_e32 v115, v115
	v_rcp_f32_e32 v116, v116
	v_add_f32_e32 v117, 1.0, v117
	v_rcp_f32_e32 v117, v117
	v_mul_f32_e32 v115, v106, v115
	v_mul_f32_e32 v106, v111, v116
	v_mul_f32_e32 v116, v108, v108
	v_fma_f32 v116, v116, s90, v231
; __device__ __forceinline__ unsigned cvt_pk_bf16(float lo, float hi) { unsigned r; asm volatile("v_cvt_pk_bf16_f32 %0, %1, %2" : "=v"(r) : "v"(lo), "v"(hi)); return r; }
; __device__ __forceinline__ float gelu_tanh_(float x) { const float u = 0.7978845608f * (x + 0.044715f * x * x * x); return x * __builtin_amdgcn_rcpf(1.0f + __builtin_amdgcn_exp2f(-2.88539008178f * u)); }
;     __device__ __forceinline__ void operator()(EPI_ARGS) const {
;     ...
;             for (int bj = 0; bj < 2; ++bj) { const int lc = bj * 128 + wc * 32 + 8 * fq, t = lc >> 4, h0 = lc & 15;
; #pragma unroll
;                 for (int mp = 0; mp < 2; ++mp) { unsigned px[2], py[2];
; #pragma unroll
;                     for (int h = 0; h < 2; ++h) { const int m = 2 * mp + h; f32x4 v0 = acc[ai][bj][m][0], v1 = acc[ai][bj][m][1];
; #pragma unroll
;                         for (int j = 0; j < 4; ++j) { v0[j] = gelu_tanh_(v0[j]); v1[j] = gelu_tanh_(v1[j]); }
;                         if (GLU_FP8) { px[h] = pk4_fp8(v0[0], v0[1], v0[2], v0[3]); py[h] = pk4_fp8(v1[0], v1[1], v1[2], v1[3]); }
;                         else { const int r = u.pm * 256 + ai * 128 + wr * 64 + m * 16 + fr, b = r >> 8, c = r & 255; u32x4 w; w.x = cvt_pk_bf16(v0[0], v0[1]); w.y = cvt_pk_bf16(v0[2], v0[3]); w.z = cvt_pk_bf16(v1[0], v1[1]); w.w = cvt_pk_bf16(v1[2], v1[3]);
;                             *(u32x4*)(YS + (size_t)(b * SEQ + c * CL + t) * SW + u.e * 16 + h0) = w; } }
;                     if (GLU_FP8) { const u32x4 q = pair16(px[0], py[0], px[1], py[1]);
;                         const int r = u.pm * 256 + ai * 128 + wr * 64 + (2 * mp + (fq & 1)) * 16 + fr, b = r >> 8, c = r & 255;
;                         *(u32x4*)((unsigned char*)YS + (size_t)(b * SEQ + c * CL + t) * SW + u.e * 16) = q; } } }
	v_mul_f32_e32 v116, v108, v116
	v_mul_f32_e32 v118, v112, v112
	v_mul_f32_e32 v107, v107, v117
	v_mul_f32_e32 v117, v113, v113
	v_fma_f32 v118, v118, s90, v231
	v_fma_f32 v117, v117, s90, v231
	v_mul_f32_e32 v118, v112, v118
	v_exp_f32_e32 v116, v116
	v_mul_f32_e32 v117, v113, v117
	v_exp_f32_e32 v118, v118
	v_exp_f32_e32 v117, v117
	v_add_f32_e32 v116, 1.0, v116
	v_rcp_f32_e32 v116, v116
	v_add_f32_e32 v111, 1.0, v118
	v_add_f32_e32 v117, 1.0, v117
	v_rcp_f32_e32 v111, v111
	v_rcp_f32_e32 v117, v117
	v_mul_f32_e32 v118, v109, v109
	v_fma_f32 v118, v118, s90, v231
	v_mul_f32_e32 v108, v108, v116
	v_med3_f32 v110, v110, s61, v230
	v_med3_f32 v116, v106, s61, v230
	v_mul_f32_e32 v118, v109, v118
	v_cvt_pk_fp8_f32 v106, v110, v116
	v_mul_f32_e32 v111, v112, v111
	v_mul_f32_e32 v112, v113, v117
	v_exp_f32_e32 v118, v118
	v_med3_f32 v110, v111, s61, v230
	v_med3_f32 v111, v112, s61, v230
	v_cvt_pk_fp8_f32 v106, v110, v111 op_sel:[0,0,1]
	v_med3_f32 v110, v115, s61, v230
	v_med3_f32 v111, v107, s61, v230
	v_cvt_pk_fp8_f32 v107, v110, v111
	v_mul_f32_e32 v110, v102, v102
	v_fma_f32 v110, v110, s90, v231
	v_add_f32_e32 v113, 1.0, v118
	v_mul_f32_e32 v110, v102, v110
	v_rcp_f32_e32 v113, v113
	v_exp_f32_e32 v110, v110
	v_mul_f32_e32 v109, v109, v113
	v_med3_f32 v108, v108, s61, v230
	v_med3_f32 v109, v109, s61, v230
	v_cvt_pk_fp8_f32 v107, v108, v109 op_sel:[0,0,1]
	v_add_f32_e32 v108, 1.0, v110
	v_mul_f32_e32 v109, v98, v98
	v_mul_f32_e32 v110, v103, v103
	v_fma_f32 v109, v109, s90, v231
	v_fma_f32 v110, v110, s90, v231
	v_mul_f32_e32 v109, v98, v109
	v_mul_f32_e32 v110, v103, v110
	v_exp_f32_e32 v109, v109
	v_exp_f32_e32 v110, v110
	v_mul_f32_e32 v111, v99, v99
	v_fma_f32 v111, v111, s90, v231
	v_add_f32_e32 v109, 1.0, v109
	v_add_f32_e32 v110, 1.0, v110
	v_rcp_f32_e32 v109, v109
	v_rcp_f32_e32 v110, v110
	v_mul_f32_e32 v111, v99, v111
	v_rcp_f32_e32 v108, v108
	v_exp_f32_e32 v111, v111
	v_mul_f32_e32 v98, v98, v109
	v_mul_f32_e32 v103, v103, v110
	v_mul_f32_e32 v109, v104, v104
	v_mul_f32_e32 v110, v100, v100
	v_fma_f32 v109, v109, s90, v231
	v_fma_f32 v110, v110, s90, v231
	v_mul_f32_e32 v109, v104, v109
	v_mul_f32_e32 v110, v100, v110
	v_mul_f32_e32 v102, v102, v108
	v_add_f32_e32 v108, 1.0, v111
	v_mul_f32_e32 v111, v101, v101
	v_fma_f32 v111, v111, s90, v231
	v_rcp_f32_e32 v108, v108
	v_exp_f32_e32 v109, v109
	v_exp_f32_e32 v110, v110
	v_mul_f32_e32 v111, v101, v111
	v_exp_f32_e32 v111, v111
	v_mul_f32_e32 v99, v99, v108
	v_add_f32_e32 v108, 1.0, v109
	v_add_f32_e32 v109, 1.0, v110
	v_mul_f32_e32 v110, v105, v105
	v_fma_f32 v110, v110, s90, v231
	v_rcp_f32_e32 v109, v109
	v_mul_f32_e32 v110, v105, v110
	v_add_f32_e32 v111, 1.0, v111
	v_rcp_f32_e32 v111, v111
	v_exp_f32_e32 v110, v110
	v_mul_f32_e32 v100, v100, v109
	v_med3_f32 v98, v98, s61, v230
	v_med3_f32 v99, v99, s61, v230
	v_cvt_pk_fp8_f32 v109, v98, v99
	v_rcp_f32_e32 v108, v108
	v_mul_f32_e32 v101, v101, v111
	v_add_f32_e32 v110, 1.0, v110
	v_med3_f32 v98, v100, s61, v230
	v_med3_f32 v99, v101, s61, v230
	v_rcp_f32_e32 v110, v110
	v_cvt_pk_fp8_f32 v109, v98, v99 op_sel:[0,0,1]
	v_mul_f32_e32 v99, v94, v94
	v_mul_f32_e32 v104, v104, v108
	v_med3_f32 v102, v102, s61, v230
	v_med3_f32 v103, v103, s61, v230
	v_fma_f32 v99, v99, s90, v231
	v_cvt_pk_fp8_f32 v108, v102, v103
	v_mul_f32_e32 v99, v94, v99
	v_mul_f32_e32 v105, v105, v110
	v_med3_f32 v104, v104, s61, v230
	v_med3_f32 v105, v105, s61, v230
	v_or_b32_e32 v100, 0x200, v114
	v_exp_f32_e32 v101, v99
	v_cvt_pk_fp8_f32 v108, v104, v105 op_sel:[0,0,1]
	v_or_b32_e32 v98, v100, v223
	v_ashrrev_i32_e32 v99, 31, v98
	v_lshlrev_b64 v[98:99], 10, v[98:99]
	v_lshl_add_u64 v[98:99], s[10:11], 0, v[98:99]
	v_add_f32_e32 v101, 1.0, v101
	v_permlane16_swap_b32_e32 v106, v108
	v_permlane16_swap_b32_e32 v107, v109
	v_rcp_f32_e32 v101, v101
	v_lshl_add_u64 v[98:99], v[98:99], 0, s[22:23]
	v_mul_f32_e32 v102, v90, v90
	global_store_dwordx4 v[98:99], v[106:109], off
	v_mul_f32_e32 v99, v95, v95
	v_fma_f32 v102, v102, s90, v231
	v_fma_f32 v99, v99, s90, v231
	v_mul_f32_e32 v102, v90, v102
	v_mul_f32_e32 v99, v95, v99
	v_mul_f32_e32 v94, v94, v101
	v_mul_f32_e32 v101, v91, v91
	v_fma_f32 v101, v101, s90, v231
	v_exp_f32_e32 v102, v102
	v_exp_f32_e32 v99, v99
	v_mul_f32_e32 v101, v91, v101
	v_exp_f32_e32 v101, v101
	v_add_f32_e32 v98, 1.0, v102
	v_add_f32_e32 v99, 1.0, v99
	v_rcp_f32_e32 v98, v98
	v_rcp_f32_e32 v99, v99
	v_add_f32_e32 v101, 1.0, v101
	v_rcp_f32_e32 v101, v101
	v_mul_f32_e32 v98, v90, v98
	v_mul_f32_e32 v90, v95, v99
	v_mul_f32_e32 v99, v92, v92
	v_fma_f32 v99, v99, s90, v231
	v_mul_f32_e32 v99, v92, v99
	v_mul_f32_e32 v102, v96, v96
	v_mul_f32_e32 v91, v91, v101
	v_mul_f32_e32 v101, v97, v97
	v_fma_f32 v102, v102, s90, v231
	v_fma_f32 v101, v101, s90, v231
	v_mul_f32_e32 v102, v96, v102
	v_exp_f32_e32 v99, v99
	v_mul_f32_e32 v101, v97, v101
	v_exp_f32_e32 v102, v102
	v_exp_f32_e32 v101, v101
	v_add_f32_e32 v99, 1.0, v99
	v_rcp_f32_e32 v99, v99
	v_add_f32_e32 v95, 1.0, v102
	v_add_f32_e32 v101, 1.0, v101
	v_rcp_f32_e32 v95, v95
	v_rcp_f32_e32 v101, v101
	v_mul_f32_e32 v102, v93, v93
	v_fma_f32 v102, v102, s90, v231
	v_mul_f32_e32 v92, v92, v99
	v_med3_f32 v94, v94, s61, v230
	v_med3_f32 v99, v90, s61, v230
	v_mul_f32_e32 v102, v93, v102
	v_cvt_pk_fp8_f32 v90, v94, v99
	v_mul_f32_e32 v95, v96, v95
	v_mul_f32_e32 v96, v97, v101
	v_exp_f32_e32 v102, v102
	v_med3_f32 v94, v95, s61, v230
	v_med3_f32 v95, v96, s61, v230
	v_cvt_pk_fp8_f32 v90, v94, v95 op_sel:[0,0,1]
	v_med3_f32 v94, v98, s61, v230
	v_med3_f32 v95, v91, s61, v230
	v_cvt_pk_fp8_f32 v91, v94, v95
	v_mul_f32_e32 v94, v86, v86
	v_fma_f32 v94, v94, s90, v231
	v_add_f32_e32 v97, 1.0, v102
; __device__ __forceinline__ unsigned cvt_pk_bf16(float lo, float hi) { unsigned r; asm volatile("v_cvt_pk_bf16_f32 %0, %1, %2" : "=v"(r) : "v"(lo), "v"(hi)); return r; }
; __device__ __forceinline__ float gelu_tanh_(float x) { const float u = 0.7978845608f * (x + 0.044715f * x * x * x); return x * __builtin_amdgcn_rcpf(1.0f + __builtin_amdgcn_exp2f(-2.88539008178f * u)); }
;     __device__ __forceinline__ void operator()(EPI_ARGS) const {
;     ...
;             for (int bj = 0; bj < 2; ++bj) { const int lc = bj * 128 + wc * 32 + 8 * fq, t = lc >> 4, h0 = lc & 15;
; #pragma unroll
;                 for (int mp = 0; mp < 2; ++mp) { unsigned px[2], py[2];
; #pragma unroll
;                     for (int h = 0; h < 2; ++h) { const int m = 2 * mp + h; f32x4 v0 = acc[ai][bj][m][0], v1 = acc[ai][bj][m][1];
; #pragma unroll
;                         for (int j = 0; j < 4; ++j) { v0[j] = gelu_tanh_(v0[j]); v1[j] = gelu_tanh_(v1[j]); }
;                         if (GLU_FP8) { px[h] = pk4_fp8(v0[0], v0[1], v0[2], v0[3]); py[h] = pk4_fp8(v1[0], v1[1], v1[2], v1[3]); }
;                         else { const int r = u.pm * 256 + ai * 128 + wr * 64 + m * 16 + fr, b = r >> 8, c = r & 255; u32x4 w; w.x = cvt_pk_bf16(v0[0], v0[1]); w.y = cvt_pk_bf16(v0[2], v0[3]); w.z = cvt_pk_bf16(v1[0], v1[1]); w.w = cvt_pk_bf16(v1[2], v1[3]);
;                             *(u32x4*)(YS + (size_t)(b * SEQ + c * CL + t) * SW + u.e * 16 + h0) = w; } }
;                     if (GLU_FP8) { const u32x4 q = pair16(px[0], py[0], px[1], py[1]);
;                         const int r = u.pm * 256 + ai * 128 + wr * 64 + (2 * mp + (fq & 1)) * 16 + fr, b = r >> 8, c = r & 255;
;                         *(u32x4*)((unsigned char*)YS + (size_t)(b * SEQ + c * CL + t) * SW + u.e * 16) = q; } } }
	v_mul_f32_e32 v94, v86, v94
	v_rcp_f32_e32 v97, v97
	v_exp_f32_e32 v94, v94
	v_mul_f32_e32 v93, v93, v97
	v_med3_f32 v92, v92, s61, v230
	v_med3_f32 v93, v93, s61, v230
	v_cvt_pk_fp8_f32 v91, v92, v93 op_sel:[0,0,1]
	v_add_f32_e32 v92, 1.0, v94
	v_mul_f32_e32 v93, v82, v82
	v_mul_f32_e32 v94, v87, v87
	v_fma_f32 v93, v93, s90, v231
	v_fma_f32 v94, v94, s90, v231
	v_mul_f32_e32 v93, v82, v93
	v_mul_f32_e32 v94, v87, v94
	v_exp_f32_e32 v93, v93
	v_exp_f32_e32 v94, v94
	v_mul_f32_e32 v95, v83, v83
	v_fma_f32 v95, v95, s90, v231
	v_add_f32_e32 v93, 1.0, v93
	v_add_f32_e32 v94, 1.0, v94
	v_rcp_f32_e32 v93, v93
	v_rcp_f32_e32 v94, v94
	v_mul_f32_e32 v95, v83, v95
	v_rcp_f32_e32 v92, v92
	v_exp_f32_e32 v95, v95
	v_mul_f32_e32 v82, v82, v93
	v_mul_f32_e32 v87, v87, v94
	v_mul_f32_e32 v93, v88, v88
	v_mul_f32_e32 v94, v84, v84
	v_fma_f32 v93, v93, s90, v231
	v_fma_f32 v94, v94, s90, v231
	v_mul_f32_e32 v93, v88, v93
	v_mul_f32_e32 v94, v84, v94
	v_mul_f32_e32 v86, v86, v92
	v_add_f32_e32 v92, 1.0, v95
	v_mul_f32_e32 v95, v85, v85
	v_fma_f32 v95, v95, s90, v231
	v_rcp_f32_e32 v92, v92
	v_exp_f32_e32 v93, v93
	v_exp_f32_e32 v94, v94
	v_mul_f32_e32 v95, v85, v95
	v_exp_f32_e32 v95, v95
	v_mul_f32_e32 v83, v83, v92
	v_add_f32_e32 v92, 1.0, v93
	v_add_f32_e32 v93, 1.0, v94
	v_mul_f32_e32 v94, v89, v89
	v_fma_f32 v94, v94, s90, v231
	v_rcp_f32_e32 v93, v93
	v_mul_f32_e32 v94, v89, v94
	v_add_f32_e32 v95, 1.0, v95
	v_rcp_f32_e32 v95, v95
	v_exp_f32_e32 v94, v94
	v_mul_f32_e32 v84, v84, v93
	v_med3_f32 v82, v82, s61, v230
	v_med3_f32 v83, v83, s61, v230
	v_cvt_pk_fp8_f32 v93, v82, v83
	v_rcp_f32_e32 v92, v92
	v_mul_f32_e32 v85, v85, v95
	v_add_f32_e32 v94, 1.0, v94
	v_med3_f32 v82, v84, s61, v230
	v_med3_f32 v83, v85, s61, v230
	v_rcp_f32_e32 v94, v94
	v_cvt_pk_fp8_f32 v93, v82, v83 op_sel:[0,0,1]
	v_mul_f32_e32 v83, v78, v78
	v_mul_f32_e32 v88, v88, v92
	v_med3_f32 v86, v86, s61, v230
	v_med3_f32 v87, v87, s61, v230
	v_fma_f32 v83, v83, s90, v231
	v_cvt_pk_fp8_f32 v92, v86, v87
	v_mul_f32_e32 v83, v78, v83
	v_mul_f32_e32 v89, v89, v94
	v_med3_f32 v88, v88, s61, v230
	v_med3_f32 v89, v89, s61, v230
	v_exp_f32_e32 v84, v83
	v_cvt_pk_fp8_f32 v92, v88, v89 op_sel:[0,0,1]
	v_or_b32_e32 v82, v114, v224
	v_ashrrev_i32_e32 v83, 31, v82
	v_lshlrev_b64 v[82:83], 10, v[82:83]
	v_lshl_add_u64 v[82:83], s[10:11], 0, v[82:83]
	v_add_f32_e32 v84, 1.0, v84
	v_permlane16_swap_b32_e32 v90, v92
	v_permlane16_swap_b32_e32 v91, v93
	v_rcp_f32_e32 v84, v84
	v_lshl_add_u64 v[82:83], v[82:83], 0, s[22:23]
	v_mul_f32_e32 v85, v74, v74
	global_store_dwordx4 v[82:83], v[90:93], off
	v_mul_f32_e32 v83, v79, v79
	v_fma_f32 v85, v85, s90, v231
	v_fma_f32 v83, v83, s90, v231
	v_mul_f32_e32 v85, v74, v85
	v_mul_f32_e32 v83, v79, v83
	v_mul_f32_e32 v78, v78, v84
	v_mul_f32_e32 v84, v75, v75
	v_fma_f32 v84, v84, s90, v231
	v_exp_f32_e32 v85, v85
	v_exp_f32_e32 v83, v83
	v_mul_f32_e32 v84, v75, v84
	v_exp_f32_e32 v84, v84
	v_add_f32_e32 v82, 1.0, v85
	v_add_f32_e32 v83, 1.0, v83
	v_rcp_f32_e32 v82, v82
	v_rcp_f32_e32 v83, v83
	v_add_f32_e32 v84, 1.0, v84
	v_rcp_f32_e32 v84, v84
	v_mul_f32_e32 v82, v74, v82
	v_mul_f32_e32 v74, v79, v83
	v_mul_f32_e32 v83, v76, v76
	v_fma_f32 v83, v83, s90, v231
	v_mul_f32_e32 v83, v76, v83
	v_mul_f32_e32 v85, v80, v80
	v_mul_f32_e32 v75, v75, v84
	v_mul_f32_e32 v84, v81, v81
	v_fma_f32 v85, v85, s90, v231
	v_fma_f32 v84, v84, s90, v231
	v_mul_f32_e32 v85, v80, v85
	v_exp_f32_e32 v83, v83
	v_mul_f32_e32 v84, v81, v84
	v_exp_f32_e32 v85, v85
	v_exp_f32_e32 v84, v84
	v_add_f32_e32 v83, 1.0, v83
	v_rcp_f32_e32 v83, v83
	v_add_f32_e32 v79, 1.0, v85
	v_add_f32_e32 v84, 1.0, v84
	v_rcp_f32_e32 v79, v79
	v_rcp_f32_e32 v84, v84
	v_mul_f32_e32 v85, v77, v77
	v_fma_f32 v85, v85, s90, v231
	v_mul_f32_e32 v76, v76, v83
	v_med3_f32 v78, v78, s61, v230
	v_med3_f32 v83, v74, s61, v230
	v_mul_f32_e32 v85, v77, v85
	v_cvt_pk_fp8_f32 v74, v78, v83
	v_mul_f32_e32 v79, v80, v79
	v_mul_f32_e32 v80, v81, v84
	v_exp_f32_e32 v85, v85
	v_med3_f32 v78, v79, s61, v230
	v_med3_f32 v79, v80, s61, v230
	v_cvt_pk_fp8_f32 v74, v78, v79 op_sel:[0,0,1]
	v_med3_f32 v78, v82, s61, v230
	v_med3_f32 v79, v75, s61, v230
	v_cvt_pk_fp8_f32 v75, v78, v79
	v_mul_f32_e32 v78, v70, v70
	v_fma_f32 v78, v78, s90, v231
	v_add_f32_e32 v81, 1.0, v85
	v_mul_f32_e32 v78, v70, v78
	v_rcp_f32_e32 v81, v81
	v_exp_f32_e32 v78, v78
	v_mul_f32_e32 v77, v77, v81
	v_med3_f32 v76, v76, s61, v230
	v_med3_f32 v77, v77, s61, v230
	v_cvt_pk_fp8_f32 v75, v76, v77 op_sel:[0,0,1]
	v_add_f32_e32 v76, 1.0, v78
	v_mul_f32_e32 v77, v66, v66
	v_mul_f32_e32 v78, v71, v71
	v_fma_f32 v77, v77, s90, v231
	v_fma_f32 v78, v78, s90, v231
	v_mul_f32_e32 v77, v66, v77
	v_mul_f32_e32 v78, v71, v78
	v_exp_f32_e32 v77, v77
	v_exp_f32_e32 v78, v78
	v_mul_f32_e32 v79, v67, v67
	v_fma_f32 v79, v79, s90, v231
	v_add_f32_e32 v77, 1.0, v77
	v_add_f32_e32 v78, 1.0, v78
	v_rcp_f32_e32 v77, v77
	v_rcp_f32_e32 v78, v78
	v_mul_f32_e32 v79, v67, v79
	v_rcp_f32_e32 v76, v76
	v_exp_f32_e32 v79, v79
	v_mul_f32_e32 v66, v66, v77
	v_mul_f32_e32 v71, v71, v78
	v_mul_f32_e32 v77, v72, v72
	v_mul_f32_e32 v78, v68, v68
	v_fma_f32 v77, v77, s90, v231
	v_fma_f32 v78, v78, s90, v231
	v_mul_f32_e32 v77, v72, v77
	v_mul_f32_e32 v78, v68, v78
	v_mul_f32_e32 v70, v70, v76
	v_add_f32_e32 v76, 1.0, v79
	v_mul_f32_e32 v79, v69, v69
	v_fma_f32 v79, v79, s90, v231
	v_rcp_f32_e32 v76, v76
	v_exp_f32_e32 v77, v77
	v_exp_f32_e32 v78, v78
	v_mul_f32_e32 v79, v69, v79
	v_exp_f32_e32 v79, v79
	v_mul_f32_e32 v67, v67, v76
	v_add_f32_e32 v76, 1.0, v77
	v_add_f32_e32 v77, 1.0, v78
	v_mul_f32_e32 v78, v73, v73
	v_fma_f32 v78, v78, s90, v231
	v_rcp_f32_e32 v77, v77
; __device__ __forceinline__ unsigned cvt_pk_bf16(float lo, float hi) { unsigned r; asm volatile("v_cvt_pk_bf16_f32 %0, %1, %2" : "=v"(r) : "v"(lo), "v"(hi)); return r; }
; __device__ __forceinline__ float gelu_tanh_(float x) { const float u = 0.7978845608f * (x + 0.044715f * x * x * x); return x * __builtin_amdgcn_rcpf(1.0f + __builtin_amdgcn_exp2f(-2.88539008178f * u)); }
;     __device__ __forceinline__ void operator()(EPI_ARGS) const {
;     ...
;             for (int bj = 0; bj < 2; ++bj) { const int lc = bj * 128 + wc * 32 + 8 * fq, t = lc >> 4, h0 = lc & 15;
; #pragma unroll
;                 for (int mp = 0; mp < 2; ++mp) { unsigned px[2], py[2];
; #pragma unroll
;                     for (int h = 0; h < 2; ++h) { const int m = 2 * mp + h; f32x4 v0 = acc[ai][bj][m][0], v1 = acc[ai][bj][m][1];
; #pragma unroll
;                         for (int j = 0; j < 4; ++j) { v0[j] = gelu_tanh_(v0[j]); v1[j] = gelu_tanh_(v1[j]); }
;                         if (GLU_FP8) { px[h] = pk4_fp8(v0[0], v0[1], v0[2], v0[3]); py[h] = pk4_fp8(v1[0], v1[1], v1[2], v1[3]); }
;                         else { const int r = u.pm * 256 + ai * 128 + wr * 64 + m * 16 + fr, b = r >> 8, c = r & 255; u32x4 w; w.x = cvt_pk_bf16(v0[0], v0[1]); w.y = cvt_pk_bf16(v0[2], v0[3]); w.z = cvt_pk_bf16(v1[0], v1[1]); w.w = cvt_pk_bf16(v1[2], v1[3]);
;                             *(u32x4*)(YS + (size_t)(b * SEQ + c * CL + t) * SW + u.e * 16 + h0) = w; } }
;                     if (GLU_FP8) { const u32x4 q = pair16(px[0], py[0], px[1], py[1]);
;                         const int r = u.pm * 256 + ai * 128 + wr * 64 + (2 * mp + (fq & 1)) * 16 + fr, b = r >> 8, c = r & 255;
;                         *(u32x4*)((unsigned char*)YS + (size_t)(b * SEQ + c * CL + t) * SW + u.e * 16) = q; } } }
	v_mul_f32_e32 v78, v73, v78
	v_add_f32_e32 v79, 1.0, v79
	v_rcp_f32_e32 v79, v79
	v_exp_f32_e32 v78, v78
	v_mul_f32_e32 v68, v68, v77
	v_med3_f32 v66, v66, s61, v230
	v_med3_f32 v67, v67, s61, v230
	v_cvt_pk_fp8_f32 v77, v66, v67
	v_rcp_f32_e32 v76, v76
	v_mul_f32_e32 v69, v69, v79
	v_add_f32_e32 v78, 1.0, v78
	v_med3_f32 v66, v68, s61, v230
	v_med3_f32 v67, v69, s61, v230
	v_rcp_f32_e32 v78, v78
	v_cvt_pk_fp8_f32 v77, v66, v67 op_sel:[0,0,1]
	v_mul_f32_e32 v67, v62, v62
	v_mul_f32_e32 v72, v72, v76
	v_med3_f32 v70, v70, s61, v230
	v_med3_f32 v71, v71, s61, v230
	v_fma_f32 v67, v67, s90, v231
	v_cvt_pk_fp8_f32 v76, v70, v71
	v_mul_f32_e32 v67, v62, v67
	v_mul_f32_e32 v73, v73, v78
	v_med3_f32 v72, v72, s61, v230
	v_med3_f32 v73, v73, s61, v230
	v_exp_f32_e32 v68, v67
	v_cvt_pk_fp8_f32 v76, v72, v73 op_sel:[0,0,1]
	v_or_b32_e32 v66, v100, v224
	v_ashrrev_i32_e32 v67, 31, v66
	v_lshlrev_b64 v[66:67], 10, v[66:67]
	v_lshl_add_u64 v[66:67], s[10:11], 0, v[66:67]
	v_add_f32_e32 v68, 1.0, v68
	v_permlane16_swap_b32_e32 v74, v76
	v_permlane16_swap_b32_e32 v75, v77
	v_rcp_f32_e32 v68, v68
	v_lshl_add_u64 v[66:67], v[66:67], 0, s[22:23]
	v_mul_f32_e32 v69, v58, v58
	global_store_dwordx4 v[66:67], v[74:77], off
	v_mul_f32_e32 v67, v63, v63
	v_fma_f32 v69, v69, s90, v231
	v_fma_f32 v67, v67, s90, v231
	v_mul_f32_e32 v69, v58, v69
	v_mul_f32_e32 v67, v63, v67
	v_mul_f32_e32 v62, v62, v68
	v_mul_f32_e32 v68, v59, v59
	v_fma_f32 v68, v68, s90, v231
	v_exp_f32_e32 v69, v69
	v_exp_f32_e32 v67, v67
	v_mul_f32_e32 v68, v59, v68
	v_exp_f32_e32 v68, v68
	v_add_f32_e32 v66, 1.0, v69
	v_add_f32_e32 v67, 1.0, v67
	v_rcp_f32_e32 v66, v66
	v_rcp_f32_e32 v67, v67
	v_add_f32_e32 v68, 1.0, v68
	v_rcp_f32_e32 v68, v68
	v_mul_f32_e32 v66, v58, v66
	v_mul_f32_e32 v58, v63, v67
	v_mul_f32_e32 v67, v60, v60
	v_fma_f32 v67, v67, s90, v231
	v_mul_f32_e32 v67, v60, v67
	v_mul_f32_e32 v69, v64, v64
	v_mul_f32_e32 v59, v59, v68
	v_mul_f32_e32 v68, v65, v65
	v_fma_f32 v69, v69, s90, v231
	v_fma_f32 v68, v68, s90, v231
	v_mul_f32_e32 v69, v64, v69
	v_exp_f32_e32 v67, v67
	v_mul_f32_e32 v68, v65, v68
	v_exp_f32_e32 v69, v69
	v_exp_f32_e32 v68, v68
	v_add_f32_e32 v67, 1.0, v67
	v_rcp_f32_e32 v67, v67
	v_add_f32_e32 v63, 1.0, v69
	v_add_f32_e32 v68, 1.0, v68
	v_rcp_f32_e32 v63, v63
	v_rcp_f32_e32 v68, v68
	v_mul_f32_e32 v69, v61, v61
	v_fma_f32 v69, v69, s90, v231
	v_mul_f32_e32 v60, v60, v67
	v_med3_f32 v62, v62, s61, v230
	v_med3_f32 v67, v58, s61, v230
	v_mul_f32_e32 v69, v61, v69
	v_cvt_pk_fp8_f32 v58, v62, v67
	v_mul_f32_e32 v63, v64, v63
	v_mul_f32_e32 v64, v65, v68
	v_exp_f32_e32 v69, v69
	v_med3_f32 v62, v63, s61, v230
	v_med3_f32 v63, v64, s61, v230
	v_cvt_pk_fp8_f32 v58, v62, v63 op_sel:[0,0,1]
	v_med3_f32 v62, v66, s61, v230
	v_med3_f32 v63, v59, s61, v230
	v_cvt_pk_fp8_f32 v59, v62, v63
	v_mul_f32_e32 v62, v54, v54
	v_fma_f32 v62, v62, s90, v231
	v_add_f32_e32 v65, 1.0, v69
	v_mul_f32_e32 v62, v54, v62
	v_rcp_f32_e32 v65, v65
	v_exp_f32_e32 v62, v62
	v_mul_f32_e32 v61, v61, v65
	v_med3_f32 v60, v60, s61, v230
	v_med3_f32 v61, v61, s61, v230
	v_cvt_pk_fp8_f32 v59, v60, v61 op_sel:[0,0,1]
	v_add_f32_e32 v60, 1.0, v62
	v_mul_f32_e32 v61, v50, v50
	v_mul_f32_e32 v62, v55, v55
	v_fma_f32 v61, v61, s90, v231
	v_fma_f32 v62, v62, s90, v231
	v_mul_f32_e32 v61, v50, v61
	v_mul_f32_e32 v62, v55, v62
	v_exp_f32_e32 v61, v61
	v_exp_f32_e32 v62, v62
	v_mul_f32_e32 v63, v51, v51
	v_fma_f32 v63, v63, s90, v231
	v_add_f32_e32 v61, 1.0, v61
	v_add_f32_e32 v62, 1.0, v62
	v_rcp_f32_e32 v61, v61
	v_rcp_f32_e32 v62, v62
	v_mul_f32_e32 v63, v51, v63
	v_rcp_f32_e32 v60, v60
	v_exp_f32_e32 v63, v63
	v_mul_f32_e32 v50, v50, v61
	v_mul_f32_e32 v55, v55, v62
	v_mul_f32_e32 v61, v56, v56
	v_mul_f32_e32 v62, v52, v52
	v_fma_f32 v61, v61, s90, v231
	v_fma_f32 v62, v62, s90, v231
	v_mul_f32_e32 v61, v56, v61
	v_mul_f32_e32 v62, v52, v62
	v_mul_f32_e32 v54, v54, v60
	v_add_f32_e32 v60, 1.0, v63
	v_mul_f32_e32 v63, v53, v53
	v_fma_f32 v63, v63, s90, v231
	v_rcp_f32_e32 v60, v60
	v_exp_f32_e32 v61, v61
	v_exp_f32_e32 v62, v62
	v_mul_f32_e32 v63, v53, v63
	v_exp_f32_e32 v63, v63
	v_mul_f32_e32 v51, v51, v60
	v_add_f32_e32 v60, 1.0, v61
	v_add_f32_e32 v61, 1.0, v62
	v_mul_f32_e32 v62, v57, v57
	v_fma_f32 v62, v62, s90, v231
	v_rcp_f32_e32 v61, v61
	v_mul_f32_e32 v62, v57, v62
	v_add_f32_e32 v63, 1.0, v63
	v_rcp_f32_e32 v63, v63
	v_exp_f32_e32 v62, v62
	v_mul_f32_e32 v52, v52, v61
	v_med3_f32 v50, v50, s61, v230
	v_med3_f32 v51, v51, s61, v230
	v_cvt_pk_fp8_f32 v61, v50, v51
	v_rcp_f32_e32 v60, v60
	v_mul_f32_e32 v53, v53, v63
	v_add_f32_e32 v62, 1.0, v62
	v_med3_f32 v50, v52, s61, v230
	v_med3_f32 v51, v53, s61, v230
	v_rcp_f32_e32 v62, v62
	v_cvt_pk_fp8_f32 v61, v50, v51 op_sel:[0,0,1]
	v_mul_f32_e32 v51, v46, v46
	v_mul_f32_e32 v56, v56, v60
	v_med3_f32 v54, v54, s61, v230
	v_med3_f32 v55, v55, s61, v230
	v_fma_f32 v51, v51, s90, v231
	v_cvt_pk_fp8_f32 v60, v54, v55
	v_mul_f32_e32 v51, v46, v51
	v_mul_f32_e32 v57, v57, v62
	v_med3_f32 v56, v56, s61, v230
	v_med3_f32 v57, v57, s61, v230
	v_add_u32_e32 v52, 0x800, v114
	v_exp_f32_e32 v53, v51
	v_cvt_pk_fp8_f32 v60, v56, v57 op_sel:[0,0,1]
	v_or_b32_e32 v50, v52, v223
	v_ashrrev_i32_e32 v51, 31, v50
	v_lshlrev_b64 v[50:51], 10, v[50:51]
	v_lshl_add_u64 v[50:51], s[10:11], 0, v[50:51]
	v_add_f32_e32 v53, 1.0, v53
	v_permlane16_swap_b32_e32 v58, v60
	v_permlane16_swap_b32_e32 v59, v61
	v_rcp_f32_e32 v53, v53
	v_lshl_add_u64 v[50:51], v[50:51], 0, s[22:23]
	v_mul_f32_e32 v54, v42, v42
	global_store_dwordx4 v[50:51], v[58:61], off
	v_mul_f32_e32 v51, v47, v47
	v_fma_f32 v54, v54, s90, v231
	v_fma_f32 v51, v51, s90, v231
	v_mul_f32_e32 v54, v42, v54
; __device__ __forceinline__ unsigned cvt_pk_bf16(float lo, float hi) { unsigned r; asm volatile("v_cvt_pk_bf16_f32 %0, %1, %2" : "=v"(r) : "v"(lo), "v"(hi)); return r; }
; __device__ __forceinline__ float gelu_tanh_(float x) { const float u = 0.7978845608f * (x + 0.044715f * x * x * x); return x * __builtin_amdgcn_rcpf(1.0f + __builtin_amdgcn_exp2f(-2.88539008178f * u)); }
;     __device__ __forceinline__ void operator()(EPI_ARGS) const {
;     ...
;             for (int bj = 0; bj < 2; ++bj) { const int lc = bj * 128 + wc * 32 + 8 * fq, t = lc >> 4, h0 = lc & 15;
; #pragma unroll
;                 for (int mp = 0; mp < 2; ++mp) { unsigned px[2], py[2];
; #pragma unroll
;                     for (int h = 0; h < 2; ++h) { const int m = 2 * mp + h; f32x4 v0 = acc[ai][bj][m][0], v1 = acc[ai][bj][m][1];
; #pragma unroll
;                         for (int j = 0; j < 4; ++j) { v0[j] = gelu_tanh_(v0[j]); v1[j] = gelu_tanh_(v1[j]); }
;                         if (GLU_FP8) { px[h] = pk4_fp8(v0[0], v0[1], v0[2], v0[3]); py[h] = pk4_fp8(v1[0], v1[1], v1[2], v1[3]); }
;                         else { const int r = u.pm * 256 + ai * 128 + wr * 64 + m * 16 + fr, b = r >> 8, c = r & 255; u32x4 w; w.x = cvt_pk_bf16(v0[0], v0[1]); w.y = cvt_pk_bf16(v0[2], v0[3]); w.z = cvt_pk_bf16(v1[0], v1[1]); w.w = cvt_pk_bf16(v1[2], v1[3]);
;                             *(u32x4*)(YS + (size_t)(b * SEQ + c * CL + t) * SW + u.e * 16 + h0) = w; } }
;                     if (GLU_FP8) { const u32x4 q = pair16(px[0], py[0], px[1], py[1]);
;                         const int r = u.pm * 256 + ai * 128 + wr * 64 + (2 * mp + (fq & 1)) * 16 + fr, b = r >> 8, c = r & 255;
;                         *(u32x4*)((unsigned char*)YS + (size_t)(b * SEQ + c * CL + t) * SW + u.e * 16) = q; } } }
	v_mul_f32_e32 v51, v47, v51
	v_mul_f32_e32 v46, v46, v53
	v_mul_f32_e32 v53, v43, v43
	v_fma_f32 v53, v53, s90, v231
	v_exp_f32_e32 v54, v54
	v_exp_f32_e32 v51, v51
	v_mul_f32_e32 v53, v43, v53
	v_exp_f32_e32 v53, v53
	v_add_f32_e32 v50, 1.0, v54
	v_add_f32_e32 v51, 1.0, v51
	v_rcp_f32_e32 v50, v50
	v_rcp_f32_e32 v51, v51
	v_add_f32_e32 v53, 1.0, v53
	v_rcp_f32_e32 v53, v53
	v_mul_f32_e32 v50, v42, v50
	v_mul_f32_e32 v42, v47, v51
	v_mul_f32_e32 v51, v44, v44
	v_fma_f32 v51, v51, s90, v231
	v_mul_f32_e32 v51, v44, v51
	v_mul_f32_e32 v54, v48, v48
	v_mul_f32_e32 v43, v43, v53
	v_mul_f32_e32 v53, v49, v49
	v_fma_f32 v54, v54, s90, v231
	v_fma_f32 v53, v53, s90, v231
	v_mul_f32_e32 v54, v48, v54
	v_exp_f32_e32 v51, v51
	v_mul_f32_e32 v53, v49, v53
	v_exp_f32_e32 v54, v54
	v_exp_f32_e32 v53, v53
	v_add_f32_e32 v51, 1.0, v51
	v_rcp_f32_e32 v51, v51
	v_add_f32_e32 v47, 1.0, v54
	v_add_f32_e32 v53, 1.0, v53
	v_rcp_f32_e32 v47, v47
	v_rcp_f32_e32 v53, v53
	v_mul_f32_e32 v54, v45, v45
	v_fma_f32 v54, v54, s90, v231
	v_mul_f32_e32 v44, v44, v51
	v_med3_f32 v46, v46, s61, v230
	v_med3_f32 v51, v42, s61, v230
	v_mul_f32_e32 v54, v45, v54
	v_cvt_pk_fp8_f32 v42, v46, v51
	v_mul_f32_e32 v47, v48, v47
	v_mul_f32_e32 v48, v49, v53
	v_exp_f32_e32 v54, v54
	v_med3_f32 v46, v47, s61, v230
	v_med3_f32 v47, v48, s61, v230
	v_cvt_pk_fp8_f32 v42, v46, v47 op_sel:[0,0,1]
	v_med3_f32 v46, v50, s61, v230
	v_med3_f32 v47, v43, s61, v230
	v_cvt_pk_fp8_f32 v43, v46, v47
	v_mul_f32_e32 v46, v38, v38
	v_fma_f32 v46, v46, s90, v231
	v_add_f32_e32 v49, 1.0, v54
	v_mul_f32_e32 v46, v38, v46
	v_rcp_f32_e32 v49, v49
	v_exp_f32_e32 v46, v46
	v_mul_f32_e32 v45, v45, v49
	v_med3_f32 v44, v44, s61, v230
	v_med3_f32 v45, v45, s61, v230
	v_cvt_pk_fp8_f32 v43, v44, v45 op_sel:[0,0,1]
	v_add_f32_e32 v44, 1.0, v46
	v_mul_f32_e32 v45, v34, v34
	v_mul_f32_e32 v46, v39, v39
	v_fma_f32 v45, v45, s90, v231
	v_fma_f32 v46, v46, s90, v231
	v_mul_f32_e32 v45, v34, v45
	v_mul_f32_e32 v46, v39, v46
	v_exp_f32_e32 v45, v45
	v_exp_f32_e32 v46, v46
	v_mul_f32_e32 v47, v35, v35
	v_fma_f32 v47, v47, s90, v231
	v_add_f32_e32 v45, 1.0, v45
	v_add_f32_e32 v46, 1.0, v46
	v_rcp_f32_e32 v45, v45
	v_rcp_f32_e32 v46, v46
	v_mul_f32_e32 v47, v35, v47
	v_rcp_f32_e32 v44, v44
	v_exp_f32_e32 v47, v47
	v_mul_f32_e32 v34, v34, v45
	v_mul_f32_e32 v39, v39, v46
	v_mul_f32_e32 v45, v40, v40
	v_mul_f32_e32 v46, v36, v36
	v_fma_f32 v45, v45, s90, v231
	v_fma_f32 v46, v46, s90, v231
	v_mul_f32_e32 v45, v40, v45
	v_mul_f32_e32 v46, v36, v46
	v_mul_f32_e32 v38, v38, v44
	v_add_f32_e32 v44, 1.0, v47
	v_mul_f32_e32 v47, v37, v37
	v_fma_f32 v47, v47, s90, v231
	v_rcp_f32_e32 v44, v44
	v_exp_f32_e32 v45, v45
	v_exp_f32_e32 v46, v46
	v_mul_f32_e32 v47, v37, v47
	v_exp_f32_e32 v47, v47
	v_mul_f32_e32 v35, v35, v44
	v_add_f32_e32 v44, 1.0, v45
	v_add_f32_e32 v45, 1.0, v46
	v_mul_f32_e32 v46, v41, v41
	v_fma_f32 v46, v46, s90, v231
	v_rcp_f32_e32 v45, v45
	v_mul_f32_e32 v46, v41, v46
	v_add_f32_e32 v47, 1.0, v47
	v_rcp_f32_e32 v47, v47
	v_exp_f32_e32 v46, v46
	v_mul_f32_e32 v36, v36, v45
	v_med3_f32 v34, v34, s61, v230
	v_med3_f32 v35, v35, s61, v230
	v_cvt_pk_fp8_f32 v45, v34, v35
	v_rcp_f32_e32 v44, v44
	v_mul_f32_e32 v37, v37, v47
	v_add_f32_e32 v46, 1.0, v46
	v_med3_f32 v34, v36, s61, v230
	v_med3_f32 v35, v37, s61, v230
	v_rcp_f32_e32 v46, v46
	v_cvt_pk_fp8_f32 v45, v34, v35 op_sel:[0,0,1]
	v_mul_f32_e32 v35, v30, v30
	v_mul_f32_e32 v40, v40, v44
	v_med3_f32 v38, v38, s61, v230
	v_med3_f32 v39, v39, s61, v230
	v_fma_f32 v35, v35, s90, v231
	v_cvt_pk_fp8_f32 v44, v38, v39
	v_mul_f32_e32 v35, v30, v35
	v_mul_f32_e32 v41, v41, v46
	v_med3_f32 v40, v40, s61, v230
	v_med3_f32 v41, v41, s61, v230
	v_add_u32_e32 v36, 0xa00, v114
	v_exp_f32_e32 v37, v35
	v_cvt_pk_fp8_f32 v44, v40, v41 op_sel:[0,0,1]
	v_or_b32_e32 v34, v36, v223
	v_ashrrev_i32_e32 v35, 31, v34
	v_lshlrev_b64 v[34:35], 10, v[34:35]
	v_lshl_add_u64 v[34:35], s[10:11], 0, v[34:35]
	v_add_f32_e32 v37, 1.0, v37
	v_permlane16_swap_b32_e32 v42, v44
	v_permlane16_swap_b32_e32 v43, v45
	v_rcp_f32_e32 v37, v37
	v_lshl_add_u64 v[34:35], v[34:35], 0, s[22:23]
	v_mul_f32_e32 v38, v26, v26
	global_store_dwordx4 v[34:35], v[42:45], off
	v_mul_f32_e32 v35, v31, v31
	v_fma_f32 v38, v38, s90, v231
	v_fma_f32 v35, v35, s90, v231
	v_mul_f32_e32 v38, v26, v38
	v_mul_f32_e32 v35, v31, v35
	v_mul_f32_e32 v30, v30, v37
	v_mul_f32_e32 v37, v27, v27
	v_fma_f32 v37, v37, s90, v231
	v_exp_f32_e32 v38, v38
	v_exp_f32_e32 v35, v35
	v_mul_f32_e32 v37, v27, v37
	v_exp_f32_e32 v37, v37
	v_add_f32_e32 v34, 1.0, v38
	v_add_f32_e32 v35, 1.0, v35
	v_rcp_f32_e32 v34, v34
	v_rcp_f32_e32 v35, v35
	v_add_f32_e32 v37, 1.0, v37
	v_rcp_f32_e32 v37, v37
	v_mul_f32_e32 v34, v26, v34
	v_mul_f32_e32 v26, v31, v35
	v_mul_f32_e32 v35, v28, v28
	v_fma_f32 v35, v35, s90, v231
	v_mul_f32_e32 v35, v28, v35
	v_mul_f32_e32 v38, v32, v32
	v_mul_f32_e32 v27, v27, v37
	v_mul_f32_e32 v37, v33, v33
	v_fma_f32 v38, v38, s90, v231
	v_fma_f32 v37, v37, s90, v231
	v_mul_f32_e32 v38, v32, v38
	v_exp_f32_e32 v35, v35
	v_mul_f32_e32 v37, v33, v37
	v_exp_f32_e32 v38, v38
	v_exp_f32_e32 v37, v37
	v_add_f32_e32 v35, 1.0, v35
	v_rcp_f32_e32 v35, v35
	v_add_f32_e32 v31, 1.0, v38
	v_add_f32_e32 v37, 1.0, v37
	v_rcp_f32_e32 v31, v31
	v_rcp_f32_e32 v37, v37
	v_mul_f32_e32 v38, v29, v29
	v_fma_f32 v38, v38, s90, v231
	v_mul_f32_e32 v28, v28, v35
	v_med3_f32 v30, v30, s61, v230
	v_med3_f32 v35, v26, s61, v230
	v_mul_f32_e32 v38, v29, v38
	v_cvt_pk_fp8_f32 v26, v30, v35
	v_mul_f32_e32 v31, v32, v31
	v_mul_f32_e32 v32, v33, v37
	v_exp_f32_e32 v38, v38
	v_med3_f32 v30, v31, s61, v230
	v_med3_f32 v31, v32, s61, v230
	v_cvt_pk_fp8_f32 v26, v30, v31 op_sel:[0,0,1]
; __device__ __forceinline__ unsigned cvt_pk_bf16(float lo, float hi) { unsigned r; asm volatile("v_cvt_pk_bf16_f32 %0, %1, %2" : "=v"(r) : "v"(lo), "v"(hi)); return r; }
; __device__ __forceinline__ float gelu_tanh_(float x) { const float u = 0.7978845608f * (x + 0.044715f * x * x * x); return x * __builtin_amdgcn_rcpf(1.0f + __builtin_amdgcn_exp2f(-2.88539008178f * u)); }
;     __device__ __forceinline__ void operator()(EPI_ARGS) const {
;     ...
;             for (int bj = 0; bj < 2; ++bj) { const int lc = bj * 128 + wc * 32 + 8 * fq, t = lc >> 4, h0 = lc & 15;
; #pragma unroll
;                 for (int mp = 0; mp < 2; ++mp) { unsigned px[2], py[2];
; #pragma unroll
;                     for (int h = 0; h < 2; ++h) { const int m = 2 * mp + h; f32x4 v0 = acc[ai][bj][m][0], v1 = acc[ai][bj][m][1];
; #pragma unroll
;                         for (int j = 0; j < 4; ++j) { v0[j] = gelu_tanh_(v0[j]); v1[j] = gelu_tanh_(v1[j]); }
;                         if (GLU_FP8) { px[h] = pk4_fp8(v0[0], v0[1], v0[2], v0[3]); py[h] = pk4_fp8(v1[0], v1[1], v1[2], v1[3]); }
;                         else { const int r = u.pm * 256 + ai * 128 + wr * 64 + m * 16 + fr, b = r >> 8, c = r & 255; u32x4 w; w.x = cvt_pk_bf16(v0[0], v0[1]); w.y = cvt_pk_bf16(v0[2], v0[3]); w.z = cvt_pk_bf16(v1[0], v1[1]); w.w = cvt_pk_bf16(v1[2], v1[3]);
;                             *(u32x4*)(YS + (size_t)(b * SEQ + c * CL + t) * SW + u.e * 16 + h0) = w; } }
;                     if (GLU_FP8) { const u32x4 q = pair16(px[0], py[0], px[1], py[1]);
;                         const int r = u.pm * 256 + ai * 128 + wr * 64 + (2 * mp + (fq & 1)) * 16 + fr, b = r >> 8, c = r & 255;
;                         *(u32x4*)((unsigned char*)YS + (size_t)(b * SEQ + c * CL + t) * SW + u.e * 16) = q; } } }
	v_med3_f32 v30, v34, s61, v230
	v_med3_f32 v31, v27, s61, v230
	v_cvt_pk_fp8_f32 v27, v30, v31
	v_mul_f32_e32 v30, v18, v18
	v_fma_f32 v30, v30, s90, v231
	v_add_f32_e32 v33, 1.0, v38
	v_mul_f32_e32 v30, v18, v30
	v_rcp_f32_e32 v33, v33
	v_exp_f32_e32 v30, v30
	v_mul_f32_e32 v29, v29, v33
	v_med3_f32 v28, v28, s61, v230
	v_med3_f32 v29, v29, s61, v230
	v_cvt_pk_fp8_f32 v27, v28, v29 op_sel:[0,0,1]
	v_add_f32_e32 v28, 1.0, v30
	v_mul_f32_e32 v29, v22, v22
	v_mul_f32_e32 v30, v19, v19
	v_fma_f32 v29, v29, s90, v231
	v_fma_f32 v30, v30, s90, v231
	v_mul_f32_e32 v29, v22, v29
	v_mul_f32_e32 v30, v19, v30
	v_exp_f32_e32 v29, v29
	v_exp_f32_e32 v30, v30
	v_mul_f32_e32 v31, v23, v23
	v_fma_f32 v31, v31, s90, v231
	v_add_f32_e32 v29, 1.0, v29
	v_add_f32_e32 v30, 1.0, v30
	v_rcp_f32_e32 v29, v29
	v_rcp_f32_e32 v30, v30
	v_mul_f32_e32 v31, v23, v31
	v_rcp_f32_e32 v28, v28
	v_exp_f32_e32 v31, v31
	v_mul_f32_e32 v22, v22, v29
	v_mul_f32_e32 v19, v19, v30
	v_mul_f32_e32 v29, v20, v20
	v_mul_f32_e32 v30, v24, v24
	v_fma_f32 v29, v29, s90, v231
	v_fma_f32 v30, v30, s90, v231
	v_mul_f32_e32 v29, v20, v29
	v_mul_f32_e32 v30, v24, v30
	v_mul_f32_e32 v18, v18, v28
	v_add_f32_e32 v28, 1.0, v31
	v_mul_f32_e32 v31, v25, v25
	v_rcp_f32_e32 v28, v28
	v_exp_f32_e32 v29, v29
	v_exp_f32_e32 v30, v30
	v_fma_f32 v31, v31, s90, v231
	v_mul_f32_e32 v31, v25, v31
	v_mul_f32_e32 v23, v23, v28
	v_add_f32_e32 v28, 1.0, v29
	v_add_f32_e32 v29, 1.0, v30
	v_mul_f32_e32 v30, v21, v21
	v_exp_f32_e32 v31, v31
	v_rcp_f32_e32 v28, v28
	v_fma_f32 v30, v30, s90, v231
	v_mul_f32_e32 v30, v21, v30
	v_rcp_f32_e32 v29, v29
	v_add_f32_e32 v31, 1.0, v31
	v_exp_f32_e32 v30, v30
	v_rcp_f32_e32 v31, v31
	v_mul_f32_e32 v20, v20, v28
	v_med3_f32 v18, v18, s61, v230
	v_med3_f32 v19, v19, s61, v230
	v_mul_f32_e32 v24, v24, v29
	v_cvt_pk_fp8_f32 v28, v18, v19
	v_med3_f32 v18, v22, s61, v230
	v_med3_f32 v19, v23, s61, v230
	v_cvt_pk_fp8_f32 v29, v18, v19
	v_add_f32_e32 v30, 1.0, v30
	v_mul_f32_e32 v25, v25, v31
	v_rcp_f32_e32 v30, v30
	v_med3_f32 v18, v24, s61, v230
	v_med3_f32 v19, v25, s61, v230
	v_cvt_pk_fp8_f32 v29, v18, v19 op_sel:[0,0,1]
	v_mul_f32_e32 v19, v14, v14
	v_fma_f32 v19, v19, s90, v231
	v_mul_f32_e32 v19, v14, v19
	v_mul_f32_e32 v21, v21, v30
	v_med3_f32 v20, v20, s61, v230
	v_med3_f32 v21, v21, s61, v230
	v_cvt_pk_fp8_f32 v28, v20, v21 op_sel:[0,0,1]
	v_exp_f32_e32 v20, v19
	v_or_b32_e32 v18, v52, v224
	v_ashrrev_i32_e32 v19, 31, v18
	v_lshlrev_b64 v[18:19], 10, v[18:19]
	v_lshl_add_u64 v[18:19], s[10:11], 0, v[18:19]
	v_add_f32_e32 v20, 1.0, v20
	v_permlane16_swap_b32_e32 v26, v28
	v_permlane16_swap_b32_e32 v27, v29
	v_rcp_f32_e32 v20, v20
	v_lshl_add_u64 v[18:19], v[18:19], 0, s[22:23]
	v_mul_f32_e32 v21, v10, v10
	global_store_dwordx4 v[18:19], v[26:29], off
	v_mul_f32_e32 v19, v15, v15
	v_fma_f32 v21, v21, s90, v231
	v_fma_f32 v19, v19, s90, v231
	v_mul_f32_e32 v21, v10, v21
	v_mul_f32_e32 v19, v15, v19
	v_mul_f32_e32 v14, v14, v20
	v_mul_f32_e32 v20, v11, v11
	v_fma_f32 v20, v20, s90, v231
	v_exp_f32_e32 v21, v21
	v_exp_f32_e32 v19, v19
	v_mul_f32_e32 v20, v11, v20
	v_exp_f32_e32 v20, v20
	v_add_f32_e32 v18, 1.0, v21
	v_add_f32_e32 v19, 1.0, v19
	v_rcp_f32_e32 v18, v18
	v_rcp_f32_e32 v19, v19
	v_add_f32_e32 v20, 1.0, v20
	v_rcp_f32_e32 v20, v20
	v_mul_f32_e32 v18, v10, v18
	v_mul_f32_e32 v10, v15, v19
	v_mul_f32_e32 v19, v12, v12
	v_fma_f32 v19, v19, s90, v231
	v_mul_f32_e32 v19, v12, v19
	v_mul_f32_e32 v21, v16, v16
	v_mul_f32_e32 v11, v11, v20
	v_mul_f32_e32 v20, v17, v17
	v_fma_f32 v21, v21, s90, v231
	v_fma_f32 v20, v20, s90, v231
	v_mul_f32_e32 v21, v16, v21
	v_exp_f32_e32 v19, v19
	v_mul_f32_e32 v20, v17, v20
	v_exp_f32_e32 v21, v21
	v_exp_f32_e32 v20, v20
	v_add_f32_e32 v19, 1.0, v19
	v_rcp_f32_e32 v19, v19
	v_add_f32_e32 v15, 1.0, v21
	v_add_f32_e32 v20, 1.0, v20
	v_rcp_f32_e32 v15, v15
	v_rcp_f32_e32 v20, v20
	v_mul_f32_e32 v21, v13, v13
	v_fma_f32 v21, v21, s90, v231
	v_mul_f32_e32 v12, v12, v19
	v_med3_f32 v14, v14, s61, v230
	v_med3_f32 v19, v10, s61, v230
	v_mul_f32_e32 v21, v13, v21
	v_cvt_pk_fp8_f32 v10, v14, v19
	v_mul_f32_e32 v15, v16, v15
	v_mul_f32_e32 v16, v17, v20
	v_exp_f32_e32 v21, v21
	v_med3_f32 v14, v15, s61, v230
	v_med3_f32 v15, v16, s61, v230
	v_cvt_pk_fp8_f32 v10, v14, v15 op_sel:[0,0,1]
	v_med3_f32 v14, v18, s61, v230
	v_med3_f32 v15, v11, s61, v230
	v_cvt_pk_fp8_f32 v11, v14, v15
	v_mul_f32_e32 v14, v2, v2
	v_fma_f32 v14, v14, s90, v231
	v_add_f32_e32 v17, 1.0, v21
	v_mul_f32_e32 v14, v2, v14
	v_rcp_f32_e32 v17, v17
	v_exp_f32_e32 v14, v14
	v_mul_f32_e32 v13, v13, v17
	v_med3_f32 v12, v12, s61, v230
	v_med3_f32 v13, v13, s61, v230
	v_cvt_pk_fp8_f32 v11, v12, v13 op_sel:[0,0,1]
	v_add_f32_e32 v12, 1.0, v14
	v_mul_f32_e32 v13, v6, v6
	v_mul_f32_e32 v14, v3, v3
	v_fma_f32 v13, v13, s90, v231
	v_fma_f32 v14, v14, s90, v231
	v_mul_f32_e32 v13, v6, v13
	v_mul_f32_e32 v14, v3, v14
	v_exp_f32_e32 v13, v13
	v_exp_f32_e32 v14, v14
	v_mul_f32_e32 v15, v7, v7
	v_fma_f32 v15, v15, s90, v231
	v_add_f32_e32 v13, 1.0, v13
	v_add_f32_e32 v14, 1.0, v14
	v_rcp_f32_e32 v13, v13
	v_rcp_f32_e32 v14, v14
	v_mul_f32_e32 v15, v7, v15
	v_rcp_f32_e32 v12, v12
	v_exp_f32_e32 v15, v15
	v_mul_f32_e32 v6, v6, v13
	v_mul_f32_e32 v3, v3, v14
	v_mul_f32_e32 v13, v4, v4
	v_mul_f32_e32 v14, v8, v8
	v_fma_f32 v13, v13, s90, v231
	v_fma_f32 v14, v14, s90, v231
	v_mul_f32_e32 v13, v4, v13
	v_mul_f32_e32 v14, v8, v14
	v_mul_f32_e32 v2, v2, v12
	v_add_f32_e32 v12, 1.0, v15
	v_rcp_f32_e32 v12, v12
	v_exp_f32_e32 v13, v13
	v_exp_f32_e32 v14, v14
	v_mul_f32_e32 v15, v9, v9
	v_mul_f32_e32 v7, v7, v12
	v_add_f32_e32 v12, 1.0, v13
	v_add_f32_e32 v13, 1.0, v14
	v_mul_f32_e32 v14, v5, v5
	v_fma_f32 v14, v14, s90, v231
	v_fma_f32 v15, v15, s90, v231
	v_mul_f32_e32 v14, v5, v14
	v_mul_f32_e32 v15, v9, v15
	v_exp_f32_e32 v14, v14
	v_exp_f32_e32 v15, v15
	v_rcp_f32_e32 v12, v12
	v_rcp_f32_e32 v13, v13
	v_add_f32_e32 v14, 1.0, v14
	v_add_f32_e32 v15, 1.0, v15
	v_rcp_f32_e32 v14, v14
	v_rcp_f32_e32 v15, v15
	v_mul_f32_e32 v4, v4, v12
	v_med3_f32 v2, v2, s61, v230
	v_med3_f32 v3, v3, s61, v230
	v_mul_f32_e32 v8, v8, v13
	v_cvt_pk_fp8_f32 v12, v2, v3
	v_med3_f32 v2, v6, s61, v230
	v_med3_f32 v3, v7, s61, v230
	v_cvt_pk_fp8_f32 v13, v2, v3
	v_mul_f32_e32 v5, v5, v14
	v_mul_f32_e32 v9, v9, v15
	v_med3_f32 v4, v4, s61, v230
	v_med3_f32 v5, v5, s61, v230
	v_med3_f32 v2, v8, s61, v230
	v_med3_f32 v3, v9, s61, v230
	v_cvt_pk_fp8_f32 v12, v4, v5 op_sel:[0,0,1]
	v_cvt_pk_fp8_f32 v13, v2, v3 op_sel:[0,0,1]
	v_or_b32_e32 v2, v36, v224
	v_ashrrev_i32_e32 v3, 31, v2
	v_lshlrev_b64 v[2:3], 10, v[2:3]
	v_lshl_add_u64 v[2:3], s[10:11], 0, v[2:3]
	v_permlane16_swap_b32_e32 v10, v12
	v_permlane16_swap_b32_e32 v11, v13
	v_lshl_add_u64 v[2:3], v[2:3], 0, s[22:23]
	s_and_b64 vcc, exec, s[4:5]
	s_mov_b64 s[4:5], -1
	global_store_dwordx4 v[2:3], v[10:13], off
	s_cbranch_vccnz .LBB0_762
	s_andn2_b64 vcc, exec, s[8:9]
	s_cbranch_vccnz .LBB0_761
	s_barrier
	s_branch .LBB0_761

;     __device__ __forceinline__ void operator()(EPI_ARGS) const {
;         const int j0 = u.pn * 128 + wc * 32 + 8 * fq, j0q = u.pn * 128 + wc * 32 + 8 * (fq & ~1);
;         f32x4 ba0, ba1, bb0, bb1; u32x4 glq[2][2], ypq[2][2][2];
;         EPI_ALD16(ba0, bglu + j0); EPI_ALD16(ba1, bglu + j0 + 4); EPI_ALD16(bb0, bglu + D + j0); EPI_ALD16(bb1, bglu + D + j0 + 4);
; #pragma unroll
;         for (int ai = 0; ai < 2; ++ai)
; #pragma unroll
;             for (int mp = 0; mp < 2; ++mp) {
;                 if (GATE_FP8) { const int rowq = u.pm * 256 + ai * 128 + wr * 64 + (2 * mp + (fq & 1)) * 16 + fr;
;                     const unsigned char* gp = (const unsigned char*)SGS + (size_t)rowq * D + j0q; EPI_ALD16(glq[ai][mp], gp); }
; #pragma unroll
;                 for (int h = 0; h < 2; ++h) { const int row = u.pm * 256 + ai * 128 + wr * 64 + (2 * mp + h) * 16 + fr; const bf16* yq = YPG + (size_t)row * D + j0; EPI_ALD16(ypq[ai][mp][h], yq); } }
;         asm volatile("s_waitcnt vmcnt(0)" : "+v"(ba0), "+v"(ba1), "+v"(bb0), "+v"(bb1), "+v"(ypq[0][0][0]), "+v"(ypq[0][0][1]), "+v"(ypq[0][1][0]), "+v"(ypq[0][1][1]), "+v"(ypq[1][0][0]), "+v"(ypq[1][0][1]), "+v"(ypq[1][1][0]), "+v"(ypq[1][1][1]));
;         if (GATE_FP8) asm volatile("" : "+v"(glq[0][0]), "+v"(glq[0][1]), "+v"(glq[1][0]), "+v"(glq[1][1]));
; #pragma unroll
;         for (int ai = 0; ai < 2; ++ai)
; #pragma unroll
;             for (int mp = 0; mp < 2; ++mp) { unsigned px[2], py[2]; unsigned gq[2][2] = {{0u, 0u}, {0u, 0u}};
;                 if (GATE_FP8) unpair16(glq[ai][mp], gq[0][0], gq[0][1], gq[1][0], gq[1][1]);
; #pragma unroll
;                 for (int h = 0; h < 2; ++h) { const int m = 2 * mp + h; const int row = u.pm * 256 + ai * 128 + wr * 64 + m * 16 + fr; const size_t off = (size_t)row * D + j0;
;                     const u32x4 yp = ypq[ai][mp][h]; float gsf[8];
;                     if (GATE_FP8) { v2u g8; g8.x = gq[h][0]; g8.y = gq[h][1]; const float k255 = 1.0f / 255.0f;
;                         gsf[0] = (float)(g8.x & 0xffu) * k255; gsf[1] = (float)((g8.x >> 8) & 0xffu) * k255; gsf[2] = (float)((g8.x >> 16) & 0xffu) * k255; gsf[3] = (float)(g8.x >> 24) * k255;
;                         gsf[4] = (float)(g8.y & 0xffu) * k255; gsf[5] = (float)((g8.y >> 8) & 0xffu) * k255; gsf[6] = (float)((g8.y >> 16) & 0xffu) * k255; gsf[7] = (float)(g8.y >> 24) * k255; }
.LBB0_906:
	s_lshl_b32 s14, s75, 7
	s_or_b32 s14, s14, s66
	v_or_b32_e32 v18, s14, v195
	v_or_b32_e32 v58, s14, v219
	s_lshl_b32 s14, s38, 8
	s_add_i32 s14, s14, s65
	v_or_b32_e32 v20, s14, v1
	v_ashrrev_i32_e32 v19, 31, v18
	v_or_b32_e32 v22, v20, v220
	v_lshlrev_b64 v[10:11], 2, v[18:19]
	v_ashrrev_i32_e32 v23, 31, v22
	v_lshl_add_u64 v[12:13], s[6:7], 0, v[10:11]
	v_lshlrev_b64 v[22:23], 11, v[22:23]
	v_lshl_add_u64 v[2:3], v[12:13], 0, 16
	v_lshl_add_u64 v[10:11], s[20:21], 0, v[10:11]
	v_ashrrev_i32_e32 v59, 31, v58
	v_lshl_add_u64 v[22:23], s[10:11], 0, v[22:23]
	s_nop 15
	s_nop 15
	global_load_dwordx4 v[6:9], v[12:13], off
	global_load_dwordx4 v[2:5], v[2:3], off
	global_load_dwordx4 v[14:17], v[10:11], off
	v_lshl_add_u64 v[10:11], v[12:13], 0, s[24:25]
	v_lshl_add_u64 v[22:23], v[22:23], 0, v[58:59]
	v_ashrrev_i32_e32 v21, 31, v20
	global_load_dwordx4 v[10:13], v[10:11], off
	global_load_dwordx4 v[62:65], v[22:23], off
	v_lshlrev_b64 v[22:23], 12, v[20:21]
	v_lshl_add_u64 v[22:23], s[12:13], 0, v[22:23]
	v_lshlrev_b64 v[18:19], 1, v[18:19]
	v_lshl_add_u64 v[22:23], v[22:23], 0, v[18:19]
	global_load_dwordx4 v[214:217], v[22:23], off
	v_or_b32_e32 v22, 16, v20
	v_ashrrev_i32_e32 v23, 31, v22
	v_lshlrev_b64 v[22:23], 12, v[22:23]
	v_lshl_add_u64 v[22:23], s[12:13], 0, v[22:23]
	v_lshl_add_u64 v[22:23], v[22:23], 0, v[18:19]
	global_load_dwordx4 v[54:57], v[22:23], off
	v_or_b32_e32 v22, v20, v221
	v_ashrrev_i32_e32 v23, 31, v22
	v_lshlrev_b64 v[22:23], 11, v[22:23]
	v_lshl_add_u64 v[22:23], s[10:11], 0, v[22:23]
	v_lshl_add_u64 v[22:23], v[22:23], 0, v[58:59]
	global_load_dwordx4 v[50:53], v[22:23], off
	v_or_b32_e32 v22, 32, v20
	v_or_b32_e32 v20, 48, v20
	v_ashrrev_i32_e32 v21, 31, v20
	v_ashrrev_i32_e32 v23, 31, v22
	v_lshlrev_b64 v[20:21], 12, v[20:21]
	v_lshlrev_b64 v[22:23], 12, v[22:23]
	v_lshl_add_u64 v[20:21], s[12:13], 0, v[20:21]
	v_lshl_add_u64 v[22:23], s[12:13], 0, v[22:23]
	v_lshl_add_u64 v[20:21], v[20:21], 0, v[18:19]
	v_lshl_add_u64 v[22:23], v[22:23], 0, v[18:19]
	global_load_dwordx4 v[46:49], v[22:23], off
	global_load_dwordx4 v[42:45], v[20:21], off
	v_add_u32_e32 v20, s14, v218
	v_or_b32_e32 v22, v20, v220
	v_ashrrev_i32_e32 v23, 31, v22
	v_lshlrev_b64 v[22:23], 11, v[22:23]
	v_lshl_add_u64 v[22:23], s[10:11], 0, v[22:23]
	v_lshl_add_u64 v[22:23], v[22:23], 0, v[58:59]
	v_ashrrev_i32_e32 v21, 31, v20
	global_load_dwordx4 v[38:41], v[22:23], off
	v_lshlrev_b64 v[22:23], 12, v[20:21]
	v_lshl_add_u64 v[22:23], s[12:13], 0, v[22:23]
	v_lshl_add_u64 v[22:23], v[22:23], 0, v[18:19]
	global_load_dwordx4 v[34:37], v[22:23], off
	v_or_b32_e32 v22, 16, v20
	v_ashrrev_i32_e32 v23, 31, v22
	v_lshlrev_b64 v[22:23], 12, v[22:23]
	v_lshl_add_u64 v[22:23], s[12:13], 0, v[22:23]
	v_lshl_add_u64 v[22:23], v[22:23], 0, v[18:19]
	global_load_dwordx4 v[30:33], v[22:23], off
	v_or_b32_e32 v22, v20, v221
	v_ashrrev_i32_e32 v23, 31, v22
	v_lshlrev_b64 v[22:23], 11, v[22:23]
	v_lshl_add_u64 v[22:23], s[10:11], 0, v[22:23]
	v_lshl_add_u64 v[22:23], v[22:23], 0, v[58:59]
	global_load_dwordx4 v[26:29], v[22:23], off
	v_or_b32_e32 v22, 32, v20
	v_or_b32_e32 v20, 48, v20
	v_ashrrev_i32_e32 v23, 31, v22
	v_ashrrev_i32_e32 v21, 31, v20
	v_lshlrev_b64 v[22:23], 12, v[22:23]
	v_lshlrev_b64 v[20:21], 12, v[20:21]
	v_lshl_add_u64 v[22:23], s[12:13], 0, v[22:23]
	v_lshl_add_u64 v[20:21], s[12:13], 0, v[20:21]
	v_lshl_add_u64 v[22:23], v[22:23], 0, v[18:19]
	v_lshl_add_u64 v[18:19], v[20:21], 0, v[18:19]
	global_load_dwordx4 v[22:25], v[22:23], off
	global_load_dwordx4 v[18:21], v[18:19], off
	v_or_b32_e32 v60, s14, v222
	s_andn2_b64 vcc, exec, s[4:5]
	s_waitcnt vmcnt(11)
	v_mul_f32_e32 v10, 0xbfb8aa3b, v10
	v_mul_f32_e32 v11, 0xbfb8aa3b, v11
	v_mul_f32_e32 v12, 0xbfb8aa3b, v12
	v_mul_f32_e32 v13, 0xbfb8aa3b, v13
	v_mul_f32_e32 v14, 0xbfb8aa3b, v14
	v_mul_f32_e32 v15, 0xbfb8aa3b, v15
	v_mul_f32_e32 v16, 0xbfb8aa3b, v16
	v_mul_f32_e32 v17, 0xbfb8aa3b, v17
	v_mov_b32_e32 v240, v65
	s_nop 1
	v_permlane16_swap_b32_e32 v63, v240
	v_cvt_f32_ubyte0_e32 v232, v63
	v_cvt_f32_ubyte1_e32 v234, v63
	v_cvt_f32_ubyte2_e32 v236, v63
	v_cvt_f32_ubyte3_e32 v238, v63
	v_fmamk_f32 v63, v182, 0xbd38aa3b, v14
	v_fmamk_f32 v178, v178, 0xbd38aa3b, v10
	v_exp_f32_e32 v63, v63
	v_exp_f32_e32 v178, v178
	v_fmamk_f32 v233, v186, 0x3d000000, v2
	v_add_f32_e32 v63, 1.0, v63
	v_rcp_f32_e32 v213, v63
	v_add_f32_e32 v63, 1.0, v178
	v_rcp_f32_e32 v182, v63
	v_fmamk_f32 v63, v183, 0xbd38aa3b, v15
	v_fmamk_f32 v178, v179, 0xbd38aa3b, v11
	v_exp_f32_e32 v63, v63
	v_exp_f32_e32 v178, v178
	v_fmamk_f32 v181, v181, 0xbd38aa3b, v13
	v_add_f32_e32 v63, 1.0, v63
	v_rcp_f32_e32 v179, v63
	v_add_f32_e32 v63, 1.0, v178
	v_rcp_f32_e32 v186, v63
	v_fmamk_f32 v63, v184, 0xbd38aa3b, v16
	v_fmamk_f32 v178, v180, 0xbd38aa3b, v12
	v_exp_f32_e32 v63, v63
	v_exp_f32_e32 v178, v178
	v_add_f32_e32 v63, 1.0, v63
	v_rcp_f32_e32 v180, v63
	v_add_f32_e32 v63, 1.0, v178
	v_fmamk_f32 v178, v185, 0xbd38aa3b, v17
	v_exp_f32_e32 v178, v178
	v_exp_f32_e32 v181, v181
	v_mov_b32_e32 v61, v64
	s_nop 1
	v_permlane16_swap_b32_e32 v62, v61
	v_add_f32_e32 v178, 1.0, v178
	v_rcp_f32_e32 v183, v178
	v_cvt_f32_ubyte0_e32 v64, v62
	v_fmamk_f32 v65, v190, 0x3d000000, v6
	v_cvt_f32_ubyte1_e32 v228, v62
	v_fmamk_f32 v229, v191, 0x3d000000, v7
	v_add_f32_e32 v178, 1.0, v181
	v_pk_mul_f32 v[64:65], v[64:65], v[212:213]
	v_cvt_f32_ubyte2_e32 v230, v62
	v_fmamk_f32 v231, v192, 0x3d000000, v8
	v_fmamk_f32 v237, v188, 0x3d000000, v4
	v_rcp_f32_e32 v188, v178
	v_mul_f32_e32 v178, v228, v212
	v_mul_f32_e32 v179, v229, v179
	v_cvt_f32_ubyte3_e32 v62, v62
	v_fmamk_f32 v235, v187, 0x3d000000, v3
	v_rcp_f32_e32 v187, v63
	v_fmamk_f32 v63, v193, 0x3d000000, v9
	v_mul_f32_e32 v181, v231, v180
	v_mul_f32_e32 v180, v230, v212
	s_waitcnt vmcnt(10)
;     __device__ __forceinline__ void operator()(EPI_ARGS) const {
;     ...
;             for (int mp = 0; mp < 2; ++mp) { unsigned px[2], py[2]; unsigned gq[2][2] = {{0u, 0u}, {0u, 0u}};
;                 if (GATE_FP8) unpair16(glq[ai][mp], gq[0][0], gq[0][1], gq[1][0], gq[1][1]);
; #pragma unroll
;                 for (int h = 0; h < 2; ++h) { const int m = 2 * mp + h; const int row = u.pm * 256 + ai * 128 + wr * 64 + m * 16 + fr; const size_t off = (size_t)row * D + j0;
;                     const u32x4 yp = ypq[ai][mp][h]; float gsf[8];
;                     if (GATE_FP8) { v2u g8; g8.x = gq[h][0]; g8.y = gq[h][1]; const float k255 = 1.0f / 255.0f;
;                         gsf[0] = (float)(g8.x & 0xffu) * k255; gsf[1] = (float)((g8.x >> 8) & 0xffu) * k255; gsf[2] = (float)((g8.x >> 16) & 0xffu) * k255; gsf[3] = (float)(g8.x >> 24) * k255;
;                         gsf[4] = (float)(g8.y & 0xffu) * k255; gsf[5] = (float)((g8.y >> 8) & 0xffu) * k255; gsf[6] = (float)((g8.y >> 16) & 0xffu) * k255; gsf[7] = (float)(g8.y >> 24) * k255; }
;                     else { const u32x4 gs = *(const u32x4*)(SGS + off); gsf[0] = bf_lo(gs.x); gsf[1] = bf_hi(gs.x); gsf[2] = bf_lo(gs.y); gsf[3] = bf_hi(gs.y); gsf[4] = bf_lo(gs.z); gsf[5] = bf_hi(gs.z); gsf[6] = bf_lo(gs.w); gsf[7] = bf_hi(gs.w); }
;                     const f32x4 a0 = acc[ai][0][m][0] * asc + ba0, a1 = acc[ai][0][m][1] * asc + ba1, b0 = acc[ai][1][m][0] * asc + bb0, b1 = acc[ai][1][m][1] * asc + bb1;
;                     float o[8];
; #pragma unroll
;                     for (int j = 0; j < 4; ++j) { o[j] = a0[j] * sigmoidf_(b0[j]); o[4 + j] = a1[j] * sigmoidf_(b1[j]); }
;                     float mo[8] = {bf_lo(yp.x) + gsf[0] * o[0], bf_hi(yp.x) + gsf[1] * o[1], bf_lo(yp.y) + gsf[2] * o[2], bf_hi(yp.y) + gsf[3] * o[3],
;                                    bf_lo(yp.z) + gsf[4] * o[4], bf_hi(yp.z) + gsf[5] * o[5], bf_lo(yp.w) + gsf[6] * o[6], bf_hi(yp.w) + gsf[7] * o[7]};
;                     if (OUT_FP8) { px[h] = pk4_fp8(mo[0], mo[1], mo[2], mo[3]); py[h] = pk4_fp8(mo[4], mo[5], mo[6], mo[7]); }
;                     else { u32x4 w; w.x = cvt_pk_bf16(mo[0], mo[1]); w.y = cvt_pk_bf16(mo[2], mo[3]); w.z = cvt_pk_bf16(mo[4], mo[5]); w.w = cvt_pk_bf16(mo[6], mo[7]); *(u32x4*)(MG + off) = w; } }
;                 if (OUT_FP8) { const u32x4 q = pair16(px[0], py[0], px[1], py[1]);
	v_lshlrev_b32_e32 v190, 16, v214
	v_mul_f32_e32 v62, v62, v212
	v_mul_f32_e32 v63, v63, v183
	v_fmac_f32_e32 v190, v64, v65
	v_and_b32_e32 v64, 0xffff0000, v214
	v_mul_f32_e32 v183, v233, v182
	v_mul_f32_e32 v182, v232, v212
	v_fmac_f32_e32 v64, v178, v179
	v_and_b32_e32 v178, 0xffff0000, v215
	v_mul_f32_e32 v184, v234, v212
	v_mul_f32_e32 v185, v235, v186
	v_fmac_f32_e32 v178, v62, v63
	v_lshlrev_b32_e32 v63, 16, v216
	v_and_b32_e32 v179, 0xffff0000, v216
	v_fmac_f32_e32 v63, v182, v183
	v_fmac_f32_e32 v179, v184, v185
	v_med3_f32 v182, v190, s74, v227
	v_med3_f32 v64, v64, s74, v227
	v_fmamk_f32 v163, v163, 0xbd38aa3b, v11
	v_cvt_pk_fp8_f32 v62, v182, v64
	v_med3_f32 v64, v63, s74, v227
	v_med3_f32 v179, v179, s74, v227
	v_fmamk_f32 v239, v189, 0x3d000000, v5
	v_mul_f32_e32 v186, v236, v212
	v_mul_f32_e32 v187, v237, v187
	v_lshlrev_b32_e32 v65, 16, v215
	v_cvt_pk_fp8_f32 v63, v64, v179
	v_exp_f32_e32 v163, v163
	v_mul_f32_e32 v189, v239, v188
	v_mul_f32_e32 v188, v238, v212
	v_fmac_f32_e32 v65, v180, v181
	v_lshlrev_b32_e32 v180, 16, v217
	v_and_b32_e32 v181, 0xffff0000, v217
	v_fmac_f32_e32 v180, v186, v187
	v_fmac_f32_e32 v181, v188, v189
	v_med3_f32 v65, v65, s74, v227
	v_med3_f32 v178, v178, s74, v227
	v_cvt_pk_fp8_f32 v62, v65, v178 op_sel:[0,0,1]
	v_med3_f32 v64, v180, s74, v227
	v_med3_f32 v65, v181, s74, v227
	v_cvt_pk_fp8_f32 v63, v64, v65 op_sel:[0,0,1]
	v_cvt_f32_ubyte0_e32 v64, v61
	v_cvt_f32_ubyte1_e32 v178, v61
	v_cvt_f32_ubyte2_e32 v180, v61
	v_cvt_f32_ubyte3_e32 v182, v61
	v_fmamk_f32 v61, v166, 0xbd38aa3b, v14
	v_add_f32_e32 v163, 1.0, v163
	v_fmamk_f32 v162, v162, 0xbd38aa3b, v10
	v_fmamk_f32 v185, v170, 0x3d000000, v2
	v_rcp_f32_e32 v170, v163
	v_fmamk_f32 v163, v168, 0xbd38aa3b, v16
	v_exp_f32_e32 v61, v61
	v_fmamk_f32 v164, v164, 0xbd38aa3b, v12
	v_exp_f32_e32 v162, v162
	v_exp_f32_e32 v163, v163
	v_exp_f32_e32 v164, v164
	v_add_f32_e32 v61, 1.0, v61
	v_rcp_f32_e32 v213, v61
	v_add_f32_e32 v61, 1.0, v162
	v_fmamk_f32 v162, v167, 0xbd38aa3b, v15
	v_add_f32_e32 v163, 1.0, v163
	v_rcp_f32_e32 v166, v163
	v_add_f32_e32 v163, 1.0, v164
	v_exp_f32_e32 v162, v162
	v_fmamk_f32 v189, v172, 0x3d000000, v4
	v_rcp_f32_e32 v172, v163
	v_fmamk_f32 v163, v169, 0xbd38aa3b, v17
	v_exp_f32_e32 v163, v163
	v_fmamk_f32 v164, v165, 0xbd38aa3b, v13
	v_add_f32_e32 v162, 1.0, v162
	v_rcp_f32_e32 v162, v162
	v_exp_f32_e32 v164, v164
	v_add_f32_e32 v163, 1.0, v163
	v_rcp_f32_e32 v167, v163
	v_fmamk_f32 v65, v174, 0x3d000000, v6
	v_rcp_f32_e32 v61, v61
	v_fmamk_f32 v179, v175, 0x3d000000, v7
	v_add_f32_e32 v163, 1.0, v164
	v_pk_mul_f32 v[64:65], v[64:65], v[212:213]
	v_fmamk_f32 v181, v176, 0x3d000000, v8
	v_rcp_f32_e32 v174, v163
	v_mul_f32_e32 v163, v179, v162
	v_mul_f32_e32 v162, v178, v212
	v_fmamk_f32 v183, v177, 0x3d000000, v9
	v_mul_f32_e32 v164, v180, v212
	v_mul_f32_e32 v165, v181, v166
	v_cvt_f32_ubyte0_e32 v184, v240
	v_mul_f32_e32 v166, v182, v212
	v_mul_f32_e32 v167, v183, v167
	v_mov_b32_e32 v213, v61
	s_waitcnt vmcnt(9)
	v_lshlrev_b32_e32 v61, 16, v54
	v_cvt_f32_ubyte1_e32 v186, v240
	v_fmamk_f32 v187, v171, 0x3d000000, v3
	v_pk_mul_f32 v[168:169], v[184:185], v[212:213]
	v_fmac_f32_e32 v61, v64, v65
	v_and_b32_e32 v54, 0xffff0000, v54
	v_lshlrev_b32_e32 v64, 16, v55
	v_mul_f32_e32 v171, v187, v170
	v_mul_f32_e32 v170, v186, v212
	v_fmac_f32_e32 v54, v162, v163
	v_fmac_f32_e32 v64, v164, v165
	v_lshlrev_b32_e32 v65, 16, v56
	v_and_b32_e32 v56, 0xffff0000, v56
	v_fmac_f32_e32 v65, v168, v169
	v_fmac_f32_e32 v56, v170, v171
	v_med3_f32 v61, v61, s74, v227
	v_med3_f32 v54, v54, s74, v227
	v_med3_f32 v163, v64, s74, v227
	v_cvt_f32_ubyte2_e32 v188, v240
	v_cvt_pk_fp8_f32 v64, v61, v54
	v_med3_f32 v54, v65, s74, v227
	v_med3_f32 v56, v56, s74, v227
	v_cvt_f32_ubyte3_e32 v190, v240
	v_fmamk_f32 v191, v173, 0x3d000000, v5
	v_mul_f32_e32 v173, v189, v172
	v_mul_f32_e32 v172, v188, v212
	v_mov_b32_e32 v213, v174
	v_and_b32_e32 v55, 0xffff0000, v55
	v_cvt_pk_fp8_f32 v65, v54, v56
	v_pk_mul_f32 v[174:175], v[190:191], v[212:213]
	v_fmac_f32_e32 v55, v166, v167
	v_lshlrev_b32_e32 v162, 16, v57
	v_and_b32_e32 v57, 0xffff0000, v57
	v_fmac_f32_e32 v162, v172, v173
	v_fmac_f32_e32 v57, v174, v175
	v_med3_f32 v55, v55, s74, v227
	v_cvt_pk_fp8_f32 v64, v163, v55 op_sel:[0,0,1]
	v_med3_f32 v54, v162, s74, v227
	v_med3_f32 v55, v57, s74, v227
	v_cvt_pk_fp8_f32 v65, v54, v55 op_sel:[0,0,1]
	v_ashrrev_i32_e32 v61, 31, v60
	v_lshlrev_b64 v[54:55], 11, v[60:61]
	v_lshl_add_u64 v[54:55], s[16:17], 0, v[54:55]
	s_waitcnt vmcnt(8)
	v_mov_b32_e32 v61, v52
	v_permlane16_swap_b32_e32 v62, v64
	v_permlane16_swap_b32_e32 v63, v65
	v_lshl_add_u64 v[54:55], v[54:55], 0, v[58:59]
	v_permlane16_swap_b32_e32 v50, v61
	global_store_dwordx4 v[54:55], v[62:65], off
	v_mov_b32_e32 v166, v53
	v_cvt_f32_ubyte0_e32 v53, v50
	v_cvt_f32_ubyte1_e32 v55, v50
	v_cvt_f32_ubyte2_e32 v57, v50
	v_cvt_f32_ubyte3_e32 v63, v50
	v_fmamk_f32 v50, v150, 0xbd38aa3b, v14
	v_fmamk_f32 v54, v146, 0xbd38aa3b, v10
	v_exp_f32_e32 v50, v50
	v_exp_f32_e32 v54, v54
	v_fmamk_f32 v56, v147, 0xbd38aa3b, v11
	v_add_f32_e32 v50, 1.0, v50
	v_rcp_f32_e32 v146, v50
	v_add_f32_e32 v50, 1.0, v54
	v_rcp_f32_e32 v150, v50
	v_fmamk_f32 v50, v151, 0xbd38aa3b, v15
	v_exp_f32_e32 v50, v50
	v_exp_f32_e32 v56, v56
	v_fmamk_f32 v64, v154, 0x3d000000, v2
	v_add_f32_e32 v50, 1.0, v50
	v_rcp_f32_e32 v154, v50
	v_add_f32_e32 v50, 1.0, v56
	v_fmamk_f32 v52, v158, 0x3d000000, v6
	v_rcp_f32_e32 v158, v50
	v_fmamk_f32 v50, v152, 0xbd38aa3b, v16
	v_fmamk_f32 v62, v148, 0xbd38aa3b, v12
	v_exp_f32_e32 v50, v50
	v_exp_f32_e32 v62, v62
	v_fmamk_f32 v147, v149, 0xbd38aa3b, v13
	v_add_f32_e32 v50, 1.0, v50
	v_rcp_f32_e32 v148, v50
	v_add_f32_e32 v50, 1.0, v62
	v_rcp_f32_e32 v152, v50
	v_fmamk_f32 v50, v153, 0xbd38aa3b, v17
	v_exp_f32_e32 v147, v147
	v_exp_f32_e32 v50, v50
	v_fmamk_f32 v56, v160, 0x3d000000, v8
	v_add_f32_e32 v147, 1.0, v147
	v_rcp_f32_e32 v160, v147
	v_permlane16_swap_b32_e32 v51, v166
	v_add_f32_e32 v50, 1.0, v50
	v_cvt_f32_ubyte0_e32 v65, v51
	v_fmamk_f32 v54, v159, 0x3d000000, v7
	v_fmamk_f32 v162, v155, 0x3d000000, v3
	v_fmamk_f32 v164, v156, 0x3d000000, v4
	v_rcp_f32_e32 v156, v50
	v_mov_b32_e32 v155, v212
	v_mov_b32_e32 v151, v212
	v_cvt_f32_ubyte1_e32 v163, v51
	v_cvt_f32_ubyte2_e32 v165, v51
	v_cvt_f32_ubyte3_e32 v51, v51
	v_fmamk_f32 v62, v161, 0x3d000000, v9
	v_fmamk_f32 v50, v157, 0x3d000000, v5
	v_mul_f32_e32 v52, v52, v146
	v_mul_f32_e32 v53, v53, v212
	v_pk_mul_f32 v[54:55], v[54:55], v[154:155]
	v_pk_mul_f32 v[64:65], v[64:65], v[150:151]
	v_mov_b32_e32 v161, v212
	s_waitcnt vmcnt(7)
;     __device__ __forceinline__ void operator()(EPI_ARGS) const {
;     ...
;             for (int mp = 0; mp < 2; ++mp) { unsigned px[2], py[2]; unsigned gq[2][2] = {{0u, 0u}, {0u, 0u}};
;                 if (GATE_FP8) unpair16(glq[ai][mp], gq[0][0], gq[0][1], gq[1][0], gq[1][1]);
; #pragma unroll
;                 for (int h = 0; h < 2; ++h) { const int m = 2 * mp + h; const int row = u.pm * 256 + ai * 128 + wr * 64 + m * 16 + fr; const size_t off = (size_t)row * D + j0;
;                     const u32x4 yp = ypq[ai][mp][h]; float gsf[8];
;                     if (GATE_FP8) { v2u g8; g8.x = gq[h][0]; g8.y = gq[h][1]; const float k255 = 1.0f / 255.0f;
;                         gsf[0] = (float)(g8.x & 0xffu) * k255; gsf[1] = (float)((g8.x >> 8) & 0xffu) * k255; gsf[2] = (float)((g8.x >> 16) & 0xffu) * k255; gsf[3] = (float)(g8.x >> 24) * k255;
;                         gsf[4] = (float)(g8.y & 0xffu) * k255; gsf[5] = (float)((g8.y >> 8) & 0xffu) * k255; gsf[6] = (float)((g8.y >> 16) & 0xffu) * k255; gsf[7] = (float)(g8.y >> 24) * k255; }
;                     else { const u32x4 gs = *(const u32x4*)(SGS + off); gsf[0] = bf_lo(gs.x); gsf[1] = bf_hi(gs.x); gsf[2] = bf_lo(gs.y); gsf[3] = bf_hi(gs.y); gsf[4] = bf_lo(gs.z); gsf[5] = bf_hi(gs.z); gsf[6] = bf_lo(gs.w); gsf[7] = bf_hi(gs.w); }
;                     const f32x4 a0 = acc[ai][0][m][0] * asc + ba0, a1 = acc[ai][0][m][1] * asc + ba1, b0 = acc[ai][1][m][0] * asc + bb0, b1 = acc[ai][1][m][1] * asc + bb1;
;                     float o[8];
; #pragma unroll
;                     for (int j = 0; j < 4; ++j) { o[j] = a0[j] * sigmoidf_(b0[j]); o[4 + j] = a1[j] * sigmoidf_(b1[j]); }
;                     float mo[8] = {bf_lo(yp.x) + gsf[0] * o[0], bf_hi(yp.x) + gsf[1] * o[1], bf_lo(yp.y) + gsf[2] * o[2], bf_hi(yp.y) + gsf[3] * o[3],
;                                    bf_lo(yp.z) + gsf[4] * o[4], bf_hi(yp.z) + gsf[5] * o[5], bf_lo(yp.w) + gsf[6] * o[6], bf_hi(yp.w) + gsf[7] * o[7]};
;                     if (OUT_FP8) { px[h] = pk4_fp8(mo[0], mo[1], mo[2], mo[3]); py[h] = pk4_fp8(mo[4], mo[5], mo[6], mo[7]); }
;                     else { u32x4 w; w.x = cvt_pk_bf16(mo[0], mo[1]); w.y = cvt_pk_bf16(mo[2], mo[3]); w.z = cvt_pk_bf16(mo[4], mo[5]); w.w = cvt_pk_bf16(mo[6], mo[7]); *(u32x4*)(MG + off) = w; } }
;                 if (OUT_FP8) { const u32x4 q = pair16(px[0], py[0], px[1], py[1]);
	v_lshlrev_b32_e32 v150, 16, v46
	v_and_b32_e32 v46, 0xffff0000, v46
	v_pk_mul_f32 v[50:51], v[50:51], v[160:161]
	v_fmac_f32_e32 v150, v52, v53
	v_fmac_f32_e32 v46, v54, v55
	v_lshlrev_b32_e32 v54, 16, v49
	v_and_b32_e32 v49, 0xffff0000, v49
	v_mov_b32_e32 v157, v212
	v_mov_b32_e32 v159, v212
	v_fmac_f32_e32 v49, v50, v51
	v_med3_f32 v50, v150, s74, v227
	v_med3_f32 v51, v46, s74, v227
	v_pk_mul_f32 v[62:63], v[62:63], v[156:157]
	v_pk_mul_f32 v[146:147], v[162:163], v[158:159]
	v_lshlrev_b32_e32 v52, 16, v47
	v_and_b32_e32 v47, 0xffff0000, v47
	v_lshlrev_b32_e32 v53, 16, v48
	v_and_b32_e32 v48, 0xffff0000, v48
	v_cvt_pk_fp8_f32 v46, v50, v51
	v_mul_f32_e32 v56, v56, v148
	v_mul_f32_e32 v57, v57, v212
	v_fmac_f32_e32 v47, v62, v63
	v_fmac_f32_e32 v53, v64, v65
	v_fmac_f32_e32 v48, v146, v147
	v_fmac_f32_e32 v52, v56, v57
	v_med3_f32 v55, v47, s74, v227
	v_med3_f32 v50, v53, s74, v227
	v_med3_f32 v48, v48, s74, v227
	v_med3_f32 v52, v52, s74, v227
	v_cvt_pk_fp8_f32 v47, v50, v48
	v_fmamk_f32 v50, v134, 0xbd38aa3b, v14
	v_cvt_pk_fp8_f32 v46, v52, v55 op_sel:[0,0,1]
	v_fmamk_f32 v52, v130, 0xbd38aa3b, v10
	v_exp_f32_e32 v50, v50
	v_exp_f32_e32 v52, v52
	v_mov_b32_e32 v153, v212
	v_pk_mul_f32 v[148:149], v[164:165], v[152:153]
	v_add_f32_e32 v50, 1.0, v50
	v_fmac_f32_e32 v54, v148, v149
	v_rcp_f32_e32 v130, v50
	v_add_f32_e32 v50, 1.0, v52
	v_fmamk_f32 v52, v135, 0xbd38aa3b, v15
	v_med3_f32 v48, v54, s74, v227
	v_fmamk_f32 v54, v131, 0xbd38aa3b, v11
	v_exp_f32_e32 v52, v52
	v_exp_f32_e32 v54, v54
	v_med3_f32 v49, v49, s74, v227
	v_add_f32_e32 v52, 1.0, v52
	v_fmamk_f32 v56, v138, 0x3d000000, v2
	v_rcp_f32_e32 v138, v52
	v_add_f32_e32 v52, 1.0, v54
	v_fmamk_f32 v54, v136, 0xbd38aa3b, v16
	v_cvt_pk_fp8_f32 v47, v48, v49 op_sel:[0,0,1]
	v_cvt_f32_ubyte0_e32 v49, v61
	v_cvt_f32_ubyte1_e32 v51, v61
	v_cvt_f32_ubyte2_e32 v53, v61
	v_cvt_f32_ubyte3_e32 v55, v61
	v_fmamk_f32 v61, v132, 0xbd38aa3b, v12
	v_exp_f32_e32 v54, v54
	v_exp_f32_e32 v61, v61
	v_fmamk_f32 v131, v133, 0xbd38aa3b, v13
	v_add_f32_e32 v54, 1.0, v54
	v_rcp_f32_e32 v132, v54
	v_add_f32_e32 v54, 1.0, v61
	v_fmamk_f32 v61, v137, 0xbd38aa3b, v17
	v_exp_f32_e32 v61, v61
	v_exp_f32_e32 v131, v131
	v_fmamk_f32 v48, v142, 0x3d000000, v6
	v_rcp_f32_e32 v134, v50
	v_rcp_f32_e32 v142, v52
	v_add_f32_e32 v61, 1.0, v61
	v_fmamk_f32 v64, v140, 0x3d000000, v4
	v_rcp_f32_e32 v140, v61
	v_add_f32_e32 v61, 1.0, v131
	v_fmamk_f32 v50, v143, 0x3d000000, v7
	v_fmamk_f32 v62, v139, 0x3d000000, v3
	v_fmamk_f32 v52, v144, 0x3d000000, v8
	v_rcp_f32_e32 v144, v61
	v_mul_f32_e32 v48, v48, v130
	v_mul_f32_e32 v49, v49, v212
	v_mov_b32_e32 v139, v212
	v_mov_b32_e32 v133, v212
	s_waitcnt vmcnt(6)
	v_lshlrev_b32_e32 v61, 16, v42
	v_cvt_f32_ubyte0_e32 v57, v166
	v_cvt_f32_ubyte1_e32 v63, v166
	v_pk_mul_f32 v[50:51], v[50:51], v[138:139]
	v_pk_mul_f32 v[52:53], v[52:53], v[132:133]
	v_mov_b32_e32 v135, v212
	v_mov_b32_e32 v143, v212
	v_fmac_f32_e32 v61, v48, v49
	v_and_b32_e32 v42, 0xffff0000, v42
	v_lshlrev_b32_e32 v48, 16, v43
	v_rcp_f32_e32 v136, v54
	v_pk_mul_f32 v[56:57], v[56:57], v[134:135]
	v_pk_mul_f32 v[62:63], v[62:63], v[142:143]
	v_fmac_f32_e32 v42, v50, v51
	v_fmac_f32_e32 v48, v52, v53
	v_lshlrev_b32_e32 v49, 16, v44
	v_and_b32_e32 v44, 0xffff0000, v44
	v_fmac_f32_e32 v49, v56, v57
	v_fmac_f32_e32 v44, v62, v63
	v_med3_f32 v51, v61, s74, v227
	v_med3_f32 v42, v42, s74, v227
	v_med3_f32 v52, v48, s74, v227
	v_fmamk_f32 v54, v145, 0x3d000000, v9
	v_fmamk_f32 v146, v141, 0x3d000000, v5
	v_mov_b32_e32 v141, v212
	v_cvt_pk_fp8_f32 v48, v51, v42
	v_med3_f32 v42, v49, s74, v227
	v_med3_f32 v44, v44, s74, v227
	v_cvt_f32_ubyte2_e32 v65, v166
	v_cvt_f32_ubyte3_e32 v147, v166
	v_pk_mul_f32 v[54:55], v[54:55], v[140:141]
	v_mov_b32_e32 v137, v212
	v_mov_b32_e32 v145, v212
	v_and_b32_e32 v43, 0xffff0000, v43
	v_cvt_pk_fp8_f32 v49, v42, v44
	v_pk_mul_f32 v[64:65], v[64:65], v[136:137]
	v_pk_mul_f32 v[130:131], v[146:147], v[144:145]
	v_fmac_f32_e32 v43, v54, v55
	v_lshlrev_b32_e32 v50, 16, v45
	v_and_b32_e32 v45, 0xffff0000, v45
	v_fmac_f32_e32 v50, v64, v65
	v_fmac_f32_e32 v45, v130, v131
	v_med3_f32 v43, v43, s74, v227
	v_cvt_pk_fp8_f32 v48, v52, v43 op_sel:[0,0,1]
	v_med3_f32 v42, v50, s74, v227
	v_med3_f32 v43, v45, s74, v227
	v_cvt_pk_fp8_f32 v49, v42, v43 op_sel:[0,0,1]
	v_or_b32_e32 v42, 32, v60
	v_ashrrev_i32_e32 v43, 31, v42
	v_lshlrev_b64 v[42:43], 11, v[42:43]
	v_lshl_add_u64 v[42:43], s[16:17], 0, v[42:43]
	v_permlane16_swap_b32_e32 v46, v48
	v_permlane16_swap_b32_e32 v47, v49
	v_lshl_add_u64 v[42:43], v[42:43], 0, v[58:59]
	global_store_dwordx4 v[42:43], v[46:49], off
	s_waitcnt vmcnt(5)
	v_mov_b32_e32 v43, v40
	s_nop 1
	v_permlane16_swap_b32_e32 v38, v43
	v_mov_b32_e32 v61, v41
	v_cvt_f32_ubyte0_e32 v41, v38
	v_cvt_f32_ubyte1_e32 v45, v38
	v_cvt_f32_ubyte2_e32 v47, v38
	v_cvt_f32_ubyte3_e32 v49, v38
	v_fmamk_f32 v38, v126, 0xbd38aa3b, v14
	v_fmamk_f32 v44, v122, 0xbd38aa3b, v10
	v_exp_f32_e32 v38, v38
	v_exp_f32_e32 v44, v44
	v_fmamk_f32 v46, v123, 0xbd38aa3b, v11
	v_add_f32_e32 v38, 1.0, v38
	v_rcp_f32_e32 v56, v38
	v_add_f32_e32 v38, 1.0, v44
	v_rcp_f32_e32 v62, v38
	v_fmamk_f32 v38, v127, 0xbd38aa3b, v15
	v_exp_f32_e32 v38, v38
	v_exp_f32_e32 v46, v46
	v_fmamk_f32 v50, v114, 0x3d000000, v2
	v_add_f32_e32 v38, 1.0, v38
	v_rcp_f32_e32 v64, v38
	v_add_f32_e32 v38, 1.0, v46
	v_rcp_f32_e32 v114, v38
	v_fmamk_f32 v38, v128, 0xbd38aa3b, v16
	v_fmamk_f32 v48, v124, 0xbd38aa3b, v12
	v_exp_f32_e32 v38, v38
	v_exp_f32_e32 v48, v48
	v_fmamk_f32 v57, v125, 0xbd38aa3b, v13
	v_add_f32_e32 v38, 1.0, v38
	v_fmamk_f32 v40, v118, 0x3d000000, v6
	v_rcp_f32_e32 v118, v38
	v_add_f32_e32 v38, 1.0, v48
	v_fmamk_f32 v54, v116, 0x3d000000, v4
	v_rcp_f32_e32 v116, v38
	v_fmamk_f32 v38, v129, 0xbd38aa3b, v17
	v_exp_f32_e32 v57, v57
	v_exp_f32_e32 v38, v38
	v_permlane16_swap_b32_e32 v39, v61
	v_add_f32_e32 v57, 1.0, v57
	v_rcp_f32_e32 v122, v57
	v_add_f32_e32 v38, 1.0, v38
	v_fmamk_f32 v44, v119, 0x3d000000, v7
	v_fmamk_f32 v46, v120, 0x3d000000, v8
	v_rcp_f32_e32 v120, v38
	v_mov_b32_e32 v57, v212
	v_mov_b32_e32 v65, v212
	v_cvt_f32_ubyte0_e32 v51, v39
	v_cvt_f32_ubyte1_e32 v53, v39
	v_cvt_f32_ubyte2_e32 v55, v39
	v_cvt_f32_ubyte3_e32 v39, v39
	v_fmamk_f32 v38, v117, 0x3d000000, v5
	v_pk_mul_f32 v[40:41], v[40:41], v[56:57]
	v_pk_mul_f32 v[44:45], v[44:45], v[64:65]
	v_mov_b32_e32 v123, v212
	s_waitcnt vmcnt(4)
;     __device__ __forceinline__ void operator()(EPI_ARGS) const {
;     ...
;         for (int ai = 0; ai < 2; ++ai)
; #pragma unroll
;             for (int mp = 0; mp < 2; ++mp) { unsigned px[2], py[2]; unsigned gq[2][2] = {{0u, 0u}, {0u, 0u}};
;                 if (GATE_FP8) unpair16(glq[ai][mp], gq[0][0], gq[0][1], gq[1][0], gq[1][1]);
; #pragma unroll
;                 for (int h = 0; h < 2; ++h) { const int m = 2 * mp + h; const int row = u.pm * 256 + ai * 128 + wr * 64 + m * 16 + fr; const size_t off = (size_t)row * D + j0;
;                     const u32x4 yp = ypq[ai][mp][h]; float gsf[8];
;                     if (GATE_FP8) { v2u g8; g8.x = gq[h][0]; g8.y = gq[h][1]; const float k255 = 1.0f / 255.0f;
;                         gsf[0] = (float)(g8.x & 0xffu) * k255; gsf[1] = (float)((g8.x >> 8) & 0xffu) * k255; gsf[2] = (float)((g8.x >> 16) & 0xffu) * k255; gsf[3] = (float)(g8.x >> 24) * k255;
;                         gsf[4] = (float)(g8.y & 0xffu) * k255; gsf[5] = (float)((g8.y >> 8) & 0xffu) * k255; gsf[6] = (float)((g8.y >> 16) & 0xffu) * k255; gsf[7] = (float)(g8.y >> 24) * k255; }
;                     else { const u32x4 gs = *(const u32x4*)(SGS + off); gsf[0] = bf_lo(gs.x); gsf[1] = bf_hi(gs.x); gsf[2] = bf_lo(gs.y); gsf[3] = bf_hi(gs.y); gsf[4] = bf_lo(gs.z); gsf[5] = bf_hi(gs.z); gsf[6] = bf_lo(gs.w); gsf[7] = bf_hi(gs.w); }
;                     const f32x4 a0 = acc[ai][0][m][0] * asc + ba0, a1 = acc[ai][0][m][1] * asc + ba1, b0 = acc[ai][1][m][0] * asc + bb0, b1 = acc[ai][1][m][1] * asc + bb1;
;                     float o[8];
; #pragma unroll
;                     for (int j = 0; j < 4; ++j) { o[j] = a0[j] * sigmoidf_(b0[j]); o[4 + j] = a1[j] * sigmoidf_(b1[j]); }
;                     float mo[8] = {bf_lo(yp.x) + gsf[0] * o[0], bf_hi(yp.x) + gsf[1] * o[1], bf_lo(yp.y) + gsf[2] * o[2], bf_hi(yp.y) + gsf[3] * o[3],
;                                    bf_lo(yp.z) + gsf[4] * o[4], bf_hi(yp.z) + gsf[5] * o[5], bf_lo(yp.w) + gsf[6] * o[6], bf_hi(yp.w) + gsf[7] * o[7]};
;                     if (OUT_FP8) { px[h] = pk4_fp8(mo[0], mo[1], mo[2], mo[3]); py[h] = pk4_fp8(mo[4], mo[5], mo[6], mo[7]); }
;                     else { u32x4 w; w.x = cvt_pk_bf16(mo[0], mo[1]); w.y = cvt_pk_bf16(mo[2], mo[3]); w.z = cvt_pk_bf16(mo[4], mo[5]); w.w = cvt_pk_bf16(mo[6], mo[7]); *(u32x4*)(MG + off) = w; } }
	v_lshlrev_b32_e32 v56, 16, v34
	v_and_b32_e32 v34, 0xffff0000, v34
	v_pk_mul_f32 v[38:39], v[38:39], v[122:123]
	v_fmac_f32_e32 v56, v40, v41
	v_fmac_f32_e32 v34, v44, v45
	v_lshlrev_b32_e32 v44, 16, v37
	v_and_b32_e32 v37, 0xffff0000, v37
	v_fmamk_f32 v52, v115, 0x3d000000, v3
	v_fmamk_f32 v48, v121, 0x3d000000, v9
	v_mov_b32_e32 v121, v212
	v_mov_b32_e32 v63, v212
	v_mov_b32_e32 v115, v212
	v_fmac_f32_e32 v37, v38, v39
	v_med3_f32 v38, v56, s74, v227
	v_med3_f32 v39, v34, s74, v227
	v_mov_b32_e32 v119, v212
	v_pk_mul_f32 v[48:49], v[48:49], v[120:121]
	v_pk_mul_f32 v[50:51], v[50:51], v[62:63]
	v_pk_mul_f32 v[52:53], v[52:53], v[114:115]
	v_lshlrev_b32_e32 v40, 16, v35
	v_and_b32_e32 v35, 0xffff0000, v35
	v_lshlrev_b32_e32 v41, 16, v36
	v_and_b32_e32 v36, 0xffff0000, v36
	v_cvt_pk_fp8_f32 v34, v38, v39
	v_pk_mul_f32 v[46:47], v[46:47], v[118:119]
	v_fmac_f32_e32 v35, v48, v49
	v_fmac_f32_e32 v41, v50, v51
	v_fmac_f32_e32 v36, v52, v53
	v_fmac_f32_e32 v40, v46, v47
	v_med3_f32 v45, v35, s74, v227
	v_med3_f32 v38, v41, s74, v227
	v_med3_f32 v36, v36, s74, v227
	v_med3_f32 v40, v40, s74, v227
	v_cvt_pk_fp8_f32 v35, v38, v36
	v_fmamk_f32 v38, v110, 0xbd38aa3b, v14
	v_cvt_pk_fp8_f32 v34, v40, v45 op_sel:[0,0,1]
	v_fmamk_f32 v40, v106, 0xbd38aa3b, v10
	v_exp_f32_e32 v38, v38
	v_exp_f32_e32 v40, v40
	v_mov_b32_e32 v117, v212
	v_pk_mul_f32 v[54:55], v[54:55], v[116:117]
	v_add_f32_e32 v38, 1.0, v38
	v_fmac_f32_e32 v44, v54, v55
	v_med3_f32 v36, v44, s74, v227
	v_med3_f32 v37, v37, s74, v227
	v_rcp_f32_e32 v54, v38
	v_add_f32_e32 v38, 1.0, v40
	v_fmamk_f32 v40, v111, 0xbd38aa3b, v15
	v_cvt_pk_fp8_f32 v35, v36, v37 op_sel:[0,0,1]
	v_cvt_f32_ubyte0_e32 v37, v43
	v_cvt_f32_ubyte1_e32 v39, v43
	v_cvt_f32_ubyte2_e32 v41, v43
	v_cvt_f32_ubyte3_e32 v45, v43
	v_fmamk_f32 v43, v107, 0xbd38aa3b, v11
	v_exp_f32_e32 v40, v40
	v_exp_f32_e32 v43, v43
	v_fmamk_f32 v44, v108, 0xbd38aa3b, v12
	v_add_f32_e32 v40, 1.0, v40
	v_rcp_f32_e32 v62, v40
	v_add_f32_e32 v40, 1.0, v43
	v_fmamk_f32 v43, v112, 0xbd38aa3b, v16
	v_exp_f32_e32 v43, v43
	v_exp_f32_e32 v44, v44
	v_fmamk_f32 v46, v98, 0x3d000000, v2
	v_add_f32_e32 v43, 1.0, v43
	v_rcp_f32_e32 v98, v43
	v_add_f32_e32 v43, 1.0, v44
	v_fmamk_f32 v50, v100, 0x3d000000, v4
	v_rcp_f32_e32 v100, v43
	v_fmamk_f32 v43, v113, 0xbd38aa3b, v17
	v_fmamk_f32 v52, v109, 0xbd38aa3b, v13
	v_exp_f32_e32 v43, v43
	v_exp_f32_e32 v55, v52
	v_rcp_f32_e32 v56, v38
	v_rcp_f32_e32 v64, v40
	v_add_f32_e32 v43, 1.0, v43
	v_fmamk_f32 v36, v102, 0x3d000000, v6
	v_rcp_f32_e32 v102, v43
	v_add_f32_e32 v43, 1.0, v55
	v_mov_b32_e32 v55, v212
	v_fmamk_f32 v38, v103, 0x3d000000, v7
	v_fmamk_f32 v48, v99, 0x3d000000, v3
	v_fmamk_f32 v40, v104, 0x3d000000, v8
	v_rcp_f32_e32 v104, v43
	v_pk_mul_f32 v[36:37], v[36:37], v[54:55]
	v_mov_b32_e32 v99, v212
	s_waitcnt vmcnt(3)
	v_lshlrev_b32_e32 v43, 16, v30
	v_cvt_f32_ubyte0_e32 v47, v61
	v_cvt_f32_ubyte1_e32 v49, v61
	v_pk_mul_f32 v[38:39], v[38:39], v[62:63]
	v_pk_mul_f32 v[40:41], v[40:41], v[98:99]
	v_fmac_f32_e32 v43, v36, v37
	v_and_b32_e32 v30, 0xffff0000, v30
	v_lshlrev_b32_e32 v36, 16, v31
	v_pk_mul_f32 v[46:47], v[46:47], v[56:57]
	v_pk_mul_f32 v[48:49], v[48:49], v[64:65]
	v_fmac_f32_e32 v30, v38, v39
	v_fmac_f32_e32 v36, v40, v41
	v_lshlrev_b32_e32 v37, 16, v32
	v_and_b32_e32 v32, 0xffff0000, v32
	v_fmac_f32_e32 v37, v46, v47
	v_fmac_f32_e32 v32, v48, v49
	v_med3_f32 v39, v43, s74, v227
	v_med3_f32 v30, v30, s74, v227
	v_med3_f32 v40, v36, s74, v227
	v_fmamk_f32 v44, v105, 0x3d000000, v9
	v_mov_b32_e32 v103, v212
	v_cvt_pk_fp8_f32 v36, v39, v30
	v_med3_f32 v30, v37, s74, v227
	v_med3_f32 v32, v32, s74, v227
	v_cvt_f32_ubyte2_e32 v51, v61
	v_cvt_f32_ubyte3_e32 v53, v61
	v_fmamk_f32 v52, v101, 0x3d000000, v5
	v_pk_mul_f32 v[44:45], v[44:45], v[102:103]
	v_mov_b32_e32 v101, v212
	v_mov_b32_e32 v105, v212
	v_and_b32_e32 v31, 0xffff0000, v31
	v_cvt_pk_fp8_f32 v37, v30, v32
	v_pk_mul_f32 v[50:51], v[50:51], v[100:101]
	v_pk_mul_f32 v[52:53], v[52:53], v[104:105]
	v_fmac_f32_e32 v31, v44, v45
	v_lshlrev_b32_e32 v38, 16, v33
	v_and_b32_e32 v33, 0xffff0000, v33
	v_fmac_f32_e32 v38, v50, v51
	v_fmac_f32_e32 v33, v52, v53
	v_med3_f32 v31, v31, s74, v227
	v_cvt_pk_fp8_f32 v36, v40, v31 op_sel:[0,0,1]
	v_med3_f32 v30, v38, s74, v227
	v_med3_f32 v31, v33, s74, v227
	v_add_u32_e32 v42, 0x80, v60
	v_cvt_pk_fp8_f32 v37, v30, v31 op_sel:[0,0,1]
	v_ashrrev_i32_e32 v43, 31, v42
	v_lshlrev_b64 v[30:31], 11, v[42:43]
	v_lshl_add_u64 v[30:31], s[16:17], 0, v[30:31]
	s_waitcnt vmcnt(2)
	v_mov_b32_e32 v61, v28
	v_permlane16_swap_b32_e32 v34, v36
	v_permlane16_swap_b32_e32 v35, v37
	v_lshl_add_u64 v[30:31], v[30:31], 0, v[58:59]
	v_permlane16_swap_b32_e32 v26, v61
	global_store_dwordx4 v[30:31], v[34:37], off
	v_mov_b32_e32 v62, v29
	v_cvt_f32_ubyte0_e32 v29, v26
	v_cvt_f32_ubyte1_e32 v31, v26
	v_cvt_f32_ubyte2_e32 v33, v26
	v_cvt_f32_ubyte3_e32 v35, v26
	v_fmamk_f32 v26, v94, 0xbd38aa3b, v14
	v_fmamk_f32 v30, v90, 0xbd38aa3b, v10
	v_exp_f32_e32 v26, v26
	v_exp_f32_e32 v30, v30
	v_fmamk_f32 v32, v91, 0xbd38aa3b, v11
	v_add_f32_e32 v26, 1.0, v26
	v_rcp_f32_e32 v42, v26
	v_add_f32_e32 v26, 1.0, v30
	v_rcp_f32_e32 v44, v26
	v_fmamk_f32 v26, v95, 0xbd38aa3b, v15
	v_exp_f32_e32 v26, v26
	v_exp_f32_e32 v32, v32
	v_fmamk_f32 v34, v92, 0xbd38aa3b, v12
	v_add_f32_e32 v26, 1.0, v26
	v_rcp_f32_e32 v46, v26
	v_add_f32_e32 v26, 1.0, v32
	v_rcp_f32_e32 v48, v26
	v_fmamk_f32 v26, v96, 0xbd38aa3b, v16
	v_exp_f32_e32 v26, v26
	v_exp_f32_e32 v34, v34
	v_fmamk_f32 v43, v93, 0xbd38aa3b, v13
	v_add_f32_e32 v26, 1.0, v26
	v_rcp_f32_e32 v50, v26
	v_add_f32_e32 v26, 1.0, v34
	v_rcp_f32_e32 v52, v26
	v_fmamk_f32 v26, v97, 0xbd38aa3b, v17
	v_exp_f32_e32 v26, v26
	v_exp_f32_e32 v43, v43
	v_fmamk_f32 v10, v74, 0xbd38aa3b, v10
	v_add_f32_e32 v26, 1.0, v26
	v_add_f32_e32 v43, 1.0, v43
	v_rcp_f32_e32 v54, v26
	v_rcp_f32_e32 v56, v43
	v_permlane16_swap_b32_e32 v27, v62
	v_fmamk_f32 v28, v86, 0x3d000000, v6
	v_fmamk_f32 v30, v87, 0x3d000000, v7
	v_mov_b32_e32 v43, v212
	v_mov_b32_e32 v47, v212
	v_exp_f32_e32 v10, v10
	v_cvt_f32_ubyte0_e32 v37, v27
	v_cvt_f32_ubyte1_e32 v39, v27
	v_cvt_f32_ubyte2_e32 v41, v27
	v_cvt_f32_ubyte3_e32 v27, v27
	v_fmamk_f32 v36, v82, 0x3d000000, v2
	v_fmamk_f32 v38, v83, 0x3d000000, v3
	v_fmamk_f32 v34, v89, 0x3d000000, v9
	v_fmamk_f32 v26, v85, 0x3d000000, v5
	v_pk_mul_f32 v[28:29], v[28:29], v[42:43]
	v_pk_mul_f32 v[30:31], v[30:31], v[46:47]
	v_mov_b32_e32 v45, v212
	v_mov_b32_e32 v49, v212
	s_waitcnt vmcnt(1)
;     __device__ __forceinline__ void operator()(EPI_ARGS) const {
;     ...
;         for (int ai = 0; ai < 2; ++ai)
; #pragma unroll
;             for (int mp = 0; mp < 2; ++mp) { unsigned px[2], py[2]; unsigned gq[2][2] = {{0u, 0u}, {0u, 0u}};
;                 if (GATE_FP8) unpair16(glq[ai][mp], gq[0][0], gq[0][1], gq[1][0], gq[1][1]);
; #pragma unroll
;                 for (int h = 0; h < 2; ++h) { const int m = 2 * mp + h; const int row = u.pm * 256 + ai * 128 + wr * 64 + m * 16 + fr; const size_t off = (size_t)row * D + j0;
;                     const u32x4 yp = ypq[ai][mp][h]; float gsf[8];
;                     if (GATE_FP8) { v2u g8; g8.x = gq[h][0]; g8.y = gq[h][1]; const float k255 = 1.0f / 255.0f;
;                         gsf[0] = (float)(g8.x & 0xffu) * k255; gsf[1] = (float)((g8.x >> 8) & 0xffu) * k255; gsf[2] = (float)((g8.x >> 16) & 0xffu) * k255; gsf[3] = (float)(g8.x >> 24) * k255;
;                         gsf[4] = (float)(g8.y & 0xffu) * k255; gsf[5] = (float)((g8.y >> 8) & 0xffu) * k255; gsf[6] = (float)((g8.y >> 16) & 0xffu) * k255; gsf[7] = (float)(g8.y >> 24) * k255; }
;                     else { const u32x4 gs = *(const u32x4*)(SGS + off); gsf[0] = bf_lo(gs.x); gsf[1] = bf_hi(gs.x); gsf[2] = bf_lo(gs.y); gsf[3] = bf_hi(gs.y); gsf[4] = bf_lo(gs.z); gsf[5] = bf_hi(gs.z); gsf[6] = bf_lo(gs.w); gsf[7] = bf_hi(gs.w); }
;                     const f32x4 a0 = acc[ai][0][m][0] * asc + ba0, a1 = acc[ai][0][m][1] * asc + ba1, b0 = acc[ai][1][m][0] * asc + bb0, b1 = acc[ai][1][m][1] * asc + bb1;
;                     float o[8];
; #pragma unroll
;                     for (int j = 0; j < 4; ++j) { o[j] = a0[j] * sigmoidf_(b0[j]); o[4 + j] = a1[j] * sigmoidf_(b1[j]); }
;                     float mo[8] = {bf_lo(yp.x) + gsf[0] * o[0], bf_hi(yp.x) + gsf[1] * o[1], bf_lo(yp.y) + gsf[2] * o[2], bf_hi(yp.y) + gsf[3] * o[3],
;                                    bf_lo(yp.z) + gsf[4] * o[4], bf_hi(yp.z) + gsf[5] * o[5], bf_lo(yp.w) + gsf[6] * o[6], bf_hi(yp.w) + gsf[7] * o[7]};
;                     if (OUT_FP8) { px[h] = pk4_fp8(mo[0], mo[1], mo[2], mo[3]); py[h] = pk4_fp8(mo[4], mo[5], mo[6], mo[7]); }
;                     else { u32x4 w; w.x = cvt_pk_bf16(mo[0], mo[1]); w.y = cvt_pk_bf16(mo[2], mo[3]); w.z = cvt_pk_bf16(mo[4], mo[5]); w.w = cvt_pk_bf16(mo[6], mo[7]); *(u32x4*)(MG + off) = w; } }
	v_lshlrev_b32_e32 v42, 16, v22
	v_and_b32_e32 v22, 0xffff0000, v22
	v_fmamk_f32 v32, v88, 0x3d000000, v8
	v_mov_b32_e32 v51, v212
	v_pk_mul_f32 v[34:35], v[34:35], v[54:55]
	v_pk_mul_f32 v[36:37], v[36:37], v[44:45]
	v_pk_mul_f32 v[38:39], v[38:39], v[48:49]
	v_pk_mul_f32 v[26:27], v[26:27], v[56:57]
	v_fmac_f32_e32 v42, v28, v29
	v_fmac_f32_e32 v22, v30, v31
	v_lshlrev_b32_e32 v28, 16, v23
	v_and_b32_e32 v23, 0xffff0000, v23
	v_lshlrev_b32_e32 v29, 16, v24
	v_and_b32_e32 v24, 0xffff0000, v24
	v_lshlrev_b32_e32 v30, 16, v25
	v_and_b32_e32 v25, 0xffff0000, v25
	v_pk_mul_f32 v[32:33], v[32:33], v[50:51]
	v_fmac_f32_e32 v23, v34, v35
	v_fmac_f32_e32 v29, v36, v37
	v_fmac_f32_e32 v24, v38, v39
	v_fmac_f32_e32 v25, v26, v27
	v_med3_f32 v26, v42, s74, v227
	v_med3_f32 v27, v22, s74, v227
	v_fmac_f32_e32 v28, v32, v33
	v_med3_f32 v31, v23, s74, v227
	v_cvt_pk_fp8_f32 v22, v26, v27
	v_med3_f32 v26, v29, s74, v227
	v_med3_f32 v24, v24, s74, v227
	v_fmamk_f32 v32, v66, 0x3d000000, v2
	v_add_f32_e32 v2, 1.0, v10
	v_fmamk_f32 v10, v75, 0xbd38aa3b, v11
	v_cvt_pk_fp8_f32 v23, v26, v24
	v_fmamk_f32 v26, v71, 0x3d000000, v7
	v_fmamk_f32 v7, v79, 0xbd38aa3b, v15
	v_exp_f32_e32 v11, v10
	v_fmamk_f32 v40, v84, 0x3d000000, v4
	v_mov_b32_e32 v53, v212
	v_exp_f32_e32 v7, v7
	v_pk_mul_f32 v[40:41], v[40:41], v[52:53]
	v_med3_f32 v25, v25, s74, v227
	v_fmac_f32_e32 v30, v40, v41
	v_med3_f32 v24, v30, s74, v227
	v_fmamk_f32 v34, v67, 0x3d000000, v3
	v_add_f32_e32 v3, 1.0, v11
	v_cvt_pk_fp8_f32 v23, v24, v25 op_sel:[0,0,1]
	v_fmamk_f32 v24, v70, 0x3d000000, v6
	v_fmamk_f32 v6, v78, 0xbd38aa3b, v14
	v_add_f32_e32 v7, 1.0, v7
	v_rcp_f32_e32 v14, v3
	v_fmamk_f32 v3, v80, 0xbd38aa3b, v16
	v_rcp_f32_e32 v10, v7
	v_fmamk_f32 v7, v76, 0xbd38aa3b, v12
	v_exp_f32_e32 v3, v3
	v_exp_f32_e32 v7, v7
	v_exp_f32_e32 v6, v6
	v_add_f32_e32 v3, 1.0, v3
	v_med3_f32 v28, v28, s74, v227
	v_rcp_f32_e32 v12, v3
	v_add_f32_e32 v3, 1.0, v7
	v_cvt_pk_fp8_f32 v22, v28, v31 op_sel:[0,0,1]
	v_fmamk_f32 v28, v72, 0x3d000000, v8
	v_rcp_f32_e32 v8, v3
	v_fmamk_f32 v3, v81, 0xbd38aa3b, v17
	v_fmamk_f32 v36, v68, 0x3d000000, v4
	v_exp_f32_e32 v3, v3
	v_fmamk_f32 v4, v77, 0xbd38aa3b, v13
	v_add_f32_e32 v6, 1.0, v6
	v_exp_f32_e32 v4, v4
	v_rcp_f32_e32 v6, v6
	v_rcp_f32_e32 v2, v2
	v_add_f32_e32 v3, 1.0, v3
	v_cvt_f32_ubyte0_e32 v25, v61
	v_rcp_f32_e32 v16, v3
	v_add_f32_e32 v3, 1.0, v4
	v_mov_b32_e32 v7, v212
	v_cvt_f32_ubyte1_e32 v27, v61
	v_rcp_f32_e32 v4, v3
	v_pk_mul_f32 v[6:7], v[24:25], v[6:7]
	v_mov_b32_e32 v11, v212
	s_waitcnt vmcnt(0)
	v_lshlrev_b32_e32 v24, 16, v18
	v_cvt_f32_ubyte0_e32 v33, v62
	v_fmac_f32_e32 v9, 0x3d000000, v73
	v_pk_mul_f32 v[10:11], v[26:27], v[10:11]
	v_mov_b32_e32 v3, v212
	v_fmac_f32_e32 v24, v6, v7
	v_and_b32_e32 v6, 0xffff0000, v18
	v_cvt_f32_ubyte2_e32 v37, v62
	v_fmac_f32_e32 v5, 0x3d000000, v69
	v_mov_b32_e32 v30, v9
	v_pk_mul_f32 v[2:3], v[32:33], v[2:3]
	v_mov_b32_e32 v9, v212
	v_fmac_f32_e32 v6, v10, v11
	v_lshlrev_b32_e32 v11, 16, v20
	v_cvt_f32_ubyte1_e32 v35, v62
	v_cvt_f32_ubyte3_e32 v39, v62
	v_mov_b32_e32 v15, v212
	v_pk_mul_f32 v[8:9], v[36:37], v[8:9]
	v_mov_b32_e32 v38, v5
	v_mov_b32_e32 v5, v212
	v_fmac_f32_e32 v11, v2, v3
	v_lshlrev_b32_e32 v3, 16, v21
	v_pk_mul_f32 v[14:15], v[34:35], v[14:15]
	v_pk_mul_f32 v[4:5], v[38:39], v[4:5]
	v_and_b32_e32 v2, 0xffff0000, v20
	v_fmac_f32_e32 v3, v8, v9
	v_and_b32_e32 v8, 0xffff0000, v21
	v_fmac_f32_e32 v2, v14, v15
	v_fmac_f32_e32 v8, v4, v5
	v_med3_f32 v4, v24, s74, v227
	v_med3_f32 v5, v6, s74, v227
	v_cvt_pk_fp8_f32 v24, v4, v5
	v_med3_f32 v4, v11, s74, v227
	v_med3_f32 v2, v2, s74, v227
	v_cvt_f32_ubyte2_e32 v29, v61
	v_cvt_f32_ubyte3_e32 v31, v61
	v_mov_b32_e32 v13, v212
	v_mov_b32_e32 v17, v212
	v_cvt_pk_fp8_f32 v25, v4, v2
	v_pk_mul_f32 v[12:13], v[28:29], v[12:13]
	v_pk_mul_f32 v[16:17], v[30:31], v[16:17]
	v_lshlrev_b32_e32 v7, 16, v19
	v_and_b32_e32 v10, 0xffff0000, v19
	v_fmac_f32_e32 v7, v12, v13
	v_fmac_f32_e32 v10, v16, v17
	v_med3_f32 v6, v7, s74, v227
	v_med3_f32 v7, v10, s74, v227
	v_med3_f32 v2, v3, s74, v227
	v_med3_f32 v3, v8, s74, v227
	v_cvt_pk_fp8_f32 v24, v6, v7 op_sel:[0,0,1]
	v_cvt_pk_fp8_f32 v25, v2, v3 op_sel:[0,0,1]
	v_add_u32_e32 v2, 0xa0, v60
	v_ashrrev_i32_e32 v3, 31, v2
	v_lshlrev_b64 v[2:3], 11, v[2:3]
	v_lshl_add_u64 v[2:3], s[16:17], 0, v[2:3]
	v_permlane16_swap_b32_e32 v22, v24
	v_permlane16_swap_b32_e32 v23, v25
	v_lshl_add_u64 v[2:3], v[2:3], 0, v[58:59]
	s_mov_b64 s[4:5], -1
	global_store_dwordx4 v[2:3], v[22:25], off
	s_cbranch_vccnz .LBB0_885
	s_andn2_b64 vcc, exec, s[8:9]
	s_cbranch_vccnz .LBB0_884
	s_barrier
	s_branch .LBB0_884

; __device__ __forceinline__ float bf_lo(unsigned w) { return __uint_as_float(w << 16); }
; __device__ __forceinline__ float bf_hi(unsigned w) { return __uint_as_float(w & 0xffff0000u); }
; __global__ void __launch_bounds__(NWAVES * 64, 2) fwd_kernel(Args args) {
;     ...
;             f32x4 v[4][8]; float rstd[4], ssq[4] = {0.f, 0.f, 0.f, 0.f};
; #pragma unroll
;             for (int j = 0; j < 8; ++j) { const int k = 4 * lane + 256 * j;
; #pragma unroll
;                 for (int rr = 0; rr < 4; ++rr) { const size_t off = (size_t)(R0 + 4 * wave + rr) * D + k; const v2u mq = *(const v2u*)(X1B + off);
;                     v[rr][j] = (f32x4){bf_lo(mq.x), bf_hi(mq.x), bf_lo(mq.y), bf_hi(mq.y)};
;                     ssq[rr] += v[rr][j][0] * v[rr][j][0] + v[rr][j][1] * v[rr][j][1] + v[rr][j][2] * v[rr][j][2] + v[rr][j][3] * v[rr][j][3]; } }
.LBB0_1061:
	s_add_i32 s62, s49, s70
	s_add_i32 s60, s62, 1
	s_add_i32 s58, s62, 2
	s_add_i32 s56, s62, 3
	s_ashr_i32 s63, s62, 31
	s_ashr_i32 s61, s60, 31
	s_ashr_i32 s59, s58, 31
	s_ashr_i32 s57, s56, 31
	s_lshl_b64 s[2:3], s[62:63], 12
	s_lshl_b64 s[14:15], s[60:61], 12
	s_lshl_b64 s[16:17], s[58:59], 12
	s_lshl_b64 s[80:81], s[56:57], 12
	v_lshl_add_u64 v[2:3], v[50:51], 0, s[2:3]
	v_lshl_add_u64 v[4:5], v[50:51], 0, s[14:15]
	s_add_u32 s64, s28, s2
	global_load_dwordx2 v[2:3], v[2:3], off
	s_addc_u32 s65, s29, s3
	global_load_dwordx2 v[6:7], v[4:5], off
	v_lshl_add_u64 v[4:5], v[50:51], 0, s[16:17]
	global_load_dwordx2 v[8:9], v[4:5], off
	v_lshl_add_u64 v[4:5], v[50:51], 0, s[80:81]
	s_add_u32 s52, s28, s14
	global_load_dwordx2 v[10:11], v[4:5], off
	v_lshlrev_b32_e32 v4, 1, v52
	s_addc_u32 s53, s29, s15
	global_load_dwordx2 v[12:13], v4, s[64:65]
	global_load_dwordx2 v[14:15], v4, s[52:53]
	s_add_u32 s16, s28, s16
	s_addc_u32 s17, s29, s17
	s_add_u32 s2, s28, s80
	global_load_dwordx2 v[16:17], v4, s[16:17]
	s_addc_u32 s3, s29, s81
	global_load_dwordx2 v[18:19], v4, s[2:3]
	v_lshlrev_b32_e32 v4, 1, v54
	v_lshlrev_b32_e32 v20, 1, v56
	global_load_dwordx2 v[22:23], v4, s[64:65]
	global_load_dwordx2 v[24:25], v20, s[64:65]
	global_load_dwordx2 v[26:27], v20, s[52:53]
	global_load_dwordx2 v[28:29], v20, s[16:17]
	global_load_dwordx2 v[30:31], v4, s[52:53]
	global_load_dwordx2 v[32:33], v4, s[16:17]
	global_load_dwordx2 v[34:35], v4, s[2:3]
	v_lshlrev_b32_e32 v71, 1, v60
	global_load_dwordx2 v[40:41], v71, s[64:65]
	v_lshlrev_b32_e32 v79, 1, v64
	v_lshlrev_b32_e32 v78, 1, v62
	v_mov_b32_e32 v177, 0
	v_mov_b32_e32 v178, 0
	v_mov_b32_e32 v179, 0
	s_lshl_b64 s[14:15], s[56:57], 11
	s_waitcnt vmcnt(15)
	v_and_b32_e32 v5, 0xffff0000, v2
	v_lshlrev_b32_e32 v4, 16, v2
	s_waitcnt vmcnt(14)
	v_and_b32_e32 v157, 0xffff0000, v6
	v_lshlrev_b32_e32 v156, 16, v6
	v_lshlrev_b32_e32 v154, 16, v7
	v_and_b32_e32 v155, 0xffff0000, v7
	s_waitcnt vmcnt(13)
	v_and_b32_e32 v153, 0xffff0000, v8
	s_waitcnt vmcnt(12)
	v_lshlrev_b32_e32 v148, 16, v10
	v_and_b32_e32 v149, 0xffff0000, v10
	v_mul_f32_e32 v10, v157, v157
	s_waitcnt vmcnt(11)
	v_lshlrev_b32_e32 v6, 16, v13
	s_waitcnt vmcnt(10)
	v_and_b32_e32 v145, 0xffff0000, v14
	v_and_b32_e32 v7, 0xffff0000, v13
	v_lshlrev_b32_e32 v144, 16, v14
	v_mul_f32_e32 v13, v145, v145
	v_fmac_f32_e32 v10, v156, v156
	v_lshlrev_b32_e32 v142, 16, v15
	v_fmac_f32_e32 v13, v144, v144
	v_fmac_f32_e32 v10, v154, v154
	v_and_b32_e32 v143, 0xffff0000, v15
	v_fmac_f32_e32 v13, v142, v142
	v_lshlrev_b32_e32 v150, 16, v9
	v_and_b32_e32 v151, 0xffff0000, v9
	v_and_b32_e32 v9, 0xffff0000, v12
	v_fmac_f32_e32 v10, v155, v155
	s_waitcnt vmcnt(9)
	v_and_b32_e32 v135, 0xffff0000, v16
	v_fmac_f32_e32 v13, v143, v143
	v_mul_f32_e32 v21, v5, v5
	v_lshlrev_b32_e32 v152, 16, v8
	v_lshlrev_b32_e32 v146, 16, v11
	v_and_b32_e32 v147, 0xffff0000, v11
	v_mul_f32_e32 v11, v153, v153
	v_lshlrev_b32_e32 v8, 16, v12
	v_mul_f32_e32 v12, v9, v9
	v_lshlrev_b32_e32 v134, 16, v16
	v_add_f32_e32 v16, v10, v13
	v_mul_f32_e32 v10, v135, v135
	s_waitcnt vmcnt(2)
	v_and_b32_e32 v113, 0xffff0000, v32
	v_lshlrev_b32_e32 v2, 16, v3
	v_fmac_f32_e32 v21, v4, v4
	v_fmac_f32_e32 v11, v152, v152
	v_fmac_f32_e32 v12, v8, v8
	v_lshlrev_b32_e32 v136, 16, v17
	v_fmac_f32_e32 v10, v134, v134
	v_lshlrev_b32_e32 v110, 16, v30
	v_and_b32_e32 v111, 0xffff0000, v30
	v_lshlrev_b32_e32 v112, 16, v32
	v_mul_f32_e32 v30, v113, v113
	v_and_b32_e32 v3, 0xffff0000, v3
	v_fmac_f32_e32 v21, v2, v2
	v_fmac_f32_e32 v11, v150, v150
	v_fmac_f32_e32 v12, v6, v6
	v_and_b32_e32 v137, 0xffff0000, v17
	v_fmac_f32_e32 v10, v136, v136
	v_lshlrev_b32_e32 v108, 16, v33
	v_fmac_f32_e32 v30, v112, v112
	v_fmac_f32_e32 v21, v3, v3
	v_fmac_f32_e32 v11, v151, v151
	v_fmac_f32_e32 v12, v7, v7
	v_fmac_f32_e32 v10, v137, v137
	v_and_b32_e32 v121, 0xffff0000, v18
	v_and_b32_e32 v109, 0xffff0000, v33
	v_fmac_f32_e32 v30, v108, v108
	v_mul_f32_e32 v36, v149, v149
	v_add_f32_e32 v14, v21, v12
	v_add_f32_e32 v37, v11, v10
	v_lshlrev_b32_e32 v120, 16, v18
	v_mul_f32_e32 v12, v121, v121
	v_fmac_f32_e32 v30, v109, v109
	s_waitcnt vmcnt(1)
	v_and_b32_e32 v107, 0xffff0000, v34
	v_fmac_f32_e32 v36, v148, v148
	global_load_dwordx2 v[10:11], v20, s[2:3]
	v_lshlrev_b32_e32 v132, 16, v19
	v_fmac_f32_e32 v12, v120, v120
	v_add_f32_e32 v70, v37, v30
	v_lshlrev_b32_e32 v106, 16, v34
	v_mul_f32_e32 v30, v107, v107
	v_fmac_f32_e32 v36, v146, v146
	v_and_b32_e32 v133, 0xffff0000, v19
	v_fmac_f32_e32 v12, v132, v132
	v_lshlrev_b32_e32 v32, 16, v35
	v_fmac_f32_e32 v30, v106, v106
	v_fmac_f32_e32 v36, v147, v147
	v_fmac_f32_e32 v12, v133, v133
	v_and_b32_e32 v33, 0xffff0000, v35
	v_fmac_f32_e32 v30, v32, v32
	v_add_f32_e32 v36, v36, v12
	v_fmac_f32_e32 v30, v33, v33
	v_and_b32_e32 v21, 0xffff0000, v22
	v_lshlrev_b32_e32 v102, 16, v31
	v_and_b32_e32 v103, 0xffff0000, v31
	v_add_f32_e32 v72, v36, v30
	v_lshlrev_b32_e32 v104, 16, v24
	v_and_b32_e32 v105, 0xffff0000, v24
	v_lshlrev_b32_e32 v30, 16, v25
	v_and_b32_e32 v31, 0xffff0000, v25
	v_lshlrev_b32_e32 v90, 16, v26
	v_and_b32_e32 v91, 0xffff0000, v26
	v_lshlrev_b32_e32 v24, 16, v27
	v_and_b32_e32 v25, 0xffff0000, v27
	global_load_dwordx2 v[26:27], v71, s[52:53]
	v_lshlrev_b32_e32 v96, 16, v28
	v_and_b32_e32 v97, 0xffff0000, v28
	v_lshlrev_b32_e32 v36, 16, v29
	v_and_b32_e32 v37, 0xffff0000, v29
	global_load_dwordx2 v[28:29], v71, s[16:17]
	v_lshlrev_b32_e32 v20, 16, v22
	v_lshlrev_b32_e32 v22, 1, v58
	global_load_dwordx2 v[12:13], v22, s[64:65]
	global_load_dwordx2 v[38:39], v22, s[2:3]
	v_mul_f32_e32 v15, v21, v21
	v_lshlrev_b32_e32 v18, 16, v23
	v_fmac_f32_e32 v15, v20, v20
	v_and_b32_e32 v19, 0xffff0000, v23
	v_fmac_f32_e32 v15, v18, v18
	v_fmac_f32_e32 v15, v19, v19
	v_add_f32_e32 v23, v14, v15
	global_load_dwordx2 v[14:15], v22, s[52:53]
	v_mul_f32_e32 v17, v111, v111
	v_fmac_f32_e32 v17, v110, v110
	v_fmac_f32_e32 v17, v102, v102
	v_fmac_f32_e32 v17, v103, v103
	v_add_f32_e32 v69, v16, v17
	global_load_dwordx2 v[16:17], v22, s[16:17]
	v_mul_f32_e32 v22, v105, v105
	v_fmac_f32_e32 v22, v104, v104
	v_fmac_f32_e32 v22, v30, v30
	v_fmac_f32_e32 v22, v31, v31
	v_add_f32_e32 v74, v23, v22
	v_mul_f32_e32 v22, v91, v91
	v_fmac_f32_e32 v22, v90, v90
	v_fmac_f32_e32 v22, v24, v24
	v_fmac_f32_e32 v22, v25, v25
	v_add_f32_e32 v69, v69, v22
	v_mul_f32_e32 v22, v97, v97
	v_fmac_f32_e32 v22, v96, v96
	v_fmac_f32_e32 v22, v36, v36
	v_fmac_f32_e32 v22, v37, v37
	v_add_f32_e32 v76, v70, v22
	global_load_dwordx2 v[70:71], v71, s[2:3]
	s_waitcnt vmcnt(8)
; __device__ __forceinline__ float bf_lo(unsigned w) { return __uint_as_float(w << 16); }
; __device__ __forceinline__ float bf_hi(unsigned w) { return __uint_as_float(w & 0xffff0000u); }
; __global__ void __launch_bounds__(NWAVES * 64, 2) fwd_kernel(Args args) {
;     ...
; #pragma unroll
;             for (int j = 0; j < 8; ++j) { const int k = 4 * lane + 256 * j;
; #pragma unroll
;                 for (int rr = 0; rr < 4; ++rr) { const size_t off = (size_t)(R0 + 4 * wave + rr) * D + k; const v2u mq = *(const v2u*)(X1B + off);
;                     v[rr][j] = (f32x4){bf_lo(mq.x), bf_hi(mq.x), bf_lo(mq.y), bf_hi(mq.y)};
;                     ssq[rr] += v[rr][j][0] * v[rr][j][0] + v[rr][j][1] * v[rr][j][1] + v[rr][j][2] * v[rr][j][2] + v[rr][j][3] * v[rr][j][3]; } }
; #pragma unroll
;             for (int rr = 0; rr < 4; ++rr) rstd[rr] = 1.0f / sqrtf(wave_sum(ssq[rr]) * (1.0f / D) + RMS_EPS);
	v_and_b32_e32 v141, 0xffff0000, v40
	v_lshlrev_b32_e32 v140, 16, v40
	v_lshlrev_b32_e32 v138, 16, v41
	v_and_b32_e32 v139, 0xffff0000, v41
	s_waitcnt vmcnt(7)
	v_and_b32_e32 v35, 0xffff0000, v10
	v_lshlrev_b32_e32 v34, 16, v10
	v_mul_f32_e32 v10, v35, v35
	v_lshlrev_b32_e32 v22, 16, v11
	v_fmac_f32_e32 v10, v34, v34
	v_and_b32_e32 v23, 0xffff0000, v11
	v_fmac_f32_e32 v10, v22, v22
	v_fmac_f32_e32 v10, v23, v23
	v_add_f32_e32 v77, v72, v10
	global_load_dwordx2 v[10:11], v79, s[64:65]
	global_load_dwordx2 v[72:73], v78, s[64:65]
	s_waitcnt vmcnt(8)
	v_and_b32_e32 v123, 0xffff0000, v26
	v_lshlrev_b32_e32 v122, 16, v26
	v_mul_f32_e32 v26, v123, v123
	v_lshlrev_b32_e32 v118, 16, v27
	v_fmac_f32_e32 v26, v122, v122
	v_and_b32_e32 v119, 0xffff0000, v27
	v_fmac_f32_e32 v26, v118, v118
	v_fmac_f32_e32 v26, v119, v119
	s_waitcnt vmcnt(6)
	v_and_b32_e32 v127, 0xffff0000, v12
	v_lshlrev_b32_e32 v126, 16, v12
	v_mul_f32_e32 v12, v127, v127
	v_lshlrev_b32_e32 v124, 16, v13
	v_fmac_f32_e32 v12, v126, v126
	v_and_b32_e32 v125, 0xffff0000, v13
	v_fmac_f32_e32 v12, v124, v124
	v_fmac_f32_e32 v12, v125, v125
	v_add_f32_e32 v80, v74, v12
	global_load_dwordx2 v[12:13], v79, s[52:53]
	global_load_dwordx2 v[74:75], v78, s[52:53]
	s_waitcnt vmcnt(6)
	v_and_b32_e32 v101, 0xffff0000, v14
	v_lshlrev_b32_e32 v100, 16, v14
	v_mul_f32_e32 v14, v101, v101
	v_lshlrev_b32_e32 v94, 16, v15
	v_fmac_f32_e32 v14, v100, v100
	v_and_b32_e32 v95, 0xffff0000, v15
	v_fmac_f32_e32 v14, v94, v94
	v_fmac_f32_e32 v14, v95, v95
	v_add_f32_e32 v69, v69, v14
	global_load_dwordx2 v[14:15], v79, s[16:17]
	global_load_dwordx2 v[88:89], v78, s[16:17]
	global_load_dwordx2 v[166:167], v79, s[2:3]
	global_load_dwordx2 v[168:169], v78, s[2:3]
	s_waitcnt vmcnt(9)
	v_and_b32_e32 v117, 0xffff0000, v16
	v_lshlrev_b32_e32 v116, 16, v16
	v_mul_f32_e32 v16, v117, v117
	v_lshlrev_b32_e32 v130, 16, v38
	v_and_b32_e32 v131, 0xffff0000, v38
	v_mul_f32_e32 v38, v141, v141
	v_lshlrev_b32_e32 v114, 16, v17
	v_fmac_f32_e32 v16, v116, v116
	v_fmac_f32_e32 v38, v140, v140
	v_and_b32_e32 v115, 0xffff0000, v17
	v_fmac_f32_e32 v16, v114, v114
	v_fmac_f32_e32 v38, v138, v138
	v_fmac_f32_e32 v16, v115, v115
	v_fmac_f32_e32 v38, v139, v139
	v_add_f32_e32 v16, v76, v16
	v_lshlrev_b32_e32 v128, 16, v39
	v_and_b32_e32 v129, 0xffff0000, v39
	v_add_f32_e32 v76, v80, v38
	v_mul_f32_e32 v17, v131, v131
	v_fmac_f32_e32 v17, v130, v130
	v_and_b32_e32 v99, 0xffff0000, v28
	v_fmac_f32_e32 v17, v128, v128
	v_add_f32_e32 v69, v69, v26
	v_lshlrev_b32_e32 v98, 16, v28
	v_mul_f32_e32 v26, v99, v99
	v_fmac_f32_e32 v17, v129, v129
	v_lshlrev_b32_e32 v92, 16, v29
	v_fmac_f32_e32 v26, v98, v98
	v_add_f32_e32 v17, v77, v17
	v_and_b32_e32 v93, 0xffff0000, v29
	s_waitcnt vmcnt(7)
	v_and_b32_e32 v39, 0xffff0000, v10
	s_waitcnt vmcnt(6)
	v_and_b32_e32 v38, 0xffff0000, v72
	v_lshlrev_b32_e32 v41, 16, v10
	v_lshlrev_b32_e32 v40, 16, v72
	v_lshlrev_b32_e32 v87, 16, v11
	v_and_b32_e32 v85, 0xffff0000, v11
	v_pk_mul_f32 v[10:11], v[38:39], v[38:39]
	v_lshlrev_b32_e32 v86, 16, v73
	v_pk_fma_f32 v[10:11], v[40:41], v[40:41], v[10:11]
	v_and_b32_e32 v84, 0xffff0000, v73
	v_pk_fma_f32 v[10:11], v[86:87], v[86:87], v[10:11]
	v_fmac_f32_e32 v26, v92, v92
	v_pk_fma_f32 v[10:11], v[84:85], v[84:85], v[10:11]
	v_fmac_f32_e32 v26, v93, v93
	v_add_f32_e32 v10, v76, v10
	v_and_b32_e32 v29, 0xffff0000, v70
	v_add_f32_e32 v162, v10, v11
	v_add_f32_e32 v158, v16, v26
	v_lshlrev_b32_e32 v28, 16, v70
	v_mul_f32_e32 v16, v29, v29
	v_lshlrev_b32_e32 v26, 16, v71
	v_fmac_f32_e32 v16, v28, v28
	v_and_b32_e32 v27, 0xffff0000, v71
	v_fmac_f32_e32 v16, v26, v26
	v_fmac_f32_e32 v16, v27, v27
	v_add_f32_e32 v160, v17, v16
	s_lshl_b64 s[52:53], s[60:61], 11
	s_waitcnt vmcnt(5)
	v_and_b32_e32 v77, 0xffff0000, v12
	s_waitcnt vmcnt(4)
	v_and_b32_e32 v76, 0xffff0000, v74
	v_lshlrev_b32_e32 v79, 16, v12
	v_lshlrev_b32_e32 v78, 16, v74
	v_pk_mul_f32 v[10:11], v[76:77], v[76:77]
	v_lshlrev_b32_e32 v83, 16, v13
	v_lshlrev_b32_e32 v82, 16, v75
	v_pk_fma_f32 v[10:11], v[78:79], v[78:79], v[10:11]
	v_and_b32_e32 v81, 0xffff0000, v13
	v_and_b32_e32 v80, 0xffff0000, v75
	v_pk_fma_f32 v[10:11], v[82:83], v[82:83], v[10:11]
	s_waitcnt vmcnt(2)
	v_lshlrev_b32_e32 v70, 16, v88
	v_pk_fma_f32 v[10:11], v[80:81], v[80:81], v[10:11]
	v_and_b32_e32 v17, 0xffff0000, v14
	v_add_f32_e32 v10, v69, v10
	v_and_b32_e32 v69, 64, v211
	v_and_b32_e32 v16, 0xffff0000, v88
	v_add_u32_e32 v88, 64, v69
	v_xor_b32_e32 v69, 1, v211
	v_add_f32_e32 v164, v10, v11
	v_lshlrev_b32_e32 v71, 16, v14
	v_pk_mul_f32 v[10:11], v[16:17], v[16:17]
	v_cmp_lt_i32_e32 vcc, v69, v88
	v_lshlrev_b32_e32 v75, 16, v15
	v_lshlrev_b32_e32 v74, 16, v89
	v_pk_fma_f32 v[10:11], v[70:71], v[70:71], v[10:11]
	v_cndmask_b32_e32 v69, v211, v69, vcc
	v_and_b32_e32 v73, 0xffff0000, v15
	v_and_b32_e32 v72, 0xffff0000, v89
	v_pk_fma_f32 v[10:11], v[74:75], v[74:75], v[10:11]
	v_lshlrev_b32_e32 v69, 2, v69
	v_pk_fma_f32 v[10:11], v[72:73], v[72:73], v[10:11]
	ds_bpermute_b32 v89, v69, v162
	v_add_f32_e32 v10, v158, v10
	v_add_f32_e32 v158, v10, v11
	s_waitcnt vmcnt(1)
	v_lshlrev_b32_e32 v11, 16, v166
	v_and_b32_e32 v13, 0xffff0000, v166
	v_xor_b32_e32 v166, 2, v211
	v_cmp_lt_i32_e32 vcc, v166, v88
	s_waitcnt lgkmcnt(0)
	v_add_f32_e32 v89, v162, v89
	s_waitcnt vmcnt(0)
	v_lshlrev_b32_e32 v10, 16, v168
	v_cndmask_b32_e32 v166, v211, v166, vcc
	v_lshlrev_b32_e32 v216, 2, v166
	ds_bpermute_b32 v162, v216, v89
	v_xor_b32_e32 v166, 4, v211
	v_cmp_lt_i32_e32 vcc, v166, v88
	v_and_b32_e32 v12, 0xffff0000, v168
	v_lshlrev_b32_e32 v14, 16, v169
	v_cndmask_b32_e32 v166, v211, v166, vcc
	v_lshlrev_b32_e32 v217, 2, v166
	s_waitcnt lgkmcnt(0)
; #define LAS __attribute__((address_space(3)))
; __device__ __forceinline__ float wave_sum(float v) {
; #pragma unroll
;     for (int o = 1; o < 64; o <<= 1) v += __shfl_xor(v, o);
;     return v;
; }
; __global__ void __launch_bounds__(NWAVES * 64, 2) fwd_kernel(Args args) {
;     ...
; #pragma unroll
;             for (int rr = 0; rr < 4; ++rr) rstd[rr] = 1.0f / sqrtf(wave_sum(ssq[rr]) * (1.0f / D) + RMS_EPS);
; #pragma unroll
;             for (int j = 0; j < 8; ++j) { const int k = 4 * lane + 256 * j; const f32x4 Aj = *(const LAS f32x4*)(PVA + k), sh = *(const LAS f32x4*)(PVS + k);
; #pragma unroll
;                 for (int rr = 0; rr < 4; ++rr) { const int row = R0 + 4 * wave + rr; v[rr][j] = v[rr][j] * rstd[rr] * Aj + sh;
	v_add_f32_e32 v89, v89, v162
	ds_bpermute_b32 v162, v217, v89
	v_xor_b32_e32 v166, 8, v211
	v_cmp_lt_i32_e32 vcc, v166, v88
	v_lshlrev_b32_e32 v15, 16, v167
	ds_bpermute_b32 v173, v69, v158
	v_cndmask_b32_e32 v166, v211, v166, vcc
	v_lshlrev_b32_e32 v218, 2, v166
	s_waitcnt lgkmcnt(1)
	v_add_f32_e32 v89, v89, v162
	ds_bpermute_b32 v162, v218, v89
	v_xor_b32_e32 v166, 16, v211
	v_cmp_lt_i32_e32 vcc, v166, v88
	s_waitcnt lgkmcnt(1)
	v_add_f32_e32 v158, v158, v173
	ds_bpermute_b32 v173, v216, v158
	v_cndmask_b32_e32 v166, v211, v166, vcc
	v_lshlrev_b32_e32 v219, 2, v166
	s_waitcnt lgkmcnt(1)
	v_add_f32_e32 v89, v89, v162
	ds_bpermute_b32 v162, v219, v89
	v_xor_b32_e32 v166, 32, v211
	v_cmp_lt_i32_e32 vcc, v166, v88
	s_waitcnt lgkmcnt(1)
	v_add_f32_e32 v158, v158, v173
	ds_bpermute_b32 v173, v217, v158
	v_cndmask_b32_e32 v88, v211, v166, vcc
	v_lshlrev_b32_e32 v168, 2, v88
	s_waitcnt lgkmcnt(1)
	v_add_f32_e32 v162, v89, v162
	ds_bpermute_b32 v170, v168, v162
	v_and_b32_e32 v88, 0xffff0000, v169
	v_and_b32_e32 v89, 0xffff0000, v167
	v_pk_mul_f32 v[166:167], v[12:13], v[12:13]
	s_waitcnt lgkmcnt(1)
	v_add_f32_e32 v158, v158, v173
	s_waitcnt lgkmcnt(0)
	v_add_f32_e32 v162, v162, v170
	ds_bpermute_b32 v170, v69, v164
	v_fmamk_f32 v162, v162, 0x3a000000, v204
	v_mul_f32_e32 v169, 0x4f800000, v162
	v_cmp_gt_f32_e32 vcc, s73, v162
	v_pk_fma_f32 v[166:167], v[10:11], v[10:11], v[166:167]
	s_waitcnt lgkmcnt(0)
	v_add_f32_e32 v164, v164, v170
	ds_bpermute_b32 v170, v216, v164
	v_cndmask_b32_e32 v162, v162, v169, vcc
	v_sqrt_f32_e32 v169, v162
	v_pk_fma_f32 v[166:167], v[14:15], v[14:15], v[166:167]
	s_waitcnt lgkmcnt(0)
	v_add_f32_e32 v164, v164, v170
	ds_bpermute_b32 v170, v217, v164
	v_add_u32_e32 v171, -1, v169
	v_fma_f32 v172, -v171, v169, v162
	v_cmp_ge_f32_e64 s[2:3], 0, v172
	v_add_u32_e32 v172, 1, v169
	s_waitcnt lgkmcnt(0)
	v_add_f32_e32 v164, v164, v170
	v_cndmask_b32_e64 v171, v169, v171, s[2:3]
	v_fma_f32 v169, -v172, v169, v162
	ds_bpermute_b32 v170, v218, v164
	v_cmp_lt_f32_e64 s[2:3], 0, v169
	v_pk_fma_f32 v[166:167], v[88:89], v[88:89], v[166:167]
	s_waitcnt lgkmcnt(0)
	v_add_f32_e32 v164, v164, v170
	v_cndmask_b32_e64 v169, v171, v172, s[2:3]
	v_mul_f32_e32 v171, 0x37800000, v169
	v_cndmask_b32_e32 v169, v169, v171, vcc
	v_cmp_class_f32_e32 vcc, v162, v205
	ds_bpermute_b32 v170, v219, v164
	v_add_f32_e32 v160, v160, v166
	v_cndmask_b32_e32 v162, v169, v162, vcc
	v_div_scale_f32 v169, s[2:3], v162, v162, 1.0
	v_rcp_f32_e32 v171, v169
	s_waitcnt lgkmcnt(0)
	v_add_f32_e32 v164, v164, v170
	v_add_f32_e32 v160, v160, v167
	v_div_scale_f32 v167, vcc, 1.0, v162, 1.0
	v_fma_f32 v166, -v169, v171, 1.0
	v_fmac_f32_e32 v171, v166, v171
	ds_bpermute_b32 v166, v168, v164
	v_mul_f32_e32 v170, v167, v171
	v_fma_f32 v172, -v169, v170, v167
	v_fmac_f32_e32 v170, v172, v171
	v_fma_f32 v167, -v169, v170, v167
	s_waitcnt lgkmcnt(0)
	v_add_f32_e32 v164, v164, v166
	v_fmamk_f32 v164, v164, 0x3a000000, v204
	v_mul_f32_e32 v166, 0x4f800000, v164
	v_cmp_gt_f32_e64 s[2:3], s73, v164
	s_nop 1
	v_cndmask_b32_e64 v164, v164, v166, s[2:3]
	v_sqrt_f32_e32 v166, v164
	s_nop 0
	v_add_u32_e32 v169, -1, v166
	v_fma_f32 v172, -v169, v166, v164
	v_cmp_ge_f32_e64 s[16:17], 0, v172
	v_add_u32_e32 v172, 1, v166
	s_nop 0
	v_cndmask_b32_e64 v169, v166, v169, s[16:17]
	v_fma_f32 v166, -v172, v166, v164
	v_cmp_lt_f32_e64 s[16:17], 0, v166
	s_nop 1
	v_cndmask_b32_e64 v166, v169, v172, s[16:17]
	v_mul_f32_e32 v169, 0x37800000, v166
	v_cndmask_b32_e64 v166, v166, v169, s[2:3]
	ds_bpermute_b32 v169, v218, v158
	v_cmp_class_f32_e64 s[2:3], v164, v205
	s_waitcnt lgkmcnt(0)
	v_add_f32_e32 v169, v158, v169
	v_cndmask_b32_e64 v164, v166, v164, s[2:3]
	v_div_scale_f32 v166, s[2:3], v164, v164, 1.0
	v_rcp_f32_e32 v172, v166
	ds_bpermute_b32 v173, v219, v169
	v_div_fmas_f32 v158, v167, v171, v170
	v_div_fixup_f32 v158, v158, v162, 1.0
	v_fma_f32 v162, -v166, v172, 1.0
	v_fmac_f32_e32 v172, v162, v172
	s_waitcnt lgkmcnt(0)
	v_add_f32_e32 v162, v169, v173
	ds_bpermute_b32 v167, v168, v162
	ds_bpermute_b32 v173, v69, v160
	v_div_scale_f32 v169, vcc, 1.0, v164, 1.0
	v_mul_f32_e32 v170, v169, v172
	s_waitcnt lgkmcnt(1)
	v_add_f32_e32 v162, v162, v167
	v_fmamk_f32 v162, v162, 0x3a000000, v204
	v_mul_f32_e32 v167, 0x4f800000, v162
	v_cmp_gt_f32_e64 s[2:3], s73, v162
	s_waitcnt lgkmcnt(0)
	v_add_f32_e32 v160, v160, v173
	ds_bpermute_b32 v173, v216, v160
	v_cndmask_b32_e64 v162, v162, v167, s[2:3]
	v_sqrt_f32_e32 v167, v162
	v_fma_f32 v171, -v166, v170, v169
	v_fmac_f32_e32 v170, v171, v172
	v_fma_f32 v166, -v166, v170, v169
	v_add_u32_e32 v169, -1, v167
	s_waitcnt lgkmcnt(0)
	v_add_f32_e32 v160, v160, v173
	v_fma_f32 v171, -v169, v167, v162
	ds_bpermute_b32 v173, v217, v160
	v_cmp_ge_f32_e64 s[16:17], 0, v171
	v_add_u32_e32 v171, 1, v167
	v_pk_mul_f32 v[4:5], v[4:5], v[158:159] op_sel_hi:[1,0]
	v_cndmask_b32_e64 v169, v167, v169, s[16:17]
	v_fma_f32 v167, -v171, v167, v162
	v_cmp_lt_f32_e64 s[16:17], 0, v167
	s_waitcnt lgkmcnt(0)
	v_add_f32_e32 v160, v160, v173
	v_pk_mul_f32 v[8:9], v[8:9], v[158:159] op_sel_hi:[1,0]
	v_cndmask_b32_e64 v167, v169, v171, s[16:17]
	v_mul_f32_e32 v169, 0x37800000, v167
	v_cndmask_b32_e64 v167, v167, v169, s[2:3]
	ds_bpermute_b32 v169, v218, v160
	v_cmp_class_f32_e64 s[2:3], v162, v205
	v_pk_mul_f32 v[20:21], v[20:21], v[158:159] op_sel_hi:[1,0]
	s_waitcnt lgkmcnt(0)
	v_add_f32_e32 v169, v160, v169
	ds_bpermute_b32 v173, v219, v169
	v_div_fmas_f32 v160, v166, v172, v170
	v_cndmask_b32_e64 v162, v167, v162, s[2:3]
	v_div_scale_f32 v167, s[2:3], v162, v162, 1.0
	s_waitcnt lgkmcnt(0)
; #define LAS __attribute__((address_space(3)))
; __global__ void __launch_bounds__(NWAVES * 64, 2) fwd_kernel(Args args) {
;     ...
;             for (int rr = 0; rr < 4; ++rr) rstd[rr] = 1.0f / sqrtf(wave_sum(ssq[rr]) * (1.0f / D) + RMS_EPS);
; #pragma unroll
;             for (int j = 0; j < 8; ++j) { const int k = 4 * lane + 256 * j; const f32x4 Aj = *(const LAS f32x4*)(PVA + k), sh = *(const LAS f32x4*)(PVS + k);
; #pragma unroll
;                 for (int rr = 0; rr < 4; ++rr) { const int row = R0 + 4 * wave + rr; v[rr][j] = v[rr][j] * rstd[rr] * Aj + sh;
;                     *(unsigned*)(XN8 + (size_t)row * D + k) = pk4_fp8(v[rr][j][0], v[rr][j][1], v[rr][j][2], v[rr][j][3]); } }
	v_add_f32_e32 v166, v169, v173
	ds_bpermute_b32 v168, v168, v166
	v_rcp_f32_e32 v171, v167
	v_div_fixup_f32 v160, v160, v164, 1.0
	v_pk_mul_f32 v[156:157], v[156:157], v[160:161] op_sel_hi:[1,0]
	v_pk_mul_f32 v[144:145], v[144:145], v[160:161] op_sel_hi:[1,0]
	s_waitcnt lgkmcnt(0)
	v_add_f32_e32 v166, v166, v168
	v_fmamk_f32 v166, v166, 0x3a000000, v204
	v_mul_f32_e32 v168, 0x4f800000, v166
	v_cmp_gt_f32_e64 s[2:3], s73, v166
	v_fma_f32 v164, -v167, v171, 1.0
	v_fmac_f32_e32 v171, v164, v171
	v_cndmask_b32_e64 v166, v166, v168, s[2:3]
	v_div_scale_f32 v164, vcc, 1.0, v162, 1.0
	v_sqrt_f32_e32 v168, v166
	v_mul_f32_e32 v169, v164, v171
	v_fma_f32 v170, -v167, v169, v164
	v_fmac_f32_e32 v169, v170, v171
	v_fma_f32 v164, -v167, v169, v164
	v_add_u32_e32 v167, -1, v168
	v_fma_f32 v170, -v167, v168, v166
	v_cmp_ge_f32_e64 s[16:17], 0, v170
	v_add_u32_e32 v170, 1, v168
	v_div_fmas_f32 v164, v164, v171, v169
	v_cndmask_b32_e64 v167, v168, v167, s[16:17]
	v_fma_f32 v168, -v170, v168, v166
	v_cmp_lt_f32_e64 s[16:17], 0, v168
	v_div_fixup_f32 v162, v164, v162, 1.0
	v_pk_mul_f32 v[152:153], v[152:153], v[162:163] op_sel_hi:[1,0]
	v_cndmask_b32_e64 v167, v167, v170, s[16:17]
	v_mul_f32_e32 v168, 0x37800000, v167
	v_cndmask_b32_e64 v167, v167, v168, s[2:3]
	v_cmp_class_f32_e64 s[2:3], v166, v205
	s_lshl_b64 s[16:17], s[58:59], 11
	v_pk_mul_f32 v[134:135], v[134:135], v[162:163] op_sel_hi:[1,0]
	v_cndmask_b32_e64 v176, v167, v166, s[2:3]
	v_div_scale_f32 v166, s[2:3], v176, v176, 1.0
	v_rcp_f32_e32 v174, v166
	s_lshl_b64 s[2:3], s[62:63], 11
	v_pk_mul_f32 v[136:137], v[136:137], v[162:163] op_sel_hi:[1,0]
	v_pk_mul_f32 v[110:111], v[110:111], v[160:161] op_sel_hi:[1,0]
	v_fma_f32 v164, -v166, v174, 1.0
	v_fmac_f32_e32 v174, v164, v174
	v_div_scale_f32 v164, vcc, 1.0, v176, 1.0
	v_mul_f32_e32 v175, v164, v174
	v_fma_f32 v167, -v166, v175, v164
	v_fmac_f32_e32 v175, v167, v174
	v_fma_f32 v164, -v166, v175, v164
	ds_read_b128 v[166:169], v185
	ds_read_b128 v[170:173], v186
	v_div_fmas_f32 v164, v164, v174, v175
	v_pk_mul_f32 v[174:175], v[2:3], v[158:159] op_sel_hi:[1,0]
	v_div_fixup_f32 v164, v164, v176, 1.0
	v_pk_mul_f32 v[148:149], v[148:149], v[164:165] op_sel_hi:[1,0]
	s_waitcnt lgkmcnt(0)
	v_pk_fma_f32 v[2:3], v[166:167], v[4:5], v[170:171]
	v_pk_mul_f32 v[120:121], v[120:121], v[164:165] op_sel_hi:[1,0]
	v_med3_f32 v4, v2, s74, v212
	v_med3_f32 v5, v3, s74, v212
	v_cvt_pk_fp8_f32 v177, v4, v5
	v_pk_fma_f32 v[4:5], v[168:169], v[174:175], v[172:173]
	v_pk_mul_f32 v[132:133], v[132:133], v[164:165] op_sel_hi:[1,0]
	v_med3_f32 v174, v4, s74, v212
	v_med3_f32 v175, v5, s74, v212
	v_cvt_pk_fp8_f32 v177, v174, v175 op_sel:[0,0,1]
	v_lshl_add_u64 v[174:175], v[66:67], 0, s[2:3]
	s_add_u32 s2, s26, s2
	s_addc_u32 s3, s27, s3
	global_store_dword v[174:175], v177, off
	v_pk_mul_f32 v[174:175], v[154:155], v[160:161] op_sel_hi:[1,0]
	v_pk_fma_f32 v[154:155], v[166:167], v[156:157], v[170:171]
	v_pk_mul_f32 v[176:177], v[150:151], v[162:163] op_sel_hi:[1,0]
	v_med3_f32 v156, v154, s74, v212
	v_med3_f32 v157, v155, s74, v212
	v_pk_fma_f32 v[150:151], v[166:167], v[152:153], v[170:171]
	v_cvt_pk_fp8_f32 v178, v156, v157
	v_med3_f32 v152, v150, s74, v212
	v_med3_f32 v153, v151, s74, v212
	v_cvt_pk_fp8_f32 v179, v152, v153
	v_pk_fma_f32 v[156:157], v[168:169], v[174:175], v[172:173]
	v_pk_fma_f32 v[152:153], v[168:169], v[176:177], v[172:173]
	v_med3_f32 v174, v156, s74, v212
	v_med3_f32 v175, v157, s74, v212
	v_cvt_pk_fp8_f32 v178, v174, v175 op_sel:[0,0,1]
	v_med3_f32 v176, v152, s74, v212
	v_med3_f32 v177, v153, s74, v212
	v_cvt_pk_fp8_f32 v179, v176, v177 op_sel:[0,0,1]
	v_lshl_add_u64 v[174:175], v[66:67], 0, s[52:53]
	global_store_dword v[174:175], v178, off
	v_lshl_add_u64 v[174:175], v[66:67], 0, s[16:17]
	global_store_dword v[174:175], v179, off
	v_pk_mul_f32 v[174:175], v[146:147], v[164:165] op_sel_hi:[1,0]
	v_pk_fma_f32 v[146:147], v[166:167], v[148:149], v[170:171]
	v_med3_f32 v148, v146, s74, v212
	v_med3_f32 v149, v147, s74, v212
	v_cvt_pk_fp8_f32 v178, v148, v149
	v_pk_fma_f32 v[148:149], v[168:169], v[174:175], v[172:173]
	ds_read_b128 v[170:173], v187
	ds_read_b128 v[174:177], v188
	v_med3_f32 v166, v148, s74, v212
	v_med3_f32 v167, v149, s74, v212
	v_cvt_pk_fp8_f32 v178, v166, v167 op_sel:[0,0,1]
	v_lshl_add_u64 v[166:167], v[66:67], 0, s[14:15]
	s_add_u32 s52, s26, s52
	global_store_dword v[166:167], v178, off
	v_pk_mul_f32 v[166:167], v[6:7], v[158:159] op_sel_hi:[1,0]
	s_waitcnt lgkmcnt(0)
	v_pk_fma_f32 v[6:7], v[170:171], v[8:9], v[174:175]
	s_addc_u32 s53, s27, s53
	v_med3_f32 v8, v6, s74, v212
	v_med3_f32 v9, v7, s74, v212
	v_cvt_pk_fp8_f32 v168, v8, v9
	v_pk_fma_f32 v[8:9], v[172:173], v[166:167], v[176:177]
	v_pk_fma_f32 v[134:135], v[170:171], v[134:135], v[174:175]
	v_med3_f32 v166, v8, s74, v212
	v_med3_f32 v167, v9, s74, v212
	v_cvt_pk_fp8_f32 v168, v166, v167 op_sel:[0,0,1]
	v_lshl_add_u64 v[166:167], s[2:3], 0, v[52:53]
	s_add_u32 s16, s26, s16
	s_addc_u32 s17, s27, s17
	global_store_dword v[166:167], v168, off
	v_pk_mul_f32 v[166:167], v[142:143], v[160:161] op_sel_hi:[1,0]
	v_pk_fma_f32 v[142:143], v[170:171], v[144:145], v[174:175]
	v_med3_f32 v144, v142, s74, v212
	v_med3_f32 v145, v143, s74, v212
	v_cvt_pk_fp8_f32 v168, v144, v145
	v_pk_fma_f32 v[144:145], v[172:173], v[166:167], v[176:177]
	v_pk_fma_f32 v[170:171], v[170:171], v[120:121], v[174:175]
	v_med3_f32 v166, v144, s74, v212
	v_med3_f32 v167, v145, s74, v212
	v_cvt_pk_fp8_f32 v168, v166, v167 op_sel:[0,0,1]
	v_lshl_add_u64 v[166:167], s[52:53], 0, v[52:53]
	v_med3_f32 v120, v170, s74, v212
	v_med3_f32 v121, v171, s74, v212
	global_store_dword v[166:167], v168, off
	v_med3_f32 v166, v134, s74, v212
	v_med3_f32 v167, v135, s74, v212
	v_cvt_pk_fp8_f32 v168, v166, v167
	v_pk_fma_f32 v[166:167], v[172:173], v[136:137], v[176:177]
	v_pk_fma_f32 v[174:175], v[172:173], v[132:133], v[176:177]
	v_med3_f32 v136, v166, s74, v212
	v_med3_f32 v137, v167, s74, v212
	v_cvt_pk_fp8_f32 v168, v136, v137 op_sel:[0,0,1]
	v_lshl_add_u64 v[136:137], s[16:17], 0, v[52:53]
	s_add_u32 s56, s26, s14
	global_store_dword v[136:137], v168, off
	ds_read_b128 v[176:179], v189
	ds_read_b128 v[220:223], v190
	v_cvt_pk_fp8_f32 v136, v120, v121
	v_med3_f32 v120, v174, s74, v212
	v_med3_f32 v121, v175, s74, v212
	s_addc_u32 s57, s27, s15
	v_cvt_pk_fp8_f32 v136, v120, v121 op_sel:[0,0,1]
	v_pk_mul_f32 v[120:121], v[18:19], v[158:159] op_sel_hi:[1,0]
	s_waitcnt lgkmcnt(0)
; #define LAS __attribute__((address_space(3)))
; __global__ void __launch_bounds__(NWAVES * 64, 2) fwd_kernel(Args args) {
;     ...
; #pragma unroll
;             for (int j = 0; j < 8; ++j) { const int k = 4 * lane + 256 * j; const f32x4 Aj = *(const LAS f32x4*)(PVA + k), sh = *(const LAS f32x4*)(PVS + k);
; #pragma unroll
;                 for (int rr = 0; rr < 4; ++rr) { const int row = R0 + 4 * wave + rr; v[rr][j] = v[rr][j] * rstd[rr] * Aj + sh;
;                     *(unsigned*)(XN8 + (size_t)row * D + k) = pk4_fp8(v[rr][j][0], v[rr][j][1], v[rr][j][2], v[rr][j][3]); } }
	v_pk_fma_f32 v[18:19], v[176:177], v[20:21], v[220:221]
	v_pk_mul_f32 v[112:113], v[112:113], v[162:163] op_sel_hi:[1,0]
	v_med3_f32 v20, v18, s74, v212
	v_med3_f32 v21, v19, s74, v212
	v_cvt_pk_fp8_f32 v132, v20, v21
	v_pk_fma_f32 v[20:21], v[178:179], v[120:121], v[222:223]
	v_med3_f32 v120, v20, s74, v212
	v_med3_f32 v121, v21, s74, v212
	v_cvt_pk_fp8_f32 v132, v120, v121 op_sel:[0,0,1]
	v_lshl_add_u64 v[120:121], s[56:57], 0, v[52:53]
	global_store_dword v[120:121], v136, off
	v_lshl_add_u64 v[120:121], s[2:3], 0, v[54:55]
	global_store_dword v[120:121], v132, off
	v_pk_mul_f32 v[120:121], v[102:103], v[160:161] op_sel_hi:[1,0]
	v_pk_fma_f32 v[102:103], v[176:177], v[110:111], v[220:221]
	v_med3_f32 v110, v102, s74, v212
	v_med3_f32 v111, v103, s74, v212
	v_cvt_pk_fp8_f32 v132, v110, v111
	v_pk_fma_f32 v[110:111], v[178:179], v[120:121], v[222:223]
	v_pk_mul_f32 v[32:33], v[32:33], v[164:165] op_sel_hi:[1,0]
	v_med3_f32 v120, v110, s74, v212
	v_med3_f32 v121, v111, s74, v212
	v_cvt_pk_fp8_f32 v132, v120, v121 op_sel:[0,0,1]
	v_pk_mul_f32 v[120:121], v[108:109], v[162:163] op_sel_hi:[1,0]
	v_pk_fma_f32 v[108:109], v[176:177], v[112:113], v[220:221]
	v_pk_mul_f32 v[90:91], v[90:91], v[160:161] op_sel_hi:[1,0]
	v_med3_f32 v112, v108, s74, v212
	v_med3_f32 v113, v109, s74, v212
	v_cvt_pk_fp8_f32 v133, v112, v113
	v_pk_fma_f32 v[112:113], v[178:179], v[120:121], v[222:223]
	v_pk_mul_f32 v[24:25], v[24:25], v[160:161] op_sel_hi:[1,0]
	v_med3_f32 v120, v112, s74, v212
	v_med3_f32 v121, v113, s74, v212
	v_cvt_pk_fp8_f32 v133, v120, v121 op_sel:[0,0,1]
	v_lshl_add_u64 v[120:121], s[52:53], 0, v[54:55]
	global_store_dword v[120:121], v132, off
	v_lshl_add_u64 v[120:121], s[16:17], 0, v[54:55]
	global_store_dword v[120:121], v133, off
	v_pk_mul_f32 v[120:121], v[106:107], v[164:165] op_sel_hi:[1,0]
	v_pk_fma_f32 v[106:107], v[178:179], v[32:33], v[222:223]
	v_pk_fma_f32 v[120:121], v[176:177], v[120:121], v[220:221]
	v_med3_f32 v32, v120, s74, v212
	v_med3_f32 v33, v121, s74, v212
	v_cvt_pk_fp8_f32 v133, v32, v33
	ds_read_b128 v[178:181], v191
	ds_read_b128 v[220:223], v192
	v_med3_f32 v132, v106, s74, v212
	v_med3_f32 v32, v107, s74, v212
	v_cvt_pk_fp8_f32 v133, v132, v32 op_sel:[0,0,1]
	v_pk_mul_f32 v[32:33], v[104:105], v[158:159] op_sel_hi:[1,0]
	v_pk_mul_f32 v[104:105], v[30:31], v[158:159] op_sel_hi:[1,0]
	s_waitcnt lgkmcnt(0)
	v_pk_fma_f32 v[30:31], v[178:179], v[32:33], v[220:221]
	v_med3_f32 v32, v30, s74, v212
	v_med3_f32 v33, v31, s74, v212
	v_cvt_pk_fp8_f32 v132, v32, v33
	v_pk_fma_f32 v[32:33], v[180:181], v[104:105], v[222:223]
	v_pk_fma_f32 v[136:137], v[180:181], v[24:25], v[222:223]
	v_med3_f32 v104, v32, s74, v212
	v_med3_f32 v105, v33, s74, v212
	v_cvt_pk_fp8_f32 v132, v104, v105 op_sel:[0,0,1]
	v_lshl_add_u64 v[104:105], s[56:57], 0, v[54:55]
	global_store_dword v[104:105], v133, off
	v_lshl_add_u64 v[104:105], s[2:3], 0, v[56:57]
	global_store_dword v[104:105], v132, off
	v_pk_fma_f32 v[132:133], v[178:179], v[90:91], v[220:221]
	v_med3_f32 v90, v132, s74, v212
	v_med3_f32 v91, v133, s74, v212
	v_cvt_pk_fp8_f32 v104, v90, v91
	v_med3_f32 v24, v136, s74, v212
	v_med3_f32 v25, v137, s74, v212
	v_cvt_pk_fp8_f32 v104, v24, v25 op_sel:[0,0,1]
	v_pk_mul_f32 v[24:25], v[96:97], v[162:163] op_sel_hi:[1,0]
	v_pk_mul_f32 v[36:37], v[36:37], v[162:163] op_sel_hi:[1,0]
	v_pk_fma_f32 v[168:169], v[178:179], v[24:25], v[220:221]
	v_pk_fma_f32 v[172:173], v[180:181], v[36:37], v[222:223]
	v_med3_f32 v24, v168, s74, v212
	v_med3_f32 v25, v169, s74, v212
	v_cvt_pk_fp8_f32 v90, v24, v25
	v_med3_f32 v24, v172, s74, v212
	v_med3_f32 v25, v173, s74, v212
	v_pk_mul_f32 v[22:23], v[22:23], v[164:165] op_sel_hi:[1,0]
	v_cvt_pk_fp8_f32 v90, v24, v25 op_sel:[0,0,1]
	v_lshl_add_u64 v[24:25], s[52:53], 0, v[56:57]
	global_store_dword v[24:25], v104, off
	v_lshl_add_u64 v[24:25], s[16:17], 0, v[56:57]
	global_store_dword v[24:25], v90, off
	v_pk_mul_f32 v[24:25], v[34:35], v[164:165] op_sel_hi:[1,0]
	v_pk_fma_f32 v[176:177], v[180:181], v[22:23], v[222:223]
	v_pk_fma_f32 v[178:179], v[178:179], v[24:25], v[220:221]
	v_med3_f32 v22, v178, s74, v212
	v_med3_f32 v23, v179, s74, v212
	v_cvt_pk_fp8_f32 v96, v22, v23
	ds_read_b128 v[34:37], v193
	ds_read_b128 v[220:223], v195
	v_med3_f32 v24, v176, s74, v212
	v_med3_f32 v22, v177, s74, v212
	v_cvt_pk_fp8_f32 v96, v24, v22 op_sel:[0,0,1]
	v_pk_mul_f32 v[22:23], v[126:127], v[158:159] op_sel_hi:[1,0]
	s_waitcnt lgkmcnt(0)
	v_pk_fma_f32 v[22:23], v[34:35], v[22:23], v[220:221]
	v_pk_mul_f32 v[24:25], v[124:125], v[158:159] op_sel_hi:[1,0]
	v_med3_f32 v90, v22, s74, v212
	v_med3_f32 v91, v23, s74, v212
	v_cvt_pk_fp8_f32 v97, v90, v91
	v_pk_fma_f32 v[24:25], v[36:37], v[24:25], v[222:223]
	v_med3_f32 v90, v24, s74, v212
	v_med3_f32 v91, v25, s74, v212
	v_cvt_pk_fp8_f32 v97, v90, v91 op_sel:[0,0,1]
	v_lshl_add_u64 v[90:91], s[56:57], 0, v[56:57]
	global_store_dword v[90:91], v96, off
	v_lshl_add_u64 v[90:91], s[2:3], 0, v[58:59]
	global_store_dword v[90:91], v97, off
	v_pk_mul_f32 v[90:91], v[100:101], v[160:161] op_sel_hi:[1,0]
	v_pk_mul_f32 v[94:95], v[94:95], v[160:161] op_sel_hi:[1,0]
	v_pk_fma_f32 v[90:91], v[34:35], v[90:91], v[220:221]
	v_pk_fma_f32 v[94:95], v[36:37], v[94:95], v[222:223]
	v_med3_f32 v96, v90, s74, v212
	v_med3_f32 v97, v91, s74, v212
	v_cvt_pk_fp8_f32 v124, v96, v97
	v_med3_f32 v96, v94, s74, v212
	v_med3_f32 v97, v95, s74, v212
	v_pk_mul_f32 v[100:101], v[114:115], v[162:163] op_sel_hi:[1,0]
	v_cvt_pk_fp8_f32 v124, v96, v97 op_sel:[0,0,1]
	v_pk_mul_f32 v[96:97], v[116:117], v[162:163] op_sel_hi:[1,0]
	v_pk_fma_f32 v[96:97], v[34:35], v[96:97], v[220:221]
	v_pk_fma_f32 v[100:101], v[36:37], v[100:101], v[222:223]
	v_med3_f32 v104, v96, s74, v212
	v_med3_f32 v105, v97, s74, v212
	v_cvt_pk_fp8_f32 v114, v104, v105
	v_med3_f32 v104, v100, s74, v212
	v_med3_f32 v105, v101, s74, v212
	v_pk_mul_f32 v[116:117], v[128:129], v[164:165] op_sel_hi:[1,0]
	v_cvt_pk_fp8_f32 v114, v104, v105 op_sel:[0,0,1]
	v_lshl_add_u64 v[104:105], s[52:53], 0, v[58:59]
	global_store_dword v[104:105], v124, off
	v_lshl_add_u64 v[104:105], s[16:17], 0, v[58:59]
	global_store_dword v[104:105], v114, off
	v_pk_mul_f32 v[104:105], v[130:131], v[164:165] op_sel_hi:[1,0]
	v_pk_fma_f32 v[124:125], v[36:37], v[116:117], v[222:223]
	v_pk_fma_f32 v[114:115], v[34:35], v[104:105], v[220:221]
	v_med3_f32 v34, v114, s74, v212
	v_med3_f32 v35, v115, s74, v212
	v_cvt_pk_fp8_f32 v104, v34, v35
	v_med3_f32 v34, v124, s74, v212
	v_med3_f32 v35, v125, s74, v212
	ds_read_b128 v[220:223], v196
	ds_read_b128 v[224:227], v197
	v_cvt_pk_fp8_f32 v104, v34, v35 op_sel:[0,0,1]
	v_lshl_add_u64 v[34:35], s[56:57], 0, v[58:59]
	v_pk_mul_f32 v[36:37], v[138:139], v[158:159] op_sel_hi:[1,0]
	global_store_dword v[34:35], v104, off
	v_pk_mul_f32 v[34:35], v[140:141], v[158:159] op_sel_hi:[1,0]
	s_waitcnt lgkmcnt(0)
; #define LAS __attribute__((address_space(3)))
; __global__ void __launch_bounds__(NWAVES * 64, 2) fwd_kernel(Args args) {
;     ...
; #pragma unroll
;             for (int j = 0; j < 8; ++j) { const int k = 4 * lane + 256 * j; const f32x4 Aj = *(const LAS f32x4*)(PVA + k), sh = *(const LAS f32x4*)(PVS + k);
; #pragma unroll
;                 for (int rr = 0; rr < 4; ++rr) { const int row = R0 + 4 * wave + rr; v[rr][j] = v[rr][j] * rstd[rr] * Aj + sh;
;                     *(unsigned*)(XN8 + (size_t)row * D + k) = pk4_fp8(v[rr][j][0], v[rr][j][1], v[rr][j][2], v[rr][j][3]); } }
	v_pk_fma_f32 v[36:37], v[222:223], v[36:37], v[226:227]
	v_pk_fma_f32 v[34:35], v[220:221], v[34:35], v[224:225]
	v_pk_mul_f32 v[116:117], v[118:119], v[160:161] op_sel_hi:[1,0]
	v_med3_f32 v104, v34, s74, v212
	v_med3_f32 v105, v35, s74, v212
	v_cvt_pk_fp8_f32 v130, v104, v105
	v_med3_f32 v104, v36, s74, v212
	v_med3_f32 v105, v37, s74, v212
	v_cvt_pk_fp8_f32 v130, v104, v105 op_sel:[0,0,1]
	v_pk_mul_f32 v[104:105], v[122:123], v[160:161] op_sel_hi:[1,0]
	v_pk_fma_f32 v[128:129], v[222:223], v[116:117], v[226:227]
	v_pk_fma_f32 v[126:127], v[220:221], v[104:105], v[224:225]
	v_pk_mul_f32 v[98:99], v[98:99], v[162:163] op_sel_hi:[1,0]
	v_med3_f32 v104, v126, s74, v212
	v_med3_f32 v105, v127, s74, v212
	v_cvt_pk_fp8_f32 v118, v104, v105
	v_med3_f32 v104, v128, s74, v212
	v_med3_f32 v105, v129, s74, v212
	v_pk_mul_f32 v[92:93], v[92:93], v[162:163] op_sel_hi:[1,0]
	v_cvt_pk_fp8_f32 v118, v104, v105 op_sel:[0,0,1]
	v_lshl_add_u64 v[104:105], s[2:3], 0, v[60:61]
	global_store_dword v[104:105], v130, off
	v_lshl_add_u64 v[104:105], s[52:53], 0, v[60:61]
	v_pk_fma_f32 v[130:131], v[220:221], v[98:99], v[224:225]
	global_store_dword v[104:105], v118, off
	v_med3_f32 v98, v130, s74, v212
	v_med3_f32 v99, v131, s74, v212
	v_cvt_pk_fp8_f32 v104, v98, v99
	v_pk_fma_f32 v[138:139], v[222:223], v[92:93], v[226:227]
	v_pk_mul_f32 v[28:29], v[28:29], v[164:165] op_sel_hi:[1,0]
	v_med3_f32 v92, v138, s74, v212
	v_med3_f32 v93, v139, s74, v212
	v_pk_fma_f32 v[140:141], v[220:221], v[28:29], v[224:225]
	v_cvt_pk_fp8_f32 v104, v92, v93 op_sel:[0,0,1]
	v_med3_f32 v28, v140, s74, v212
	v_med3_f32 v29, v141, s74, v212
	v_cvt_pk_fp8_f32 v92, v28, v29
	v_pk_mul_f32 v[26:27], v[26:27], v[164:165] op_sel_hi:[1,0]
	v_mov_b32_e32 v29, v84
	v_pk_fma_f32 v[180:181], v[222:223], v[26:27], v[226:227]
	v_med3_f32 v26, v180, s74, v212
	v_med3_f32 v27, v181, s74, v212
	v_cvt_pk_fp8_f32 v92, v26, v27 op_sel:[0,0,1]
	v_lshl_add_u64 v[26:27], s[16:17], 0, v[60:61]
	global_store_dword v[26:27], v104, off
	v_lshl_add_u64 v[26:27], s[56:57], 0, v[60:61]
	global_store_dword v[26:27], v92, off
	ds_read_b128 v[220:223], v198
	ds_read_b128 v[224:227], v199
	v_mov_b32_e32 v26, v40
	v_mov_b32_e32 v27, v38
	v_pk_mul_f32 v[26:27], v[26:27], v[158:159] op_sel_hi:[1,0]
	v_mov_b32_e32 v28, v86
	s_waitcnt lgkmcnt(0)
	v_pk_fma_f32 v[26:27], v[220:221], v[26:27], v[224:225]
	v_pk_mul_f32 v[28:29], v[28:29], v[158:159] op_sel_hi:[1,0]
	v_med3_f32 v38, v26, s74, v212
	v_med3_f32 v40, v27, s74, v212
	v_cvt_pk_fp8_f32 v84, v38, v40
	v_mov_b32_e32 v92, v78
	v_mov_b32_e32 v93, v76
	v_pk_fma_f32 v[28:29], v[222:223], v[28:29], v[226:227]
	v_pk_mul_f32 v[92:93], v[92:93], v[160:161] op_sel_hi:[1,0]
	v_med3_f32 v38, v28, s74, v212
	v_med3_f32 v40, v29, s74, v212
	v_pk_fma_f32 v[92:93], v[220:221], v[92:93], v[224:225]
	v_cvt_pk_fp8_f32 v84, v38, v40 op_sel:[0,0,1]
	v_med3_f32 v38, v92, s74, v212
	v_med3_f32 v40, v93, s74, v212
	v_mov_b32_e32 v98, v82
	v_mov_b32_e32 v99, v80
	v_cvt_pk_fp8_f32 v76, v38, v40
	v_pk_mul_f32 v[98:99], v[98:99], v[160:161] op_sel_hi:[1,0]
	v_lshl_add_u64 v[104:105], s[2:3], 0, v[62:63]
	v_pk_fma_f32 v[98:99], v[222:223], v[98:99], v[226:227]
	global_store_dword v[104:105], v84, off
	v_med3_f32 v38, v98, s74, v212
	v_med3_f32 v40, v99, s74, v212
	v_cvt_pk_fp8_f32 v76, v38, v40 op_sel:[0,0,1]
	v_lshl_add_u64 v[104:105], s[52:53], 0, v[62:63]
	v_mov_b32_e32 v118, v10
	v_mov_b32_e32 v119, v12
	global_store_dword v[104:105], v76, off
	v_mov_b32_e32 v104, v70
	v_mov_b32_e32 v105, v16
	v_pk_mul_f32 v[104:105], v[104:105], v[162:163] op_sel_hi:[1,0]
	v_pk_mul_f32 v[118:119], v[118:119], v[164:165] op_sel_hi:[1,0]
	v_pk_fma_f32 v[104:105], v[220:221], v[104:105], v[224:225]
	v_med3_f32 v16, v104, s74, v212
	v_med3_f32 v38, v105, s74, v212
	v_pk_fma_f32 v[118:119], v[220:221], v[118:119], v[224:225]
	v_mov_b32_e32 v116, v74
	v_mov_b32_e32 v117, v72
	v_cvt_pk_fp8_f32 v40, v16, v38
	v_mov_b32_e32 v122, v14
	v_med3_f32 v10, v118, s74, v212
	v_med3_f32 v12, v119, s74, v212
	v_pk_mul_f32 v[116:117], v[116:117], v[162:163] op_sel_hi:[1,0]
	v_mov_b32_e32 v123, v88
	v_cvt_pk_fp8_f32 v14, v10, v12
	v_pk_fma_f32 v[116:117], v[222:223], v[116:117], v[226:227]
	v_pk_mul_f32 v[122:123], v[122:123], v[164:165] op_sel_hi:[1,0]
	v_med3_f32 v16, v116, s74, v212
	v_med3_f32 v38, v117, s74, v212
	v_pk_fma_f32 v[122:123], v[222:223], v[122:123], v[226:227]
	v_cvt_pk_fp8_f32 v40, v16, v38 op_sel:[0,0,1]
	v_med3_f32 v10, v122, s74, v212
	v_med3_f32 v12, v123, s74, v212
	v_cvt_pk_fp8_f32 v14, v10, v12 op_sel:[0,0,1]
	v_lshl_add_u64 v[220:221], s[16:17], 0, v[62:63]
	global_store_dword v[220:221], v40, off
	v_lshl_add_u64 v[220:221], s[56:57], 0, v[62:63]
	global_store_dword v[220:221], v14, off
	ds_read_b128 v[220:223], v200
	ds_read_b128 v[224:227], v201
	v_mov_b32_e32 v38, v41
	v_pk_mul_f32 v[38:39], v[38:39], v[158:159] op_sel_hi:[1,0]
	v_mov_b32_e32 v84, v87
	s_waitcnt lgkmcnt(0)
; #define LAS __attribute__((address_space(3)))
; #define RB_WAIT() do { asm volatile("s_waitcnt vmcnt(0)" : "+v"(bq[0]), "+v"(bq[1]), "+v"(bq[2]), "+v"(bq[3]), "+v"(bq[4]), "+v"(bq[5]), "+v"(bq[6]), "+v"(bq[7])); \
;                     asm volatile("" : "+v"(bq[8]), "+v"(bq[9]), "+v"(bq[10]), "+v"(bq[11]), "+v"(bq[12]), "+v"(bq[13]), "+v"(bq[14]), "+v"(bq[15])); } while (0)
; __global__ void __launch_bounds__(NWAVES * 64, 2) fwd_kernel(Args args) {
;     ...
; #pragma unroll
;             for (int j = 0; j < 8; ++j) { const int k = 4 * lane + 256 * j; const f32x4 Aj = *(const LAS f32x4*)(PVA + k), sh = *(const LAS f32x4*)(PVS + k);
; #pragma unroll
;                 for (int rr = 0; rr < 4; ++rr) { const int row = R0 + 4 * wave + rr; v[rr][j] = v[rr][j] * rstd[rr] * Aj + sh;
;                     *(unsigned*)(XN8 + (size_t)row * D + k) = pk4_fp8(v[rr][j][0], v[rr][j][1], v[rr][j][2], v[rr][j][3]); } }
;             if (tid < 32) HIST[tid] = 0;
;             f32x16 lacc;
; #pragma unroll
;             for (int j = 0; j < 16; ++j) lacc[j] = 0.f;
; #pragma unroll
;             for (int q = 0; q < 4; ++q) {
;                 float bq[16];
;                 const float* wr0 = w_router + (size_t)(q * 512 + 64 * wave) * NE; const float* wr1 = wr0 + 16 * 2 * NE; const unsigned wvo = (unsigned)((lane >> 5) * NE + (lane & 31)) * 4u;
;     ...
;                 RB_LD16(wr0);
;                 __syncthreads();
; #pragma unroll
;                 for (int rr = 0; rr < 4; ++rr)
; #pragma unroll
;                     for (int jj = 0; jj < 2; ++jj) { const int lk = 4 * lane + 256 * jj; LAS float* hp = HT + (4 * wave + rr) * 513 + lk; const f32x4 q4 = v[rr][2 * q + jj]; hp[0] = q4[0]; hp[1] = q4[1]; hp[2] = q4[2]; hp[3] = q4[3]; }
;                 __syncthreads();
;                 const LAS float* ap = HT + (lane & 31) * 513 + 64 * wave + (lane >> 5);
;                 RB_WAIT();
;                 float bq2[16];
;     ...
;                 RB_LD2(0, 0); RB_LD2(1, 256); RB_LD2(2, 512); RB_LD2(3, 768); RB_LD2(4, 1024); RB_LD2(5, 1280); RB_LD2(6, 1536); RB_LD2(7, 1792);
;                 RB_LD2(8, 2048); RB_LD2(9, 2304); RB_LD2(10, 2560); RB_LD2(11, 2816); RB_LD2(12, 3072); RB_LD2(13, 3328); RB_LD2(14, 3584); RB_LD2(15, 3840);
; #pragma unroll
;                 for (int s = 0; s < 16; ++s) lacc = __builtin_amdgcn_mfma_f32_32x32x2f32(ap[2 * s], bq[s], lacc, 0, 0, 0);
	v_pk_fma_f32 v[38:39], v[220:221], v[38:39], v[224:225]
	v_pk_mul_f32 v[40:41], v[84:85], v[158:159] op_sel_hi:[1,0]
	v_med3_f32 v10, v38, s74, v212
	v_med3_f32 v12, v39, s74, v212
	v_cvt_pk_fp8_f32 v14, v10, v12
	v_mov_b32_e32 v76, v79
	v_pk_fma_f32 v[40:41], v[222:223], v[40:41], v[226:227]
	v_pk_mul_f32 v[76:77], v[76:77], v[160:161] op_sel_hi:[1,0]
	v_med3_f32 v10, v40, s74, v212
	v_med3_f32 v12, v41, s74, v212
	v_pk_fma_f32 v[76:77], v[220:221], v[76:77], v[224:225]
	v_cvt_pk_fp8_f32 v14, v10, v12 op_sel:[0,0,1]
	v_med3_f32 v10, v76, s74, v212
	v_med3_f32 v12, v77, s74, v212
	v_mov_b32_e32 v80, v83
	v_cvt_pk_fp8_f32 v16, v10, v12
	v_pk_mul_f32 v[78:79], v[80:81], v[160:161] op_sel_hi:[1,0]
	v_lshl_add_u64 v[80:81], s[2:3], 0, v[64:65]
	v_pk_fma_f32 v[78:79], v[222:223], v[78:79], v[226:227]
	global_store_dword v[80:81], v14, off
	v_med3_f32 v10, v78, s74, v212
	v_med3_f32 v12, v79, s74, v212
	v_cvt_pk_fp8_f32 v16, v10, v12 op_sel:[0,0,1]
	v_lshl_add_u64 v[80:81], s[52:53], 0, v[64:65]
	v_mov_b32_e32 v72, v75
	global_store_dword v[80:81], v16, off
	v_mov_b32_e32 v16, v71
	v_pk_mul_f32 v[16:17], v[16:17], v[162:163] op_sel_hi:[1,0]
	v_pk_mul_f32 v[72:73], v[72:73], v[162:163] op_sel_hi:[1,0]
	v_pk_fma_f32 v[70:71], v[220:221], v[16:17], v[224:225]
	v_pk_fma_f32 v[72:73], v[222:223], v[72:73], v[226:227]
	v_med3_f32 v10, v70, s74, v212
	v_med3_f32 v12, v71, s74, v212
	v_cvt_pk_fp8_f32 v14, v10, v12
	v_med3_f32 v10, v72, s74, v212
	v_med3_f32 v12, v73, s74, v212
	v_mov_b32_e32 v88, v15
	v_cvt_pk_fp8_f32 v14, v10, v12 op_sel:[0,0,1]
	v_mov_b32_e32 v12, v11
	v_pk_mul_f32 v[10:11], v[12:13], v[164:165] op_sel_hi:[1,0]
	v_pk_fma_f32 v[74:75], v[220:221], v[10:11], v[224:225]
	v_pk_mul_f32 v[12:13], v[88:89], v[164:165] op_sel_hi:[1,0]
	v_med3_f32 v10, v74, s74, v212
	v_med3_f32 v11, v75, s74, v212
	v_cvt_pk_fp8_f32 v15, v10, v11
	v_pk_fma_f32 v[80:81], v[222:223], v[12:13], v[226:227]
	s_nop 0
	v_med3_f32 v10, v80, s74, v212
	v_med3_f32 v11, v81, s74, v212
	v_cvt_pk_fp8_f32 v15, v10, v11 op_sel:[0,0,1]
	v_lshl_add_u64 v[10:11], s[16:17], 0, v[64:65]
	global_store_dword v[10:11], v14, off
	v_lshl_add_u64 v[10:11], s[56:57], 0, v[64:65]
	global_store_dword v[10:11], v15, off
	s_and_saveexec_b64 s[2:3], s[4:5]
	ds_write_b32 v161, v43
	s_or_b64 exec, exec, s[2:3]
	v_add_u32_e32 v87, 0x1408, v206
	global_load_dword v10, v165, s[18:19] offset:0
	global_load_dword v158, v165, s[18:19] offset:256
	global_load_dword v160, v165, s[18:19] offset:512
	global_load_dword v162, v165, s[18:19] offset:768
	global_load_dword v164, v165, s[18:19] offset:1024
	global_load_dword v220, v165, s[18:19] offset:1280
	global_load_dword v221, v165, s[18:19] offset:1536
	global_load_dword v222, v165, s[18:19] offset:1792
	global_load_dword v223, v165, s[18:19] offset:2048
	global_load_dword v224, v165, s[18:19] offset:2304
	global_load_dword v225, v165, s[18:19] offset:2560
	global_load_dword v226, v165, s[18:19] offset:2816
	global_load_dword v227, v165, s[18:19] offset:3072
	global_load_dword v228, v165, s[18:19] offset:3328
	global_load_dword v229, v165, s[18:19] offset:3584
	global_load_dword v230, v165, s[18:19] offset:3840
	s_waitcnt lgkmcnt(0)
	s_barrier
	ds_write_b128 v206, v[2:5]
	ds_write_b128 v206, v[6:9] offset:1024
	v_add_u32_e32 v82, 0x804, v206
	v_add_u32_e32 v83, 0x80c, v206
	v_add_u32_e32 v84, 0xc04, v206
	v_add_u32_e32 v85, 0xc0c, v206
	v_add_u32_e32 v86, 0x1008, v206
	ds_write2_b64 v87, v[134:135], v[166:167] offset1:1
	v_add_u32_e32 v88, 0x180c, v206
	v_add_u32_e32 v89, 0x1814, v206
	v_add_u32_e32 v134, 0x1c0c, v206
	v_add_u32_e32 v135, 0x1c14, v206
	ds_write2_b32 v82, v154, v155 offset1:1
	ds_write2_b32 v83, v156, v157 offset1:1
	ds_write2_b32 v84, v142, v143 offset1:1
	ds_write2_b32 v85, v144, v145 offset1:1
	ds_write2_b64 v86, v[150:151], v[152:153] offset1:1
	ds_write2_b32 v88, v146, v147 offset1:1
	ds_write2_b32 v89, v148, v149 offset1:1
	ds_write2_b32 v134, v170, v171 offset1:1
	ds_write2_b32 v135, v174, v175 offset1:1
	s_waitcnt lgkmcnt(0)
	s_barrier
	s_waitcnt vmcnt(0)
	global_load_dword v144, v165, s[30:31] offset:0
	global_load_dword v145, v165, s[30:31] offset:256
	global_load_dword v146, v165, s[30:31] offset:512
	global_load_dword v147, v165, s[30:31] offset:768
	global_load_dword v148, v165, s[30:31] offset:1024
	global_load_dword v149, v165, s[30:31] offset:1280
	global_load_dword v150, v165, s[30:31] offset:1536
	global_load_dword v151, v165, s[30:31] offset:1792
	global_load_dword v152, v165, s[30:31] offset:2048
	global_load_dword v153, v165, s[30:31] offset:2304
	global_load_dword v154, v165, s[30:31] offset:2560
	global_load_dword v155, v165, s[30:31] offset:2816
	global_load_dword v156, v165, s[30:31] offset:3072
	global_load_dword v157, v165, s[30:31] offset:3328
	global_load_dword v166, v165, s[30:31] offset:3584
	global_load_dword v167, v165, s[30:31] offset:3840
	ds_read2_b32 v[142:143], v182 offset1:2
	s_waitcnt lgkmcnt(0)
	v_mfma_f32_32x32x2_f32 v[2:17], v142, v10, 0
	v_mfma_f32_32x32x2_f32 v[2:17], v143, v158, v[2:17]
	ds_read2_b32 v[142:143], v182 offset0:4 offset1:6
	s_waitcnt lgkmcnt(0)
	v_mfma_f32_32x32x2_f32 v[2:17], v142, v160, v[2:17]
	v_mfma_f32_32x32x2_f32 v[2:17], v143, v162, v[2:17]
	ds_read2_b32 v[142:143], v182 offset0:8 offset1:10
	s_waitcnt lgkmcnt(0)
	v_mfma_f32_32x32x2_f32 v[2:17], v142, v164, v[2:17]
	v_mfma_f32_32x32x2_f32 v[2:17], v143, v220, v[2:17]
	ds_read2_b32 v[142:143], v182 offset0:12 offset1:14
	s_waitcnt lgkmcnt(0)
	v_mfma_f32_32x32x2_f32 v[2:17], v142, v221, v[2:17]
	v_mfma_f32_32x32x2_f32 v[2:17], v143, v222, v[2:17]
	ds_read2_b32 v[142:143], v182 offset0:16 offset1:18
	s_waitcnt lgkmcnt(0)
; #define LAS __attribute__((address_space(3)))
; #define RB_WAIT() do { asm volatile("s_waitcnt vmcnt(0)" : "+v"(bq[0]), "+v"(bq[1]), "+v"(bq[2]), "+v"(bq[3]), "+v"(bq[4]), "+v"(bq[5]), "+v"(bq[6]), "+v"(bq[7])); \
;                     asm volatile("" : "+v"(bq[8]), "+v"(bq[9]), "+v"(bq[10]), "+v"(bq[11]), "+v"(bq[12]), "+v"(bq[13]), "+v"(bq[14]), "+v"(bq[15])); } while (0)
; #define RB_LD2(i_, off_) asm volatile("global_load_dword %0, %1, %2 offset:" #off_ : "=v"(bq2[i_]) : "v"(wvo), "s"(wr1))
; __global__ void __launch_bounds__(NWAVES * 64, 2) fwd_kernel(Args args) {
;     ...
;             for (int q = 0; q < 4; ++q) {
;                 float bq[16];
;                 const float* wr0 = w_router + (size_t)(q * 512 + 64 * wave) * NE; const float* wr1 = wr0 + 16 * 2 * NE; const unsigned wvo = (unsigned)((lane >> 5) * NE + (lane & 31)) * 4u;
;     ...
;                 RB_LD16(wr0);
;                 __syncthreads();
; #pragma unroll
;                 for (int rr = 0; rr < 4; ++rr)
; #pragma unroll
;                     for (int jj = 0; jj < 2; ++jj) { const int lk = 4 * lane + 256 * jj; LAS float* hp = HT + (4 * wave + rr) * 513 + lk; const f32x4 q4 = v[rr][2 * q + jj]; hp[0] = q4[0]; hp[1] = q4[1]; hp[2] = q4[2]; hp[3] = q4[3]; }
;                 __syncthreads();
;                 const LAS float* ap = HT + (lane & 31) * 513 + 64 * wave + (lane >> 5);
;                 RB_WAIT();
;                 float bq2[16];
;     ...
;                 RB_LD2(0, 0); RB_LD2(1, 256); RB_LD2(2, 512); RB_LD2(3, 768); RB_LD2(4, 1024); RB_LD2(5, 1280); RB_LD2(6, 1536); RB_LD2(7, 1792);
;                 RB_LD2(8, 2048); RB_LD2(9, 2304); RB_LD2(10, 2560); RB_LD2(11, 2816); RB_LD2(12, 3072); RB_LD2(13, 3328); RB_LD2(14, 3584); RB_LD2(15, 3840);
; #pragma unroll
;                 for (int s = 0; s < 16; ++s) lacc = __builtin_amdgcn_mfma_f32_32x32x2f32(ap[2 * s], bq[s], lacc, 0, 0, 0);
;                 asm volatile("" : "+v"(lacc));
;                 asm volatile("s_waitcnt vmcnt(0)" : "+v"(bq2[0]), "+v"(bq2[1]), "+v"(bq2[2]), "+v"(bq2[3]), "+v"(bq2[4]), "+v"(bq2[5]), "+v"(bq2[6]), "+v"(bq2[7]));
;                 asm volatile("" : "+v"(bq2[8]), "+v"(bq2[9]), "+v"(bq2[10]), "+v"(bq2[11]), "+v"(bq2[12]), "+v"(bq2[13]), "+v"(bq2[14]), "+v"(bq2[15]));
; #pragma unroll
;                 for (int s = 0; s < 16; ++s) lacc = __builtin_amdgcn_mfma_f32_32x32x2f32(ap[32 + 2 * s], bq2[s], lacc, 0, 0, 0);
	v_mfma_f32_32x32x2_f32 v[2:17], v142, v223, v[2:17]
	v_mfma_f32_32x32x2_f32 v[2:17], v143, v224, v[2:17]
	ds_read2_b32 v[142:143], v182 offset0:20 offset1:22
	s_waitcnt lgkmcnt(0)
	v_mfma_f32_32x32x2_f32 v[2:17], v142, v225, v[2:17]
	v_mfma_f32_32x32x2_f32 v[2:17], v143, v226, v[2:17]
	ds_read2_b32 v[142:143], v182 offset0:24 offset1:26
	s_waitcnt lgkmcnt(0)
	v_mfma_f32_32x32x2_f32 v[2:17], v142, v227, v[2:17]
	v_mfma_f32_32x32x2_f32 v[2:17], v143, v228, v[2:17]
	ds_read2_b32 v[142:143], v182 offset0:28 offset1:30
	s_waitcnt lgkmcnt(0)
	v_mfma_f32_32x32x2_f32 v[2:17], v142, v229, v[2:17]
	v_mfma_f32_32x32x2_f32 v[2:17], v143, v230, v[2:17]
	s_waitcnt vmcnt(0)
	ds_read2_b32 v[142:143], v182 offset0:32 offset1:34
	s_waitcnt lgkmcnt(0)
	v_mfma_f32_32x32x2_f32 v[2:17], v142, v144, v[2:17]
	v_mfma_f32_32x32x2_f32 v[2:17], v143, v145, v[2:17]
	ds_read2_b32 v[142:143], v182 offset0:36 offset1:38
	s_waitcnt lgkmcnt(0)
	v_mfma_f32_32x32x2_f32 v[2:17], v142, v146, v[2:17]
	v_mfma_f32_32x32x2_f32 v[2:17], v143, v147, v[2:17]
	ds_read2_b32 v[142:143], v182 offset0:40 offset1:42
	s_waitcnt lgkmcnt(0)
	v_mfma_f32_32x32x2_f32 v[2:17], v142, v148, v[2:17]
	v_mfma_f32_32x32x2_f32 v[2:17], v143, v149, v[2:17]
	ds_read2_b32 v[142:143], v182 offset0:44 offset1:46
	s_waitcnt lgkmcnt(0)
	v_mfma_f32_32x32x2_f32 v[2:17], v142, v150, v[2:17]
	v_mfma_f32_32x32x2_f32 v[2:17], v143, v151, v[2:17]
	ds_read2_b32 v[142:143], v182 offset0:48 offset1:50
	s_waitcnt lgkmcnt(0)
	v_mfma_f32_32x32x2_f32 v[2:17], v142, v152, v[2:17]
	v_mfma_f32_32x32x2_f32 v[2:17], v143, v153, v[2:17]
	ds_read2_b32 v[142:143], v182 offset0:52 offset1:54
	s_waitcnt lgkmcnt(0)
	v_mfma_f32_32x32x2_f32 v[2:17], v142, v154, v[2:17]
	v_mfma_f32_32x32x2_f32 v[2:17], v143, v155, v[2:17]
	ds_read2_b32 v[142:143], v182 offset0:56 offset1:58
	s_waitcnt lgkmcnt(0)
	v_mfma_f32_32x32x2_f32 v[2:17], v142, v156, v[2:17]
	v_mfma_f32_32x32x2_f32 v[2:17], v143, v157, v[2:17]
	ds_read2_b32 v[142:143], v182 offset0:60 offset1:62
	s_waitcnt lgkmcnt(0)
	v_mfma_f32_32x32x2_f32 v[2:17], v142, v166, v[2:17]
	v_mfma_f32_32x32x2_f32 v[2:17], v143, v167, v[2:17]
	global_load_dword v142, v165, s[36:37] offset:0
	global_load_dword v143, v165, s[36:37] offset:256
	global_load_dword v144, v165, s[36:37] offset:512
	global_load_dword v145, v165, s[36:37] offset:768
	global_load_dword v146, v165, s[36:37] offset:1024
	global_load_dword v147, v165, s[36:37] offset:1280
	global_load_dword v148, v165, s[36:37] offset:1536
	global_load_dword v149, v165, s[36:37] offset:1792
	global_load_dword v150, v165, s[36:37] offset:2048
	global_load_dword v151, v165, s[36:37] offset:2304
	global_load_dword v152, v165, s[36:37] offset:2560
	global_load_dword v153, v165, s[36:37] offset:2816
	global_load_dword v154, v165, s[36:37] offset:3072
	global_load_dword v155, v165, s[36:37] offset:3328
	global_load_dword v156, v165, s[36:37] offset:3584
	global_load_dword v157, v165, s[36:37] offset:3840
	s_barrier
	ds_write_b128 v206, v[18:21]
	ds_write_b128 v206, v[30:33] offset:1024
	ds_write2_b32 v82, v102, v103 offset1:1
	ds_write2_b32 v83, v110, v111 offset1:1
	ds_write2_b32 v84, v132, v133 offset1:1
	ds_write2_b32 v85, v136, v137 offset1:1
	ds_write2_b64 v86, v[108:109], v[112:113] offset1:1
	ds_write2_b64 v87, v[168:169], v[172:173] offset1:1
	ds_write2_b32 v88, v120, v121 offset1:1
	ds_write2_b32 v89, v106, v107 offset1:1
	ds_write2_b32 v134, v178, v179 offset1:1
	ds_write2_b32 v135, v176, v177 offset1:1
	s_waitcnt lgkmcnt(0)
	s_barrier
	s_waitcnt vmcnt(0)
	global_load_dword v20, v165, s[38:39] offset:0
	global_load_dword v21, v165, s[38:39] offset:256
	global_load_dword v30, v165, s[38:39] offset:512
	global_load_dword v31, v165, s[38:39] offset:768
	global_load_dword v32, v165, s[38:39] offset:1024
	global_load_dword v33, v165, s[38:39] offset:1280
	global_load_dword v102, v165, s[38:39] offset:1536
	global_load_dword v103, v165, s[38:39] offset:1792
	global_load_dword v106, v165, s[38:39] offset:2048
	global_load_dword v107, v165, s[38:39] offset:2304
	global_load_dword v108, v165, s[38:39] offset:2560
	global_load_dword v109, v165, s[38:39] offset:2816
	global_load_dword v110, v165, s[38:39] offset:3072
	global_load_dword v111, v165, s[38:39] offset:3328
	global_load_dword v112, v165, s[38:39] offset:3584
	global_load_dword v113, v165, s[38:39] offset:3840
	ds_read2_b32 v[18:19], v182 offset1:2
	s_waitcnt lgkmcnt(0)
	v_mfma_f32_32x32x2_f32 v[2:17], v18, v142, v[2:17]
	v_mfma_f32_32x32x2_f32 v[2:17], v19, v143, v[2:17]
	ds_read2_b32 v[18:19], v182 offset0:4 offset1:6
	s_waitcnt lgkmcnt(0)
	v_mfma_f32_32x32x2_f32 v[2:17], v18, v144, v[2:17]
	v_mfma_f32_32x32x2_f32 v[2:17], v19, v145, v[2:17]
	ds_read2_b32 v[18:19], v182 offset0:8 offset1:10
	s_waitcnt lgkmcnt(0)
	v_mfma_f32_32x32x2_f32 v[2:17], v18, v146, v[2:17]
	v_mfma_f32_32x32x2_f32 v[2:17], v19, v147, v[2:17]
	ds_read2_b32 v[18:19], v182 offset0:12 offset1:14
	s_waitcnt lgkmcnt(0)
	v_mfma_f32_32x32x2_f32 v[2:17], v18, v148, v[2:17]
	v_mfma_f32_32x32x2_f32 v[2:17], v19, v149, v[2:17]
	ds_read2_b32 v[18:19], v182 offset0:16 offset1:18
	s_waitcnt lgkmcnt(0)
	v_mfma_f32_32x32x2_f32 v[2:17], v18, v150, v[2:17]
	v_mfma_f32_32x32x2_f32 v[2:17], v19, v151, v[2:17]
	ds_read2_b32 v[18:19], v182 offset0:20 offset1:22
	s_waitcnt lgkmcnt(0)
	v_mfma_f32_32x32x2_f32 v[2:17], v18, v152, v[2:17]
	v_mfma_f32_32x32x2_f32 v[2:17], v19, v153, v[2:17]
	ds_read2_b32 v[18:19], v182 offset0:24 offset1:26
	s_waitcnt lgkmcnt(0)
	v_mfma_f32_32x32x2_f32 v[2:17], v18, v154, v[2:17]
	v_mfma_f32_32x32x2_f32 v[2:17], v19, v155, v[2:17]
	ds_read2_b32 v[18:19], v182 offset0:28 offset1:30
	s_waitcnt lgkmcnt(0)
; #define LAS __attribute__((address_space(3)))
; #define RB_WAIT() do { asm volatile("s_waitcnt vmcnt(0)" : "+v"(bq[0]), "+v"(bq[1]), "+v"(bq[2]), "+v"(bq[3]), "+v"(bq[4]), "+v"(bq[5]), "+v"(bq[6]), "+v"(bq[7])); \
;                     asm volatile("" : "+v"(bq[8]), "+v"(bq[9]), "+v"(bq[10]), "+v"(bq[11]), "+v"(bq[12]), "+v"(bq[13]), "+v"(bq[14]), "+v"(bq[15])); } while (0)
; #define RB_LD2(i_, off_) asm volatile("global_load_dword %0, %1, %2 offset:" #off_ : "=v"(bq2[i_]) : "v"(wvo), "s"(wr1))
; __global__ void __launch_bounds__(NWAVES * 64, 2) fwd_kernel(Args args) {
;     ...
;             for (int q = 0; q < 4; ++q) {
;                 float bq[16];
;                 const float* wr0 = w_router + (size_t)(q * 512 + 64 * wave) * NE; const float* wr1 = wr0 + 16 * 2 * NE; const unsigned wvo = (unsigned)((lane >> 5) * NE + (lane & 31)) * 4u;
;     ...
;                 RB_LD16(wr0);
;                 __syncthreads();
; #pragma unroll
;                 for (int rr = 0; rr < 4; ++rr)
; #pragma unroll
;                     for (int jj = 0; jj < 2; ++jj) { const int lk = 4 * lane + 256 * jj; LAS float* hp = HT + (4 * wave + rr) * 513 + lk; const f32x4 q4 = v[rr][2 * q + jj]; hp[0] = q4[0]; hp[1] = q4[1]; hp[2] = q4[2]; hp[3] = q4[3]; }
;                 __syncthreads();
;                 const LAS float* ap = HT + (lane & 31) * 513 + 64 * wave + (lane >> 5);
;                 RB_WAIT();
;                 float bq2[16];
;     ...
;                 RB_LD2(0, 0); RB_LD2(1, 256); RB_LD2(2, 512); RB_LD2(3, 768); RB_LD2(4, 1024); RB_LD2(5, 1280); RB_LD2(6, 1536); RB_LD2(7, 1792);
;                 RB_LD2(8, 2048); RB_LD2(9, 2304); RB_LD2(10, 2560); RB_LD2(11, 2816); RB_LD2(12, 3072); RB_LD2(13, 3328); RB_LD2(14, 3584); RB_LD2(15, 3840);
; #pragma unroll
;                 for (int s = 0; s < 16; ++s) lacc = __builtin_amdgcn_mfma_f32_32x32x2f32(ap[2 * s], bq[s], lacc, 0, 0, 0);
;                 asm volatile("" : "+v"(lacc));
;                 asm volatile("s_waitcnt vmcnt(0)" : "+v"(bq2[0]), "+v"(bq2[1]), "+v"(bq2[2]), "+v"(bq2[3]), "+v"(bq2[4]), "+v"(bq2[5]), "+v"(bq2[6]), "+v"(bq2[7]));
;                 asm volatile("" : "+v"(bq2[8]), "+v"(bq2[9]), "+v"(bq2[10]), "+v"(bq2[11]), "+v"(bq2[12]), "+v"(bq2[13]), "+v"(bq2[14]), "+v"(bq2[15]));
; #pragma unroll
;                 for (int s = 0; s < 16; ++s) lacc = __builtin_amdgcn_mfma_f32_32x32x2f32(ap[32 + 2 * s], bq2[s], lacc, 0, 0, 0);
	v_mfma_f32_32x32x2_f32 v[2:17], v18, v156, v[2:17]
	v_mfma_f32_32x32x2_f32 v[2:17], v19, v157, v[2:17]
	s_waitcnt vmcnt(0)
	ds_read2_b32 v[18:19], v182 offset0:32 offset1:34
	s_waitcnt lgkmcnt(0)
	v_mfma_f32_32x32x2_f32 v[2:17], v18, v20, v[2:17]
	v_mfma_f32_32x32x2_f32 v[2:17], v19, v21, v[2:17]
	ds_read2_b32 v[18:19], v182 offset0:36 offset1:38
	s_waitcnt lgkmcnt(0)
	v_mfma_f32_32x32x2_f32 v[2:17], v18, v30, v[2:17]
	v_mfma_f32_32x32x2_f32 v[2:17], v19, v31, v[2:17]
	ds_read2_b32 v[18:19], v182 offset0:40 offset1:42
	s_waitcnt lgkmcnt(0)
	v_mfma_f32_32x32x2_f32 v[2:17], v18, v32, v[2:17]
	v_mfma_f32_32x32x2_f32 v[2:17], v19, v33, v[2:17]
	ds_read2_b32 v[18:19], v182 offset0:44 offset1:46
	s_waitcnt lgkmcnt(0)
	v_mfma_f32_32x32x2_f32 v[2:17], v18, v102, v[2:17]
	v_mfma_f32_32x32x2_f32 v[2:17], v19, v103, v[2:17]
	ds_read2_b32 v[18:19], v182 offset0:48 offset1:50
	s_waitcnt lgkmcnt(0)
	v_mfma_f32_32x32x2_f32 v[2:17], v18, v106, v[2:17]
	v_mfma_f32_32x32x2_f32 v[2:17], v19, v107, v[2:17]
	ds_read2_b32 v[18:19], v182 offset0:52 offset1:54
	s_waitcnt lgkmcnt(0)
	v_mfma_f32_32x32x2_f32 v[2:17], v18, v108, v[2:17]
	v_mfma_f32_32x32x2_f32 v[2:17], v19, v109, v[2:17]
	ds_read2_b32 v[18:19], v182 offset0:56 offset1:58
	s_waitcnt lgkmcnt(0)
	v_mfma_f32_32x32x2_f32 v[2:17], v18, v110, v[2:17]
	v_mfma_f32_32x32x2_f32 v[2:17], v19, v111, v[2:17]
	ds_read2_b32 v[18:19], v182 offset0:60 offset1:62
	s_waitcnt lgkmcnt(0)
	v_mfma_f32_32x32x2_f32 v[2:17], v18, v112, v[2:17]
	v_mfma_f32_32x32x2_f32 v[2:17], v19, v113, v[2:17]
	global_load_dword v20, v165, s[40:41] offset:0
	global_load_dword v21, v165, s[40:41] offset:256
	global_load_dword v30, v165, s[40:41] offset:512
	global_load_dword v31, v165, s[40:41] offset:768
	global_load_dword v32, v165, s[40:41] offset:1024
	global_load_dword v33, v165, s[40:41] offset:1280
	global_load_dword v102, v165, s[40:41] offset:1536
	global_load_dword v103, v165, s[40:41] offset:1792
	global_load_dword v106, v165, s[40:41] offset:2048
	global_load_dword v107, v165, s[40:41] offset:2304
	global_load_dword v108, v165, s[40:41] offset:2560
	global_load_dword v109, v165, s[40:41] offset:2816
	global_load_dword v110, v165, s[40:41] offset:3072
	global_load_dword v111, v165, s[40:41] offset:3328
	global_load_dword v112, v165, s[40:41] offset:3584
	global_load_dword v113, v165, s[40:41] offset:3840
	s_barrier
	ds_write_b128 v206, v[22:25]
	ds_write_b128 v206, v[34:37] offset:1024
	ds_write2_b32 v82, v90, v91 offset1:1
	ds_write2_b32 v83, v94, v95 offset1:1
	ds_write2_b32 v84, v126, v127 offset1:1
	ds_write2_b32 v85, v128, v129 offset1:1
	ds_write2_b64 v86, v[96:97], v[100:101] offset1:1
	ds_write2_b64 v87, v[130:131], v[138:139] offset1:1
	ds_write2_b32 v88, v114, v115 offset1:1
	ds_write2_b32 v89, v124, v125 offset1:1
	ds_write2_b32 v134, v140, v141 offset1:1
	ds_write2_b32 v135, v180, v181 offset1:1
	s_waitcnt lgkmcnt(0)
	s_barrier
	s_waitcnt vmcnt(0)
	global_load_dword v22, v165, s[42:43] offset:0
	global_load_dword v23, v165, s[42:43] offset:256
	global_load_dword v24, v165, s[42:43] offset:512
	global_load_dword v25, v165, s[42:43] offset:768
	global_load_dword v34, v165, s[42:43] offset:1024
	global_load_dword v35, v165, s[42:43] offset:1280
	global_load_dword v36, v165, s[42:43] offset:1536
	global_load_dword v37, v165, s[42:43] offset:1792
	global_load_dword v90, v165, s[42:43] offset:2048
	global_load_dword v91, v165, s[42:43] offset:2304
	global_load_dword v94, v165, s[42:43] offset:2560
	global_load_dword v95, v165, s[42:43] offset:2816
	global_load_dword v96, v165, s[42:43] offset:3072
	global_load_dword v97, v165, s[42:43] offset:3328
	global_load_dword v100, v165, s[42:43] offset:3584
	global_load_dword v101, v165, s[42:43] offset:3840
	ds_read2_b32 v[18:19], v182 offset1:2
	s_waitcnt lgkmcnt(0)
	v_mfma_f32_32x32x2_f32 v[2:17], v18, v20, v[2:17]
	v_mfma_f32_32x32x2_f32 v[2:17], v19, v21, v[2:17]
	ds_read2_b32 v[18:19], v182 offset0:4 offset1:6
	s_waitcnt lgkmcnt(0)
	v_mfma_f32_32x32x2_f32 v[2:17], v18, v30, v[2:17]
	v_mfma_f32_32x32x2_f32 v[2:17], v19, v31, v[2:17]
	ds_read2_b32 v[18:19], v182 offset0:8 offset1:10
	s_waitcnt lgkmcnt(0)
	v_mfma_f32_32x32x2_f32 v[2:17], v18, v32, v[2:17]
	v_mfma_f32_32x32x2_f32 v[2:17], v19, v33, v[2:17]
	ds_read2_b32 v[18:19], v182 offset0:12 offset1:14
	s_waitcnt lgkmcnt(0)
	v_mfma_f32_32x32x2_f32 v[2:17], v18, v102, v[2:17]
	v_mfma_f32_32x32x2_f32 v[2:17], v19, v103, v[2:17]
	ds_read2_b32 v[18:19], v182 offset0:16 offset1:18
	s_waitcnt lgkmcnt(0)
	v_mfma_f32_32x32x2_f32 v[2:17], v18, v106, v[2:17]
	v_mfma_f32_32x32x2_f32 v[2:17], v19, v107, v[2:17]
	ds_read2_b32 v[18:19], v182 offset0:20 offset1:22
	s_waitcnt lgkmcnt(0)
	v_mfma_f32_32x32x2_f32 v[2:17], v18, v108, v[2:17]
	v_mfma_f32_32x32x2_f32 v[2:17], v19, v109, v[2:17]
	ds_read2_b32 v[18:19], v182 offset0:24 offset1:26
	s_waitcnt lgkmcnt(0)
	v_mfma_f32_32x32x2_f32 v[2:17], v18, v110, v[2:17]
	v_mfma_f32_32x32x2_f32 v[2:17], v19, v111, v[2:17]
	ds_read2_b32 v[18:19], v182 offset0:28 offset1:30
	s_waitcnt lgkmcnt(0)
	v_mfma_f32_32x32x2_f32 v[2:17], v18, v112, v[2:17]
	v_mfma_f32_32x32x2_f32 v[2:17], v19, v113, v[2:17]
	s_waitcnt vmcnt(0)
	ds_read2_b32 v[18:19], v182 offset0:32 offset1:34
	s_waitcnt lgkmcnt(0)
	v_mfma_f32_32x32x2_f32 v[2:17], v18, v22, v[2:17]
	v_mfma_f32_32x32x2_f32 v[2:17], v19, v23, v[2:17]
	ds_read2_b32 v[18:19], v182 offset0:36 offset1:38
	s_waitcnt lgkmcnt(0)
	v_mfma_f32_32x32x2_f32 v[2:17], v18, v24, v[2:17]
	v_mfma_f32_32x32x2_f32 v[2:17], v19, v25, v[2:17]
	ds_read2_b32 v[18:19], v182 offset0:40 offset1:42
	s_waitcnt lgkmcnt(0)
; #define LAS __attribute__((address_space(3)))
; #define RB_WAIT() do { asm volatile("s_waitcnt vmcnt(0)" : "+v"(bq[0]), "+v"(bq[1]), "+v"(bq[2]), "+v"(bq[3]), "+v"(bq[4]), "+v"(bq[5]), "+v"(bq[6]), "+v"(bq[7])); \
;                     asm volatile("" : "+v"(bq[8]), "+v"(bq[9]), "+v"(bq[10]), "+v"(bq[11]), "+v"(bq[12]), "+v"(bq[13]), "+v"(bq[14]), "+v"(bq[15])); } while (0)
; #define RB_LD2(i_, off_) asm volatile("global_load_dword %0, %1, %2 offset:" #off_ : "=v"(bq2[i_]) : "v"(wvo), "s"(wr1))
; __global__ void __launch_bounds__(NWAVES * 64, 2) fwd_kernel(Args args) {
;     ...
;             for (int q = 0; q < 4; ++q) {
;                 float bq[16];
;                 const float* wr0 = w_router + (size_t)(q * 512 + 64 * wave) * NE; const float* wr1 = wr0 + 16 * 2 * NE; const unsigned wvo = (unsigned)((lane >> 5) * NE + (lane & 31)) * 4u;
;     ...
;                 RB_LD16(wr0);
;                 __syncthreads();
; #pragma unroll
;                 for (int rr = 0; rr < 4; ++rr)
; #pragma unroll
;                     for (int jj = 0; jj < 2; ++jj) { const int lk = 4 * lane + 256 * jj; LAS float* hp = HT + (4 * wave + rr) * 513 + lk; const f32x4 q4 = v[rr][2 * q + jj]; hp[0] = q4[0]; hp[1] = q4[1]; hp[2] = q4[2]; hp[3] = q4[3]; }
;                 __syncthreads();
;                 const LAS float* ap = HT + (lane & 31) * 513 + 64 * wave + (lane >> 5);
;                 RB_WAIT();
;                 float bq2[16];
;     ...
;                 RB_LD2(0, 0); RB_LD2(1, 256); RB_LD2(2, 512); RB_LD2(3, 768); RB_LD2(4, 1024); RB_LD2(5, 1280); RB_LD2(6, 1536); RB_LD2(7, 1792);
;                 RB_LD2(8, 2048); RB_LD2(9, 2304); RB_LD2(10, 2560); RB_LD2(11, 2816); RB_LD2(12, 3072); RB_LD2(13, 3328); RB_LD2(14, 3584); RB_LD2(15, 3840);
; #pragma unroll
;                 for (int s = 0; s < 16; ++s) lacc = __builtin_amdgcn_mfma_f32_32x32x2f32(ap[2 * s], bq[s], lacc, 0, 0, 0);
;                 asm volatile("" : "+v"(lacc));
;                 asm volatile("s_waitcnt vmcnt(0)" : "+v"(bq2[0]), "+v"(bq2[1]), "+v"(bq2[2]), "+v"(bq2[3]), "+v"(bq2[4]), "+v"(bq2[5]), "+v"(bq2[6]), "+v"(bq2[7]));
;                 asm volatile("" : "+v"(bq2[8]), "+v"(bq2[9]), "+v"(bq2[10]), "+v"(bq2[11]), "+v"(bq2[12]), "+v"(bq2[13]), "+v"(bq2[14]), "+v"(bq2[15]));
; #pragma unroll
;                 for (int s = 0; s < 16; ++s) lacc = __builtin_amdgcn_mfma_f32_32x32x2f32(ap[32 + 2 * s], bq2[s], lacc, 0, 0, 0);
	v_mfma_f32_32x32x2_f32 v[2:17], v18, v34, v[2:17]
	v_mfma_f32_32x32x2_f32 v[2:17], v19, v35, v[2:17]
	ds_read2_b32 v[18:19], v182 offset0:44 offset1:46
	s_waitcnt lgkmcnt(0)
	v_mfma_f32_32x32x2_f32 v[2:17], v18, v36, v[2:17]
	v_mfma_f32_32x32x2_f32 v[2:17], v19, v37, v[2:17]
	ds_read2_b32 v[18:19], v182 offset0:48 offset1:50
	s_waitcnt lgkmcnt(0)
	v_mfma_f32_32x32x2_f32 v[2:17], v18, v90, v[2:17]
	v_mfma_f32_32x32x2_f32 v[2:17], v19, v91, v[2:17]
	ds_read2_b32 v[18:19], v182 offset0:52 offset1:54
	s_waitcnt lgkmcnt(0)
	v_mfma_f32_32x32x2_f32 v[2:17], v18, v94, v[2:17]
	v_mfma_f32_32x32x2_f32 v[2:17], v19, v95, v[2:17]
	ds_read2_b32 v[18:19], v182 offset0:56 offset1:58
	s_waitcnt lgkmcnt(0)
	v_mfma_f32_32x32x2_f32 v[2:17], v18, v96, v[2:17]
	v_mfma_f32_32x32x2_f32 v[2:17], v19, v97, v[2:17]
	ds_read2_b32 v[18:19], v182 offset0:60 offset1:62
	s_waitcnt lgkmcnt(0)
	v_mfma_f32_32x32x2_f32 v[2:17], v18, v100, v[2:17]
	v_mfma_f32_32x32x2_f32 v[2:17], v19, v101, v[2:17]
	global_load_dword v20, v165, s[44:45] offset:0
	global_load_dword v21, v165, s[44:45] offset:256
	global_load_dword v22, v165, s[44:45] offset:512
	global_load_dword v23, v165, s[44:45] offset:768
	global_load_dword v24, v165, s[44:45] offset:1024
	global_load_dword v25, v165, s[44:45] offset:1280
	global_load_dword v30, v165, s[44:45] offset:1536
	global_load_dword v31, v165, s[44:45] offset:1792
	global_load_dword v32, v165, s[44:45] offset:2048
	global_load_dword v33, v165, s[44:45] offset:2304
	global_load_dword v34, v165, s[44:45] offset:2560
	global_load_dword v35, v165, s[44:45] offset:2816
	global_load_dword v36, v165, s[44:45] offset:3072
	global_load_dword v37, v165, s[44:45] offset:3328
	global_load_dword v90, v165, s[44:45] offset:3584
	global_load_dword v91, v165, s[44:45] offset:3840
	s_barrier
	ds_write_b128 v206, v[26:29]
	ds_write_b128 v206, v[38:41] offset:1024
	ds_write2_b32 v82, v92, v93 offset1:1
	ds_write2_b32 v83, v98, v99 offset1:1
	ds_write2_b32 v84, v76, v77 offset1:1
	ds_write2_b32 v85, v78, v79 offset1:1
	ds_write2_b64 v86, v[104:105], v[116:117] offset1:1
	ds_write2_b64 v87, v[70:71], v[72:73] offset1:1
	ds_write2_b32 v88, v118, v119 offset1:1
	ds_write2_b32 v89, v122, v123 offset1:1
	ds_write2_b32 v134, v74, v75 offset1:1
	ds_write2_b32 v135, v80, v81 offset1:1
	s_waitcnt lgkmcnt(0)
	s_barrier
; __global__ void __launch_bounds__(NWAVES * 64, 2) fwd_kernel(Args args) {
;     ...
;                 for (int s = 0; s < 16; ++s) lacc = __builtin_amdgcn_mfma_f32_32x32x2f32(ap[2 * s], bq[s], lacc, 0, 0, 0);
;                 asm volatile("" : "+v"(lacc));
;                 asm volatile("s_waitcnt vmcnt(0)" : "+v"(bq2[0]), "+v"(bq2[1]), "+v"(bq2[2]), "+v"(bq2[3]), "+v"(bq2[4]), "+v"(bq2[5]), "+v"(bq2[6]), "+v"(bq2[7]));
;                 asm volatile("" : "+v"(bq2[8]), "+v"(bq2[9]), "+v"(bq2[10]), "+v"(bq2[11]), "+v"(bq2[12]), "+v"(bq2[13]), "+v"(bq2[14]), "+v"(bq2[15]));
; #pragma unroll
;                 for (int s = 0; s < 16; ++s) lacc = __builtin_amdgcn_mfma_f32_32x32x2f32(ap[32 + 2 * s], bq2[s], lacc, 0, 0, 0);
;                 asm volatile("" : "+v"(lacc));
;             }
; #pragma unroll
;             for (int rg = 0; rg < 16; ++rg) { const int i = (rg & 3) + 8 * (rg >> 2) + 4 * (lane >> 5); RED[(wave * 32 + i) * 32 + (lane & 31)] = lacc[rg]; }
;             __syncthreads();
; #pragma unroll
;             for (int pp = 0; pp < 2; ++pp) { const int p = tid + pp * 512, i = p >> 5, j = p & 31; float s = b_router[j];
; #pragma unroll
;                 for (int w = 0; w < 8; ++w) s += RED[(w * 32 + i) * 32 + j];
;                 LG[i * 33 + j] = s; }
;             __syncthreads();
;             int ae[2], al[2]; float aw[2];
;             { const int hw = tid >> 5, l32 = tid & 31;
; #pragma unroll
;               for (int it = 0; it < 2; ++it) { const int i = hw * 2 + it; float val = LG[i * 33 + l32]; float tv[4]; int ti[4];
; #pragma unroll
;                 for (int k = 0; k < 4; ++k) { float bv = val; int bi = l32;
; #pragma unroll
;                     for (int off = 16; off >= 1; off >>= 1) { const float ov = __shfl_xor(bv, off); const int oi = __shfl_xor(bi, off); if (ov > bv || (ov == bv && oi < bi)) { bv = ov; bi = oi; } }
;                     tv[k] = bv; ti[k] = bi; if (l32 == bi) val = -3.0e38f; }
;                 float den = 0.f, ex[4];
; #pragma unroll
;                 for (int k = 0; k < 4; ++k) { ex[k] = expf(tv[k] - tv[0]); den += ex[k]; }
;                 const int ke = l32 & 3; ae[it] = ke == 0 ? ti[0] : (ke == 1 ? ti[1] : (ke == 2 ? ti[2] : ti[3])); aw[it] = (ke == 0 ? ex[0] : (ke == 1 ? ex[1] : (ke == 2 ? ex[2] : ex[3]))) / den;
;                 al[it] = (l32 < 4) ? atomicAdd((int*)&HIST[ae[it]], 1) : 0; } }
	s_waitcnt vmcnt(0)
	global_load_dword v26, v165, s[46:47] offset:0
	global_load_dword v27, v165, s[46:47] offset:256
	global_load_dword v28, v165, s[46:47] offset:512
	global_load_dword v29, v165, s[46:47] offset:768
	global_load_dword v38, v165, s[46:47] offset:1024
	global_load_dword v39, v165, s[46:47] offset:1280
	global_load_dword v40, v165, s[46:47] offset:1536
	global_load_dword v41, v165, s[46:47] offset:1792
	global_load_dword v70, v165, s[46:47] offset:2048
	global_load_dword v71, v165, s[46:47] offset:2304
	global_load_dword v72, v165, s[46:47] offset:2560
	global_load_dword v73, v165, s[46:47] offset:2816
	global_load_dword v74, v165, s[46:47] offset:3072
	global_load_dword v75, v165, s[46:47] offset:3328
	global_load_dword v76, v165, s[46:47] offset:3584
	global_load_dword v77, v165, s[46:47] offset:3840
	ds_read2_b32 v[18:19], v182 offset1:2
	s_waitcnt lgkmcnt(0)
	v_mfma_f32_32x32x2_f32 v[2:17], v18, v20, v[2:17]
	v_add_u32_e32 v20, 0x800, v207
	v_mfma_f32_32x32x2_f32 v[2:17], v19, v21, v[2:17]
	ds_read2_b32 v[18:19], v182 offset0:4 offset1:6
	v_add_u32_e32 v21, 0xc00, v207
	s_waitcnt lgkmcnt(0)
	v_mfma_f32_32x32x2_f32 v[2:17], v18, v22, v[2:17]
	v_mfma_f32_32x32x2_f32 v[2:17], v19, v23, v[2:17]
	ds_read2_b32 v[18:19], v182 offset0:8 offset1:10
	s_waitcnt lgkmcnt(0)
	v_mfma_f32_32x32x2_f32 v[2:17], v18, v24, v[2:17]
	v_mfma_f32_32x32x2_f32 v[2:17], v19, v25, v[2:17]
	ds_read2_b32 v[18:19], v182 offset0:12 offset1:14
	s_waitcnt lgkmcnt(0)
	v_mfma_f32_32x32x2_f32 v[2:17], v18, v30, v[2:17]
	v_mfma_f32_32x32x2_f32 v[2:17], v19, v31, v[2:17]
	ds_read2_b32 v[18:19], v182 offset0:16 offset1:18
	s_waitcnt lgkmcnt(0)
	v_mfma_f32_32x32x2_f32 v[2:17], v18, v32, v[2:17]
	v_mfma_f32_32x32x2_f32 v[2:17], v19, v33, v[2:17]
	ds_read2_b32 v[18:19], v182 offset0:20 offset1:22
	s_waitcnt lgkmcnt(0)
	v_mfma_f32_32x32x2_f32 v[2:17], v18, v34, v[2:17]
	v_mfma_f32_32x32x2_f32 v[2:17], v19, v35, v[2:17]
	ds_read2_b32 v[18:19], v182 offset0:24 offset1:26
	s_waitcnt lgkmcnt(0)
	v_mfma_f32_32x32x2_f32 v[2:17], v18, v36, v[2:17]
	v_mfma_f32_32x32x2_f32 v[2:17], v19, v37, v[2:17]
	ds_read2_b32 v[18:19], v182 offset0:28 offset1:30
	s_waitcnt lgkmcnt(0)
	v_mfma_f32_32x32x2_f32 v[2:17], v18, v90, v[2:17]
	v_mfma_f32_32x32x2_f32 v[2:17], v19, v91, v[2:17]
	s_waitcnt vmcnt(0)
	ds_read2_b32 v[18:19], v182 offset0:32 offset1:34
	s_waitcnt lgkmcnt(0)
	v_mfma_f32_32x32x2_f32 v[2:17], v18, v26, v[2:17]
	v_mfma_f32_32x32x2_f32 v[2:17], v19, v27, v[2:17]
	ds_read2_b32 v[18:19], v182 offset0:36 offset1:38
	s_waitcnt lgkmcnt(0)
	v_mfma_f32_32x32x2_f32 v[2:17], v18, v28, v[2:17]
	v_mfma_f32_32x32x2_f32 v[2:17], v19, v29, v[2:17]
	ds_read2_b32 v[18:19], v182 offset0:40 offset1:42
	s_waitcnt lgkmcnt(0)
	v_mfma_f32_32x32x2_f32 v[2:17], v18, v38, v[2:17]
	v_mfma_f32_32x32x2_f32 v[2:17], v19, v39, v[2:17]
	ds_read2_b32 v[18:19], v182 offset0:44 offset1:46
	s_waitcnt lgkmcnt(0)
	v_mfma_f32_32x32x2_f32 v[2:17], v18, v40, v[2:17]
	v_mfma_f32_32x32x2_f32 v[2:17], v19, v41, v[2:17]
	ds_read2_b32 v[18:19], v182 offset0:48 offset1:50
	s_waitcnt lgkmcnt(0)
	v_mfma_f32_32x32x2_f32 v[2:17], v18, v70, v[2:17]
	v_mfma_f32_32x32x2_f32 v[2:17], v19, v71, v[2:17]
	ds_read2_b32 v[18:19], v182 offset0:52 offset1:54
	s_waitcnt lgkmcnt(0)
	v_mfma_f32_32x32x2_f32 v[2:17], v18, v72, v[2:17]
	v_mfma_f32_32x32x2_f32 v[2:17], v19, v73, v[2:17]
	ds_read2_b32 v[18:19], v182 offset0:56 offset1:58
	s_waitcnt lgkmcnt(0)
	v_mfma_f32_32x32x2_f32 v[2:17], v18, v74, v[2:17]
	v_mfma_f32_32x32x2_f32 v[2:17], v19, v75, v[2:17]
	ds_read2_b32 v[18:19], v182 offset0:60 offset1:62
	s_waitcnt lgkmcnt(0)
	v_mfma_f32_32x32x2_f32 v[2:17], v18, v76, v[2:17]
	v_add_u32_e32 v18, 0x400, v207
	v_mfma_f32_32x32x2_f32 v[2:17], v19, v77, v[2:17]
	s_nop 15
	s_nop 1
	ds_write2_b32 v207, v2, v3 offset1:32
	ds_write2_b32 v207, v4, v5 offset0:64 offset1:96
	ds_write2_b32 v18, v6, v7 offset1:32
	ds_write2_b32 v18, v8, v9 offset0:64 offset1:96
	ds_write2_b32 v20, v10, v11 offset1:32
	ds_write2_b32 v20, v12, v13 offset0:64 offset1:96
	ds_write2_b32 v21, v14, v15 offset1:32
	ds_write2_b32 v21, v16, v17 offset0:64 offset1:96
	s_waitcnt lgkmcnt(0)
	s_barrier
	global_load_dword v10, v[48:49], off
	ds_read2st64_b32 v[2:3], v202 offset1:16
	ds_read2st64_b32 v[4:5], v202 offset0:32 offset1:48
	ds_read2st64_b32 v[6:7], v202 offset0:64 offset1:80
	ds_read2st64_b32 v[8:9], v202 offset0:96 offset1:112
	s_waitcnt vmcnt(0) lgkmcnt(3)
	v_add_f32_e32 v2, v10, v2
	v_add_f32_e32 v2, v2, v3
	s_waitcnt lgkmcnt(2)
	v_add_f32_e32 v2, v2, v4
	v_add_f32_e32 v2, v2, v5
	s_waitcnt lgkmcnt(1)
	v_add_f32_e32 v2, v2, v6
	v_add_f32_e32 v2, v2, v7
	s_waitcnt lgkmcnt(0)
	v_add_f32_e32 v2, v2, v8
	v_add_f32_e32 v2, v2, v9
	ds_write_b32 v208, v2
	ds_read2st64_b32 v[2:3], v203 offset1:16
	ds_read2st64_b32 v[4:5], v203 offset0:32 offset1:48
	ds_read2st64_b32 v[6:7], v203 offset0:64 offset1:80
	ds_read2st64_b32 v[8:9], v203 offset0:96 offset1:112
	s_waitcnt lgkmcnt(3)
	v_add_f32_e32 v2, v10, v2
	v_add_f32_e32 v2, v2, v3
	s_waitcnt lgkmcnt(2)
	v_add_f32_e32 v2, v2, v4
	v_add_f32_e32 v2, v2, v5
	s_waitcnt lgkmcnt(1)
	v_add_f32_e32 v2, v2, v6
	v_add_f32_e32 v2, v2, v7
	s_waitcnt lgkmcnt(0)
	v_add_f32_e32 v2, v2, v8
	v_add_f32_e32 v2, v2, v9
	ds_write_b32 v209, v2
	s_waitcnt lgkmcnt(0)
	s_barrier
	ds_read_b32 v4, v213
	ds_bpermute_b32 v7, v219, v163
	s_waitcnt lgkmcnt(1)
	ds_bpermute_b32 v6, v219, v4
	s_waitcnt lgkmcnt(0)
	v_cmp_lt_f32_e64 s[14:15], v4, v6
	v_cmp_nlt_f32_e32 vcc, v4, v6
	s_and_saveexec_b64 s[16:17], vcc
	v_cmp_eq_f32_e32 vcc, v4, v6
	v_cmp_lt_i32_e64 s[2:3], v7, v163
	s_and_b64 s[2:3], vcc, s[2:3]
	s_andn2_b64 s[14:15], s[14:15], exec
	s_and_b64 s[2:3], s[2:3], exec
	s_or_b64 s[14:15], s[14:15], s[2:3]
	s_or_b64 exec, exec, s[16:17]
	v_mov_b32_e32 v5, v4
	v_mov_b32_e32 v2, v163
	v_mov_b32_e32 v3, v4
	s_and_saveexec_b64 s[2:3], s[14:15]
	v_mov_b32_e32 v5, v6
	v_mov_b32_e32 v2, v7
	v_mov_b32_e32 v3, v6
	s_or_b64 exec, exec, s[2:3]
	ds_bpermute_b32 v6, v218, v5
	ds_bpermute_b32 v7, v218, v2
	s_waitcnt lgkmcnt(1)
	v_cmp_lt_f32_e64 s[14:15], v3, v6
	v_cmp_nlt_f32_e32 vcc, v3, v6
	s_and_saveexec_b64 s[16:17], vcc
	s_cbranch_execz .LBB0_1069
	v_cmp_eq_f32_e32 vcc, v3, v6
	s_waitcnt lgkmcnt(0)
	v_cmp_lt_i32_e64 s[2:3], v7, v2
	s_and_b64 s[2:3], vcc, s[2:3]
	s_andn2_b64 s[14:15], s[14:15], exec
	s_and_b64 s[2:3], s[2:3], exec
	s_or_b64 s[14:15], s[14:15], s[2:3]

; __device__ __forceinline__ float sigmoidf_(float x) { return __builtin_amdgcn_rcpf(1.0f + __builtin_amdgcn_exp2f(-1.44269504089f * x)); }
;     __device__ __forceinline__ void operator()(EPI_ARGS) const {
;     ...
;                 for (int h = 0; h < 2; ++h) { const int m = 2 * mp + h;
;                     const f32x4 a0 = acc[ai][0][m][0] * 0.03125f + ba0, a1 = acc[ai][0][m][1] * 0.03125f + ba1, l0 = acc[ai][1][m][0] * 0.03125f + bl0, l1 = acc[ai][1][m][1] * 0.03125f + bl1;
;                     float o[8];
; #pragma unroll
;                     for (int j = 0; j < 4; ++j) { const float g0 = fminf(a0[j], 7.0f), g1 = fminf(a1[j], 7.0f), x0 = fminf(fmaxf(l0[j], -7.0f), 7.0f), x1 = fminf(fmaxf(l1[j], -7.0f), 7.0f);
;                         o[j] = g0 * sigmoidf_(1.702f * g0) * (x0 + 1.0f); o[4 + j] = g1 * sigmoidf_(1.702f * g1) * (x1 + 1.0f); }
;                     px[h] = pk4_fp8(o[0], o[1], o[2], o[3]); py[h] = pk4_fp8(o[4], o[5], o[6], o[7]); }
;                 const u32x4 q = pair16(px[0], py[0], px[1], py[1]);
;                 const int row = u.pm * 256 + ai * 128 + wr * 64 + (2 * mp + (fq & 1)) * 16 + fr;
;                 *(u32x4*)(ACT + (size_t)row * FE + j0q) = q; }
.LBB0_1334:
	s_lshl_b32 s8, s30, 7
	s_or_b32 s10, s8, s69
	s_lshl_b32 s8, s81, 8
	s_nop 15
	v_mul_f32_e32 v10, 0xc01d265f, v240
	v_mul_f32_e32 v11, 0xc01d265f, v241
	v_mul_f32_e32 v12, 0xc01d265f, v242
	v_mul_f32_e32 v13, 0xc01d265f, v243
	v_mul_f32_e32 v6, 0xc01d265f, v244
	v_mul_f32_e32 v7, 0xc01d265f, v245
	v_mul_f32_e32 v8, 0xc01d265f, v246
	v_mul_f32_e32 v9, 0xc01d265f, v247
	v_add_f32_e32 v14, 1.0, v248
	v_mul_f32_e32 v14, 0xbed083aa, v14
	v_add_f32_e32 v15, 1.0, v249
	v_mul_f32_e32 v15, 0xbed083aa, v15
	v_add_f32_e32 v16, 1.0, v250
	v_mul_f32_e32 v16, 0xbed083aa, v16
	v_add_f32_e32 v17, 1.0, v251
	v_mul_f32_e32 v17, 0xbed083aa, v17
	v_add_f32_e32 v2, 1.0, v252
	v_mul_f32_e32 v2, 0xbed083aa, v2
	v_add_f32_e32 v3, 1.0, v253
	v_mul_f32_e32 v3, 0xbed083aa, v3
	v_add_f32_e32 v4, 1.0, v255
	v_mul_f32_e32 v4, 0xbed083aa, v4
	v_add_f32_e32 v5, 1.0, v239
	v_mul_f32_e32 v5, 0xbed083aa, v5
	s_waitcnt lgkmcnt(0)
	v_or_b32_e32 v18, s10, v207
	v_ashrrev_i32_e32 v19, 31, v18
	s_and_b64 vcc, exec, s[6:7]
	s_mov_b64 s[6:7], -1
	v_fmamk_f32 v20, v190, 0xbd9d265f, v10
	v_max_f32_e32 v20, 0xc1898193, v20
	v_exp_f32_e32 v30, v20
	v_fmamk_f32 v21, v186, 0xbd9d265f, v6
	v_max_f32_e32 v21, 0xc1898193, v21
	v_add_f32_e32 v30, 1.0, v30
	v_exp_f32_e32 v31, v21
	v_rcp_f32_e32 v30, v30
	v_fmamk_f32 v22, v191, 0xbd9d265f, v11
	v_fmamk_f32 v23, v187, 0xbd9d265f, v7
	v_fmamk_f32 v27, v189, 0xbd9d265f, v9
	v_max_f32_e32 v22, 0xc1898193, v22
	v_max_f32_e32 v23, 0xc1898193, v23
	v_max_f32_e32 v27, 0xc1898193, v27
	v_add_f32_e32 v31, 1.0, v31
	v_mul_f32_e32 v20, v20, v30
	v_exp_f32_e32 v34, v22
	v_rcp_f32_e32 v31, v31
	v_fmamk_f32 v25, v188, 0xbd9d265f, v8
	v_exp_f32_e32 v35, v23
	v_exp_f32_e32 v30, v27
	v_max_f32_e32 v25, 0xc1898193, v25
	v_fmamk_f32 v29, v178, 0xbc5083aa, v2
	v_fmamk_f32 v24, v192, 0xbd9d265f, v12
	v_fmamk_f32 v26, v193, 0xbd9d265f, v13
	v_med3_f32 v29, v29, s76, v225
	v_max_f32_e32 v24, 0xc1898193, v24
	v_max_f32_e32 v26, 0xc1898193, v26
	v_add_f32_e32 v34, 1.0, v34
	v_mul_f32_e32 v21, v21, v31
	v_fmamk_f32 v28, v182, 0xbc5083aa, v14
	v_exp_f32_e32 v39, v25
	v_add_f32_e32 v35, 1.0, v35
	v_rcp_f32_e32 v34, v34
	v_mul_f32_e32 v21, v29, v21
	v_add_f32_e32 v30, 1.0, v30
	v_med3_f32 v28, v28, s76, v225
	v_rcp_f32_e32 v35, v35
	v_rcp_f32_e32 v30, v30
	v_fmamk_f32 v32, v183, 0xbc5083aa, v15
	v_exp_f32_e32 v38, v24
	v_exp_f32_e32 v29, v26
	v_fmamk_f32 v33, v179, 0xbc5083aa, v3
	v_med3_f32 v32, v32, s76, v225
	v_mul_f32_e32 v20, v28, v20
	v_fmamk_f32 v28, v181, 0xbc5083aa, v5
	v_med3_f32 v33, v33, s76, v225
	v_add_f32_e32 v39, 1.0, v39
	v_mul_f32_e32 v22, v22, v34
	v_med3_f32 v28, v28, s76, v225
	v_rcp_f32_e32 v39, v39
	v_mul_f32_e32 v23, v23, v35
	v_mul_f32_e32 v22, v32, v22
	v_mul_f32_e32 v27, v27, v30
	v_add_f32_e32 v38, 1.0, v38
	v_mul_f32_e32 v23, v33, v23
	v_add_f32_e32 v29, 1.0, v29
	v_mul_f32_e32 v27, v28, v27
	v_mov_b32_e32 v28, v22
	v_fmamk_f32 v37, v180, 0xbc5083aa, v4
	v_rcp_f32_e32 v38, v38
	v_rcp_f32_e32 v29, v29
	v_cvt_pk_fp8_f32 v22, v20, v28
	v_mov_b32_e32 v20, v21
	v_mov_b32_e32 v21, v23
	v_med3_f32 v37, v37, s76, v225
	v_cvt_pk_fp8_f32 v23, v20, v21
	v_fmamk_f32 v36, v184, 0xbc5083aa, v16
	v_fmamk_f32 v40, v185, 0xbc5083aa, v17
	v_mul_f32_e32 v25, v25, v39
	v_med3_f32 v36, v36, s76, v225
	v_med3_f32 v40, v40, s76, v225
	v_mul_f32_e32 v25, v37, v25
	v_mul_f32_e32 v24, v24, v38
	v_mul_f32_e32 v26, v26, v29
	v_mul_f32_e32 v24, v36, v24
	v_mul_f32_e32 v26, v40, v26
	v_cvt_pk_fp8_f32 v23, v25, v27 op_sel:[0, 0, 1]
	v_fmamk_f32 v20, v174, 0xbd9d265f, v10
	v_max_f32_e32 v20, 0xc1898193, v20
	v_fmamk_f32 v21, v170, 0xbd9d265f, v6
	v_cvt_pk_fp8_f32 v22, v24, v26 op_sel:[0,0,1]
	v_max_f32_e32 v21, 0xc1898193, v21
	v_exp_f32_e32 v26, v20
	v_exp_f32_e32 v27, v21
	v_fmamk_f32 v24, v166, 0xbc5083aa, v14
	v_add_f32_e32 v26, 1.0, v26
	v_rcp_f32_e32 v26, v26
	v_add_f32_e32 v27, 1.0, v27
	v_rcp_f32_e32 v27, v27
	v_med3_f32 v24, v24, s76, v225
	v_fmamk_f32 v25, v162, 0xbc5083aa, v2
	v_med3_f32 v25, v25, s76, v225
	v_mul_f32_e32 v20, v20, v26
	v_mul_f32_e32 v20, v24, v20
	v_mul_f32_e32 v21, v21, v27
	v_mul_f32_e32 v21, v25, v21
	v_fmamk_f32 v24, v175, 0xbd9d265f, v11
	v_max_f32_e32 v24, 0xc1898193, v24
	v_fmamk_f32 v25, v171, 0xbd9d265f, v7
	v_max_f32_e32 v25, 0xc1898193, v25
	v_exp_f32_e32 v28, v24
	v_exp_f32_e32 v29, v25
	v_fmamk_f32 v26, v167, 0xbc5083aa, v15
	v_add_f32_e32 v28, 1.0, v28
	v_rcp_f32_e32 v28, v28
	v_add_f32_e32 v29, 1.0, v29
	v_rcp_f32_e32 v29, v29
	v_med3_f32 v26, v26, s76, v225
	v_fmamk_f32 v27, v163, 0xbc5083aa, v3
	v_med3_f32 v27, v27, s76, v225
	v_mul_f32_e32 v24, v24, v28
	v_mul_f32_e32 v24, v26, v24
	v_mul_f32_e32 v25, v25, v29
	v_mul_f32_e32 v25, v27, v25
	v_fmamk_f32 v26, v176, 0xbd9d265f, v12
	v_max_f32_e32 v26, 0xc1898193, v26
	v_fmamk_f32 v27, v172, 0xbd9d265f, v8
	v_max_f32_e32 v27, 0xc1898193, v27
	v_exp_f32_e32 v30, v26
	v_exp_f32_e32 v31, v27
	v_fmamk_f32 v28, v168, 0xbc5083aa, v16
	v_add_f32_e32 v30, 1.0, v30
	v_rcp_f32_e32 v30, v30
	v_add_f32_e32 v31, 1.0, v31
	v_rcp_f32_e32 v31, v31
	v_med3_f32 v28, v28, s76, v225
	v_fmamk_f32 v29, v164, 0xbc5083aa, v4
	v_med3_f32 v29, v29, s76, v225
	v_mul_f32_e32 v26, v26, v30
	v_mul_f32_e32 v26, v28, v26
	v_mul_f32_e32 v27, v27, v31
	v_mul_f32_e32 v27, v29, v27
	v_fmamk_f32 v28, v177, 0xbd9d265f, v13
	v_max_f32_e32 v28, 0xc1898193, v28
	v_fmamk_f32 v29, v173, 0xbd9d265f, v9
	v_max_f32_e32 v29, 0xc1898193, v29
	v_exp_f32_e32 v32, v28
	v_exp_f32_e32 v33, v29
	v_fmamk_f32 v30, v169, 0xbc5083aa, v17
	v_add_f32_e32 v32, 1.0, v32
	v_rcp_f32_e32 v32, v32
	v_add_f32_e32 v33, 1.0, v33
	v_rcp_f32_e32 v33, v33
	v_med3_f32 v30, v30, s76, v225
	v_fmamk_f32 v31, v165, 0xbc5083aa, v5
; __device__ __forceinline__ float sigmoidf_(float x) { return __builtin_amdgcn_rcpf(1.0f + __builtin_amdgcn_exp2f(-1.44269504089f * x)); }
;     __device__ __forceinline__ void operator()(EPI_ARGS) const {
;     ...
;                 for (int h = 0; h < 2; ++h) { const int m = 2 * mp + h;
;                     const f32x4 a0 = acc[ai][0][m][0] * 0.03125f + ba0, a1 = acc[ai][0][m][1] * 0.03125f + ba1, l0 = acc[ai][1][m][0] * 0.03125f + bl0, l1 = acc[ai][1][m][1] * 0.03125f + bl1;
;                     float o[8];
; #pragma unroll
;                     for (int j = 0; j < 4; ++j) { const float g0 = fminf(a0[j], 7.0f), g1 = fminf(a1[j], 7.0f), x0 = fminf(fmaxf(l0[j], -7.0f), 7.0f), x1 = fminf(fmaxf(l1[j], -7.0f), 7.0f);
;                         o[j] = g0 * sigmoidf_(1.702f * g0) * (x0 + 1.0f); o[4 + j] = g1 * sigmoidf_(1.702f * g1) * (x1 + 1.0f); }
;                     px[h] = pk4_fp8(o[0], o[1], o[2], o[3]); py[h] = pk4_fp8(o[4], o[5], o[6], o[7]); }
;                 const u32x4 q = pair16(px[0], py[0], px[1], py[1]);
;                 const int row = u.pm * 256 + ai * 128 + wr * 64 + (2 * mp + (fq & 1)) * 16 + fr;
;                 *(u32x4*)(ACT + (size_t)row * FE + j0q) = q; }
	v_med3_f32 v31, v31, s76, v225
	v_mul_f32_e32 v28, v28, v32
	v_mul_f32_e32 v28, v30, v28
	v_mul_f32_e32 v29, v29, v33
	v_mul_f32_e32 v29, v31, v29
	v_cvt_pk_fp8_f32 v24, v20, v24
	v_mov_b32_e32 v20, v21
	v_cvt_pk_fp8_f32 v25, v20, v25
	v_cvt_pk_fp8_f32 v24, v26, v28 op_sel:[0,0,1]
	v_cvt_pk_fp8_f32 v25, v27, v29 op_sel:[0, 0, 1]
	v_add_u32_e32 v20, s8, v219
	v_ashrrev_i32_e32 v21, 31, v20
	v_lshlrev_b64 v[26:27], 11, v[20:21]
	v_lshl_add_u64 v[26:27], s[16:17], 0, v[26:27]
	v_permlane16_swap_b32_e32 v22, v24
	v_permlane16_swap_b32_e32 v23, v25
	v_lshl_add_u64 v[26:27], v[26:27], 0, v[18:19]
	v_fmamk_f32 v21, v158, 0xbd9d265f, v10
	global_store_dwordx4 v[26:27], v[22:25], off
	v_max_f32_e32 v21, 0xc1898193, v21
	s_nop 0
	v_fmamk_f32 v22, v154, 0xbd9d265f, v6
	v_max_f32_e32 v22, 0xc1898193, v22
	v_exp_f32_e32 v25, v21
	v_exp_f32_e32 v26, v22
	v_fmamk_f32 v23, v150, 0xbc5083aa, v14
	v_add_f32_e32 v25, 1.0, v25
	v_rcp_f32_e32 v25, v25
	v_add_f32_e32 v26, 1.0, v26
	v_rcp_f32_e32 v26, v26
	v_med3_f32 v23, v23, s76, v225
	v_fmamk_f32 v24, v146, 0xbc5083aa, v2
	v_med3_f32 v24, v24, s76, v225
	v_mul_f32_e32 v21, v21, v25
	v_mul_f32_e32 v21, v23, v21
	v_mul_f32_e32 v22, v22, v26
	v_mov_b32_e32 v23, v24
	v_mul_f32_e32 v23, v23, v22
	v_fmamk_f32 v22, v159, 0xbd9d265f, v11
	v_max_f32_e32 v22, 0xc1898193, v22
	v_fmamk_f32 v24, v155, 0xbd9d265f, v7
	v_max_f32_e32 v24, 0xc1898193, v24
	v_exp_f32_e32 v27, v22
	v_exp_f32_e32 v28, v24
	v_fmamk_f32 v25, v151, 0xbc5083aa, v15
	v_add_f32_e32 v27, 1.0, v27
	v_rcp_f32_e32 v27, v27
	v_add_f32_e32 v28, 1.0, v28
	v_rcp_f32_e32 v28, v28
	v_med3_f32 v25, v25, s76, v225
	v_fmamk_f32 v26, v147, 0xbc5083aa, v3
	v_med3_f32 v26, v26, s76, v225
	v_mul_f32_e32 v22, v22, v27
	v_mul_f32_e32 v22, v25, v22
	v_mul_f32_e32 v24, v24, v28
	v_mul_f32_e32 v24, v26, v24
	v_fmamk_f32 v25, v160, 0xbd9d265f, v12
	v_max_f32_e32 v25, 0xc1898193, v25
	v_fmamk_f32 v26, v156, 0xbd9d265f, v8
	v_max_f32_e32 v26, 0xc1898193, v26
	v_exp_f32_e32 v29, v25
	v_exp_f32_e32 v30, v26
	v_fmamk_f32 v27, v152, 0xbc5083aa, v16
	v_add_f32_e32 v29, 1.0, v29
	v_rcp_f32_e32 v29, v29
	v_add_f32_e32 v30, 1.0, v30
	v_rcp_f32_e32 v30, v30
	v_med3_f32 v27, v27, s76, v225
	v_fmamk_f32 v28, v148, 0xbc5083aa, v4
	v_med3_f32 v28, v28, s76, v225
	v_mul_f32_e32 v25, v25, v29
	v_mul_f32_e32 v25, v27, v25
	v_mul_f32_e32 v26, v26, v30
	v_mul_f32_e32 v26, v28, v26
	v_fmamk_f32 v27, v161, 0xbd9d265f, v13
	v_max_f32_e32 v27, 0xc1898193, v27
	v_fmamk_f32 v28, v157, 0xbd9d265f, v9
	v_max_f32_e32 v28, 0xc1898193, v28
	v_exp_f32_e32 v31, v27
	v_exp_f32_e32 v32, v28
	v_fmamk_f32 v29, v153, 0xbc5083aa, v17
	v_add_f32_e32 v31, 1.0, v31
	v_rcp_f32_e32 v31, v31
	v_add_f32_e32 v32, 1.0, v32
	v_rcp_f32_e32 v32, v32
	v_med3_f32 v29, v29, s76, v225
	v_fmamk_f32 v30, v149, 0xbc5083aa, v5
	v_med3_f32 v30, v30, s76, v225
	v_mul_f32_e32 v27, v27, v31
	v_mul_f32_e32 v27, v29, v27
	v_mul_f32_e32 v28, v28, v32
	v_mul_f32_e32 v28, v30, v28
	v_cvt_pk_fp8_f32 v22, v21, v22
	v_cvt_pk_fp8_f32 v23, v23, v24
	v_cvt_pk_fp8_f32 v23, v26, v28 op_sel:[0, 0, 1]
	v_fmamk_f32 v21, v142, 0xbd9d265f, v10
	v_max_f32_e32 v21, 0xc1898193, v21
	v_fmamk_f32 v24, v138, 0xbd9d265f, v6
	v_cvt_pk_fp8_f32 v22, v25, v27 op_sel:[0,0,1]
	v_max_f32_e32 v24, 0xc1898193, v24
	v_exp_f32_e32 v27, v21
	v_exp_f32_e32 v28, v24
	v_fmamk_f32 v25, v134, 0xbc5083aa, v14
	v_add_f32_e32 v27, 1.0, v27
	v_rcp_f32_e32 v27, v27
	v_add_f32_e32 v28, 1.0, v28
	v_rcp_f32_e32 v28, v28
	v_med3_f32 v25, v25, s76, v225
	v_fmamk_f32 v26, v130, 0xbc5083aa, v2
	v_med3_f32 v26, v26, s76, v225
	v_mul_f32_e32 v21, v21, v27
	v_mul_f32_e32 v21, v25, v21
	v_mul_f32_e32 v24, v24, v28
	v_mov_b32_e32 v25, v26
	v_mul_f32_e32 v25, v25, v24
	v_fmamk_f32 v24, v143, 0xbd9d265f, v11
	v_max_f32_e32 v24, 0xc1898193, v24
	v_fmamk_f32 v26, v139, 0xbd9d265f, v7
	v_max_f32_e32 v26, 0xc1898193, v26
	v_exp_f32_e32 v29, v24
	v_exp_f32_e32 v30, v26
	v_fmamk_f32 v27, v135, 0xbc5083aa, v15
	v_add_f32_e32 v29, 1.0, v29
	v_rcp_f32_e32 v29, v29
	v_add_f32_e32 v30, 1.0, v30
	v_rcp_f32_e32 v30, v30
	v_med3_f32 v27, v27, s76, v225
	v_fmamk_f32 v28, v131, 0xbc5083aa, v3
	v_med3_f32 v28, v28, s76, v225
	v_mul_f32_e32 v24, v24, v29
	v_mul_f32_e32 v24, v27, v24
	v_mul_f32_e32 v26, v26, v30
	v_mul_f32_e32 v26, v28, v26
	v_fmamk_f32 v27, v144, 0xbd9d265f, v12
	v_max_f32_e32 v27, 0xc1898193, v27
	v_fmamk_f32 v28, v140, 0xbd9d265f, v8
	v_max_f32_e32 v28, 0xc1898193, v28
	v_exp_f32_e32 v31, v27
	v_exp_f32_e32 v32, v28
	v_fmamk_f32 v29, v136, 0xbc5083aa, v16
	v_add_f32_e32 v31, 1.0, v31
	v_rcp_f32_e32 v31, v31
	v_add_f32_e32 v32, 1.0, v32
	v_rcp_f32_e32 v32, v32
	v_med3_f32 v29, v29, s76, v225
	v_fmamk_f32 v30, v132, 0xbc5083aa, v4
	v_med3_f32 v30, v30, s76, v225
	v_mul_f32_e32 v27, v27, v31
	v_mul_f32_e32 v27, v29, v27
	v_mul_f32_e32 v28, v28, v32
	v_mul_f32_e32 v28, v30, v28
	v_fmamk_f32 v29, v145, 0xbd9d265f, v13
	v_max_f32_e32 v29, 0xc1898193, v29
	v_fmamk_f32 v30, v141, 0xbd9d265f, v9
	v_max_f32_e32 v30, 0xc1898193, v30
	v_exp_f32_e32 v33, v29
	v_exp_f32_e32 v34, v30
	v_fmamk_f32 v31, v137, 0xbc5083aa, v17
	v_add_f32_e32 v33, 1.0, v33
	v_rcp_f32_e32 v33, v33
	v_add_f32_e32 v34, 1.0, v34
	v_rcp_f32_e32 v34, v34
	v_med3_f32 v31, v31, s76, v225
	v_fmamk_f32 v32, v133, 0xbc5083aa, v5
	v_med3_f32 v32, v32, s76, v225
	v_mul_f32_e32 v29, v29, v33
	v_mul_f32_e32 v29, v31, v29
	v_mul_f32_e32 v30, v30, v34
	v_mul_f32_e32 v30, v32, v30
	v_cvt_pk_fp8_f32 v24, v21, v24
	v_cvt_pk_fp8_f32 v25, v25, v26
	v_cvt_pk_fp8_f32 v24, v27, v29 op_sel:[0,0,1]
	v_cvt_pk_fp8_f32 v25, v28, v30 op_sel:[0, 0, 1]
	v_add_u32_e32 v26, s8, v220
	v_ashrrev_i32_e32 v27, 31, v26
	v_lshlrev_b64 v[26:27], 11, v[26:27]
; __device__ __forceinline__ float sigmoidf_(float x) { return __builtin_amdgcn_rcpf(1.0f + __builtin_amdgcn_exp2f(-1.44269504089f * x)); }
;     __device__ __forceinline__ void operator()(EPI_ARGS) const {
;     ...
;                 for (int h = 0; h < 2; ++h) { const int m = 2 * mp + h;
;                     const f32x4 a0 = acc[ai][0][m][0] * 0.03125f + ba0, a1 = acc[ai][0][m][1] * 0.03125f + ba1, l0 = acc[ai][1][m][0] * 0.03125f + bl0, l1 = acc[ai][1][m][1] * 0.03125f + bl1;
;                     float o[8];
; #pragma unroll
;                     for (int j = 0; j < 4; ++j) { const float g0 = fminf(a0[j], 7.0f), g1 = fminf(a1[j], 7.0f), x0 = fminf(fmaxf(l0[j], -7.0f), 7.0f), x1 = fminf(fmaxf(l1[j], -7.0f), 7.0f);
;                         o[j] = g0 * sigmoidf_(1.702f * g0) * (x0 + 1.0f); o[4 + j] = g1 * sigmoidf_(1.702f * g1) * (x1 + 1.0f); }
;                     px[h] = pk4_fp8(o[0], o[1], o[2], o[3]); py[h] = pk4_fp8(o[4], o[5], o[6], o[7]); }
;                 const u32x4 q = pair16(px[0], py[0], px[1], py[1]);
;                 const int row = u.pm * 256 + ai * 128 + wr * 64 + (2 * mp + (fq & 1)) * 16 + fr;
;                 *(u32x4*)(ACT + (size_t)row * FE + j0q) = q; }
	v_lshl_add_u64 v[26:27], s[16:17], 0, v[26:27]
	v_permlane16_swap_b32_e32 v22, v24
	v_permlane16_swap_b32_e32 v23, v25
	v_lshl_add_u64 v[26:27], v[26:27], 0, v[18:19]
	v_fmamk_f32 v21, v126, 0xbd9d265f, v10
	global_store_dwordx4 v[26:27], v[22:25], off
	v_max_f32_e32 v21, 0xc1898193, v21
	s_nop 0
	v_fmamk_f32 v22, v122, 0xbd9d265f, v6
	v_max_f32_e32 v22, 0xc1898193, v22
	v_exp_f32_e32 v25, v21
	v_exp_f32_e32 v26, v22
	v_fmamk_f32 v23, v118, 0xbc5083aa, v14
	v_add_f32_e32 v25, 1.0, v25
	v_rcp_f32_e32 v25, v25
	v_add_f32_e32 v26, 1.0, v26
	v_rcp_f32_e32 v26, v26
	v_med3_f32 v23, v23, s76, v225
	v_fmamk_f32 v24, v114, 0xbc5083aa, v2
	v_med3_f32 v24, v24, s76, v225
	v_mul_f32_e32 v21, v21, v25
	v_mul_f32_e32 v21, v23, v21
	v_mul_f32_e32 v22, v22, v26
	v_mov_b32_e32 v23, v24
	v_mul_f32_e32 v23, v23, v22
	v_fmamk_f32 v22, v127, 0xbd9d265f, v11
	v_max_f32_e32 v22, 0xc1898193, v22
	v_fmamk_f32 v24, v123, 0xbd9d265f, v7
	v_max_f32_e32 v24, 0xc1898193, v24
	v_exp_f32_e32 v27, v22
	v_exp_f32_e32 v28, v24
	v_fmamk_f32 v25, v119, 0xbc5083aa, v15
	v_add_f32_e32 v27, 1.0, v27
	v_rcp_f32_e32 v27, v27
	v_add_f32_e32 v28, 1.0, v28
	v_rcp_f32_e32 v28, v28
	v_med3_f32 v25, v25, s76, v225
	v_fmamk_f32 v26, v115, 0xbc5083aa, v3
	v_med3_f32 v26, v26, s76, v225
	v_mul_f32_e32 v22, v22, v27
	v_mul_f32_e32 v22, v25, v22
	v_mul_f32_e32 v24, v24, v28
	v_mul_f32_e32 v24, v26, v24
	v_fmamk_f32 v25, v128, 0xbd9d265f, v12
	v_max_f32_e32 v25, 0xc1898193, v25
	v_fmamk_f32 v26, v124, 0xbd9d265f, v8
	v_max_f32_e32 v26, 0xc1898193, v26
	v_exp_f32_e32 v29, v25
	v_exp_f32_e32 v30, v26
	v_fmamk_f32 v27, v120, 0xbc5083aa, v16
	v_add_f32_e32 v29, 1.0, v29
	v_rcp_f32_e32 v29, v29
	v_add_f32_e32 v30, 1.0, v30
	v_rcp_f32_e32 v30, v30
	v_med3_f32 v27, v27, s76, v225
	v_fmamk_f32 v28, v116, 0xbc5083aa, v4
	v_med3_f32 v28, v28, s76, v225
	v_mul_f32_e32 v25, v25, v29
	v_mul_f32_e32 v25, v27, v25
	v_mul_f32_e32 v26, v26, v30
	v_mul_f32_e32 v26, v28, v26
	v_fmamk_f32 v27, v129, 0xbd9d265f, v13
	v_max_f32_e32 v27, 0xc1898193, v27
	v_fmamk_f32 v28, v125, 0xbd9d265f, v9
	v_max_f32_e32 v28, 0xc1898193, v28
	v_exp_f32_e32 v31, v27
	v_exp_f32_e32 v32, v28
	v_fmamk_f32 v29, v121, 0xbc5083aa, v17
	v_add_f32_e32 v31, 1.0, v31
	v_rcp_f32_e32 v31, v31
	v_add_f32_e32 v32, 1.0, v32
	v_rcp_f32_e32 v32, v32
	v_med3_f32 v29, v29, s76, v225
	v_fmamk_f32 v30, v117, 0xbc5083aa, v5
	v_med3_f32 v30, v30, s76, v225
	v_mul_f32_e32 v27, v27, v31
	v_mul_f32_e32 v27, v29, v27
	v_mul_f32_e32 v28, v28, v32
	v_mul_f32_e32 v28, v30, v28
	v_cvt_pk_fp8_f32 v22, v21, v22
	v_cvt_pk_fp8_f32 v23, v23, v24
	v_cvt_pk_fp8_f32 v23, v26, v28 op_sel:[0, 0, 1]
	v_fmamk_f32 v21, v110, 0xbd9d265f, v10
	v_max_f32_e32 v21, 0xc1898193, v21
	v_fmamk_f32 v24, v106, 0xbd9d265f, v6
	v_cvt_pk_fp8_f32 v22, v25, v27 op_sel:[0,0,1]
	v_max_f32_e32 v24, 0xc1898193, v24
	v_exp_f32_e32 v27, v21
	v_exp_f32_e32 v28, v24
	v_fmamk_f32 v25, v102, 0xbc5083aa, v14
	v_add_f32_e32 v27, 1.0, v27
	v_rcp_f32_e32 v27, v27
	v_add_f32_e32 v28, 1.0, v28
	v_rcp_f32_e32 v28, v28
	v_med3_f32 v25, v25, s76, v225
	v_fmamk_f32 v26, v98, 0xbc5083aa, v2
	v_med3_f32 v26, v26, s76, v225
	v_mul_f32_e32 v21, v21, v27
	v_mul_f32_e32 v21, v25, v21
	v_mul_f32_e32 v24, v24, v28
	v_mov_b32_e32 v25, v26
	v_mul_f32_e32 v25, v25, v24
	v_fmamk_f32 v24, v111, 0xbd9d265f, v11
	v_max_f32_e32 v24, 0xc1898193, v24
	v_fmamk_f32 v26, v107, 0xbd9d265f, v7
	v_max_f32_e32 v26, 0xc1898193, v26
	v_exp_f32_e32 v29, v24
	v_exp_f32_e32 v30, v26
	v_fmamk_f32 v27, v103, 0xbc5083aa, v15
	v_add_f32_e32 v29, 1.0, v29
	v_rcp_f32_e32 v29, v29
	v_add_f32_e32 v30, 1.0, v30
	v_rcp_f32_e32 v30, v30
	v_med3_f32 v27, v27, s76, v225
	v_fmamk_f32 v28, v99, 0xbc5083aa, v3
	v_med3_f32 v28, v28, s76, v225
	v_mul_f32_e32 v24, v24, v29
	v_mul_f32_e32 v24, v27, v24
	v_mul_f32_e32 v26, v26, v30
	v_mul_f32_e32 v26, v28, v26
	v_fmamk_f32 v27, v112, 0xbd9d265f, v12
	v_max_f32_e32 v27, 0xc1898193, v27
	v_fmamk_f32 v28, v108, 0xbd9d265f, v8
	v_max_f32_e32 v28, 0xc1898193, v28
	v_exp_f32_e32 v31, v27
	v_exp_f32_e32 v32, v28
	v_fmamk_f32 v29, v104, 0xbc5083aa, v16
	v_add_f32_e32 v31, 1.0, v31
	v_rcp_f32_e32 v31, v31
	v_add_f32_e32 v32, 1.0, v32
	v_rcp_f32_e32 v32, v32
	v_med3_f32 v29, v29, s76, v225
	v_fmamk_f32 v30, v100, 0xbc5083aa, v4
	v_med3_f32 v30, v30, s76, v225
	v_mul_f32_e32 v27, v27, v31
	v_mul_f32_e32 v27, v29, v27
	v_mul_f32_e32 v28, v28, v32
	v_mul_f32_e32 v28, v30, v28
	v_fmamk_f32 v29, v113, 0xbd9d265f, v13
	v_max_f32_e32 v29, 0xc1898193, v29
	v_fmamk_f32 v30, v109, 0xbd9d265f, v9
	v_max_f32_e32 v30, 0xc1898193, v30
	v_exp_f32_e32 v33, v29
	v_exp_f32_e32 v34, v30
	v_fmamk_f32 v31, v105, 0xbc5083aa, v17
	v_add_f32_e32 v33, 1.0, v33
	v_rcp_f32_e32 v33, v33
	v_add_f32_e32 v34, 1.0, v34
	v_rcp_f32_e32 v34, v34
	v_med3_f32 v31, v31, s76, v225
	v_fmamk_f32 v32, v101, 0xbc5083aa, v5
	v_med3_f32 v32, v32, s76, v225
	v_mul_f32_e32 v29, v29, v33
	v_mul_f32_e32 v29, v31, v29
	v_mul_f32_e32 v30, v30, v34
	v_mul_f32_e32 v30, v32, v30
	v_cvt_pk_fp8_f32 v24, v21, v24
	v_cvt_pk_fp8_f32 v25, v25, v26
	v_cvt_pk_fp8_f32 v24, v27, v29 op_sel:[0,0,1]
	v_cvt_pk_fp8_f32 v25, v28, v30 op_sel:[0, 0, 1]
	v_add_u32_e32 v26, 0x80, v20
	v_ashrrev_i32_e32 v27, 31, v26
	v_lshlrev_b64 v[26:27], 11, v[26:27]
	v_lshl_add_u64 v[26:27], s[16:17], 0, v[26:27]
; __device__ __forceinline__ float sigmoidf_(float x) { return __builtin_amdgcn_rcpf(1.0f + __builtin_amdgcn_exp2f(-1.44269504089f * x)); }
;     __device__ __forceinline__ void operator()(EPI_ARGS) const {
;     ...
;                 for (int h = 0; h < 2; ++h) { const int m = 2 * mp + h;
;                     const f32x4 a0 = acc[ai][0][m][0] * 0.03125f + ba0, a1 = acc[ai][0][m][1] * 0.03125f + ba1, l0 = acc[ai][1][m][0] * 0.03125f + bl0, l1 = acc[ai][1][m][1] * 0.03125f + bl1;
;                     float o[8];
; #pragma unroll
;                     for (int j = 0; j < 4; ++j) { const float g0 = fminf(a0[j], 7.0f), g1 = fminf(a1[j], 7.0f), x0 = fminf(fmaxf(l0[j], -7.0f), 7.0f), x1 = fminf(fmaxf(l1[j], -7.0f), 7.0f);
;                         o[j] = g0 * sigmoidf_(1.702f * g0) * (x0 + 1.0f); o[4 + j] = g1 * sigmoidf_(1.702f * g1) * (x1 + 1.0f); }
;                     px[h] = pk4_fp8(o[0], o[1], o[2], o[3]); py[h] = pk4_fp8(o[4], o[5], o[6], o[7]); }
;                 const u32x4 q = pair16(px[0], py[0], px[1], py[1]);
;                 const int row = u.pm * 256 + ai * 128 + wr * 64 + (2 * mp + (fq & 1)) * 16 + fr;
;                 *(u32x4*)(ACT + (size_t)row * FE + j0q) = q; }
	v_permlane16_swap_b32_e32 v22, v24
	v_permlane16_swap_b32_e32 v23, v25
	v_lshl_add_u64 v[26:27], v[26:27], 0, v[18:19]
	v_fmamk_f32 v21, v94, 0xbd9d265f, v10
	global_store_dwordx4 v[26:27], v[22:25], off
	v_max_f32_e32 v21, 0xc1898193, v21
	v_fmamk_f32 v10, v78, 0xbd9d265f, v10
	v_fmamk_f32 v22, v90, 0xbd9d265f, v6
	v_max_f32_e32 v22, 0xc1898193, v22
	v_exp_f32_e32 v25, v21
	v_exp_f32_e32 v26, v22
	v_fmamk_f32 v23, v86, 0xbc5083aa, v14
	v_add_f32_e32 v25, 1.0, v25
	v_rcp_f32_e32 v25, v25
	v_add_f32_e32 v26, 1.0, v26
	v_rcp_f32_e32 v26, v26
	v_med3_f32 v23, v23, s76, v225
	v_fmamk_f32 v24, v82, 0xbc5083aa, v2
	v_med3_f32 v24, v24, s76, v225
	v_mul_f32_e32 v21, v21, v25
	v_mul_f32_e32 v21, v23, v21
	v_mul_f32_e32 v22, v22, v26
	v_mov_b32_e32 v23, v24
	v_mul_f32_e32 v23, v23, v22
	v_fmamk_f32 v22, v95, 0xbd9d265f, v11
	v_max_f32_e32 v22, 0xc1898193, v22
	v_fmamk_f32 v24, v91, 0xbd9d265f, v7
	v_max_f32_e32 v24, 0xc1898193, v24
	v_exp_f32_e32 v27, v22
	v_exp_f32_e32 v28, v24
	v_fmamk_f32 v25, v87, 0xbc5083aa, v15
	v_add_f32_e32 v27, 1.0, v27
	v_rcp_f32_e32 v27, v27
	v_add_f32_e32 v28, 1.0, v28
	v_rcp_f32_e32 v28, v28
	v_med3_f32 v25, v25, s76, v225
	v_fmamk_f32 v26, v83, 0xbc5083aa, v3
	v_med3_f32 v26, v26, s76, v225
	v_mul_f32_e32 v22, v22, v27
	v_mul_f32_e32 v22, v25, v22
	v_mul_f32_e32 v24, v24, v28
	v_mul_f32_e32 v24, v26, v24
	v_fmamk_f32 v25, v96, 0xbd9d265f, v12
	v_max_f32_e32 v25, 0xc1898193, v25
	v_fmamk_f32 v26, v92, 0xbd9d265f, v8
	v_max_f32_e32 v26, 0xc1898193, v26
	v_exp_f32_e32 v29, v25
	v_exp_f32_e32 v30, v26
	v_fmamk_f32 v27, v88, 0xbc5083aa, v16
	v_add_f32_e32 v29, 1.0, v29
	v_rcp_f32_e32 v29, v29
	v_add_f32_e32 v30, 1.0, v30
	v_rcp_f32_e32 v30, v30
	v_med3_f32 v27, v27, s76, v225
	v_fmamk_f32 v28, v84, 0xbc5083aa, v4
	v_med3_f32 v28, v28, s76, v225
	v_mul_f32_e32 v25, v25, v29
	v_mul_f32_e32 v25, v27, v25
	v_mul_f32_e32 v26, v26, v30
	v_mul_f32_e32 v26, v28, v26
	v_fmamk_f32 v27, v97, 0xbd9d265f, v13
	v_max_f32_e32 v27, 0xc1898193, v27
	v_fmamk_f32 v28, v93, 0xbd9d265f, v9
	v_max_f32_e32 v28, 0xc1898193, v28
	v_exp_f32_e32 v31, v27
	v_exp_f32_e32 v32, v28
	v_fmamk_f32 v29, v89, 0xbc5083aa, v17
	v_add_f32_e32 v31, 1.0, v31
	v_rcp_f32_e32 v31, v31
	v_add_f32_e32 v32, 1.0, v32
	v_rcp_f32_e32 v32, v32
	v_med3_f32 v29, v29, s76, v225
	v_fmamk_f32 v30, v85, 0xbc5083aa, v5
	v_med3_f32 v30, v30, s76, v225
	v_mul_f32_e32 v27, v27, v31
	v_mul_f32_e32 v27, v29, v27
	v_mul_f32_e32 v28, v28, v32
	v_mul_f32_e32 v28, v30, v28
	v_mov_b32_e32 v29, v22
	v_cvt_pk_fp8_f32 v22, v21, v29
	v_cvt_pk_fp8_f32 v23, v23, v24
	v_fmamk_f32 v6, v74, 0xbd9d265f, v6
	v_max_f32_e32 v6, 0xc1898193, v6
	v_cvt_pk_fp8_f32 v23, v26, v28 op_sel:[0, 0, 1]
	v_max_f32_e32 v10, 0xc1898193, v10
	v_exp_f32_e32 v24, v6
	v_exp_f32_e32 v21, v10
	v_fmamk_f32 v2, v66, 0xbc5083aa, v2
	v_add_f32_e32 v24, 1.0, v24
	v_rcp_f32_e32 v24, v24
	v_add_f32_e32 v21, 1.0, v21
	v_rcp_f32_e32 v21, v21
	v_med3_f32 v2, v2, s76, v225
	v_fmamk_f32 v14, v70, 0xbc5083aa, v14
	v_mul_f32_e32 v6, v6, v24
	v_med3_f32 v14, v14, s76, v225
	v_mul_f32_e32 v2, v2, v6
	v_fmamk_f32 v6, v79, 0xbd9d265f, v11
	v_mul_f32_e32 v10, v10, v21
	v_max_f32_e32 v6, 0xc1898193, v6
	v_fmamk_f32 v7, v75, 0xbd9d265f, v7
	v_mul_f32_e32 v10, v14, v10
	v_max_f32_e32 v7, 0xc1898193, v7
	v_fmamk_f32 v11, v71, 0xbc5083aa, v15
	v_exp_f32_e32 v14, v6
	v_exp_f32_e32 v15, v7
	v_fmamk_f32 v8, v76, 0xbd9d265f, v8
	v_add_f32_e32 v14, 1.0, v14
	v_rcp_f32_e32 v14, v14
	v_add_f32_e32 v15, 1.0, v15
	v_rcp_f32_e32 v15, v15
	v_fmamk_f32 v3, v67, 0xbc5083aa, v3
	v_max_f32_e32 v8, 0xc1898193, v8
	v_med3_f32 v3, v3, s76, v225
	v_mul_f32_e32 v6, v6, v14
	v_mul_f32_e32 v7, v7, v15
	v_mul_f32_e32 v3, v3, v7
	v_fmamk_f32 v7, v80, 0xbd9d265f, v12
	v_exp_f32_e32 v14, v8
	v_max_f32_e32 v7, 0xc1898193, v7
	v_exp_f32_e32 v12, v7
	v_add_f32_e32 v14, 1.0, v14
	v_rcp_f32_e32 v14, v14
	v_fmamk_f32 v4, v68, 0xbc5083aa, v4
	v_add_f32_e32 v12, 1.0, v12
	v_med3_f32 v4, v4, s76, v225
	v_fmac_f32_e32 v9, 0xbd9d265f, v77
	v_rcp_f32_e32 v12, v12
	v_mul_f32_e32 v8, v8, v14
	v_fmac_f32_e32 v13, 0xbd9d265f, v81
	v_max_f32_e32 v9, 0xc1898193, v9
	v_mul_f32_e32 v4, v4, v8
	v_max_f32_e32 v8, 0xc1898193, v13
	v_exp_f32_e32 v13, v9
	v_mul_f32_e32 v7, v7, v12
	v_exp_f32_e32 v12, v8
	v_add_f32_e32 v13, 1.0, v13
	v_rcp_f32_e32 v13, v13
	v_med3_f32 v11, v11, s76, v225
	v_fmac_f32_e32 v5, 0xbc5083aa, v69
	v_add_f32_e32 v12, 1.0, v12
	v_mul_f32_e32 v6, v11, v6
	v_fmamk_f32 v11, v72, 0xbc5083aa, v16
	v_rcp_f32_e32 v12, v12
	v_med3_f32 v5, v5, s76, v225
	v_med3_f32 v11, v11, s76, v225
	v_mul_f32_e32 v9, v9, v13
	v_cvt_pk_fp8_f32 v22, v25, v27 op_sel:[0,0,1]
	v_fmac_f32_e32 v17, 0xbc5083aa, v73
	v_mul_f32_e32 v5, v5, v9
	v_mul_f32_e32 v7, v11, v7
	v_med3_f32 v11, v17, s76, v225
	v_cvt_pk_fp8_f32 v24, v10, v6
	v_cvt_pk_fp8_f32 v25, v2, v3
	v_mul_f32_e32 v8, v8, v12
	v_mul_f32_e32 v8, v11, v8
	v_cvt_pk_fp8_f32 v24, v7, v8 op_sel:[0,0,1]
	v_cvt_pk_fp8_f32 v25, v4, v5 op_sel:[0, 0, 1]
	v_add_u32_e32 v2, 0xa0, v20
	v_ashrrev_i32_e32 v3, 31, v2
	v_lshlrev_b64 v[2:3], 11, v[2:3]
	v_lshl_add_u64 v[2:3], s[16:17], 0, v[2:3]
	v_permlane16_swap_b32_e32 v22, v24
	v_permlane16_swap_b32_e32 v23, v25
	v_lshl_add_u64 v[2:3], v[2:3], 0, v[18:19]
	global_store_dwordx4 v[2:3], v[22:25], off
	s_cbranch_vccnz .LBB0_1302
	s_branch .LBB0_1301

; #define EPI_ALD16(dst_, ptr_) asm volatile("global_load_dwordx4 %0, %1, off" : "=v"(dst_) : "v"(ptr_))
;     __device__ __forceinline__ void operator()(EPI_ARGS) const {
;         const float* bb = b2 + (size_t)u.e * D; const float* lw = lwt + (size_t)u.e * LCAP + u.rb * 256;
;         float wg[2][4]; f32x4 cb[2][2];
; #pragma unroll
;         for (int ai = 0; ai < 2; ++ai)
; #pragma unroll
;             for (int m = 0; m < 4; ++m) { const float* p_ = lw + (ai * 128 + wr * 64 + m * 16 + fr); asm volatile("global_load_dword %0, %1, off" : "=v"(wg[ai][m]) : "v"(p_)); }
; #pragma unroll
;         for (int bj = 0; bj < 2; ++bj) { const float* p_ = bb + u.pn * 256 + bj * 128 + wc * 32 + 8 * fq; EPI_ALD16(cb[bj][0], p_); EPI_ALD16(cb[bj][1], p_ + 4); }
;         asm volatile("s_waitcnt vmcnt(0)" : "+v"(wg[0][0]), "+v"(wg[0][1]), "+v"(wg[0][2]), "+v"(wg[0][3]), "+v"(wg[1][0]), "+v"(wg[1][1]), "+v"(wg[1][2]), "+v"(wg[1][3]), "+v"(cb[0][0]), "+v"(cb[0][1]), "+v"(cb[1][0]), "+v"(cb[1][1]));
; #pragma unroll
;         for (int ai = 0; ai < 2; ++ai)
; #pragma unroll
;             for (int m = 0; m < 4; ++m) { const int r = ai * 128 + wr * 64 + m * 16 + fr; wg[ai][m] = (r < u.nvalid) ? 16.0f * wg[ai][m] : 0.0f; }
; #pragma unroll
;         for (int bj = 0; bj < 2; ++bj) { const f32x4 c0 = cb[bj][0], c1 = cb[bj][1];
;             const int colq = u.pn * 256 + bj * 128 + wc * 32 + 8 * (fq & ~1);
; #pragma unroll
;             for (int ai = 0; ai < 2; ++ai)
; #pragma unroll
;                 for (int mp = 0; mp < 2; ++mp) { unsigned px[2], py[2];
; #pragma unroll
;                     for (int h = 0; h < 2; ++h) { const int m = 2 * mp + h; const f32x4 v0 = (acc[ai][bj][m][0] * 0.03125f + c0) * wg[ai][m], v1 = (acc[ai][bj][m][1] * 0.03125f + c1) * wg[ai][m];
;                         px[h] = pk4_fp8(v0[0], v0[1], v0[2], v0[3]); py[h] = pk4_fp8(v1[0], v1[1], v1[2], v1[3]); }
;                     const u32x4 q = pair16(px[0], py[0], px[1], py[1]);
;                     const int r = ai * 128 + wr * 64 + (2 * mp + (fq & 1)) * 16 + fr;
;                     *(u32x4*)(YE + ((size_t)u.pm * 256 + r) * D + colq) = q; } }
.LBB0_1433:
	s_ashr_i32 s37, s36, 31
	s_lshl_b64 s[8:9], s[36:37], 13
	s_lshl_b64 s[14:15], s[36:37], 16
	s_add_u32 s23, s73, s14
	s_addc_u32 s25, s74, s15
	s_lshl_b32 s14, s88, 8
	s_ashr_i32 s15, s14, 31
	s_lshl_b64 s[14:15], s[14:15], 2
	s_add_u32 s14, s23, s14
	s_addc_u32 s15, s25, s15
	v_lshl_add_u64 v[2:3], s[14:15], 0, v[204:205]
	v_lshl_add_u64 v[4:5], v[2:3], 0, 64
	s_mov_b64 s[14:15], 0x80
	s_nop 15
	s_nop 15
	s_waitcnt lgkmcnt(0)
	global_load_dword v18, v[2:3], off
	global_load_dword v19, v[4:5], off
	v_lshl_add_u64 v[4:5], v[2:3], 0, s[14:15]
	s_mov_b64 s[14:15], 0xc0
	global_load_dword v20, v[4:5], off
	v_lshl_add_u64 v[4:5], v[2:3], 0, s[14:15]
	global_load_dword v21, v[4:5], off
	v_lshl_add_u64 v[4:5], v[2:3], 0, s[16:17]
	s_mov_b64 s[14:15], 0x240
	s_add_u32 s23, s10, s8
	global_load_dword v22, v[4:5], off
	v_lshl_add_u64 v[4:5], v[2:3], 0, s[14:15]
	s_mov_b64 s[14:15], 0x280
	s_addc_u32 s25, s11, s9
	s_lshl_b32 s8, s38, 8
	global_load_dword v23, v[4:5], off
	v_lshl_add_u64 v[4:5], v[2:3], 0, s[14:15]
	s_mov_b64 s[14:15], 0x2c0
	s_ashr_i32 s9, s8, 31
	v_lshl_add_u64 v[2:3], v[2:3], 0, s[14:15]
	s_lshl_b64 s[14:15], s[8:9], 2
	s_add_u32 s9, s23, s14
	s_addc_u32 s15, s25, s15
	s_add_u32 s14, s9, s83
	s_addc_u32 s15, s15, 0
	v_mov_b32_e32 v217, v205
	global_load_dword v25, v[4:5], off
	global_load_dword v27, v[2:3], off
	v_lshl_add_u64 v[2:3], s[14:15], 0, v[216:217]
	v_lshl_add_u64 v[4:5], v[2:3], 0, 16
	s_mov_b64 s[14:15], 0x210
	global_load_dwordx4 v[14:17], v[2:3], off
	global_load_dwordx4 v[10:13], v[4:5], off
	v_lshl_add_u64 v[4:5], v[2:3], 0, s[16:17]
	v_lshl_add_u64 v[2:3], v[2:3], 0, s[14:15]
	global_load_dwordx4 v[6:9], v[4:5], off
	global_load_dwordx4 v[2:5], v[2:3], off
	v_cmp_gt_i32_e32 vcc, s87, v206
	s_waitcnt vmcnt(0)
	s_ashr_i32 s31, s30, 31
	v_mul_f32_e32 v18, 0x41800000, v18
	v_cndmask_b32_e32 v32, 0, v18, vcc
	v_mul_f32_e32 v18, 0x41800000, v19
	v_cmp_gt_i32_e32 vcc, s87, v1
	v_pk_fma_f32 v[38:39], v[190:191], s[18:19], v[14:15] op_sel_hi:[1,0,1]
	v_pk_fma_f32 v[42:43], v[186:187], s[18:19], v[10:11] op_sel_hi:[1,0,1]
	v_cndmask_b32_e32 v30, 0, v18, vcc
	v_mul_f32_e32 v18, 0x41800000, v20
	v_cmp_gt_i32_e32 vcc, s87, v195
	v_pk_mul_f32 v[38:39], v[38:39], v[32:33] op_sel_hi:[1,0]
	v_pk_mul_f32 v[42:43], v[42:43], v[32:33] op_sel_hi:[1,0]
	v_cndmask_b32_e32 v28, 0, v18, vcc
	v_mul_f32_e32 v18, 0x41800000, v21
	v_med3_f32 v19, v38, s84, v229
	v_med3_f32 v21, v39, s84, v229
	v_cvt_pk_fp8_f32 v38, v19, v21
	v_med3_f32 v19, v42, s84, v229
	v_med3_f32 v21, v43, s84, v229
	v_pk_fma_f32 v[40:41], v[188:189], s[18:19], v[12:13] op_sel_hi:[1,0,1]
	v_cvt_pk_fp8_f32 v39, v19, v21
	v_pk_mul_f32 v[40:41], v[40:41], v[32:33] op_sel_hi:[1,0]
	v_pk_fma_f32 v[44:45], v[178:179], s[18:19], v[10:11] op_sel_hi:[1,0,1]
	v_med3_f32 v19, v40, s84, v229
	v_med3_f32 v21, v41, s84, v229
	v_pk_fma_f32 v[40:41], v[182:183], s[18:19], v[14:15] op_sel_hi:[1,0,1]
	v_cmp_gt_i32_e32 vcc, s87, v207
	v_pk_mul_f32 v[40:41], v[40:41], v[30:31] op_sel_hi:[1,0]
	v_cvt_pk_fp8_f32 v39, v19, v21 op_sel:[0,0,1]
	v_pk_mul_f32 v[44:45], v[44:45], v[30:31] op_sel_hi:[1,0]
	v_med3_f32 v19, v40, s84, v229
	v_med3_f32 v21, v41, s84, v229
	v_cndmask_b32_e32 v26, 0, v18, vcc
	v_mul_f32_e32 v18, 0x41800000, v22
	v_cmp_gt_i32_e32 vcc, s87, v218
	v_pk_fma_f32 v[36:37], v[192:193], s[18:19], v[16:17] op_sel_hi:[1,0,1]
	v_cvt_pk_fp8_f32 v40, v19, v21
	v_med3_f32 v19, v44, s84, v229
	v_med3_f32 v21, v45, s84, v229
	v_cndmask_b32_e32 v24, 0, v18, vcc
	v_mul_f32_e32 v18, 0x41800000, v23
	v_cmp_gt_i32_e32 vcc, s87, v219
	v_pk_mul_f32 v[36:37], v[36:37], v[32:33] op_sel_hi:[1,0]
	v_cvt_pk_fp8_f32 v41, v19, v21
	v_cndmask_b32_e32 v22, 0, v18, vcc
	v_mul_f32_e32 v18, 0x41800000, v25
	v_med3_f32 v23, v36, s84, v229
	v_med3_f32 v25, v37, s84, v229
	v_pk_fma_f32 v[36:37], v[184:185], s[18:19], v[16:17] op_sel_hi:[1,0,1]
	v_pk_fma_f32 v[42:43], v[180:181], s[18:19], v[12:13] op_sel_hi:[1,0,1]
	v_pk_mul_f32 v[36:37], v[36:37], v[30:31] op_sel_hi:[1,0]
	v_pk_mul_f32 v[42:43], v[42:43], v[30:31] op_sel_hi:[1,0]
	v_cvt_pk_fp8_f32 v38, v23, v25 op_sel:[0,0,1]
	v_med3_f32 v23, v36, s84, v229
	v_med3_f32 v25, v37, s84, v229
	v_med3_f32 v19, v42, s84, v229
	v_med3_f32 v21, v43, s84, v229
	v_or_b32_e32 v34, s8, v222
	v_cvt_pk_fp8_f32 v40, v23, v25 op_sel:[0,0,1]
	v_cvt_pk_fp8_f32 v41, v19, v21 op_sel:[0,0,1]
	s_lshl_b64 s[8:9], s[30:31], 19
	s_add_u32 s8, s75, s8
	s_addc_u32 s9, s76, s9
	v_ashrrev_i32_e32 v35, 31, v34
	v_lshl_add_u64 v[36:37], s[8:9], 0, v[208:209]
	v_permlane16_swap_b32_e32 v38, v40
	v_permlane16_swap_b32_e32 v39, v41
	v_lshl_add_u64 v[36:37], v[36:37], 0, v[34:35]
	global_store_dwordx4 v[36:37], v[38:41], off
	v_pk_fma_f32 v[44:45], v[170:171], s[18:19], v[10:11] op_sel_hi:[1,0,1]
	v_pk_fma_f32 v[42:43], v[172:173], s[18:19], v[12:13] op_sel_hi:[1,0,1]
	v_pk_fma_f32 v[40:41], v[174:175], s[18:19], v[14:15] op_sel_hi:[1,0,1]
	v_pk_mul_f32 v[44:45], v[44:45], v[28:29] op_sel_hi:[1,0]
	v_pk_mul_f32 v[40:41], v[40:41], v[28:29] op_sel_hi:[1,0]
	v_pk_mul_f32 v[42:43], v[42:43], v[28:29] op_sel_hi:[1,0]
	v_med3_f32 v19, v40, s84, v229
	v_med3_f32 v21, v41, s84, v229
	v_cvt_pk_fp8_f32 v40, v19, v21
	v_med3_f32 v19, v44, s84, v229
	v_med3_f32 v21, v45, s84, v229
	v_cvt_pk_fp8_f32 v41, v19, v21
	v_med3_f32 v19, v42, s84, v229
	v_med3_f32 v21, v43, s84, v229
	v_pk_fma_f32 v[42:43], v[166:167], s[18:19], v[14:15] op_sel_hi:[1,0,1]
	v_pk_fma_f32 v[46:47], v[162:163], s[18:19], v[10:11] op_sel_hi:[1,0,1]
	v_pk_mul_f32 v[42:43], v[42:43], v[26:27] op_sel_hi:[1,0]
	v_cvt_pk_fp8_f32 v41, v19, v21 op_sel:[0,0,1]
	v_pk_mul_f32 v[46:47], v[46:47], v[26:27] op_sel_hi:[1,0]
;     __device__ __forceinline__ void operator()(EPI_ARGS) const {
;     ...
; #pragma unroll
;         for (int ai = 0; ai < 2; ++ai)
; #pragma unroll
;             for (int m = 0; m < 4; ++m) { const int r = ai * 128 + wr * 64 + m * 16 + fr; wg[ai][m] = (r < u.nvalid) ? 16.0f * wg[ai][m] : 0.0f; }
; #pragma unroll
;         for (int bj = 0; bj < 2; ++bj) { const f32x4 c0 = cb[bj][0], c1 = cb[bj][1];
;             const int colq = u.pn * 256 + bj * 128 + wc * 32 + 8 * (fq & ~1);
; #pragma unroll
;             for (int ai = 0; ai < 2; ++ai)
; #pragma unroll
;                 for (int mp = 0; mp < 2; ++mp) { unsigned px[2], py[2];
; #pragma unroll
;                     for (int h = 0; h < 2; ++h) { const int m = 2 * mp + h; const f32x4 v0 = (acc[ai][bj][m][0] * 0.03125f + c0) * wg[ai][m], v1 = (acc[ai][bj][m][1] * 0.03125f + c1) * wg[ai][m];
;                         px[h] = pk4_fp8(v0[0], v0[1], v0[2], v0[3]); py[h] = pk4_fp8(v1[0], v1[1], v1[2], v1[3]); }
;                     const u32x4 q = pair16(px[0], py[0], px[1], py[1]);
;                     const int r = ai * 128 + wr * 64 + (2 * mp + (fq & 1)) * 16 + fr;
;                     *(u32x4*)(YE + ((size_t)u.pm * 256 + r) * D + colq) = q; } }
	v_med3_f32 v19, v42, s84, v229
	v_med3_f32 v21, v43, s84, v229
	v_pk_fma_f32 v[38:39], v[176:177], s[18:19], v[16:17] op_sel_hi:[1,0,1]
	v_cvt_pk_fp8_f32 v42, v19, v21
	v_med3_f32 v19, v46, s84, v229
	v_med3_f32 v21, v47, s84, v229
	v_pk_mul_f32 v[38:39], v[38:39], v[28:29] op_sel_hi:[1,0]
	v_cvt_pk_fp8_f32 v43, v19, v21
	v_med3_f32 v23, v38, s84, v229
	v_med3_f32 v25, v39, s84, v229
	v_pk_fma_f32 v[38:39], v[168:169], s[18:19], v[16:17] op_sel_hi:[1,0,1]
	v_pk_fma_f32 v[44:45], v[164:165], s[18:19], v[12:13] op_sel_hi:[1,0,1]
	v_pk_mul_f32 v[38:39], v[38:39], v[26:27] op_sel_hi:[1,0]
	v_pk_mul_f32 v[44:45], v[44:45], v[26:27] op_sel_hi:[1,0]
	v_cvt_pk_fp8_f32 v40, v23, v25 op_sel:[0,0,1]
	v_med3_f32 v23, v38, s84, v229
	v_med3_f32 v25, v39, s84, v229
	v_med3_f32 v19, v44, s84, v229
	v_med3_f32 v21, v45, s84, v229
	v_cvt_pk_fp8_f32 v42, v23, v25 op_sel:[0,0,1]
	v_cvt_pk_fp8_f32 v43, v19, v21 op_sel:[0,0,1]
	v_lshl_add_u64 v[38:39], s[8:9], 0, v[210:211]
	v_lshl_add_u64 v[38:39], v[38:39], 0, v[34:35]
	v_permlane16_swap_b32_e32 v40, v42
	v_permlane16_swap_b32_e32 v41, v43
	global_store_dwordx4 v[38:39], v[40:43], off
	v_pk_fma_f32 v[46:47], v[154:155], s[18:19], v[10:11] op_sel_hi:[1,0,1]
	v_pk_fma_f32 v[44:45], v[156:157], s[18:19], v[12:13] op_sel_hi:[1,0,1]
	v_pk_fma_f32 v[42:43], v[158:159], s[18:19], v[14:15] op_sel_hi:[1,0,1]
	v_pk_mul_f32 v[46:47], v[46:47], v[24:25] op_sel_hi:[1,0]
	v_pk_mul_f32 v[42:43], v[42:43], v[24:25] op_sel_hi:[1,0]
	v_pk_fma_f32 v[40:41], v[160:161], s[18:19], v[16:17] op_sel_hi:[1,0,1]
	v_med3_f32 v19, v42, s84, v229
	v_med3_f32 v21, v43, s84, v229
	v_cvt_pk_fp8_f32 v42, v19, v21
	v_med3_f32 v19, v46, s84, v229
	v_med3_f32 v21, v47, s84, v229
	v_cvt_pk_fp8_f32 v43, v19, v21
	v_pk_mul_f32 v[40:41], v[40:41], v[24:25] op_sel_hi:[1,0]
	v_pk_mul_f32 v[44:45], v[44:45], v[24:25] op_sel_hi:[1,0]
	v_med3_f32 v23, v40, s84, v229
	v_med3_f32 v19, v44, s84, v229
	v_med3_f32 v21, v45, s84, v229
	v_pk_fma_f32 v[44:45], v[150:151], s[18:19], v[14:15] op_sel_hi:[1,0,1]
	v_pk_fma_f32 v[48:49], v[146:147], s[18:19], v[10:11] op_sel_hi:[1,0,1]
	v_pk_mul_f32 v[44:45], v[44:45], v[22:23] op_sel_hi:[1,0]
	v_cvt_pk_fp8_f32 v43, v19, v21 op_sel:[0,0,1]
	v_pk_mul_f32 v[48:49], v[48:49], v[22:23] op_sel_hi:[1,0]
	v_med3_f32 v19, v44, s84, v229
	v_med3_f32 v21, v45, s84, v229
	v_cvt_pk_fp8_f32 v44, v19, v21
	v_med3_f32 v19, v48, s84, v229
	v_med3_f32 v21, v49, s84, v229
	v_cvt_pk_fp8_f32 v45, v19, v21
	v_med3_f32 v25, v41, s84, v229
	v_pk_fma_f32 v[40:41], v[152:153], s[18:19], v[16:17] op_sel_hi:[1,0,1]
	v_pk_fma_f32 v[46:47], v[148:149], s[18:19], v[12:13] op_sel_hi:[1,0,1]
	v_pk_mul_f32 v[40:41], v[40:41], v[22:23] op_sel_hi:[1,0]
	v_pk_mul_f32 v[46:47], v[46:47], v[22:23] op_sel_hi:[1,0]
	v_cvt_pk_fp8_f32 v42, v23, v25 op_sel:[0,0,1]
	v_med3_f32 v23, v40, s84, v229
	v_med3_f32 v25, v41, s84, v229
	v_med3_f32 v19, v46, s84, v229
	v_med3_f32 v21, v47, s84, v229
	v_cvt_pk_fp8_f32 v44, v23, v25 op_sel:[0,0,1]
	v_cvt_pk_fp8_f32 v45, v19, v21 op_sel:[0,0,1]
	v_lshl_add_u64 v[40:41], s[8:9], 0, v[212:213]
	v_cmp_gt_i32_e32 vcc, s87, v220
	v_permlane16_swap_b32_e32 v42, v44
	v_permlane16_swap_b32_e32 v43, v45
	v_lshl_add_u64 v[40:41], v[40:41], 0, v[34:35]
	v_cndmask_b32_e32 v20, 0, v18, vcc
	global_store_dwordx4 v[40:41], v[42:45], off
	v_pk_fma_f32 v[46:47], v[140:141], s[18:19], v[12:13] op_sel_hi:[1,0,1]
	v_pk_fma_f32 v[48:49], v[138:139], s[18:19], v[10:11] op_sel_hi:[1,0,1]
	v_pk_fma_f32 v[42:43], v[144:145], s[18:19], v[16:17] op_sel_hi:[1,0,1]
	v_pk_fma_f32 v[44:45], v[142:143], s[18:19], v[14:15] op_sel_hi:[1,0,1]
	v_pk_mul_f32 v[42:43], v[42:43], v[20:21] op_sel_hi:[1,0]
	v_pk_mul_f32 v[44:45], v[44:45], v[20:21] op_sel_hi:[1,0]
	v_pk_mul_f32 v[46:47], v[46:47], v[20:21] op_sel_hi:[1,0]
	v_pk_mul_f32 v[48:49], v[48:49], v[20:21] op_sel_hi:[1,0]
	v_med3_f32 v19, v44, s84, v229
	v_med3_f32 v21, v45, s84, v229
	v_med3_f32 v23, v42, s84, v229
	v_mul_f32_e32 v18, 0x41800000, v27
	v_cmp_gt_i32_e32 vcc, s87, v221
	v_med3_f32 v25, v43, s84, v229
	v_cvt_pk_fp8_f32 v42, v19, v21
	v_med3_f32 v19, v48, s84, v229
	v_med3_f32 v21, v49, s84, v229
	v_cndmask_b32_e32 v18, 0, v18, vcc
	v_cvt_pk_fp8_f32 v43, v19, v21
	v_med3_f32 v19, v46, s84, v229
	v_pk_fma_f32 v[10:11], v[122:123], s[18:19], v[10:11] op_sel_hi:[1,0,1]
	v_pk_fma_f32 v[14:15], v[134:135], s[18:19], v[14:15] op_sel_hi:[1,0,1]
	v_pk_mul_f32 v[10:11], v[10:11], v[18:19] op_sel_hi:[1,0]
	v_pk_mul_f32 v[14:15], v[14:15], v[18:19] op_sel_hi:[1,0]
	v_med3_f32 v10, v10, s84, v229
	v_med3_f32 v11, v11, s84, v229
	v_med3_f32 v14, v14, s84, v229
	v_med3_f32 v15, v15, s84, v229
	v_cvt_pk_fp8_f32 v45, v10, v11
	v_pk_fma_f32 v[12:13], v[124:125], s[18:19], v[12:13] op_sel_hi:[1,0,1]
	v_cvt_pk_fp8_f32 v44, v14, v15
	v_pk_fma_f32 v[16:17], v[136:137], s[18:19], v[16:17] op_sel_hi:[1,0,1]
	v_pk_mul_f32 v[12:13], v[12:13], v[18:19] op_sel_hi:[1,0]
	v_pk_mul_f32 v[16:17], v[16:17], v[18:19] op_sel_hi:[1,0]
	v_med3_f32 v10, v12, s84, v229
	v_med3_f32 v11, v13, s84, v229
	v_med3_f32 v16, v16, s84, v229
	v_med3_f32 v17, v17, s84, v229
	v_cvt_pk_fp8_f32 v45, v10, v11 op_sel:[0,0,1]
	v_lshl_add_u64 v[10:11], s[8:9], 0, v[214:215]
	v_pk_fma_f32 v[12:13], v[132:133], s[18:19], v[8:9] op_sel_hi:[1,0,1]
	v_pk_fma_f32 v[14:15], v[130:131], s[18:19], v[6:7] op_sel_hi:[1,0,1]
	v_med3_f32 v21, v47, s84, v229
	v_cvt_pk_fp8_f32 v44, v16, v17 op_sel:[0,0,1]
	v_lshl_add_u64 v[10:11], v[10:11], 0, v[34:35]
	v_pk_mul_f32 v[12:13], v[12:13], v[32:33] op_sel_hi:[1,0]
	v_pk_mul_f32 v[14:15], v[14:15], v[32:33] op_sel_hi:[1,0]
	v_pk_fma_f32 v[16:17], v[128:129], s[18:19], v[4:5] op_sel_hi:[1,0,1]
;     __device__ __forceinline__ void operator()(EPI_ARGS) const {
;     ...
; #pragma unroll
;         for (int ai = 0; ai < 2; ++ai)
; #pragma unroll
;             for (int m = 0; m < 4; ++m) { const int r = ai * 128 + wr * 64 + m * 16 + fr; wg[ai][m] = (r < u.nvalid) ? 16.0f * wg[ai][m] : 0.0f; }
; #pragma unroll
;         for (int bj = 0; bj < 2; ++bj) { const f32x4 c0 = cb[bj][0], c1 = cb[bj][1];
;             const int colq = u.pn * 256 + bj * 128 + wc * 32 + 8 * (fq & ~1);
; #pragma unroll
;             for (int ai = 0; ai < 2; ++ai)
; #pragma unroll
;                 for (int mp = 0; mp < 2; ++mp) { unsigned px[2], py[2];
; #pragma unroll
;                     for (int h = 0; h < 2; ++h) { const int m = 2 * mp + h; const f32x4 v0 = (acc[ai][bj][m][0] * 0.03125f + c0) * wg[ai][m], v1 = (acc[ai][bj][m][1] * 0.03125f + c1) * wg[ai][m];
;                         px[h] = pk4_fp8(v0[0], v0[1], v0[2], v0[3]); py[h] = pk4_fp8(v1[0], v1[1], v1[2], v1[3]); }
;                     const u32x4 q = pair16(px[0], py[0], px[1], py[1]);
;                     const int r = ai * 128 + wr * 64 + (2 * mp + (fq & 1)) * 16 + fr;
;                     *(u32x4*)(YE + ((size_t)u.pm * 256 + r) * D + colq) = q; } }
	v_pk_fma_f32 v[34:35], v[126:127], s[18:19], v[2:3] op_sel_hi:[1,0,1]
	v_cvt_pk_fp8_f32 v43, v19, v21 op_sel:[0,0,1]
	v_pk_mul_f32 v[16:17], v[16:17], v[32:33] op_sel_hi:[1,0]
	v_pk_mul_f32 v[32:33], v[34:35], v[32:33] op_sel_hi:[1,0]
	v_med3_f32 v14, v14, s84, v229
	v_med3_f32 v15, v15, s84, v229
	v_med3_f32 v19, v12, s84, v229
	v_med3_f32 v21, v13, s84, v229
	v_cvt_pk_fp8_f32 v12, v14, v15
	v_med3_f32 v14, v32, s84, v229
	v_med3_f32 v15, v33, s84, v229
	v_cvt_pk_fp8_f32 v13, v14, v15
	v_med3_f32 v14, v16, s84, v229
	v_med3_f32 v15, v17, s84, v229
	v_pk_fma_f32 v[16:17], v[118:119], s[18:19], v[6:7] op_sel_hi:[1,0,1]
	v_cvt_pk_fp8_f32 v13, v14, v15 op_sel:[0,0,1]
	v_pk_fma_f32 v[14:15], v[120:121], s[18:19], v[8:9] op_sel_hi:[1,0,1]
	v_pk_mul_f32 v[16:17], v[16:17], v[30:31] op_sel_hi:[1,0]
	v_pk_mul_f32 v[14:15], v[14:15], v[30:31] op_sel_hi:[1,0]
	v_pk_fma_f32 v[32:33], v[116:117], s[18:19], v[4:5] op_sel_hi:[1,0,1]
	v_pk_fma_f32 v[34:35], v[114:115], s[18:19], v[2:3] op_sel_hi:[1,0,1]
	v_cvt_pk_fp8_f32 v12, v19, v21 op_sel:[0,0,1]
	v_pk_mul_f32 v[32:33], v[32:33], v[30:31] op_sel_hi:[1,0]
	v_pk_mul_f32 v[30:31], v[34:35], v[30:31] op_sel_hi:[1,0]
	v_med3_f32 v16, v16, s84, v229
	v_med3_f32 v17, v17, s84, v229
	v_med3_f32 v19, v14, s84, v229
	v_med3_f32 v21, v15, s84, v229
	v_cvt_pk_fp8_f32 v14, v16, v17
	v_med3_f32 v16, v30, s84, v229
	v_med3_f32 v17, v31, s84, v229
	v_cvt_pk_fp8_f32 v15, v16, v17
	v_med3_f32 v16, v32, s84, v229
	v_med3_f32 v17, v33, s84, v229
	v_cvt_pk_fp8_f32 v14, v19, v21 op_sel:[0,0,1]
	v_cvt_pk_fp8_f32 v15, v16, v17 op_sel:[0,0,1]
	v_pk_fma_f32 v[16:17], v[108:109], s[18:19], v[4:5] op_sel_hi:[1,0,1]
	v_pk_fma_f32 v[30:31], v[106:107], s[18:19], v[2:3] op_sel_hi:[1,0,1]
	v_permlane16_swap_b32_e32 v12, v14
	v_permlane16_swap_b32_e32 v13, v15
	global_store_dwordx4 v[36:37], v[12:15], off offset:128
	v_pk_mul_f32 v[16:17], v[16:17], v[28:29] op_sel_hi:[1,0]
	v_cvt_pk_fp8_f32 v42, v23, v25 op_sel:[0,0,1]
	v_pk_fma_f32 v[12:13], v[112:113], s[18:19], v[8:9] op_sel_hi:[1,0,1]
	v_pk_fma_f32 v[14:15], v[110:111], s[18:19], v[6:7] op_sel_hi:[1,0,1]
	v_pk_mul_f32 v[12:13], v[12:13], v[28:29] op_sel_hi:[1,0]
	v_pk_mul_f32 v[14:15], v[14:15], v[28:29] op_sel_hi:[1,0]
	v_pk_mul_f32 v[28:29], v[30:31], v[28:29] op_sel_hi:[1,0]
	v_med3_f32 v14, v14, s84, v229
	v_med3_f32 v15, v15, s84, v229
	v_med3_f32 v19, v12, s84, v229
	v_med3_f32 v21, v13, s84, v229
	v_cvt_pk_fp8_f32 v12, v14, v15
	v_med3_f32 v14, v28, s84, v229
	v_med3_f32 v15, v29, s84, v229
	v_cvt_pk_fp8_f32 v13, v14, v15
	v_med3_f32 v14, v16, s84, v229
	v_med3_f32 v15, v17, s84, v229
	v_pk_fma_f32 v[16:17], v[102:103], s[18:19], v[6:7] op_sel_hi:[1,0,1]
	v_cvt_pk_fp8_f32 v13, v14, v15 op_sel:[0,0,1]
	v_pk_fma_f32 v[14:15], v[104:105], s[18:19], v[8:9] op_sel_hi:[1,0,1]
	v_pk_mul_f32 v[16:17], v[16:17], v[26:27] op_sel_hi:[1,0]
	v_pk_mul_f32 v[14:15], v[14:15], v[26:27] op_sel_hi:[1,0]
	v_pk_fma_f32 v[28:29], v[100:101], s[18:19], v[4:5] op_sel_hi:[1,0,1]
	v_pk_fma_f32 v[30:31], v[98:99], s[18:19], v[2:3] op_sel_hi:[1,0,1]
	v_cvt_pk_fp8_f32 v12, v19, v21 op_sel:[0,0,1]
	v_pk_mul_f32 v[28:29], v[28:29], v[26:27] op_sel_hi:[1,0]
	v_pk_mul_f32 v[26:27], v[30:31], v[26:27] op_sel_hi:[1,0]
	v_med3_f32 v16, v16, s84, v229
	v_med3_f32 v17, v17, s84, v229
	v_med3_f32 v19, v14, s84, v229
	v_med3_f32 v21, v15, s84, v229
	v_cvt_pk_fp8_f32 v14, v16, v17
	v_med3_f32 v16, v26, s84, v229
	v_med3_f32 v17, v27, s84, v229
	v_cvt_pk_fp8_f32 v15, v16, v17
	v_med3_f32 v16, v28, s84, v229
	v_med3_f32 v17, v29, s84, v229
	v_cvt_pk_fp8_f32 v14, v19, v21 op_sel:[0,0,1]
	v_cvt_pk_fp8_f32 v15, v16, v17 op_sel:[0,0,1]
	v_pk_fma_f32 v[16:17], v[92:93], s[18:19], v[4:5] op_sel_hi:[1,0,1]
	v_pk_fma_f32 v[26:27], v[90:91], s[18:19], v[2:3] op_sel_hi:[1,0,1]
	v_permlane16_swap_b32_e32 v12, v14
	v_permlane16_swap_b32_e32 v13, v15
	global_store_dwordx4 v[38:39], v[12:15], off offset:128
	v_pk_mul_f32 v[16:17], v[16:17], v[24:25] op_sel_hi:[1,0]
;     __device__ __forceinline__ void operator()(EPI_ARGS) const {
;     ...
; #pragma unroll
;         for (int ai = 0; ai < 2; ++ai)
; #pragma unroll
;             for (int m = 0; m < 4; ++m) { const int r = ai * 128 + wr * 64 + m * 16 + fr; wg[ai][m] = (r < u.nvalid) ? 16.0f * wg[ai][m] : 0.0f; }
; #pragma unroll
;         for (int bj = 0; bj < 2; ++bj) { const f32x4 c0 = cb[bj][0], c1 = cb[bj][1];
;             const int colq = u.pn * 256 + bj * 128 + wc * 32 + 8 * (fq & ~1);
; #pragma unroll
;             for (int ai = 0; ai < 2; ++ai)
; #pragma unroll
;                 for (int mp = 0; mp < 2; ++mp) { unsigned px[2], py[2];
; #pragma unroll
;                     for (int h = 0; h < 2; ++h) { const int m = 2 * mp + h; const f32x4 v0 = (acc[ai][bj][m][0] * 0.03125f + c0) * wg[ai][m], v1 = (acc[ai][bj][m][1] * 0.03125f + c1) * wg[ai][m];
;                         px[h] = pk4_fp8(v0[0], v0[1], v0[2], v0[3]); py[h] = pk4_fp8(v1[0], v1[1], v1[2], v1[3]); }
;                     const u32x4 q = pair16(px[0], py[0], px[1], py[1]);
;                     const int r = ai * 128 + wr * 64 + (2 * mp + (fq & 1)) * 16 + fr;
;                     *(u32x4*)(YE + ((size_t)u.pm * 256 + r) * D + colq) = q; } }
	v_permlane16_swap_b32_e32 v42, v44
	v_pk_fma_f32 v[12:13], v[96:97], s[18:19], v[8:9] op_sel_hi:[1,0,1]
	v_pk_fma_f32 v[14:15], v[94:95], s[18:19], v[6:7] op_sel_hi:[1,0,1]
	v_pk_mul_f32 v[12:13], v[12:13], v[24:25] op_sel_hi:[1,0]
	v_pk_mul_f32 v[14:15], v[14:15], v[24:25] op_sel_hi:[1,0]
	v_pk_mul_f32 v[24:25], v[26:27], v[24:25] op_sel_hi:[1,0]
	v_med3_f32 v14, v14, s84, v229
	v_med3_f32 v15, v15, s84, v229
	v_med3_f32 v19, v12, s84, v229
	v_med3_f32 v21, v13, s84, v229
	v_cvt_pk_fp8_f32 v12, v14, v15
	v_med3_f32 v14, v24, s84, v229
	v_med3_f32 v15, v25, s84, v229
	v_cvt_pk_fp8_f32 v13, v14, v15
	v_med3_f32 v14, v16, s84, v229
	v_med3_f32 v15, v17, s84, v229
	v_pk_fma_f32 v[16:17], v[86:87], s[18:19], v[6:7] op_sel_hi:[1,0,1]
	v_cvt_pk_fp8_f32 v13, v14, v15 op_sel:[0,0,1]
	v_pk_fma_f32 v[14:15], v[88:89], s[18:19], v[8:9] op_sel_hi:[1,0,1]
	v_pk_mul_f32 v[16:17], v[16:17], v[22:23] op_sel_hi:[1,0]
	v_pk_mul_f32 v[14:15], v[14:15], v[22:23] op_sel_hi:[1,0]
	v_pk_fma_f32 v[24:25], v[84:85], s[18:19], v[4:5] op_sel_hi:[1,0,1]
	v_pk_fma_f32 v[26:27], v[82:83], s[18:19], v[2:3] op_sel_hi:[1,0,1]
	v_cvt_pk_fp8_f32 v12, v19, v21 op_sel:[0,0,1]
	v_pk_mul_f32 v[24:25], v[24:25], v[22:23] op_sel_hi:[1,0]
	v_pk_mul_f32 v[22:23], v[26:27], v[22:23] op_sel_hi:[1,0]
	v_med3_f32 v16, v16, s84, v229
	v_med3_f32 v17, v17, s84, v229
	v_med3_f32 v19, v14, s84, v229
	v_med3_f32 v21, v15, s84, v229
	v_cvt_pk_fp8_f32 v14, v16, v17
	v_med3_f32 v16, v22, s84, v229
	v_med3_f32 v17, v23, s84, v229
	v_cvt_pk_fp8_f32 v15, v16, v17
	v_med3_f32 v16, v24, s84, v229
	v_med3_f32 v17, v25, s84, v229
	v_cvt_pk_fp8_f32 v14, v19, v21 op_sel:[0,0,1]
	v_cvt_pk_fp8_f32 v15, v16, v17 op_sel:[0,0,1]
	v_pk_fma_f32 v[16:17], v[76:77], s[18:19], v[4:5] op_sel_hi:[1,0,1]
	v_pk_fma_f32 v[22:23], v[74:75], s[18:19], v[2:3] op_sel_hi:[1,0,1]
	v_permlane16_swap_b32_e32 v12, v14
	v_permlane16_swap_b32_e32 v13, v15
	global_store_dwordx4 v[40:41], v[12:15], off offset:128
	v_pk_mul_f32 v[16:17], v[16:17], v[20:21] op_sel_hi:[1,0]
	v_pk_fma_f32 v[2:3], v[66:67], s[18:19], v[2:3] op_sel_hi:[1,0,1]
	v_pk_fma_f32 v[12:13], v[80:81], s[18:19], v[8:9] op_sel_hi:[1,0,1]
	v_pk_fma_f32 v[14:15], v[78:79], s[18:19], v[6:7] op_sel_hi:[1,0,1]
	v_pk_mul_f32 v[12:13], v[12:13], v[20:21] op_sel_hi:[1,0]
	v_pk_mul_f32 v[14:15], v[14:15], v[20:21] op_sel_hi:[1,0]
	v_pk_mul_f32 v[20:21], v[22:23], v[20:21] op_sel_hi:[1,0]
	v_med3_f32 v14, v14, s84, v229
	v_med3_f32 v15, v15, s84, v229
	v_med3_f32 v19, v12, s84, v229
	v_med3_f32 v22, v13, s84, v229
	v_cvt_pk_fp8_f32 v12, v14, v15
	v_med3_f32 v14, v20, s84, v229
	v_med3_f32 v15, v21, s84, v229
	v_cvt_pk_fp8_f32 v13, v14, v15
	v_pk_fma_f32 v[6:7], v[70:71], s[18:19], v[6:7] op_sel_hi:[1,0,1]
	v_med3_f32 v14, v16, s84, v229
	v_med3_f32 v15, v17, s84, v229
	v_pk_mul_f32 v[6:7], v[6:7], v[18:19] op_sel_hi:[1,0]
	v_pk_mul_f32 v[2:3], v[2:3], v[18:19] op_sel_hi:[1,0]
	v_cvt_pk_fp8_f32 v13, v14, v15 op_sel:[0,0,1]
	v_med3_f32 v6, v6, s84, v229
	v_med3_f32 v7, v7, s84, v229
	v_med3_f32 v2, v2, s84, v229
	v_med3_f32 v3, v3, s84, v229
	v_cvt_pk_fp8_f32 v14, v6, v7
	v_cvt_pk_fp8_f32 v15, v2, v3
	v_pk_fma_f32 v[8:9], v[72:73], s[18:19], v[8:9] op_sel_hi:[1,0,1]
	v_pk_fma_f32 v[4:5], v[68:69], s[18:19], v[4:5] op_sel_hi:[1,0,1]
	v_pk_mul_f32 v[8:9], v[8:9], v[18:19] op_sel_hi:[1,0]
	v_pk_mul_f32 v[4:5], v[4:5], v[18:19] op_sel_hi:[1,0]
	v_med3_f32 v8, v8, s84, v229
	v_med3_f32 v9, v9, s84, v229
	v_med3_f32 v2, v4, s84, v229
	v_med3_f32 v3, v5, s84, v229
	v_cvt_pk_fp8_f32 v12, v19, v22 op_sel:[0,0,1]
	v_cvt_pk_fp8_f32 v14, v8, v9 op_sel:[0,0,1]
	v_cvt_pk_fp8_f32 v15, v2, v3 op_sel:[0,0,1]
	v_permlane16_swap_b32_e32 v43, v45
	v_permlane16_swap_b32_e32 v12, v14
	v_permlane16_swap_b32_e32 v13, v15
	s_and_b64 vcc, exec, s[6:7]
	s_mov_b64 s[6:7], -1
	global_store_dwordx4 v[10:11], v[42:45], off
	global_store_dwordx4 v[10:11], v[12:15], off offset:128
	s_cbranch_vccnz .LBB0_1406
	s_branch .LBB0_1405
